# speedup vs baseline: 1.0954x; 1.0661x over previous
_Z11proj_kernelPKDF16_S0_S0_S0_PKiPKfS4_S4_S4_S4_PDF16_S5_S5_:
	s_cmpk_lt_u32 s2, 0x100
	s_cbranch_scc1 .Lpf_go
	s_endpgm
.Lpf_go:
	s_load_dwordx8 s[24:31], s[0:1], 0x0
	s_load_dwordx8 s[32:39], s[0:1], 0x20
	s_load_dwordx8 s[40:47], s[0:1], 0x40
	s_load_dwordx2 s[48:49], s[0:1], 0x60
	s_mov_b32 s56, s0
	s_mov_b32 s57, s1
	s_mov_b32 s58, s2
	v_mov_b32_e32 v216, v0
	v_and_b32_e32 v1, 63, v0
	v_lshrrev_b32_e32 v2, 6, v0
	v_and_b32_e32 v3, 15, v0
	v_bfe_u32 v4, v0, 4, 2
	s_and_b32 s3, s2, 7
	s_lshr_b32 s4, s2, 3
	s_and_b32 s5, s4, 7
	s_bfe_u32 s6, s4, 0x10003
	s_lshr_b32 s7, s4, 4
	v_readfirstlane_b32 s18, v2
	s_movk_i32 s20, 0x80
	s_waitcnt lgkmcnt(0)
	s_load_dwordx2 s[52:53], s[32:33], 0x0
	s_cmp_eq_u32 s7, 0
	s_cbranch_scc0 .Lpf_kv
	s_lshl_b32 s8, s3, 1
	s_add_u32 s8, s8, s6
	s_lshr_b32 s9, s8, 3
	s_and_b32 s10, s8, 7
	s_lshl_b32 s10, s10, 8
	s_lshl_b32 s11, s8, 8
	s_mov_b32 s21, 0
	s_mov_b32 s12, s24
	s_mov_b32 s13, s25
	s_mov_b32 s14, s34
	s_mov_b32 s15, s35
	s_mov_b32 s16, s40
	s_mov_b32 s17, s41
	s_mov_b32 s22, s44
	s_mov_b32 s23, s45
	s_mov_b32 s19, 0x3e38aa3b
	s_branch .Lpf_common
.Lpf_kv:
	s_lshr_b32 s8, s3, 2
	s_add_u32 s21, s8, 1
	s_and_b32 s8, s3, 3
	s_and_b32 s9, s8, 1
	s_lshr_b32 s8, s8, 1
	s_lshl_b32 s8, s8, 1
	s_add_u32 s8, s8, s6
	s_mul_i32 s10, s8, 0x120
	s_lshl_b32 s11, s9, 11
	s_add_u32 s11, s11, s10
	s_cmp_eq_u32 s21, 1
	s_cselect_b32 s12, s26, s28
	s_cselect_b32 s13, s27, s29
	s_cselect_b32 s14, s36, s38
	s_cselect_b32 s15, s37, s39
	s_mov_b32 s16, s42
	s_mov_b32 s17, s43
	s_cselect_b32 s22, s46, s48
	s_cselect_b32 s23, s47, s49
	s_mov_b32 s19, 1.0
	s_waitcnt lgkmcnt(0)
	s_cmp_eq_u32 s9, 0
	s_cselect_b32 s51, s52, s53
	s_cmp_ge_i32 s10, s51
	s_cbranch_scc1 .Lpf_done
.Lpf_common:
	s_mul_i32 s8, s11, 0x880
	s_mul_hi_u32 s24, s11, 0x880
	s_add_u32 s12, s12, s8
	s_addc_u32 s13, s13, s24
	s_lshl_b32 s8, s21, 10
	s_lshl_b32 s24, s5, 7
	s_add_u32 s8, s8, s24
	s_mul_i32 s8, s8, 0x880
	s_add_u32 s6, s30, s8
	s_addc_u32 s7, s31, 0
	s_mov_b32 s4, s12
	s_mov_b32 s5, s13
	s_and_b32 s24, s18, 1
	s_lshr_b32 s25, s18, 1
	s_lshr_b32 s26, s2, 3
	s_and_b32 s26, s26, 7
	s_lshl_b32 s26, s26, 1
	s_add_u32 s26, s26, s24
	s_lshl_b32 s27, s9, 4
	s_add_u32 s27, s27, s26
	s_lshl_b32 s28, s18, 10
	s_lshl_b32 s8, s26, 8
	s_add_u32 s14, s14, s8
	s_addc_u32 s15, s15, 0
	s_lshl_b32 s8, s27, 18
	s_add_u32 s22, s22, s8
	s_addc_u32 s23, s23, 0
	v_lshrrev_b32_e32 v5, 3, v1
	v_lshl_add_u32 v5, v2, 3, v5
	v_mul_u32_u24_e32 v5, 0x880, v5
	v_and_b32_e32 v6, 7, v1
	v_lshrrev_b32_e32 v7, 4, v1
	v_and_b32_e32 v8, 1, v2
	v_lshl_or_b32 v7, v8, 2, v7
	v_xor_b32_e32 v6, v6, v7
	v_lshl_add_u32 v10, v6, 4, v5
	v_add_u32_e32 v11, 0x22000, v10
	v_add_u32_e32 v12, 0x44000, v10
	v_add_u32_e32 v13, 0x66000, v10
	v_add_u32_e32 v14, 0x88000, v10
	v_lshrrev_b32_e32 v5, 1, v3
	v_xor_b32_e32 v6, v4, v5
	v_lshlrev_b32_e32 v6, 4, v6
	v_or_b32_e32 v7, 4, v4
	v_xor_b32_e32 v7, v7, v5
	v_lshlrev_b32_e32 v7, 4, v7
	v_lshl_add_u32 v9, v8, 6, v3
	v_lshlrev_b32_e32 v9, 7, v9
	v_and_b32_e32 v5, 1, v4
	v_lshl_add_u32 v5, v5, 5, v3
	v_lshlrev_b32_e32 v5, 4, v5
	v_lshrrev_b32_e32 v8, 1, v4
	v_lshl_add_u32 v23, v8, 3, v5
	s_cmp_eq_u32 s21, 0
	s_cbranch_scc1 .Lpf_vQ
	s_cmp_lt_u32 s18, 4
	s_cselect_b32 s8, 1, 0
	s_cmp_eq_u32 s21, 1
	s_cbranch_scc0 .Lpf_vV
	s_cmp_eq_u32 s8, 1
	s_cbranch_scc1 .Lpf_vKA
	s_branch .Lpf_vKB
.Lpf_vV:
	s_cmp_eq_u32 s8, 1
	s_cbranch_scc1 .Lpf_vVA
	s_branch .Lpf_vVB
.Lpf_vQ:
	s_lshl_b32 s25, s25, 6
	s_add_u32 s29, s10, s25
	s_lshr_b32 s29, s29, 4
	v_add_u32_e32 v5, s25, v3
	v_lshlrev_b32_e32 v5, 7, v5
	v_add_u32_e32 v15, v5, v6
	v_add_u32_e32 v16, v5, v7
	v_add_u32_e32 v5, 0x8000, v9
	v_add_u32_e32 v17, v5, v6
	v_add_u32_e32 v18, v5, v7
	v_add_u32_e32 v19, 0x18000, v15
	v_add_u32_e32 v20, 0x18000, v16
	v_add_u32_e32 v21, 0x18000, v17
	v_add_u32_e32 v22, 0x18000, v18
	v_lshlrev_b32_e32 v5, 4, v4
	global_load_dwordx4 v[24:27], v5, s[14:15] offset:0
	global_load_dwordx4 v[28:31], v5, s[14:15] offset:64
	global_load_dwordx4 v[32:35], v5, s[14:15] offset:128
	global_load_dwordx4 v[36:39], v5, s[14:15] offset:192
	global_load_dwordx4 v[40:43], v5, s[16:17] offset:0
	global_load_dwordx4 v[44:47], v5, s[16:17] offset:64
	global_load_dwordx4 v[48:51], v5, s[16:17] offset:128
	global_load_dwordx4 v[52:55], v5, s[16:17] offset:192
	s_add_u32 m0, s28, 0x0
	s_nop 0
	global_load_lds_dwordx4 v10, s[4:5]
	s_add_u32 m0, s28, 0x2000
	s_nop 0
	global_load_lds_dwordx4 v11, s[4:5]
	s_add_u32 m0, s28, 0x4000
	s_nop 0
	global_load_lds_dwordx4 v12, s[4:5]
	s_add_u32 m0, s28, 0x6000
	s_nop 0
	global_load_lds_dwordx4 v13, s[4:5]
	s_add_u32 s4, s4, s20
	s_addc_u32 s5, s5, 0
	s_add_u32 m0, s28, 0x8000
	s_nop 0
	global_load_lds_dwordx4 v10, s[6:7]
	s_add_u32 m0, s28, 0xa000
	s_nop 0
	global_load_lds_dwordx4 v11, s[6:7]
	s_add_u32 s6, s6, s20
	s_addc_u32 s7, s7, 0
	s_add_u32 m0, s28, 0xc000
	s_nop 0
	global_load_lds_dwordx4 v10, s[4:5]
	s_add_u32 m0, s28, 0xe000
	s_nop 0
	global_load_lds_dwordx4 v11, s[4:5]
	s_add_u32 m0, s28, 0x10000
	s_nop 0
	global_load_lds_dwordx4 v12, s[4:5]
	s_add_u32 m0, s28, 0x12000
	s_nop 0
	global_load_lds_dwordx4 v13, s[4:5]
	s_add_u32 s4, s4, s20
	s_addc_u32 s5, s5, 0
	s_add_u32 m0, s28, 0x14000
	s_nop 0
	global_load_lds_dwordx4 v10, s[6:7]
	s_add_u32 m0, s28, 0x16000
	s_nop 0
	global_load_lds_dwordx4 v11, s[6:7]
	s_add_u32 s6, s6, s20
	s_addc_u32 s7, s7, 0
	s_add_u32 m0, s28, 0x18000
	s_nop 0
	global_load_lds_dwordx4 v10, s[4:5]
	s_add_u32 m0, s28, 0x1a000
	s_nop 0
	global_load_lds_dwordx4 v11, s[4:5]
	s_add_u32 m0, s28, 0x1c000
	s_nop 0
	global_load_lds_dwordx4 v12, s[4:5]
	s_add_u32 m0, s28, 0x1e000
	s_nop 0
	global_load_lds_dwordx4 v13, s[4:5]
	s_add_u32 s4, s4, s20
	s_addc_u32 s5, s5, 0
	s_add_u32 m0, s28, 0x20000
	s_nop 0
	global_load_lds_dwordx4 v10, s[6:7]
	s_add_u32 m0, s28, 0x22000
	s_nop 0
	global_load_lds_dwordx4 v11, s[6:7]
	s_add_u32 s6, s6, s20
	s_addc_u32 s7, s7, 0
	s_waitcnt vmcnt(12) lgkmcnt(0)
	s_barrier
	s_waitcnt lgkmcnt(7)
	ds_read_b128 v[136:139], v15
	ds_read_b128 v[156:159], v17
	ds_read_b128 v[160:163], v17 offset:2048
	ds_read_b128 v[164:167], v17 offset:4096
	ds_read_b128 v[168:171], v17 offset:6144
	ds_read_b128 v[140:143], v15 offset:2048
	ds_read_b128 v[144:147], v15 offset:4096
	ds_read_b128 v[148:151], v15 offset:6144
	s_waitcnt lgkmcnt(7)
	ds_read_b128 v[172:175], v16
	ds_read_b128 v[192:195], v18
	ds_read_b128 v[196:199], v18 offset:2048
	ds_read_b128 v[200:203], v18 offset:4096
	ds_read_b128 v[204:207], v18 offset:6144
	ds_read_b128 v[176:179], v16 offset:2048
	ds_read_b128 v[180:183], v16 offset:4096
	ds_read_b128 v[184:187], v16 offset:6144
	s_waitcnt lgkmcnt(14)
	v_mfma_f32_16x16x32_f16 v[56:59], v[156:159], v[136:139], 0
	s_waitcnt lgkmcnt(13)
	v_mfma_f32_16x16x32_f16 v[60:63], v[160:163], v[136:139], 0
	s_waitcnt lgkmcnt(12)
	v_mfma_f32_16x16x32_f16 v[64:67], v[164:167], v[136:139], 0
	s_waitcnt lgkmcnt(11)
	v_mfma_f32_16x16x32_f16 v[68:71], v[168:171], v[136:139], 0
	s_waitcnt lgkmcnt(10)
	v_mfma_f32_16x16x32_f16 v[72:75], v[156:159], v[140:143], 0
	v_mfma_f32_16x16x32_f16 v[76:79], v[160:163], v[140:143], 0
	v_mfma_f32_16x16x32_f16 v[80:83], v[164:167], v[140:143], 0
	v_mfma_f32_16x16x32_f16 v[84:87], v[168:171], v[140:143], 0
	s_waitcnt lgkmcnt(9)
	v_mfma_f32_16x16x32_f16 v[88:91], v[156:159], v[144:147], 0
	v_mfma_f32_16x16x32_f16 v[92:95], v[160:163], v[144:147], 0
	v_mfma_f32_16x16x32_f16 v[96:99], v[164:167], v[144:147], 0
	v_mfma_f32_16x16x32_f16 v[100:103], v[168:171], v[144:147], 0
	s_waitcnt lgkmcnt(8)
	v_mfma_f32_16x16x32_f16 v[104:107], v[156:159], v[148:151], 0
	v_mfma_f32_16x16x32_f16 v[108:111], v[160:163], v[148:151], 0
	v_mfma_f32_16x16x32_f16 v[112:115], v[164:167], v[148:151], 0
	v_mfma_f32_16x16x32_f16 v[116:119], v[168:171], v[148:151], 0
	s_waitcnt vmcnt(6) lgkmcnt(0)
	s_barrier
	s_waitcnt lgkmcnt(7)
	ds_read_b128 v[136:139], v15 offset:49152
	ds_read_b128 v[156:159], v17 offset:49152
	ds_read_b128 v[160:163], v17 offset:51200
	ds_read_b128 v[164:167], v17 offset:53248
	ds_read_b128 v[168:171], v17 offset:55296
	ds_read_b128 v[140:143], v15 offset:51200
	ds_read_b128 v[144:147], v15 offset:53248
	ds_read_b128 v[148:151], v15 offset:55296
	s_waitcnt lgkmcnt(14)
	v_mfma_f32_16x16x32_f16 v[56:59], v[192:195], v[172:175], v[56:59]
	s_add_u32 m0, s28, 0x0
	s_nop 0
	global_load_lds_dwordx4 v10, s[4:5]
	s_waitcnt lgkmcnt(13)
	v_mfma_f32_16x16x32_f16 v[60:63], v[196:199], v[172:175], v[60:63]
	s_waitcnt lgkmcnt(12)
	v_mfma_f32_16x16x32_f16 v[64:67], v[200:203], v[172:175], v[64:67]
	s_waitcnt lgkmcnt(11)
	v_mfma_f32_16x16x32_f16 v[68:71], v[204:207], v[172:175], v[68:71]
	s_waitcnt lgkmcnt(10)
	v_mfma_f32_16x16x32_f16 v[72:75], v[192:195], v[176:179], v[72:75]
	v_mfma_f32_16x16x32_f16 v[76:79], v[196:199], v[176:179], v[76:79]
	s_add_u32 m0, s28, 0x2000
	s_nop 0
	global_load_lds_dwordx4 v11, s[4:5]
	v_mfma_f32_16x16x32_f16 v[80:83], v[200:203], v[176:179], v[80:83]
	v_mfma_f32_16x16x32_f16 v[84:87], v[204:207], v[176:179], v[84:87]
	s_waitcnt lgkmcnt(9)
	v_mfma_f32_16x16x32_f16 v[88:91], v[192:195], v[180:183], v[88:91]
	v_mfma_f32_16x16x32_f16 v[92:95], v[196:199], v[180:183], v[92:95]
	v_mfma_f32_16x16x32_f16 v[96:99], v[200:203], v[180:183], v[96:99]
	s_add_u32 m0, s28, 0x4000
	s_nop 0
	global_load_lds_dwordx4 v12, s[4:5]
	v_mfma_f32_16x16x32_f16 v[100:103], v[204:207], v[180:183], v[100:103]
	s_waitcnt lgkmcnt(8)
	v_mfma_f32_16x16x32_f16 v[104:107], v[192:195], v[184:187], v[104:107]
	v_mfma_f32_16x16x32_f16 v[108:111], v[196:199], v[184:187], v[108:111]
	v_mfma_f32_16x16x32_f16 v[112:115], v[200:203], v[184:187], v[112:115]
	v_mfma_f32_16x16x32_f16 v[116:119], v[204:207], v[184:187], v[116:119]
	s_waitcnt lgkmcnt(7)
	ds_read_b128 v[172:175], v16 offset:49152
	ds_read_b128 v[192:195], v18 offset:49152
	ds_read_b128 v[196:199], v18 offset:51200
	ds_read_b128 v[200:203], v18 offset:53248
	ds_read_b128 v[204:207], v18 offset:55296
	ds_read_b128 v[176:179], v16 offset:51200
	ds_read_b128 v[180:183], v16 offset:53248
	ds_read_b128 v[184:187], v16 offset:55296
	s_waitcnt lgkmcnt(14)
	v_mfma_f32_16x16x32_f16 v[56:59], v[156:159], v[136:139], v[56:59]
	s_add_u32 m0, s28, 0x6000
	s_nop 0
	global_load_lds_dwordx4 v13, s[4:5]
	s_add_u32 s4, s4, s20
	s_addc_u32 s5, s5, 0
	s_waitcnt lgkmcnt(13)
	v_mfma_f32_16x16x32_f16 v[60:63], v[160:163], v[136:139], v[60:63]
	s_waitcnt lgkmcnt(12)
	v_mfma_f32_16x16x32_f16 v[64:67], v[164:167], v[136:139], v[64:67]
	s_waitcnt lgkmcnt(11)
	v_mfma_f32_16x16x32_f16 v[68:71], v[168:171], v[136:139], v[68:71]
	s_waitcnt lgkmcnt(10)
	v_mfma_f32_16x16x32_f16 v[72:75], v[156:159], v[140:143], v[72:75]
	v_mfma_f32_16x16x32_f16 v[76:79], v[160:163], v[140:143], v[76:79]
	s_add_u32 m0, s28, 0x8000
	s_nop 0
	global_load_lds_dwordx4 v10, s[6:7]
	v_mfma_f32_16x16x32_f16 v[80:83], v[164:167], v[140:143], v[80:83]
	v_mfma_f32_16x16x32_f16 v[84:87], v[168:171], v[140:143], v[84:87]
	s_waitcnt lgkmcnt(9)
	v_mfma_f32_16x16x32_f16 v[88:91], v[156:159], v[144:147], v[88:91]
	v_mfma_f32_16x16x32_f16 v[92:95], v[160:163], v[144:147], v[92:95]
	v_mfma_f32_16x16x32_f16 v[96:99], v[164:167], v[144:147], v[96:99]
	s_add_u32 m0, s28, 0xa000
	s_nop 0
	global_load_lds_dwordx4 v11, s[6:7]
	s_add_u32 s6, s6, s20
	s_addc_u32 s7, s7, 0
	v_mfma_f32_16x16x32_f16 v[100:103], v[168:171], v[144:147], v[100:103]
	s_waitcnt lgkmcnt(8)
	v_mfma_f32_16x16x32_f16 v[104:107], v[156:159], v[148:151], v[104:107]
	v_mfma_f32_16x16x32_f16 v[108:111], v[160:163], v[148:151], v[108:111]
	v_mfma_f32_16x16x32_f16 v[112:115], v[164:167], v[148:151], v[112:115]
	v_mfma_f32_16x16x32_f16 v[116:119], v[168:171], v[148:151], v[116:119]
	s_waitcnt vmcnt(6) lgkmcnt(0)
	s_barrier
	s_waitcnt lgkmcnt(7)
	ds_read_b128 v[136:139], v19
	ds_read_b128 v[156:159], v21
	ds_read_b128 v[160:163], v21 offset:2048
	ds_read_b128 v[164:167], v21 offset:4096
	ds_read_b128 v[168:171], v21 offset:6144
	ds_read_b128 v[140:143], v19 offset:2048
	ds_read_b128 v[144:147], v19 offset:4096
	ds_read_b128 v[148:151], v19 offset:6144
	s_waitcnt lgkmcnt(14)
	v_mfma_f32_16x16x32_f16 v[56:59], v[192:195], v[172:175], v[56:59]
	s_add_u32 m0, s28, 0xc000
	s_nop 0
	global_load_lds_dwordx4 v10, s[4:5]
	s_waitcnt lgkmcnt(13)
	v_mfma_f32_16x16x32_f16 v[60:63], v[196:199], v[172:175], v[60:63]
	s_waitcnt lgkmcnt(12)
	v_mfma_f32_16x16x32_f16 v[64:67], v[200:203], v[172:175], v[64:67]
	s_waitcnt lgkmcnt(11)
	v_mfma_f32_16x16x32_f16 v[68:71], v[204:207], v[172:175], v[68:71]
	s_waitcnt lgkmcnt(10)
	v_mfma_f32_16x16x32_f16 v[72:75], v[192:195], v[176:179], v[72:75]
	v_mfma_f32_16x16x32_f16 v[76:79], v[196:199], v[176:179], v[76:79]
	s_add_u32 m0, s28, 0xe000
	s_nop 0
	global_load_lds_dwordx4 v11, s[4:5]
	v_mfma_f32_16x16x32_f16 v[80:83], v[200:203], v[176:179], v[80:83]
	v_mfma_f32_16x16x32_f16 v[84:87], v[204:207], v[176:179], v[84:87]
	s_waitcnt lgkmcnt(9)
	v_mfma_f32_16x16x32_f16 v[88:91], v[192:195], v[180:183], v[88:91]
	v_mfma_f32_16x16x32_f16 v[92:95], v[196:199], v[180:183], v[92:95]
	v_mfma_f32_16x16x32_f16 v[96:99], v[200:203], v[180:183], v[96:99]
	s_add_u32 m0, s28, 0x10000
	s_nop 0
	global_load_lds_dwordx4 v12, s[4:5]
	v_mfma_f32_16x16x32_f16 v[100:103], v[204:207], v[180:183], v[100:103]
	s_waitcnt lgkmcnt(8)
	v_mfma_f32_16x16x32_f16 v[104:107], v[192:195], v[184:187], v[104:107]
	v_mfma_f32_16x16x32_f16 v[108:111], v[196:199], v[184:187], v[108:111]
	v_mfma_f32_16x16x32_f16 v[112:115], v[200:203], v[184:187], v[112:115]
	v_mfma_f32_16x16x32_f16 v[116:119], v[204:207], v[184:187], v[116:119]
	s_waitcnt lgkmcnt(7)
	ds_read_b128 v[172:175], v20
	ds_read_b128 v[192:195], v22
	ds_read_b128 v[196:199], v22 offset:2048
	ds_read_b128 v[200:203], v22 offset:4096
	ds_read_b128 v[204:207], v22 offset:6144
	ds_read_b128 v[176:179], v20 offset:2048
	ds_read_b128 v[180:183], v20 offset:4096
	ds_read_b128 v[184:187], v20 offset:6144
	s_waitcnt lgkmcnt(14)
	v_mfma_f32_16x16x32_f16 v[56:59], v[156:159], v[136:139], v[56:59]
	s_add_u32 m0, s28, 0x12000
	s_nop 0
	global_load_lds_dwordx4 v13, s[4:5]
	s_add_u32 s4, s4, s20
	s_addc_u32 s5, s5, 0
	s_waitcnt lgkmcnt(13)
	v_mfma_f32_16x16x32_f16 v[60:63], v[160:163], v[136:139], v[60:63]
	s_waitcnt lgkmcnt(12)
	v_mfma_f32_16x16x32_f16 v[64:67], v[164:167], v[136:139], v[64:67]
	s_waitcnt lgkmcnt(11)
	v_mfma_f32_16x16x32_f16 v[68:71], v[168:171], v[136:139], v[68:71]
	s_waitcnt lgkmcnt(10)
	v_mfma_f32_16x16x32_f16 v[72:75], v[156:159], v[140:143], v[72:75]
	v_mfma_f32_16x16x32_f16 v[76:79], v[160:163], v[140:143], v[76:79]
	s_add_u32 m0, s28, 0x14000
	s_nop 0
	global_load_lds_dwordx4 v10, s[6:7]
	v_mfma_f32_16x16x32_f16 v[80:83], v[164:167], v[140:143], v[80:83]
	v_mfma_f32_16x16x32_f16 v[84:87], v[168:171], v[140:143], v[84:87]
	s_waitcnt lgkmcnt(9)
	v_mfma_f32_16x16x32_f16 v[88:91], v[156:159], v[144:147], v[88:91]
	v_mfma_f32_16x16x32_f16 v[92:95], v[160:163], v[144:147], v[92:95]
	v_mfma_f32_16x16x32_f16 v[96:99], v[164:167], v[144:147], v[96:99]
	s_add_u32 m0, s28, 0x16000
	s_nop 0
	global_load_lds_dwordx4 v11, s[6:7]
	s_add_u32 s6, s6, s20
	s_addc_u32 s7, s7, 0
	v_mfma_f32_16x16x32_f16 v[100:103], v[168:171], v[144:147], v[100:103]
	s_waitcnt lgkmcnt(8)
	v_mfma_f32_16x16x32_f16 v[104:107], v[156:159], v[148:151], v[104:107]
	v_mfma_f32_16x16x32_f16 v[108:111], v[160:163], v[148:151], v[108:111]
	v_mfma_f32_16x16x32_f16 v[112:115], v[164:167], v[148:151], v[112:115]
	v_mfma_f32_16x16x32_f16 v[116:119], v[168:171], v[148:151], v[116:119]
	s_waitcnt vmcnt(6) lgkmcnt(0)
	s_barrier
	s_waitcnt lgkmcnt(7)
	ds_read_b128 v[136:139], v15
	ds_read_b128 v[156:159], v17
	ds_read_b128 v[160:163], v17 offset:2048
	ds_read_b128 v[164:167], v17 offset:4096
	ds_read_b128 v[168:171], v17 offset:6144
	ds_read_b128 v[140:143], v15 offset:2048
	ds_read_b128 v[144:147], v15 offset:4096
	ds_read_b128 v[148:151], v15 offset:6144
	s_waitcnt lgkmcnt(14)
	v_mfma_f32_16x16x32_f16 v[56:59], v[192:195], v[172:175], v[56:59]
	s_add_u32 m0, s28, 0x18000
	s_nop 0
	global_load_lds_dwordx4 v10, s[4:5]
	s_waitcnt lgkmcnt(13)
	v_mfma_f32_16x16x32_f16 v[60:63], v[196:199], v[172:175], v[60:63]
	s_waitcnt lgkmcnt(12)
	v_mfma_f32_16x16x32_f16 v[64:67], v[200:203], v[172:175], v[64:67]
	s_waitcnt lgkmcnt(11)
	v_mfma_f32_16x16x32_f16 v[68:71], v[204:207], v[172:175], v[68:71]
	s_waitcnt lgkmcnt(10)
	v_mfma_f32_16x16x32_f16 v[72:75], v[192:195], v[176:179], v[72:75]
	v_mfma_f32_16x16x32_f16 v[76:79], v[196:199], v[176:179], v[76:79]
	s_add_u32 m0, s28, 0x1a000
	s_nop 0
	global_load_lds_dwordx4 v11, s[4:5]
	v_mfma_f32_16x16x32_f16 v[80:83], v[200:203], v[176:179], v[80:83]
	v_mfma_f32_16x16x32_f16 v[84:87], v[204:207], v[176:179], v[84:87]
	s_waitcnt lgkmcnt(9)
	v_mfma_f32_16x16x32_f16 v[88:91], v[192:195], v[180:183], v[88:91]
	v_mfma_f32_16x16x32_f16 v[92:95], v[196:199], v[180:183], v[92:95]
	v_mfma_f32_16x16x32_f16 v[96:99], v[200:203], v[180:183], v[96:99]
	s_add_u32 m0, s28, 0x1c000
	s_nop 0
	global_load_lds_dwordx4 v12, s[4:5]
	v_mfma_f32_16x16x32_f16 v[100:103], v[204:207], v[180:183], v[100:103]
	s_waitcnt lgkmcnt(8)
	v_mfma_f32_16x16x32_f16 v[104:107], v[192:195], v[184:187], v[104:107]
	v_mfma_f32_16x16x32_f16 v[108:111], v[196:199], v[184:187], v[108:111]
	v_mfma_f32_16x16x32_f16 v[112:115], v[200:203], v[184:187], v[112:115]
	v_mfma_f32_16x16x32_f16 v[116:119], v[204:207], v[184:187], v[116:119]
	s_waitcnt lgkmcnt(7)
	ds_read_b128 v[172:175], v16
	ds_read_b128 v[192:195], v18
	ds_read_b128 v[196:199], v18 offset:2048
	ds_read_b128 v[200:203], v18 offset:4096
	ds_read_b128 v[204:207], v18 offset:6144
	ds_read_b128 v[176:179], v16 offset:2048
	ds_read_b128 v[180:183], v16 offset:4096
	ds_read_b128 v[184:187], v16 offset:6144
	s_waitcnt lgkmcnt(14)
	v_mfma_f32_16x16x32_f16 v[56:59], v[156:159], v[136:139], v[56:59]
	s_add_u32 m0, s28, 0x1e000
	s_nop 0
	global_load_lds_dwordx4 v13, s[4:5]
	s_add_u32 s4, s4, s20
	s_addc_u32 s5, s5, 0
	s_waitcnt lgkmcnt(13)
	v_mfma_f32_16x16x32_f16 v[60:63], v[160:163], v[136:139], v[60:63]
	s_waitcnt lgkmcnt(12)
	v_mfma_f32_16x16x32_f16 v[64:67], v[164:167], v[136:139], v[64:67]
	s_waitcnt lgkmcnt(11)
	v_mfma_f32_16x16x32_f16 v[68:71], v[168:171], v[136:139], v[68:71]
	s_waitcnt lgkmcnt(10)
	v_mfma_f32_16x16x32_f16 v[72:75], v[156:159], v[140:143], v[72:75]
	v_mfma_f32_16x16x32_f16 v[76:79], v[160:163], v[140:143], v[76:79]
	s_add_u32 m0, s28, 0x20000
	s_nop 0
	global_load_lds_dwordx4 v10, s[6:7]
	v_mfma_f32_16x16x32_f16 v[80:83], v[164:167], v[140:143], v[80:83]
	v_mfma_f32_16x16x32_f16 v[84:87], v[168:171], v[140:143], v[84:87]
	s_waitcnt lgkmcnt(9)
	v_mfma_f32_16x16x32_f16 v[88:91], v[156:159], v[144:147], v[88:91]
	v_mfma_f32_16x16x32_f16 v[92:95], v[160:163], v[144:147], v[92:95]
	v_mfma_f32_16x16x32_f16 v[96:99], v[164:167], v[144:147], v[96:99]
	s_add_u32 m0, s28, 0x22000
	s_nop 0
	global_load_lds_dwordx4 v11, s[6:7]
	s_add_u32 s6, s6, s20
	s_addc_u32 s7, s7, 0
	v_mfma_f32_16x16x32_f16 v[100:103], v[168:171], v[144:147], v[100:103]
	s_waitcnt lgkmcnt(8)
	v_mfma_f32_16x16x32_f16 v[104:107], v[156:159], v[148:151], v[104:107]
	v_mfma_f32_16x16x32_f16 v[108:111], v[160:163], v[148:151], v[108:111]
	v_mfma_f32_16x16x32_f16 v[112:115], v[164:167], v[148:151], v[112:115]
	v_mfma_f32_16x16x32_f16 v[116:119], v[168:171], v[148:151], v[116:119]
	s_waitcnt vmcnt(6) lgkmcnt(0)
	s_barrier
	s_waitcnt lgkmcnt(7)
	ds_read_b128 v[136:139], v15 offset:49152
	ds_read_b128 v[156:159], v17 offset:49152
	ds_read_b128 v[160:163], v17 offset:51200
	ds_read_b128 v[164:167], v17 offset:53248
	ds_read_b128 v[168:171], v17 offset:55296
	ds_read_b128 v[140:143], v15 offset:51200
	ds_read_b128 v[144:147], v15 offset:53248
	ds_read_b128 v[148:151], v15 offset:55296
	s_waitcnt lgkmcnt(14)
	v_mfma_f32_16x16x32_f16 v[56:59], v[192:195], v[172:175], v[56:59]
	s_add_u32 m0, s28, 0x0
	s_nop 0
	global_load_lds_dwordx4 v10, s[4:5]
	s_waitcnt lgkmcnt(13)
	v_mfma_f32_16x16x32_f16 v[60:63], v[196:199], v[172:175], v[60:63]
	s_waitcnt lgkmcnt(12)
	v_mfma_f32_16x16x32_f16 v[64:67], v[200:203], v[172:175], v[64:67]
	s_waitcnt lgkmcnt(11)
	v_mfma_f32_16x16x32_f16 v[68:71], v[204:207], v[172:175], v[68:71]
	s_waitcnt lgkmcnt(10)
	v_mfma_f32_16x16x32_f16 v[72:75], v[192:195], v[176:179], v[72:75]
	v_mfma_f32_16x16x32_f16 v[76:79], v[196:199], v[176:179], v[76:79]
	s_add_u32 m0, s28, 0x2000
	s_nop 0
	global_load_lds_dwordx4 v11, s[4:5]
	v_mfma_f32_16x16x32_f16 v[80:83], v[200:203], v[176:179], v[80:83]
	v_mfma_f32_16x16x32_f16 v[84:87], v[204:207], v[176:179], v[84:87]
	s_waitcnt lgkmcnt(9)
	v_mfma_f32_16x16x32_f16 v[88:91], v[192:195], v[180:183], v[88:91]
	v_mfma_f32_16x16x32_f16 v[92:95], v[196:199], v[180:183], v[92:95]
	v_mfma_f32_16x16x32_f16 v[96:99], v[200:203], v[180:183], v[96:99]
	s_add_u32 m0, s28, 0x4000
	s_nop 0
	global_load_lds_dwordx4 v12, s[4:5]
	v_mfma_f32_16x16x32_f16 v[100:103], v[204:207], v[180:183], v[100:103]
	s_waitcnt lgkmcnt(8)
	v_mfma_f32_16x16x32_f16 v[104:107], v[192:195], v[184:187], v[104:107]
	v_mfma_f32_16x16x32_f16 v[108:111], v[196:199], v[184:187], v[108:111]
	v_mfma_f32_16x16x32_f16 v[112:115], v[200:203], v[184:187], v[112:115]
	v_mfma_f32_16x16x32_f16 v[116:119], v[204:207], v[184:187], v[116:119]
	s_waitcnt lgkmcnt(7)
	ds_read_b128 v[172:175], v16 offset:49152
	ds_read_b128 v[192:195], v18 offset:49152
	ds_read_b128 v[196:199], v18 offset:51200
	ds_read_b128 v[200:203], v18 offset:53248
	ds_read_b128 v[204:207], v18 offset:55296
	ds_read_b128 v[176:179], v16 offset:51200
	ds_read_b128 v[180:183], v16 offset:53248
	ds_read_b128 v[184:187], v16 offset:55296
	s_waitcnt lgkmcnt(14)
	v_mfma_f32_16x16x32_f16 v[56:59], v[156:159], v[136:139], v[56:59]
	s_add_u32 m0, s28, 0x6000
	s_nop 0
	global_load_lds_dwordx4 v13, s[4:5]
	s_add_u32 s4, s4, s20
	s_addc_u32 s5, s5, 0
	s_waitcnt lgkmcnt(13)
	v_mfma_f32_16x16x32_f16 v[60:63], v[160:163], v[136:139], v[60:63]
	s_waitcnt lgkmcnt(12)
	v_mfma_f32_16x16x32_f16 v[64:67], v[164:167], v[136:139], v[64:67]
	s_waitcnt lgkmcnt(11)
	v_mfma_f32_16x16x32_f16 v[68:71], v[168:171], v[136:139], v[68:71]
	s_waitcnt lgkmcnt(10)
	v_mfma_f32_16x16x32_f16 v[72:75], v[156:159], v[140:143], v[72:75]
	v_mfma_f32_16x16x32_f16 v[76:79], v[160:163], v[140:143], v[76:79]
	s_add_u32 m0, s28, 0x8000
	s_nop 0
	global_load_lds_dwordx4 v10, s[6:7]
	v_mfma_f32_16x16x32_f16 v[80:83], v[164:167], v[140:143], v[80:83]
	v_mfma_f32_16x16x32_f16 v[84:87], v[168:171], v[140:143], v[84:87]
	s_waitcnt lgkmcnt(9)
	v_mfma_f32_16x16x32_f16 v[88:91], v[156:159], v[144:147], v[88:91]
	v_mfma_f32_16x16x32_f16 v[92:95], v[160:163], v[144:147], v[92:95]
	v_mfma_f32_16x16x32_f16 v[96:99], v[164:167], v[144:147], v[96:99]
	s_add_u32 m0, s28, 0xa000
	s_nop 0
	global_load_lds_dwordx4 v11, s[6:7]
	s_add_u32 s6, s6, s20
	s_addc_u32 s7, s7, 0
	v_mfma_f32_16x16x32_f16 v[100:103], v[168:171], v[144:147], v[100:103]
	s_waitcnt lgkmcnt(8)
	v_mfma_f32_16x16x32_f16 v[104:107], v[156:159], v[148:151], v[104:107]
	v_mfma_f32_16x16x32_f16 v[108:111], v[160:163], v[148:151], v[108:111]
	v_mfma_f32_16x16x32_f16 v[112:115], v[164:167], v[148:151], v[112:115]
	v_mfma_f32_16x16x32_f16 v[116:119], v[168:171], v[148:151], v[116:119]
	s_waitcnt vmcnt(6) lgkmcnt(0)
	s_barrier
	s_waitcnt lgkmcnt(7)
	ds_read_b128 v[136:139], v19
	ds_read_b128 v[156:159], v21
	ds_read_b128 v[160:163], v21 offset:2048
	ds_read_b128 v[164:167], v21 offset:4096
	ds_read_b128 v[168:171], v21 offset:6144
	ds_read_b128 v[140:143], v19 offset:2048
	ds_read_b128 v[144:147], v19 offset:4096
	ds_read_b128 v[148:151], v19 offset:6144
	s_waitcnt lgkmcnt(14)
	v_mfma_f32_16x16x32_f16 v[56:59], v[192:195], v[172:175], v[56:59]
	s_add_u32 m0, s28, 0xc000
	s_nop 0
	global_load_lds_dwordx4 v10, s[4:5]
	s_waitcnt lgkmcnt(13)
	v_mfma_f32_16x16x32_f16 v[60:63], v[196:199], v[172:175], v[60:63]
	s_waitcnt lgkmcnt(12)
	v_mfma_f32_16x16x32_f16 v[64:67], v[200:203], v[172:175], v[64:67]
	s_waitcnt lgkmcnt(11)
	v_mfma_f32_16x16x32_f16 v[68:71], v[204:207], v[172:175], v[68:71]
	s_waitcnt lgkmcnt(10)
	v_mfma_f32_16x16x32_f16 v[72:75], v[192:195], v[176:179], v[72:75]
	v_mfma_f32_16x16x32_f16 v[76:79], v[196:199], v[176:179], v[76:79]
	s_add_u32 m0, s28, 0xe000
	s_nop 0
	global_load_lds_dwordx4 v11, s[4:5]
	v_mfma_f32_16x16x32_f16 v[80:83], v[200:203], v[176:179], v[80:83]
	v_mfma_f32_16x16x32_f16 v[84:87], v[204:207], v[176:179], v[84:87]
	s_waitcnt lgkmcnt(9)
	v_mfma_f32_16x16x32_f16 v[88:91], v[192:195], v[180:183], v[88:91]
	v_mfma_f32_16x16x32_f16 v[92:95], v[196:199], v[180:183], v[92:95]
	v_mfma_f32_16x16x32_f16 v[96:99], v[200:203], v[180:183], v[96:99]
	s_add_u32 m0, s28, 0x10000
	s_nop 0
	global_load_lds_dwordx4 v12, s[4:5]
	v_mfma_f32_16x16x32_f16 v[100:103], v[204:207], v[180:183], v[100:103]
	s_waitcnt lgkmcnt(8)
	v_mfma_f32_16x16x32_f16 v[104:107], v[192:195], v[184:187], v[104:107]
	v_mfma_f32_16x16x32_f16 v[108:111], v[196:199], v[184:187], v[108:111]
	v_mfma_f32_16x16x32_f16 v[112:115], v[200:203], v[184:187], v[112:115]
	v_mfma_f32_16x16x32_f16 v[116:119], v[204:207], v[184:187], v[116:119]
	s_waitcnt lgkmcnt(7)
	ds_read_b128 v[172:175], v20
	ds_read_b128 v[192:195], v22
	ds_read_b128 v[196:199], v22 offset:2048
	ds_read_b128 v[200:203], v22 offset:4096
	ds_read_b128 v[204:207], v22 offset:6144
	ds_read_b128 v[176:179], v20 offset:2048
	ds_read_b128 v[180:183], v20 offset:4096
	ds_read_b128 v[184:187], v20 offset:6144
	s_waitcnt lgkmcnt(14)
	v_mfma_f32_16x16x32_f16 v[56:59], v[156:159], v[136:139], v[56:59]
	s_add_u32 m0, s28, 0x12000
	s_nop 0
	global_load_lds_dwordx4 v13, s[4:5]
	s_add_u32 s4, s4, s20
	s_addc_u32 s5, s5, 0
	s_waitcnt lgkmcnt(13)
	v_mfma_f32_16x16x32_f16 v[60:63], v[160:163], v[136:139], v[60:63]
	s_waitcnt lgkmcnt(12)
	v_mfma_f32_16x16x32_f16 v[64:67], v[164:167], v[136:139], v[64:67]
	s_waitcnt lgkmcnt(11)
	v_mfma_f32_16x16x32_f16 v[68:71], v[168:171], v[136:139], v[68:71]
	s_waitcnt lgkmcnt(10)
	v_mfma_f32_16x16x32_f16 v[72:75], v[156:159], v[140:143], v[72:75]
	v_mfma_f32_16x16x32_f16 v[76:79], v[160:163], v[140:143], v[76:79]
	s_add_u32 m0, s28, 0x14000
	s_nop 0
	global_load_lds_dwordx4 v10, s[6:7]
	v_mfma_f32_16x16x32_f16 v[80:83], v[164:167], v[140:143], v[80:83]
	v_mfma_f32_16x16x32_f16 v[84:87], v[168:171], v[140:143], v[84:87]
	s_waitcnt lgkmcnt(9)
	v_mfma_f32_16x16x32_f16 v[88:91], v[156:159], v[144:147], v[88:91]
	v_mfma_f32_16x16x32_f16 v[92:95], v[160:163], v[144:147], v[92:95]
	v_mfma_f32_16x16x32_f16 v[96:99], v[164:167], v[144:147], v[96:99]
	s_add_u32 m0, s28, 0x16000
	s_nop 0
	global_load_lds_dwordx4 v11, s[6:7]
	s_add_u32 s6, s6, s20
	s_addc_u32 s7, s7, 0
	v_mfma_f32_16x16x32_f16 v[100:103], v[168:171], v[144:147], v[100:103]
	s_waitcnt lgkmcnt(8)
	v_mfma_f32_16x16x32_f16 v[104:107], v[156:159], v[148:151], v[104:107]
	v_mfma_f32_16x16x32_f16 v[108:111], v[160:163], v[148:151], v[108:111]
	v_mfma_f32_16x16x32_f16 v[112:115], v[164:167], v[148:151], v[112:115]
	v_mfma_f32_16x16x32_f16 v[116:119], v[168:171], v[148:151], v[116:119]
	s_waitcnt vmcnt(6) lgkmcnt(0)
	s_barrier
	s_waitcnt lgkmcnt(7)
	ds_read_b128 v[136:139], v15
	ds_read_b128 v[156:159], v17
	ds_read_b128 v[160:163], v17 offset:2048
	ds_read_b128 v[164:167], v17 offset:4096
	ds_read_b128 v[168:171], v17 offset:6144
	ds_read_b128 v[140:143], v15 offset:2048
	ds_read_b128 v[144:147], v15 offset:4096
	ds_read_b128 v[148:151], v15 offset:6144
	s_waitcnt lgkmcnt(14)
	v_mfma_f32_16x16x32_f16 v[56:59], v[192:195], v[172:175], v[56:59]
	s_add_u32 m0, s28, 0x18000
	s_nop 0
	global_load_lds_dwordx4 v10, s[4:5]
	s_waitcnt lgkmcnt(13)
	v_mfma_f32_16x16x32_f16 v[60:63], v[196:199], v[172:175], v[60:63]
	s_waitcnt lgkmcnt(12)
	v_mfma_f32_16x16x32_f16 v[64:67], v[200:203], v[172:175], v[64:67]
	s_waitcnt lgkmcnt(11)
	v_mfma_f32_16x16x32_f16 v[68:71], v[204:207], v[172:175], v[68:71]
	s_waitcnt lgkmcnt(10)
	v_mfma_f32_16x16x32_f16 v[72:75], v[192:195], v[176:179], v[72:75]
	v_mfma_f32_16x16x32_f16 v[76:79], v[196:199], v[176:179], v[76:79]
	s_add_u32 m0, s28, 0x1a000
	s_nop 0
	global_load_lds_dwordx4 v11, s[4:5]
	v_mfma_f32_16x16x32_f16 v[80:83], v[200:203], v[176:179], v[80:83]
	v_mfma_f32_16x16x32_f16 v[84:87], v[204:207], v[176:179], v[84:87]
	s_waitcnt lgkmcnt(9)
	v_mfma_f32_16x16x32_f16 v[88:91], v[192:195], v[180:183], v[88:91]
	v_mfma_f32_16x16x32_f16 v[92:95], v[196:199], v[180:183], v[92:95]
	v_mfma_f32_16x16x32_f16 v[96:99], v[200:203], v[180:183], v[96:99]
	s_add_u32 m0, s28, 0x1c000
	s_nop 0
	global_load_lds_dwordx4 v12, s[4:5]
	v_mfma_f32_16x16x32_f16 v[100:103], v[204:207], v[180:183], v[100:103]
	s_waitcnt lgkmcnt(8)
	v_mfma_f32_16x16x32_f16 v[104:107], v[192:195], v[184:187], v[104:107]
	v_mfma_f32_16x16x32_f16 v[108:111], v[196:199], v[184:187], v[108:111]
	v_mfma_f32_16x16x32_f16 v[112:115], v[200:203], v[184:187], v[112:115]
	v_mfma_f32_16x16x32_f16 v[116:119], v[204:207], v[184:187], v[116:119]
	s_waitcnt lgkmcnt(7)
	ds_read_b128 v[172:175], v16
	ds_read_b128 v[192:195], v18
	ds_read_b128 v[196:199], v18 offset:2048
	ds_read_b128 v[200:203], v18 offset:4096
	ds_read_b128 v[204:207], v18 offset:6144
	ds_read_b128 v[176:179], v16 offset:2048
	ds_read_b128 v[180:183], v16 offset:4096
	ds_read_b128 v[184:187], v16 offset:6144
	s_waitcnt lgkmcnt(14)
	v_mfma_f32_16x16x32_f16 v[56:59], v[156:159], v[136:139], v[56:59]
	s_add_u32 m0, s28, 0x1e000
	s_nop 0
	global_load_lds_dwordx4 v13, s[4:5]
	s_add_u32 s4, s4, s20
	s_addc_u32 s5, s5, 0
	s_waitcnt lgkmcnt(13)
	v_mfma_f32_16x16x32_f16 v[60:63], v[160:163], v[136:139], v[60:63]
	s_waitcnt lgkmcnt(12)
	v_mfma_f32_16x16x32_f16 v[64:67], v[164:167], v[136:139], v[64:67]
	s_waitcnt lgkmcnt(11)
	v_mfma_f32_16x16x32_f16 v[68:71], v[168:171], v[136:139], v[68:71]
	s_waitcnt lgkmcnt(10)
	v_mfma_f32_16x16x32_f16 v[72:75], v[156:159], v[140:143], v[72:75]
	v_mfma_f32_16x16x32_f16 v[76:79], v[160:163], v[140:143], v[76:79]
	s_add_u32 m0, s28, 0x20000
	s_nop 0
	global_load_lds_dwordx4 v10, s[6:7]
	v_mfma_f32_16x16x32_f16 v[80:83], v[164:167], v[140:143], v[80:83]
	v_mfma_f32_16x16x32_f16 v[84:87], v[168:171], v[140:143], v[84:87]
	s_waitcnt lgkmcnt(9)
	v_mfma_f32_16x16x32_f16 v[88:91], v[156:159], v[144:147], v[88:91]
	v_mfma_f32_16x16x32_f16 v[92:95], v[160:163], v[144:147], v[92:95]
	v_mfma_f32_16x16x32_f16 v[96:99], v[164:167], v[144:147], v[96:99]
	s_add_u32 m0, s28, 0x22000
	s_nop 0
	global_load_lds_dwordx4 v11, s[6:7]
	s_add_u32 s6, s6, s20
	s_addc_u32 s7, s7, 0
	v_mfma_f32_16x16x32_f16 v[100:103], v[168:171], v[144:147], v[100:103]
	s_waitcnt lgkmcnt(8)
	v_mfma_f32_16x16x32_f16 v[104:107], v[156:159], v[148:151], v[104:107]
	v_mfma_f32_16x16x32_f16 v[108:111], v[160:163], v[148:151], v[108:111]
	v_mfma_f32_16x16x32_f16 v[112:115], v[164:167], v[148:151], v[112:115]
	v_mfma_f32_16x16x32_f16 v[116:119], v[168:171], v[148:151], v[116:119]
	s_waitcnt vmcnt(6) lgkmcnt(0)
	s_barrier
	s_waitcnt lgkmcnt(7)
	ds_read_b128 v[136:139], v15 offset:49152
	ds_read_b128 v[156:159], v17 offset:49152
	ds_read_b128 v[160:163], v17 offset:51200
	ds_read_b128 v[164:167], v17 offset:53248
	ds_read_b128 v[168:171], v17 offset:55296
	ds_read_b128 v[140:143], v15 offset:51200
	ds_read_b128 v[144:147], v15 offset:53248
	ds_read_b128 v[148:151], v15 offset:55296
	s_waitcnt lgkmcnt(14)
	v_mfma_f32_16x16x32_f16 v[56:59], v[192:195], v[172:175], v[56:59]
	s_add_u32 m0, s28, 0x0
	s_nop 0
	global_load_lds_dwordx4 v10, s[4:5]
	s_waitcnt lgkmcnt(13)
	v_mfma_f32_16x16x32_f16 v[60:63], v[196:199], v[172:175], v[60:63]
	s_waitcnt lgkmcnt(12)
	v_mfma_f32_16x16x32_f16 v[64:67], v[200:203], v[172:175], v[64:67]
	s_waitcnt lgkmcnt(11)
	v_mfma_f32_16x16x32_f16 v[68:71], v[204:207], v[172:175], v[68:71]
	s_waitcnt lgkmcnt(10)
	v_mfma_f32_16x16x32_f16 v[72:75], v[192:195], v[176:179], v[72:75]
	v_mfma_f32_16x16x32_f16 v[76:79], v[196:199], v[176:179], v[76:79]
	s_add_u32 m0, s28, 0x2000
	s_nop 0
	global_load_lds_dwordx4 v11, s[4:5]
	v_mfma_f32_16x16x32_f16 v[80:83], v[200:203], v[176:179], v[80:83]
	v_mfma_f32_16x16x32_f16 v[84:87], v[204:207], v[176:179], v[84:87]
	s_waitcnt lgkmcnt(9)
	v_mfma_f32_16x16x32_f16 v[88:91], v[192:195], v[180:183], v[88:91]
	v_mfma_f32_16x16x32_f16 v[92:95], v[196:199], v[180:183], v[92:95]
	v_mfma_f32_16x16x32_f16 v[96:99], v[200:203], v[180:183], v[96:99]
	s_add_u32 m0, s28, 0x4000
	s_nop 0
	global_load_lds_dwordx4 v12, s[4:5]
	v_mfma_f32_16x16x32_f16 v[100:103], v[204:207], v[180:183], v[100:103]
	s_waitcnt lgkmcnt(8)
	v_mfma_f32_16x16x32_f16 v[104:107], v[192:195], v[184:187], v[104:107]
	v_mfma_f32_16x16x32_f16 v[108:111], v[196:199], v[184:187], v[108:111]
	v_mfma_f32_16x16x32_f16 v[112:115], v[200:203], v[184:187], v[112:115]
	v_mfma_f32_16x16x32_f16 v[116:119], v[204:207], v[184:187], v[116:119]
	s_waitcnt lgkmcnt(7)
	ds_read_b128 v[172:175], v16 offset:49152
	ds_read_b128 v[192:195], v18 offset:49152
	ds_read_b128 v[196:199], v18 offset:51200
	ds_read_b128 v[200:203], v18 offset:53248
	ds_read_b128 v[204:207], v18 offset:55296
	ds_read_b128 v[176:179], v16 offset:51200
	ds_read_b128 v[180:183], v16 offset:53248
	ds_read_b128 v[184:187], v16 offset:55296
	s_waitcnt lgkmcnt(14)
	v_mfma_f32_16x16x32_f16 v[56:59], v[156:159], v[136:139], v[56:59]
	s_add_u32 m0, s28, 0x6000
	s_nop 0
	global_load_lds_dwordx4 v13, s[4:5]
	s_add_u32 s4, s4, s20
	s_addc_u32 s5, s5, 0
	s_waitcnt lgkmcnt(13)
	v_mfma_f32_16x16x32_f16 v[60:63], v[160:163], v[136:139], v[60:63]
	s_waitcnt lgkmcnt(12)
	v_mfma_f32_16x16x32_f16 v[64:67], v[164:167], v[136:139], v[64:67]
	s_waitcnt lgkmcnt(11)
	v_mfma_f32_16x16x32_f16 v[68:71], v[168:171], v[136:139], v[68:71]
	s_waitcnt lgkmcnt(10)
	v_mfma_f32_16x16x32_f16 v[72:75], v[156:159], v[140:143], v[72:75]
	v_mfma_f32_16x16x32_f16 v[76:79], v[160:163], v[140:143], v[76:79]
	s_add_u32 m0, s28, 0x8000
	s_nop 0
	global_load_lds_dwordx4 v10, s[6:7]
	v_mfma_f32_16x16x32_f16 v[80:83], v[164:167], v[140:143], v[80:83]
	v_mfma_f32_16x16x32_f16 v[84:87], v[168:171], v[140:143], v[84:87]
	s_waitcnt lgkmcnt(9)
	v_mfma_f32_16x16x32_f16 v[88:91], v[156:159], v[144:147], v[88:91]
	v_mfma_f32_16x16x32_f16 v[92:95], v[160:163], v[144:147], v[92:95]
	v_mfma_f32_16x16x32_f16 v[96:99], v[164:167], v[144:147], v[96:99]
	s_add_u32 m0, s28, 0xa000
	s_nop 0
	global_load_lds_dwordx4 v11, s[6:7]
	s_add_u32 s6, s6, s20
	s_addc_u32 s7, s7, 0
	v_mfma_f32_16x16x32_f16 v[100:103], v[168:171], v[144:147], v[100:103]
	s_waitcnt lgkmcnt(8)
	v_mfma_f32_16x16x32_f16 v[104:107], v[156:159], v[148:151], v[104:107]
	v_mfma_f32_16x16x32_f16 v[108:111], v[160:163], v[148:151], v[108:111]
	v_mfma_f32_16x16x32_f16 v[112:115], v[164:167], v[148:151], v[112:115]
	v_mfma_f32_16x16x32_f16 v[116:119], v[168:171], v[148:151], v[116:119]
	s_waitcnt vmcnt(6) lgkmcnt(0)
	s_barrier
	s_waitcnt lgkmcnt(7)
	ds_read_b128 v[136:139], v19
	ds_read_b128 v[156:159], v21
	ds_read_b128 v[160:163], v21 offset:2048
	ds_read_b128 v[164:167], v21 offset:4096
	ds_read_b128 v[168:171], v21 offset:6144
	ds_read_b128 v[140:143], v19 offset:2048
	ds_read_b128 v[144:147], v19 offset:4096
	ds_read_b128 v[148:151], v19 offset:6144
	s_waitcnt lgkmcnt(14)
	v_mfma_f32_16x16x32_f16 v[56:59], v[192:195], v[172:175], v[56:59]
	s_add_u32 m0, s28, 0xc000
	s_nop 0
	global_load_lds_dwordx4 v10, s[4:5]
	s_waitcnt lgkmcnt(13)
	v_mfma_f32_16x16x32_f16 v[60:63], v[196:199], v[172:175], v[60:63]
	s_waitcnt lgkmcnt(12)
	v_mfma_f32_16x16x32_f16 v[64:67], v[200:203], v[172:175], v[64:67]
	s_waitcnt lgkmcnt(11)
	v_mfma_f32_16x16x32_f16 v[68:71], v[204:207], v[172:175], v[68:71]
	s_waitcnt lgkmcnt(10)
	v_mfma_f32_16x16x32_f16 v[72:75], v[192:195], v[176:179], v[72:75]
	v_mfma_f32_16x16x32_f16 v[76:79], v[196:199], v[176:179], v[76:79]
	s_add_u32 m0, s28, 0xe000
	s_nop 0
	global_load_lds_dwordx4 v11, s[4:5]
	v_mfma_f32_16x16x32_f16 v[80:83], v[200:203], v[176:179], v[80:83]
	v_mfma_f32_16x16x32_f16 v[84:87], v[204:207], v[176:179], v[84:87]
	s_waitcnt lgkmcnt(9)
	v_mfma_f32_16x16x32_f16 v[88:91], v[192:195], v[180:183], v[88:91]
	v_mfma_f32_16x16x32_f16 v[92:95], v[196:199], v[180:183], v[92:95]
	v_mfma_f32_16x16x32_f16 v[96:99], v[200:203], v[180:183], v[96:99]
	s_add_u32 m0, s28, 0x10000
	s_nop 0
	global_load_lds_dwordx4 v12, s[4:5]
	v_mfma_f32_16x16x32_f16 v[100:103], v[204:207], v[180:183], v[100:103]
	s_waitcnt lgkmcnt(8)
	v_mfma_f32_16x16x32_f16 v[104:107], v[192:195], v[184:187], v[104:107]
	v_mfma_f32_16x16x32_f16 v[108:111], v[196:199], v[184:187], v[108:111]
	v_mfma_f32_16x16x32_f16 v[112:115], v[200:203], v[184:187], v[112:115]
	v_mfma_f32_16x16x32_f16 v[116:119], v[204:207], v[184:187], v[116:119]
	s_waitcnt lgkmcnt(7)
	ds_read_b128 v[172:175], v20
	ds_read_b128 v[192:195], v22
	ds_read_b128 v[196:199], v22 offset:2048
	ds_read_b128 v[200:203], v22 offset:4096
	ds_read_b128 v[204:207], v22 offset:6144
	ds_read_b128 v[176:179], v20 offset:2048
	ds_read_b128 v[180:183], v20 offset:4096
	ds_read_b128 v[184:187], v20 offset:6144
	s_waitcnt lgkmcnt(14)
	v_mfma_f32_16x16x32_f16 v[56:59], v[156:159], v[136:139], v[56:59]
	s_add_u32 m0, s28, 0x12000
	s_nop 0
	global_load_lds_dwordx4 v13, s[4:5]
	s_add_u32 s4, s4, s20
	s_addc_u32 s5, s5, 0
	s_waitcnt lgkmcnt(13)
	v_mfma_f32_16x16x32_f16 v[60:63], v[160:163], v[136:139], v[60:63]
	s_waitcnt lgkmcnt(12)
	v_mfma_f32_16x16x32_f16 v[64:67], v[164:167], v[136:139], v[64:67]
	s_waitcnt lgkmcnt(11)
	v_mfma_f32_16x16x32_f16 v[68:71], v[168:171], v[136:139], v[68:71]
	s_waitcnt lgkmcnt(10)
	v_mfma_f32_16x16x32_f16 v[72:75], v[156:159], v[140:143], v[72:75]
	v_mfma_f32_16x16x32_f16 v[76:79], v[160:163], v[140:143], v[76:79]
	s_add_u32 m0, s28, 0x14000
	s_nop 0
	global_load_lds_dwordx4 v10, s[6:7]
	v_mfma_f32_16x16x32_f16 v[80:83], v[164:167], v[140:143], v[80:83]
	v_mfma_f32_16x16x32_f16 v[84:87], v[168:171], v[140:143], v[84:87]
	s_waitcnt lgkmcnt(9)
	v_mfma_f32_16x16x32_f16 v[88:91], v[156:159], v[144:147], v[88:91]
	v_mfma_f32_16x16x32_f16 v[92:95], v[160:163], v[144:147], v[92:95]
	v_mfma_f32_16x16x32_f16 v[96:99], v[164:167], v[144:147], v[96:99]
	s_add_u32 m0, s28, 0x16000
	s_nop 0
	global_load_lds_dwordx4 v11, s[6:7]
	s_add_u32 s6, s6, s20
	s_addc_u32 s7, s7, 0
	v_mfma_f32_16x16x32_f16 v[100:103], v[168:171], v[144:147], v[100:103]
	s_waitcnt lgkmcnt(8)
	v_mfma_f32_16x16x32_f16 v[104:107], v[156:159], v[148:151], v[104:107]
	v_mfma_f32_16x16x32_f16 v[108:111], v[160:163], v[148:151], v[108:111]
	v_mfma_f32_16x16x32_f16 v[112:115], v[164:167], v[148:151], v[112:115]
	v_mfma_f32_16x16x32_f16 v[116:119], v[168:171], v[148:151], v[116:119]
	s_waitcnt vmcnt(6) lgkmcnt(0)
	s_barrier
	s_waitcnt lgkmcnt(7)
	ds_read_b128 v[136:139], v15
	ds_read_b128 v[156:159], v17
	ds_read_b128 v[160:163], v17 offset:2048
	ds_read_b128 v[164:167], v17 offset:4096
	ds_read_b128 v[168:171], v17 offset:6144
	ds_read_b128 v[140:143], v15 offset:2048
	ds_read_b128 v[144:147], v15 offset:4096
	ds_read_b128 v[148:151], v15 offset:6144
	s_waitcnt lgkmcnt(14)
	v_mfma_f32_16x16x32_f16 v[56:59], v[192:195], v[172:175], v[56:59]
	s_add_u32 m0, s28, 0x18000
	s_nop 0
	global_load_lds_dwordx4 v10, s[4:5]
	s_waitcnt lgkmcnt(13)
	v_mfma_f32_16x16x32_f16 v[60:63], v[196:199], v[172:175], v[60:63]
	s_waitcnt lgkmcnt(12)
	v_mfma_f32_16x16x32_f16 v[64:67], v[200:203], v[172:175], v[64:67]
	s_waitcnt lgkmcnt(11)
	v_mfma_f32_16x16x32_f16 v[68:71], v[204:207], v[172:175], v[68:71]
	s_waitcnt lgkmcnt(10)
	v_mfma_f32_16x16x32_f16 v[72:75], v[192:195], v[176:179], v[72:75]
	v_mfma_f32_16x16x32_f16 v[76:79], v[196:199], v[176:179], v[76:79]
	s_add_u32 m0, s28, 0x1a000
	s_nop 0
	global_load_lds_dwordx4 v11, s[4:5]
	v_mfma_f32_16x16x32_f16 v[80:83], v[200:203], v[176:179], v[80:83]
	v_mfma_f32_16x16x32_f16 v[84:87], v[204:207], v[176:179], v[84:87]
	s_waitcnt lgkmcnt(9)
	v_mfma_f32_16x16x32_f16 v[88:91], v[192:195], v[180:183], v[88:91]
	v_mfma_f32_16x16x32_f16 v[92:95], v[196:199], v[180:183], v[92:95]
	v_mfma_f32_16x16x32_f16 v[96:99], v[200:203], v[180:183], v[96:99]
	s_add_u32 m0, s28, 0x1c000
	s_nop 0
	global_load_lds_dwordx4 v12, s[4:5]
	v_mfma_f32_16x16x32_f16 v[100:103], v[204:207], v[180:183], v[100:103]
	s_waitcnt lgkmcnt(8)
	v_mfma_f32_16x16x32_f16 v[104:107], v[192:195], v[184:187], v[104:107]
	v_mfma_f32_16x16x32_f16 v[108:111], v[196:199], v[184:187], v[108:111]
	v_mfma_f32_16x16x32_f16 v[112:115], v[200:203], v[184:187], v[112:115]
	v_mfma_f32_16x16x32_f16 v[116:119], v[204:207], v[184:187], v[116:119]
	s_waitcnt lgkmcnt(7)
	ds_read_b128 v[172:175], v16
	ds_read_b128 v[192:195], v18
	ds_read_b128 v[196:199], v18 offset:2048
	ds_read_b128 v[200:203], v18 offset:4096
	ds_read_b128 v[204:207], v18 offset:6144
	ds_read_b128 v[176:179], v16 offset:2048
	ds_read_b128 v[180:183], v16 offset:4096
	ds_read_b128 v[184:187], v16 offset:6144
	s_waitcnt lgkmcnt(14)
	v_mfma_f32_16x16x32_f16 v[56:59], v[156:159], v[136:139], v[56:59]
	s_add_u32 m0, s28, 0x1e000
	s_nop 0
	global_load_lds_dwordx4 v13, s[4:5]
	s_add_u32 s4, s4, s20
	s_addc_u32 s5, s5, 0
	s_waitcnt lgkmcnt(13)
	v_mfma_f32_16x16x32_f16 v[60:63], v[160:163], v[136:139], v[60:63]
	s_waitcnt lgkmcnt(12)
	v_mfma_f32_16x16x32_f16 v[64:67], v[164:167], v[136:139], v[64:67]
	s_waitcnt lgkmcnt(11)
	v_mfma_f32_16x16x32_f16 v[68:71], v[168:171], v[136:139], v[68:71]
	s_waitcnt lgkmcnt(10)
	v_mfma_f32_16x16x32_f16 v[72:75], v[156:159], v[140:143], v[72:75]
	v_mfma_f32_16x16x32_f16 v[76:79], v[160:163], v[140:143], v[76:79]
	s_add_u32 m0, s28, 0x20000
	s_nop 0
	global_load_lds_dwordx4 v10, s[6:7]
	v_mfma_f32_16x16x32_f16 v[80:83], v[164:167], v[140:143], v[80:83]
	v_mfma_f32_16x16x32_f16 v[84:87], v[168:171], v[140:143], v[84:87]
	s_waitcnt lgkmcnt(9)
	v_mfma_f32_16x16x32_f16 v[88:91], v[156:159], v[144:147], v[88:91]
	v_mfma_f32_16x16x32_f16 v[92:95], v[160:163], v[144:147], v[92:95]
	v_mfma_f32_16x16x32_f16 v[96:99], v[164:167], v[144:147], v[96:99]
	s_add_u32 m0, s28, 0x22000
	s_nop 0
	global_load_lds_dwordx4 v11, s[6:7]
	s_add_u32 s6, s6, s20
	s_addc_u32 s7, s7, 0
	v_mfma_f32_16x16x32_f16 v[100:103], v[168:171], v[144:147], v[100:103]
	s_waitcnt lgkmcnt(8)
	v_mfma_f32_16x16x32_f16 v[104:107], v[156:159], v[148:151], v[104:107]
	v_mfma_f32_16x16x32_f16 v[108:111], v[160:163], v[148:151], v[108:111]
	v_mfma_f32_16x16x32_f16 v[112:115], v[164:167], v[148:151], v[112:115]
	v_mfma_f32_16x16x32_f16 v[116:119], v[168:171], v[148:151], v[116:119]
	s_waitcnt vmcnt(6) lgkmcnt(0)
	s_barrier
	s_waitcnt lgkmcnt(7)
	ds_read_b128 v[136:139], v15 offset:49152
	ds_read_b128 v[156:159], v17 offset:49152
	ds_read_b128 v[160:163], v17 offset:51200
	ds_read_b128 v[164:167], v17 offset:53248
	ds_read_b128 v[168:171], v17 offset:55296
	ds_read_b128 v[140:143], v15 offset:51200
	ds_read_b128 v[144:147], v15 offset:53248
	ds_read_b128 v[148:151], v15 offset:55296
	s_waitcnt lgkmcnt(14)
	v_mfma_f32_16x16x32_f16 v[56:59], v[192:195], v[172:175], v[56:59]
	s_add_u32 m0, s28, 0x0
	s_nop 0
	global_load_lds_dwordx4 v10, s[4:5]
	s_waitcnt lgkmcnt(13)
	v_mfma_f32_16x16x32_f16 v[60:63], v[196:199], v[172:175], v[60:63]
	s_waitcnt lgkmcnt(12)
	v_mfma_f32_16x16x32_f16 v[64:67], v[200:203], v[172:175], v[64:67]
	s_waitcnt lgkmcnt(11)
	v_mfma_f32_16x16x32_f16 v[68:71], v[204:207], v[172:175], v[68:71]
	s_waitcnt lgkmcnt(10)
	v_mfma_f32_16x16x32_f16 v[72:75], v[192:195], v[176:179], v[72:75]
	v_mfma_f32_16x16x32_f16 v[76:79], v[196:199], v[176:179], v[76:79]
	s_add_u32 m0, s28, 0x2000
	s_nop 0
	global_load_lds_dwordx4 v11, s[4:5]
	v_mfma_f32_16x16x32_f16 v[80:83], v[200:203], v[176:179], v[80:83]
	v_mfma_f32_16x16x32_f16 v[84:87], v[204:207], v[176:179], v[84:87]
	s_waitcnt lgkmcnt(9)
	v_mfma_f32_16x16x32_f16 v[88:91], v[192:195], v[180:183], v[88:91]
	v_mfma_f32_16x16x32_f16 v[92:95], v[196:199], v[180:183], v[92:95]
	v_mfma_f32_16x16x32_f16 v[96:99], v[200:203], v[180:183], v[96:99]
	s_add_u32 m0, s28, 0x4000
	s_nop 0
	global_load_lds_dwordx4 v12, s[4:5]
	v_mfma_f32_16x16x32_f16 v[100:103], v[204:207], v[180:183], v[100:103]
	s_waitcnt lgkmcnt(8)
	v_mfma_f32_16x16x32_f16 v[104:107], v[192:195], v[184:187], v[104:107]
	v_mfma_f32_16x16x32_f16 v[108:111], v[196:199], v[184:187], v[108:111]
	v_mfma_f32_16x16x32_f16 v[112:115], v[200:203], v[184:187], v[112:115]
	v_mfma_f32_16x16x32_f16 v[116:119], v[204:207], v[184:187], v[116:119]
	s_waitcnt lgkmcnt(7)
	ds_read_b128 v[172:175], v16 offset:49152
	ds_read_b128 v[192:195], v18 offset:49152
	ds_read_b128 v[196:199], v18 offset:51200
	ds_read_b128 v[200:203], v18 offset:53248
	ds_read_b128 v[204:207], v18 offset:55296
	ds_read_b128 v[176:179], v16 offset:51200
	ds_read_b128 v[180:183], v16 offset:53248
	ds_read_b128 v[184:187], v16 offset:55296
	s_waitcnt lgkmcnt(14)
	v_mfma_f32_16x16x32_f16 v[56:59], v[156:159], v[136:139], v[56:59]
	s_add_u32 m0, s28, 0x6000
	s_nop 0
	global_load_lds_dwordx4 v13, s[4:5]
	s_add_u32 s4, s4, s20
	s_addc_u32 s5, s5, 0
	s_waitcnt lgkmcnt(13)
	v_mfma_f32_16x16x32_f16 v[60:63], v[160:163], v[136:139], v[60:63]
	s_waitcnt lgkmcnt(12)
	v_mfma_f32_16x16x32_f16 v[64:67], v[164:167], v[136:139], v[64:67]
	s_waitcnt lgkmcnt(11)
	v_mfma_f32_16x16x32_f16 v[68:71], v[168:171], v[136:139], v[68:71]
	s_waitcnt lgkmcnt(10)
	v_mfma_f32_16x16x32_f16 v[72:75], v[156:159], v[140:143], v[72:75]
	v_mfma_f32_16x16x32_f16 v[76:79], v[160:163], v[140:143], v[76:79]
	s_add_u32 m0, s28, 0x8000
	s_nop 0
	global_load_lds_dwordx4 v10, s[6:7]
	v_mfma_f32_16x16x32_f16 v[80:83], v[164:167], v[140:143], v[80:83]
	v_mfma_f32_16x16x32_f16 v[84:87], v[168:171], v[140:143], v[84:87]
	s_waitcnt lgkmcnt(9)
	v_mfma_f32_16x16x32_f16 v[88:91], v[156:159], v[144:147], v[88:91]
	v_mfma_f32_16x16x32_f16 v[92:95], v[160:163], v[144:147], v[92:95]
	v_mfma_f32_16x16x32_f16 v[96:99], v[164:167], v[144:147], v[96:99]
	s_add_u32 m0, s28, 0xa000
	s_nop 0
	global_load_lds_dwordx4 v11, s[6:7]
	s_add_u32 s6, s6, s20
	s_addc_u32 s7, s7, 0
	v_mfma_f32_16x16x32_f16 v[100:103], v[168:171], v[144:147], v[100:103]
	s_waitcnt lgkmcnt(8)
	v_mfma_f32_16x16x32_f16 v[104:107], v[156:159], v[148:151], v[104:107]
	v_mfma_f32_16x16x32_f16 v[108:111], v[160:163], v[148:151], v[108:111]
	v_mfma_f32_16x16x32_f16 v[112:115], v[164:167], v[148:151], v[112:115]
	v_mfma_f32_16x16x32_f16 v[116:119], v[168:171], v[148:151], v[116:119]
	s_waitcnt vmcnt(6) lgkmcnt(0)
	s_barrier
	s_waitcnt lgkmcnt(7)
	ds_read_b128 v[136:139], v19
	ds_read_b128 v[156:159], v21
	ds_read_b128 v[160:163], v21 offset:2048
	ds_read_b128 v[164:167], v21 offset:4096
	ds_read_b128 v[168:171], v21 offset:6144
	ds_read_b128 v[140:143], v19 offset:2048
	ds_read_b128 v[144:147], v19 offset:4096
	ds_read_b128 v[148:151], v19 offset:6144
	s_waitcnt lgkmcnt(14)
	v_mfma_f32_16x16x32_f16 v[56:59], v[192:195], v[172:175], v[56:59]
	s_add_u32 m0, s28, 0xc000
	s_nop 0
	global_load_lds_dwordx4 v10, s[4:5]
	s_waitcnt lgkmcnt(13)
	v_mfma_f32_16x16x32_f16 v[60:63], v[196:199], v[172:175], v[60:63]
	s_waitcnt lgkmcnt(12)
	v_mfma_f32_16x16x32_f16 v[64:67], v[200:203], v[172:175], v[64:67]
	s_waitcnt lgkmcnt(11)
	v_mfma_f32_16x16x32_f16 v[68:71], v[204:207], v[172:175], v[68:71]
	s_waitcnt lgkmcnt(10)
	v_mfma_f32_16x16x32_f16 v[72:75], v[192:195], v[176:179], v[72:75]
	v_mfma_f32_16x16x32_f16 v[76:79], v[196:199], v[176:179], v[76:79]
	s_add_u32 m0, s28, 0xe000
	s_nop 0
	global_load_lds_dwordx4 v11, s[4:5]
	v_mfma_f32_16x16x32_f16 v[80:83], v[200:203], v[176:179], v[80:83]
	v_mfma_f32_16x16x32_f16 v[84:87], v[204:207], v[176:179], v[84:87]
	s_waitcnt lgkmcnt(9)
	v_mfma_f32_16x16x32_f16 v[88:91], v[192:195], v[180:183], v[88:91]
	v_mfma_f32_16x16x32_f16 v[92:95], v[196:199], v[180:183], v[92:95]
	v_mfma_f32_16x16x32_f16 v[96:99], v[200:203], v[180:183], v[96:99]
	s_add_u32 m0, s28, 0x10000
	s_nop 0
	global_load_lds_dwordx4 v12, s[4:5]
	v_mfma_f32_16x16x32_f16 v[100:103], v[204:207], v[180:183], v[100:103]
	s_waitcnt lgkmcnt(8)
	v_mfma_f32_16x16x32_f16 v[104:107], v[192:195], v[184:187], v[104:107]
	v_mfma_f32_16x16x32_f16 v[108:111], v[196:199], v[184:187], v[108:111]
	v_mfma_f32_16x16x32_f16 v[112:115], v[200:203], v[184:187], v[112:115]
	v_mfma_f32_16x16x32_f16 v[116:119], v[204:207], v[184:187], v[116:119]
	s_waitcnt lgkmcnt(7)
	ds_read_b128 v[172:175], v20
	ds_read_b128 v[192:195], v22
	ds_read_b128 v[196:199], v22 offset:2048
	ds_read_b128 v[200:203], v22 offset:4096
	ds_read_b128 v[204:207], v22 offset:6144
	ds_read_b128 v[176:179], v20 offset:2048
	ds_read_b128 v[180:183], v20 offset:4096
	ds_read_b128 v[184:187], v20 offset:6144
	s_waitcnt lgkmcnt(14)
	v_mfma_f32_16x16x32_f16 v[56:59], v[156:159], v[136:139], v[56:59]
	s_add_u32 m0, s28, 0x12000
	s_nop 0
	global_load_lds_dwordx4 v13, s[4:5]
	s_add_u32 s4, s4, s20
	s_addc_u32 s5, s5, 0
	s_waitcnt lgkmcnt(13)
	v_mfma_f32_16x16x32_f16 v[60:63], v[160:163], v[136:139], v[60:63]
	s_waitcnt lgkmcnt(12)
	v_mfma_f32_16x16x32_f16 v[64:67], v[164:167], v[136:139], v[64:67]
	s_waitcnt lgkmcnt(11)
	v_mfma_f32_16x16x32_f16 v[68:71], v[168:171], v[136:139], v[68:71]
	s_waitcnt lgkmcnt(10)
	v_mfma_f32_16x16x32_f16 v[72:75], v[156:159], v[140:143], v[72:75]
	v_mfma_f32_16x16x32_f16 v[76:79], v[160:163], v[140:143], v[76:79]
	s_add_u32 m0, s28, 0x14000
	s_nop 0
	global_load_lds_dwordx4 v10, s[6:7]
	v_mfma_f32_16x16x32_f16 v[80:83], v[164:167], v[140:143], v[80:83]
	v_mfma_f32_16x16x32_f16 v[84:87], v[168:171], v[140:143], v[84:87]
	s_waitcnt lgkmcnt(9)
	v_mfma_f32_16x16x32_f16 v[88:91], v[156:159], v[144:147], v[88:91]
	v_mfma_f32_16x16x32_f16 v[92:95], v[160:163], v[144:147], v[92:95]
	v_mfma_f32_16x16x32_f16 v[96:99], v[164:167], v[144:147], v[96:99]
	s_add_u32 m0, s28, 0x16000
	s_nop 0
	global_load_lds_dwordx4 v11, s[6:7]
	s_add_u32 s6, s6, s20
	s_addc_u32 s7, s7, 0
	v_mfma_f32_16x16x32_f16 v[100:103], v[168:171], v[144:147], v[100:103]
	s_waitcnt lgkmcnt(8)
	v_mfma_f32_16x16x32_f16 v[104:107], v[156:159], v[148:151], v[104:107]
	v_mfma_f32_16x16x32_f16 v[108:111], v[160:163], v[148:151], v[108:111]
	v_mfma_f32_16x16x32_f16 v[112:115], v[164:167], v[148:151], v[112:115]
	v_mfma_f32_16x16x32_f16 v[116:119], v[168:171], v[148:151], v[116:119]
	s_waitcnt vmcnt(6) lgkmcnt(0)
	s_barrier
	s_waitcnt lgkmcnt(7)
	ds_read_b128 v[136:139], v15
	ds_read_b128 v[156:159], v17
	ds_read_b128 v[160:163], v17 offset:2048
	ds_read_b128 v[164:167], v17 offset:4096
	ds_read_b128 v[168:171], v17 offset:6144
	ds_read_b128 v[140:143], v15 offset:2048
	ds_read_b128 v[144:147], v15 offset:4096
	ds_read_b128 v[148:151], v15 offset:6144
	s_waitcnt lgkmcnt(14)
	v_mfma_f32_16x16x32_f16 v[56:59], v[192:195], v[172:175], v[56:59]
	s_add_u32 m0, s28, 0x18000
	s_nop 0
	global_load_lds_dwordx4 v10, s[4:5]
	s_waitcnt lgkmcnt(13)
	v_mfma_f32_16x16x32_f16 v[60:63], v[196:199], v[172:175], v[60:63]
	s_waitcnt lgkmcnt(12)
	v_mfma_f32_16x16x32_f16 v[64:67], v[200:203], v[172:175], v[64:67]
	s_waitcnt lgkmcnt(11)
	v_mfma_f32_16x16x32_f16 v[68:71], v[204:207], v[172:175], v[68:71]
	s_waitcnt lgkmcnt(10)
	v_mfma_f32_16x16x32_f16 v[72:75], v[192:195], v[176:179], v[72:75]
	v_mfma_f32_16x16x32_f16 v[76:79], v[196:199], v[176:179], v[76:79]
	s_add_u32 m0, s28, 0x1a000
	s_nop 0
	global_load_lds_dwordx4 v11, s[4:5]
	v_mfma_f32_16x16x32_f16 v[80:83], v[200:203], v[176:179], v[80:83]
	v_mfma_f32_16x16x32_f16 v[84:87], v[204:207], v[176:179], v[84:87]
	s_waitcnt lgkmcnt(9)
	v_mfma_f32_16x16x32_f16 v[88:91], v[192:195], v[180:183], v[88:91]
	v_mfma_f32_16x16x32_f16 v[92:95], v[196:199], v[180:183], v[92:95]
	v_mfma_f32_16x16x32_f16 v[96:99], v[200:203], v[180:183], v[96:99]
	s_add_u32 m0, s28, 0x1c000
	s_nop 0
	global_load_lds_dwordx4 v12, s[4:5]
	v_mfma_f32_16x16x32_f16 v[100:103], v[204:207], v[180:183], v[100:103]
	s_waitcnt lgkmcnt(8)
	v_mfma_f32_16x16x32_f16 v[104:107], v[192:195], v[184:187], v[104:107]
	v_mfma_f32_16x16x32_f16 v[108:111], v[196:199], v[184:187], v[108:111]
	v_mfma_f32_16x16x32_f16 v[112:115], v[200:203], v[184:187], v[112:115]
	v_mfma_f32_16x16x32_f16 v[116:119], v[204:207], v[184:187], v[116:119]
	s_waitcnt lgkmcnt(7)
	ds_read_b128 v[172:175], v16
	ds_read_b128 v[192:195], v18
	ds_read_b128 v[196:199], v18 offset:2048
	ds_read_b128 v[200:203], v18 offset:4096
	ds_read_b128 v[204:207], v18 offset:6144
	ds_read_b128 v[176:179], v16 offset:2048
	ds_read_b128 v[180:183], v16 offset:4096
	ds_read_b128 v[184:187], v16 offset:6144
	s_waitcnt lgkmcnt(14)
	v_mfma_f32_16x16x32_f16 v[56:59], v[156:159], v[136:139], v[56:59]
	s_add_u32 m0, s28, 0x1e000
	s_nop 0
	global_load_lds_dwordx4 v13, s[4:5]
	s_add_u32 s4, s4, s20
	s_addc_u32 s5, s5, 0
	s_waitcnt lgkmcnt(13)
	v_mfma_f32_16x16x32_f16 v[60:63], v[160:163], v[136:139], v[60:63]
	s_waitcnt lgkmcnt(12)
	v_mfma_f32_16x16x32_f16 v[64:67], v[164:167], v[136:139], v[64:67]
	s_waitcnt lgkmcnt(11)
	v_mfma_f32_16x16x32_f16 v[68:71], v[168:171], v[136:139], v[68:71]
	s_waitcnt lgkmcnt(10)
	v_mfma_f32_16x16x32_f16 v[72:75], v[156:159], v[140:143], v[72:75]
	v_mfma_f32_16x16x32_f16 v[76:79], v[160:163], v[140:143], v[76:79]
	s_add_u32 m0, s28, 0x20000
	s_nop 0
	global_load_lds_dwordx4 v10, s[6:7]
	v_mfma_f32_16x16x32_f16 v[80:83], v[164:167], v[140:143], v[80:83]
	v_mfma_f32_16x16x32_f16 v[84:87], v[168:171], v[140:143], v[84:87]
	s_waitcnt lgkmcnt(9)
	v_mfma_f32_16x16x32_f16 v[88:91], v[156:159], v[144:147], v[88:91]
	v_mfma_f32_16x16x32_f16 v[92:95], v[160:163], v[144:147], v[92:95]
	v_mfma_f32_16x16x32_f16 v[96:99], v[164:167], v[144:147], v[96:99]
	s_add_u32 m0, s28, 0x22000
	s_nop 0
	global_load_lds_dwordx4 v11, s[6:7]
	s_add_u32 s6, s6, s20
	s_addc_u32 s7, s7, 0
	v_mfma_f32_16x16x32_f16 v[100:103], v[168:171], v[144:147], v[100:103]
	s_waitcnt lgkmcnt(8)
	v_mfma_f32_16x16x32_f16 v[104:107], v[156:159], v[148:151], v[104:107]
	v_mfma_f32_16x16x32_f16 v[108:111], v[160:163], v[148:151], v[108:111]
	v_mfma_f32_16x16x32_f16 v[112:115], v[164:167], v[148:151], v[112:115]
	v_mfma_f32_16x16x32_f16 v[116:119], v[168:171], v[148:151], v[116:119]
	s_waitcnt vmcnt(6) lgkmcnt(0)
	s_barrier
	s_waitcnt lgkmcnt(7)
	ds_read_b128 v[136:139], v15 offset:49152
	ds_read_b128 v[156:159], v17 offset:49152
	ds_read_b128 v[160:163], v17 offset:51200
	ds_read_b128 v[164:167], v17 offset:53248
	ds_read_b128 v[168:171], v17 offset:55296
	ds_read_b128 v[140:143], v15 offset:51200
	ds_read_b128 v[144:147], v15 offset:53248
	ds_read_b128 v[148:151], v15 offset:55296
	s_waitcnt lgkmcnt(14)
	v_mfma_f32_16x16x32_f16 v[56:59], v[192:195], v[172:175], v[56:59]
	s_add_u32 m0, s28, 0x0
	s_nop 0
	global_load_lds_dwordx4 v10, s[4:5]
	s_waitcnt lgkmcnt(13)
	v_mfma_f32_16x16x32_f16 v[60:63], v[196:199], v[172:175], v[60:63]
	s_waitcnt lgkmcnt(12)
	v_mfma_f32_16x16x32_f16 v[64:67], v[200:203], v[172:175], v[64:67]
	s_waitcnt lgkmcnt(11)
	v_mfma_f32_16x16x32_f16 v[68:71], v[204:207], v[172:175], v[68:71]
	s_waitcnt lgkmcnt(10)
	v_mfma_f32_16x16x32_f16 v[72:75], v[192:195], v[176:179], v[72:75]
	v_mfma_f32_16x16x32_f16 v[76:79], v[196:199], v[176:179], v[76:79]
	s_add_u32 m0, s28, 0x2000
	s_nop 0
	global_load_lds_dwordx4 v11, s[4:5]
	v_mfma_f32_16x16x32_f16 v[80:83], v[200:203], v[176:179], v[80:83]
	v_mfma_f32_16x16x32_f16 v[84:87], v[204:207], v[176:179], v[84:87]
	s_waitcnt lgkmcnt(9)
	v_mfma_f32_16x16x32_f16 v[88:91], v[192:195], v[180:183], v[88:91]
	v_mfma_f32_16x16x32_f16 v[92:95], v[196:199], v[180:183], v[92:95]
	v_mfma_f32_16x16x32_f16 v[96:99], v[200:203], v[180:183], v[96:99]
	s_add_u32 m0, s28, 0x4000
	s_nop 0
	global_load_lds_dwordx4 v12, s[4:5]
	v_mfma_f32_16x16x32_f16 v[100:103], v[204:207], v[180:183], v[100:103]
	s_waitcnt lgkmcnt(8)
	v_mfma_f32_16x16x32_f16 v[104:107], v[192:195], v[184:187], v[104:107]
	v_mfma_f32_16x16x32_f16 v[108:111], v[196:199], v[184:187], v[108:111]
	v_mfma_f32_16x16x32_f16 v[112:115], v[200:203], v[184:187], v[112:115]
	v_mfma_f32_16x16x32_f16 v[116:119], v[204:207], v[184:187], v[116:119]
	s_waitcnt lgkmcnt(7)
	ds_read_b128 v[172:175], v16 offset:49152
	ds_read_b128 v[192:195], v18 offset:49152
	ds_read_b128 v[196:199], v18 offset:51200
	ds_read_b128 v[200:203], v18 offset:53248
	ds_read_b128 v[204:207], v18 offset:55296
	ds_read_b128 v[176:179], v16 offset:51200
	ds_read_b128 v[180:183], v16 offset:53248
	ds_read_b128 v[184:187], v16 offset:55296
	s_waitcnt lgkmcnt(14)
	v_mfma_f32_16x16x32_f16 v[56:59], v[156:159], v[136:139], v[56:59]
	s_add_u32 m0, s28, 0x6000
	s_nop 0
	global_load_lds_dwordx4 v13, s[4:5]
	s_add_u32 s4, s4, s20
	s_addc_u32 s5, s5, 0
	s_waitcnt lgkmcnt(13)
	v_mfma_f32_16x16x32_f16 v[60:63], v[160:163], v[136:139], v[60:63]
	s_waitcnt lgkmcnt(12)
	v_mfma_f32_16x16x32_f16 v[64:67], v[164:167], v[136:139], v[64:67]
	s_waitcnt lgkmcnt(11)
	v_mfma_f32_16x16x32_f16 v[68:71], v[168:171], v[136:139], v[68:71]
	s_waitcnt lgkmcnt(10)
	v_mfma_f32_16x16x32_f16 v[72:75], v[156:159], v[140:143], v[72:75]
	v_mfma_f32_16x16x32_f16 v[76:79], v[160:163], v[140:143], v[76:79]
	s_add_u32 m0, s28, 0x8000
	s_nop 0
	global_load_lds_dwordx4 v10, s[6:7]
	v_mfma_f32_16x16x32_f16 v[80:83], v[164:167], v[140:143], v[80:83]
	v_mfma_f32_16x16x32_f16 v[84:87], v[168:171], v[140:143], v[84:87]
	s_waitcnt lgkmcnt(9)
	v_mfma_f32_16x16x32_f16 v[88:91], v[156:159], v[144:147], v[88:91]
	v_mfma_f32_16x16x32_f16 v[92:95], v[160:163], v[144:147], v[92:95]
	v_mfma_f32_16x16x32_f16 v[96:99], v[164:167], v[144:147], v[96:99]
	s_add_u32 m0, s28, 0xa000
	s_nop 0
	global_load_lds_dwordx4 v11, s[6:7]
	s_add_u32 s6, s6, s20
	s_addc_u32 s7, s7, 0
	v_mfma_f32_16x16x32_f16 v[100:103], v[168:171], v[144:147], v[100:103]
	s_waitcnt lgkmcnt(8)
	v_mfma_f32_16x16x32_f16 v[104:107], v[156:159], v[148:151], v[104:107]
	v_mfma_f32_16x16x32_f16 v[108:111], v[160:163], v[148:151], v[108:111]
	v_mfma_f32_16x16x32_f16 v[112:115], v[164:167], v[148:151], v[112:115]
	v_mfma_f32_16x16x32_f16 v[116:119], v[168:171], v[148:151], v[116:119]
	s_waitcnt vmcnt(6) lgkmcnt(0)
	s_barrier
	s_waitcnt lgkmcnt(7)
	ds_read_b128 v[136:139], v19
	ds_read_b128 v[156:159], v21
	ds_read_b128 v[160:163], v21 offset:2048
	ds_read_b128 v[164:167], v21 offset:4096
	ds_read_b128 v[168:171], v21 offset:6144
	ds_read_b128 v[140:143], v19 offset:2048
	ds_read_b128 v[144:147], v19 offset:4096
	ds_read_b128 v[148:151], v19 offset:6144
	s_waitcnt lgkmcnt(14)
	v_mfma_f32_16x16x32_f16 v[56:59], v[192:195], v[172:175], v[56:59]
	s_waitcnt lgkmcnt(13)
	v_mfma_f32_16x16x32_f16 v[60:63], v[196:199], v[172:175], v[60:63]
	s_waitcnt lgkmcnt(12)
	v_mfma_f32_16x16x32_f16 v[64:67], v[200:203], v[172:175], v[64:67]
	s_waitcnt lgkmcnt(11)
	v_mfma_f32_16x16x32_f16 v[68:71], v[204:207], v[172:175], v[68:71]
	s_waitcnt lgkmcnt(10)
	v_mfma_f32_16x16x32_f16 v[72:75], v[192:195], v[176:179], v[72:75]
	v_mfma_f32_16x16x32_f16 v[76:79], v[196:199], v[176:179], v[76:79]
	v_mfma_f32_16x16x32_f16 v[80:83], v[200:203], v[176:179], v[80:83]
	v_mfma_f32_16x16x32_f16 v[84:87], v[204:207], v[176:179], v[84:87]
	s_waitcnt lgkmcnt(9)
	v_mfma_f32_16x16x32_f16 v[88:91], v[192:195], v[180:183], v[88:91]
	v_mfma_f32_16x16x32_f16 v[92:95], v[196:199], v[180:183], v[92:95]
	v_mfma_f32_16x16x32_f16 v[96:99], v[200:203], v[180:183], v[96:99]
	v_mfma_f32_16x16x32_f16 v[100:103], v[204:207], v[180:183], v[100:103]
	s_waitcnt lgkmcnt(8)
	v_mfma_f32_16x16x32_f16 v[104:107], v[192:195], v[184:187], v[104:107]
	v_mfma_f32_16x16x32_f16 v[108:111], v[196:199], v[184:187], v[108:111]
	v_mfma_f32_16x16x32_f16 v[112:115], v[200:203], v[184:187], v[112:115]
	v_mfma_f32_16x16x32_f16 v[116:119], v[204:207], v[184:187], v[116:119]
	s_waitcnt lgkmcnt(7)
	ds_read_b128 v[172:175], v20
	ds_read_b128 v[192:195], v22
	ds_read_b128 v[196:199], v22 offset:2048
	ds_read_b128 v[200:203], v22 offset:4096
	ds_read_b128 v[204:207], v22 offset:6144
	ds_read_b128 v[176:179], v20 offset:2048
	ds_read_b128 v[180:183], v20 offset:4096
	ds_read_b128 v[184:187], v20 offset:6144
	s_waitcnt lgkmcnt(14)
	v_mfma_f32_16x16x32_f16 v[56:59], v[156:159], v[136:139], v[56:59]
	s_waitcnt lgkmcnt(13)
	v_mfma_f32_16x16x32_f16 v[60:63], v[160:163], v[136:139], v[60:63]
	s_waitcnt lgkmcnt(12)
	v_mfma_f32_16x16x32_f16 v[64:67], v[164:167], v[136:139], v[64:67]
	s_waitcnt lgkmcnt(11)
	v_mfma_f32_16x16x32_f16 v[68:71], v[168:171], v[136:139], v[68:71]
	s_waitcnt lgkmcnt(10)
	v_mfma_f32_16x16x32_f16 v[72:75], v[156:159], v[140:143], v[72:75]
	v_mfma_f32_16x16x32_f16 v[76:79], v[160:163], v[140:143], v[76:79]
	v_mfma_f32_16x16x32_f16 v[80:83], v[164:167], v[140:143], v[80:83]
	v_mfma_f32_16x16x32_f16 v[84:87], v[168:171], v[140:143], v[84:87]
	s_waitcnt lgkmcnt(9)
	v_mfma_f32_16x16x32_f16 v[88:91], v[156:159], v[144:147], v[88:91]
	v_mfma_f32_16x16x32_f16 v[92:95], v[160:163], v[144:147], v[92:95]
	v_mfma_f32_16x16x32_f16 v[96:99], v[164:167], v[144:147], v[96:99]
	v_mfma_f32_16x16x32_f16 v[100:103], v[168:171], v[144:147], v[100:103]
	s_waitcnt lgkmcnt(8)
	v_mfma_f32_16x16x32_f16 v[104:107], v[156:159], v[148:151], v[104:107]
	v_mfma_f32_16x16x32_f16 v[108:111], v[160:163], v[148:151], v[108:111]
	v_mfma_f32_16x16x32_f16 v[112:115], v[164:167], v[148:151], v[112:115]
	v_mfma_f32_16x16x32_f16 v[116:119], v[168:171], v[148:151], v[116:119]
	s_waitcnt vmcnt(0) lgkmcnt(0)
	s_barrier
	s_waitcnt lgkmcnt(7)
	ds_read_b128 v[136:139], v15
	ds_read_b128 v[156:159], v17
	ds_read_b128 v[160:163], v17 offset:2048
	ds_read_b128 v[164:167], v17 offset:4096
	ds_read_b128 v[168:171], v17 offset:6144
	ds_read_b128 v[140:143], v15 offset:2048
	ds_read_b128 v[144:147], v15 offset:4096
	ds_read_b128 v[148:151], v15 offset:6144
	s_waitcnt lgkmcnt(14)
	v_mfma_f32_16x16x32_f16 v[56:59], v[192:195], v[172:175], v[56:59]
	s_waitcnt lgkmcnt(13)
	v_mfma_f32_16x16x32_f16 v[60:63], v[196:199], v[172:175], v[60:63]
	s_waitcnt lgkmcnt(12)
	v_mfma_f32_16x16x32_f16 v[64:67], v[200:203], v[172:175], v[64:67]
	s_waitcnt lgkmcnt(11)
	v_mfma_f32_16x16x32_f16 v[68:71], v[204:207], v[172:175], v[68:71]
	s_waitcnt lgkmcnt(10)
	v_mfma_f32_16x16x32_f16 v[72:75], v[192:195], v[176:179], v[72:75]
	v_mfma_f32_16x16x32_f16 v[76:79], v[196:199], v[176:179], v[76:79]
	v_mfma_f32_16x16x32_f16 v[80:83], v[200:203], v[176:179], v[80:83]
	v_mfma_f32_16x16x32_f16 v[84:87], v[204:207], v[176:179], v[84:87]
	s_waitcnt lgkmcnt(9)
	v_mfma_f32_16x16x32_f16 v[88:91], v[192:195], v[180:183], v[88:91]
	v_mfma_f32_16x16x32_f16 v[92:95], v[196:199], v[180:183], v[92:95]
	v_mfma_f32_16x16x32_f16 v[96:99], v[200:203], v[180:183], v[96:99]
	v_mfma_f32_16x16x32_f16 v[100:103], v[204:207], v[180:183], v[100:103]
	s_waitcnt lgkmcnt(8)
	v_mfma_f32_16x16x32_f16 v[104:107], v[192:195], v[184:187], v[104:107]
	v_mfma_f32_16x16x32_f16 v[108:111], v[196:199], v[184:187], v[108:111]
	v_mfma_f32_16x16x32_f16 v[112:115], v[200:203], v[184:187], v[112:115]
	v_mfma_f32_16x16x32_f16 v[116:119], v[204:207], v[184:187], v[116:119]
	s_waitcnt lgkmcnt(7)
	ds_read_b128 v[172:175], v16
	ds_read_b128 v[192:195], v18
	ds_read_b128 v[196:199], v18 offset:2048
	ds_read_b128 v[200:203], v18 offset:4096
	ds_read_b128 v[204:207], v18 offset:6144
	ds_read_b128 v[176:179], v16 offset:2048
	ds_read_b128 v[180:183], v16 offset:4096
	ds_read_b128 v[184:187], v16 offset:6144
	s_waitcnt lgkmcnt(14)
	v_mfma_f32_16x16x32_f16 v[56:59], v[156:159], v[136:139], v[56:59]
	s_waitcnt lgkmcnt(13)
	v_mfma_f32_16x16x32_f16 v[60:63], v[160:163], v[136:139], v[60:63]
	s_waitcnt lgkmcnt(12)
	v_mfma_f32_16x16x32_f16 v[64:67], v[164:167], v[136:139], v[64:67]
	s_waitcnt lgkmcnt(11)
	v_mfma_f32_16x16x32_f16 v[68:71], v[168:171], v[136:139], v[68:71]
	s_waitcnt lgkmcnt(10)
	v_mfma_f32_16x16x32_f16 v[72:75], v[156:159], v[140:143], v[72:75]
	v_mfma_f32_16x16x32_f16 v[76:79], v[160:163], v[140:143], v[76:79]
	v_mfma_f32_16x16x32_f16 v[80:83], v[164:167], v[140:143], v[80:83]
	v_mfma_f32_16x16x32_f16 v[84:87], v[168:171], v[140:143], v[84:87]
	s_waitcnt lgkmcnt(9)
	v_mfma_f32_16x16x32_f16 v[88:91], v[156:159], v[144:147], v[88:91]
	v_mfma_f32_16x16x32_f16 v[92:95], v[160:163], v[144:147], v[92:95]
	v_mfma_f32_16x16x32_f16 v[96:99], v[164:167], v[144:147], v[96:99]
	v_mfma_f32_16x16x32_f16 v[100:103], v[168:171], v[144:147], v[100:103]
	s_waitcnt lgkmcnt(8)
	v_mfma_f32_16x16x32_f16 v[104:107], v[156:159], v[148:151], v[104:107]
	v_mfma_f32_16x16x32_f16 v[108:111], v[160:163], v[148:151], v[108:111]
	v_mfma_f32_16x16x32_f16 v[112:115], v[164:167], v[148:151], v[112:115]
	v_mfma_f32_16x16x32_f16 v[116:119], v[168:171], v[148:151], v[116:119]
	s_waitcnt lgkmcnt(6)
	v_mfma_f32_16x16x32_f16 v[56:59], v[192:195], v[172:175], v[56:59]
	s_waitcnt lgkmcnt(5)
	v_mfma_f32_16x16x32_f16 v[60:63], v[196:199], v[172:175], v[60:63]
	s_waitcnt lgkmcnt(4)
	v_mfma_f32_16x16x32_f16 v[64:67], v[200:203], v[172:175], v[64:67]
	s_waitcnt lgkmcnt(3)
	v_mfma_f32_16x16x32_f16 v[68:71], v[204:207], v[172:175], v[68:71]
	s_waitcnt lgkmcnt(2)
	v_mfma_f32_16x16x32_f16 v[72:75], v[192:195], v[176:179], v[72:75]
	v_mfma_f32_16x16x32_f16 v[76:79], v[196:199], v[176:179], v[76:79]
	v_mfma_f32_16x16x32_f16 v[80:83], v[200:203], v[176:179], v[80:83]
	v_mfma_f32_16x16x32_f16 v[84:87], v[204:207], v[176:179], v[84:87]
	s_waitcnt lgkmcnt(1)
	v_mfma_f32_16x16x32_f16 v[88:91], v[192:195], v[180:183], v[88:91]
	v_mfma_f32_16x16x32_f16 v[92:95], v[196:199], v[180:183], v[92:95]
	v_mfma_f32_16x16x32_f16 v[96:99], v[200:203], v[180:183], v[96:99]
	v_mfma_f32_16x16x32_f16 v[100:103], v[204:207], v[180:183], v[100:103]
	s_waitcnt lgkmcnt(0)
	v_mfma_f32_16x16x32_f16 v[104:107], v[192:195], v[184:187], v[104:107]
	v_mfma_f32_16x16x32_f16 v[108:111], v[196:199], v[184:187], v[108:111]
	v_mfma_f32_16x16x32_f16 v[112:115], v[200:203], v[184:187], v[112:115]
	v_mfma_f32_16x16x32_f16 v[116:119], v[204:207], v[184:187], v[116:119]
	s_nop 7
	s_nop 1
	v_mov_b32_e32 v211, s19
	v_add_f32_e32 v56, v56, v24
	v_add_f32_e32 v57, v57, v25
	v_add_f32_e32 v58, v58, v26
	v_add_f32_e32 v59, v59, v27
	v_add_f32_e32 v60, v60, v28
	v_add_f32_e32 v61, v61, v29
	v_add_f32_e32 v62, v62, v30
	v_add_f32_e32 v63, v63, v31
	v_add_f32_e32 v64, v64, v32
	v_add_f32_e32 v65, v65, v33
	v_add_f32_e32 v66, v66, v34
	v_add_f32_e32 v67, v67, v35
	v_add_f32_e32 v68, v68, v36
	v_add_f32_e32 v69, v69, v37
	v_add_f32_e32 v70, v70, v38
	v_add_f32_e32 v71, v71, v39
	v_mul_f32_e32 v208, v56, v56
	v_fmac_f32_e32 v208, v57, v57
	v_fmac_f32_e32 v208, v58, v58
	v_fmac_f32_e32 v208, v59, v59
	v_fmac_f32_e32 v208, v60, v60
	v_fmac_f32_e32 v208, v61, v61
	v_fmac_f32_e32 v208, v62, v62
	v_fmac_f32_e32 v208, v63, v63
	v_fmac_f32_e32 v208, v64, v64
	v_fmac_f32_e32 v208, v65, v65
	v_fmac_f32_e32 v208, v66, v66
	v_fmac_f32_e32 v208, v67, v67
	v_fmac_f32_e32 v208, v68, v68
	v_fmac_f32_e32 v208, v69, v69
	v_fmac_f32_e32 v208, v70, v70
	v_fmac_f32_e32 v208, v71, v71
	v_mov_b32_e32 v209, v208
	s_nop 1
	v_permlane16_swap_b32_e32 v208, v209
	v_add_f32_e32 v208, v208, v209
	v_mov_b32_e32 v209, v208
	s_nop 1
	v_permlane32_swap_b32_e32 v208, v209
	v_add_f32_e32 v208, v208, v209
	v_mov_b32_e32 v210, 0x358637bd
	v_fmac_f32_e32 v210, 0x3c800000, v208
	v_rsq_f32_e32 v210, v210
	s_add_u32 s24, s29, 0
	s_lshr_b32 s8, s24, 1
	s_lshl_b32 s8, s8, 12
	s_and_b32 s24, s24, 1
	s_lshl_b32 s24, s24, 8
	s_add_u32 s8, s8, s24
	v_mul_f32_e32 v210, v211, v210
	v_add_u32_e32 v212, s8, v23
	v_mul_f32_e32 v56, v56, v210
	v_mul_f32_e32 v57, v57, v210
	v_mul_f32_e32 v58, v58, v210
	v_mul_f32_e32 v59, v59, v210
	v_mul_f32_e32 v56, v56, v40
	v_mul_f32_e32 v57, v57, v41
	v_mul_f32_e32 v58, v58, v42
	v_mul_f32_e32 v59, v59, v43
	v_cvt_pk_f16_f32 v56, v56, v57
	v_cvt_pk_f16_f32 v57, v58, v59
	global_store_dwordx2 v212, v[56:57], s[22:23] offset:0
	v_mul_f32_e32 v60, v60, v210
	v_mul_f32_e32 v61, v61, v210
	v_mul_f32_e32 v62, v62, v210
	v_mul_f32_e32 v63, v63, v210
	v_mul_f32_e32 v60, v60, v44
	v_mul_f32_e32 v61, v61, v45
	v_mul_f32_e32 v62, v62, v46
	v_mul_f32_e32 v63, v63, v47
	v_cvt_pk_f16_f32 v60, v60, v61
	v_cvt_pk_f16_f32 v61, v62, v63
	global_store_dwordx2 v212, v[60:61], s[22:23] offset:1024
	v_mul_f32_e32 v64, v64, v210
	v_mul_f32_e32 v65, v65, v210
	v_mul_f32_e32 v66, v66, v210
	v_mul_f32_e32 v67, v67, v210
	v_mul_f32_e32 v64, v64, v48
	v_mul_f32_e32 v65, v65, v49
	v_mul_f32_e32 v66, v66, v50
	v_mul_f32_e32 v67, v67, v51
	v_cvt_pk_f16_f32 v64, v64, v65
	v_cvt_pk_f16_f32 v65, v66, v67
	global_store_dwordx2 v212, v[64:65], s[22:23] offset:2048
	v_mul_f32_e32 v68, v68, v210
	v_mul_f32_e32 v69, v69, v210
	v_mul_f32_e32 v70, v70, v210
	v_mul_f32_e32 v71, v71, v210
	v_mul_f32_e32 v68, v68, v52
	v_mul_f32_e32 v69, v69, v53
	v_mul_f32_e32 v70, v70, v54
	v_mul_f32_e32 v71, v71, v55
	v_cvt_pk_f16_f32 v68, v68, v69
	v_cvt_pk_f16_f32 v69, v70, v71
	global_store_dwordx2 v212, v[68:69], s[22:23] offset:3072
	v_add_f32_e32 v72, v72, v24
	v_add_f32_e32 v73, v73, v25
	v_add_f32_e32 v74, v74, v26
	v_add_f32_e32 v75, v75, v27
	v_add_f32_e32 v76, v76, v28
	v_add_f32_e32 v77, v77, v29
	v_add_f32_e32 v78, v78, v30
	v_add_f32_e32 v79, v79, v31
	v_add_f32_e32 v80, v80, v32
	v_add_f32_e32 v81, v81, v33
	v_add_f32_e32 v82, v82, v34
	v_add_f32_e32 v83, v83, v35
	v_add_f32_e32 v84, v84, v36
	v_add_f32_e32 v85, v85, v37
	v_add_f32_e32 v86, v86, v38
	v_add_f32_e32 v87, v87, v39
	v_mul_f32_e32 v208, v72, v72
	v_fmac_f32_e32 v208, v73, v73
	v_fmac_f32_e32 v208, v74, v74
	v_fmac_f32_e32 v208, v75, v75
	v_fmac_f32_e32 v208, v76, v76
	v_fmac_f32_e32 v208, v77, v77
	v_fmac_f32_e32 v208, v78, v78
	v_fmac_f32_e32 v208, v79, v79
	v_fmac_f32_e32 v208, v80, v80
	v_fmac_f32_e32 v208, v81, v81
	v_fmac_f32_e32 v208, v82, v82
	v_fmac_f32_e32 v208, v83, v83
	v_fmac_f32_e32 v208, v84, v84
	v_fmac_f32_e32 v208, v85, v85
	v_fmac_f32_e32 v208, v86, v86
	v_fmac_f32_e32 v208, v87, v87
	v_mov_b32_e32 v209, v208
	s_nop 1
	v_permlane16_swap_b32_e32 v208, v209
	v_add_f32_e32 v208, v208, v209
	v_mov_b32_e32 v209, v208
	s_nop 1
	v_permlane32_swap_b32_e32 v208, v209
	v_add_f32_e32 v208, v208, v209
	v_mov_b32_e32 v210, 0x358637bd
	v_fmac_f32_e32 v210, 0x3c800000, v208
	v_rsq_f32_e32 v210, v210
	s_add_u32 s24, s29, 1
	s_lshr_b32 s8, s24, 1
	s_lshl_b32 s8, s8, 12
	s_and_b32 s24, s24, 1
	s_lshl_b32 s24, s24, 8
	s_add_u32 s8, s8, s24
	v_mul_f32_e32 v210, v211, v210
	v_add_u32_e32 v212, s8, v23
	v_mul_f32_e32 v72, v72, v210
	v_mul_f32_e32 v73, v73, v210
	v_mul_f32_e32 v74, v74, v210
	v_mul_f32_e32 v75, v75, v210
	v_mul_f32_e32 v72, v72, v40
	v_mul_f32_e32 v73, v73, v41
	v_mul_f32_e32 v74, v74, v42
	v_mul_f32_e32 v75, v75, v43
	v_cvt_pk_f16_f32 v72, v72, v73
	v_cvt_pk_f16_f32 v73, v74, v75
	global_store_dwordx2 v212, v[72:73], s[22:23] offset:0
	v_mul_f32_e32 v76, v76, v210
	v_mul_f32_e32 v77, v77, v210
	v_mul_f32_e32 v78, v78, v210
	v_mul_f32_e32 v79, v79, v210
	v_mul_f32_e32 v76, v76, v44
	v_mul_f32_e32 v77, v77, v45
	v_mul_f32_e32 v78, v78, v46
	v_mul_f32_e32 v79, v79, v47
	v_cvt_pk_f16_f32 v76, v76, v77
	v_cvt_pk_f16_f32 v77, v78, v79
	global_store_dwordx2 v212, v[76:77], s[22:23] offset:1024
	v_mul_f32_e32 v80, v80, v210
	v_mul_f32_e32 v81, v81, v210
	v_mul_f32_e32 v82, v82, v210
	v_mul_f32_e32 v83, v83, v210
	v_mul_f32_e32 v80, v80, v48
	v_mul_f32_e32 v81, v81, v49
	v_mul_f32_e32 v82, v82, v50
	v_mul_f32_e32 v83, v83, v51
	v_cvt_pk_f16_f32 v80, v80, v81
	v_cvt_pk_f16_f32 v81, v82, v83
	global_store_dwordx2 v212, v[80:81], s[22:23] offset:2048
	v_mul_f32_e32 v84, v84, v210
	v_mul_f32_e32 v85, v85, v210
	v_mul_f32_e32 v86, v86, v210
	v_mul_f32_e32 v87, v87, v210
	v_mul_f32_e32 v84, v84, v52
	v_mul_f32_e32 v85, v85, v53
	v_mul_f32_e32 v86, v86, v54
	v_mul_f32_e32 v87, v87, v55
	v_cvt_pk_f16_f32 v84, v84, v85
	v_cvt_pk_f16_f32 v85, v86, v87
	global_store_dwordx2 v212, v[84:85], s[22:23] offset:3072
	v_add_f32_e32 v88, v88, v24
	v_add_f32_e32 v89, v89, v25
	v_add_f32_e32 v90, v90, v26
	v_add_f32_e32 v91, v91, v27
	v_add_f32_e32 v92, v92, v28
	v_add_f32_e32 v93, v93, v29
	v_add_f32_e32 v94, v94, v30
	v_add_f32_e32 v95, v95, v31
	v_add_f32_e32 v96, v96, v32
	v_add_f32_e32 v97, v97, v33
	v_add_f32_e32 v98, v98, v34
	v_add_f32_e32 v99, v99, v35
	v_add_f32_e32 v100, v100, v36
	v_add_f32_e32 v101, v101, v37
	v_add_f32_e32 v102, v102, v38
	v_add_f32_e32 v103, v103, v39
	v_mul_f32_e32 v208, v88, v88
	v_fmac_f32_e32 v208, v89, v89
	v_fmac_f32_e32 v208, v90, v90
	v_fmac_f32_e32 v208, v91, v91
	v_fmac_f32_e32 v208, v92, v92
	v_fmac_f32_e32 v208, v93, v93
	v_fmac_f32_e32 v208, v94, v94
	v_fmac_f32_e32 v208, v95, v95
	v_fmac_f32_e32 v208, v96, v96
	v_fmac_f32_e32 v208, v97, v97
	v_fmac_f32_e32 v208, v98, v98
	v_fmac_f32_e32 v208, v99, v99
	v_fmac_f32_e32 v208, v100, v100
	v_fmac_f32_e32 v208, v101, v101
	v_fmac_f32_e32 v208, v102, v102
	v_fmac_f32_e32 v208, v103, v103
	v_mov_b32_e32 v209, v208
	s_nop 1
	v_permlane16_swap_b32_e32 v208, v209
	v_add_f32_e32 v208, v208, v209
	v_mov_b32_e32 v209, v208
	s_nop 1
	v_permlane32_swap_b32_e32 v208, v209
	v_add_f32_e32 v208, v208, v209
	v_mov_b32_e32 v210, 0x358637bd
	v_fmac_f32_e32 v210, 0x3c800000, v208
	v_rsq_f32_e32 v210, v210
	s_add_u32 s24, s29, 2
	s_lshr_b32 s8, s24, 1
	s_lshl_b32 s8, s8, 12
	s_and_b32 s24, s24, 1
	s_lshl_b32 s24, s24, 8
	s_add_u32 s8, s8, s24
	v_mul_f32_e32 v210, v211, v210
	v_add_u32_e32 v212, s8, v23
	v_mul_f32_e32 v88, v88, v210
	v_mul_f32_e32 v89, v89, v210
	v_mul_f32_e32 v90, v90, v210
	v_mul_f32_e32 v91, v91, v210
	v_mul_f32_e32 v88, v88, v40
	v_mul_f32_e32 v89, v89, v41
	v_mul_f32_e32 v90, v90, v42
	v_mul_f32_e32 v91, v91, v43
	v_cvt_pk_f16_f32 v88, v88, v89
	v_cvt_pk_f16_f32 v89, v90, v91
	global_store_dwordx2 v212, v[88:89], s[22:23] offset:0
	v_mul_f32_e32 v92, v92, v210
	v_mul_f32_e32 v93, v93, v210
	v_mul_f32_e32 v94, v94, v210
	v_mul_f32_e32 v95, v95, v210
	v_mul_f32_e32 v92, v92, v44
	v_mul_f32_e32 v93, v93, v45
	v_mul_f32_e32 v94, v94, v46
	v_mul_f32_e32 v95, v95, v47
	v_cvt_pk_f16_f32 v92, v92, v93
	v_cvt_pk_f16_f32 v93, v94, v95
	global_store_dwordx2 v212, v[92:93], s[22:23] offset:1024
	v_mul_f32_e32 v96, v96, v210
	v_mul_f32_e32 v97, v97, v210
	v_mul_f32_e32 v98, v98, v210
	v_mul_f32_e32 v99, v99, v210
	v_mul_f32_e32 v96, v96, v48
	v_mul_f32_e32 v97, v97, v49
	v_mul_f32_e32 v98, v98, v50
	v_mul_f32_e32 v99, v99, v51
	v_cvt_pk_f16_f32 v96, v96, v97
	v_cvt_pk_f16_f32 v97, v98, v99
	global_store_dwordx2 v212, v[96:97], s[22:23] offset:2048
	v_mul_f32_e32 v100, v100, v210
	v_mul_f32_e32 v101, v101, v210
	v_mul_f32_e32 v102, v102, v210
	v_mul_f32_e32 v103, v103, v210
	v_mul_f32_e32 v100, v100, v52
	v_mul_f32_e32 v101, v101, v53
	v_mul_f32_e32 v102, v102, v54
	v_mul_f32_e32 v103, v103, v55
	v_cvt_pk_f16_f32 v100, v100, v101
	v_cvt_pk_f16_f32 v101, v102, v103
	global_store_dwordx2 v212, v[100:101], s[22:23] offset:3072
	v_add_f32_e32 v104, v104, v24
	v_add_f32_e32 v105, v105, v25
	v_add_f32_e32 v106, v106, v26
	v_add_f32_e32 v107, v107, v27
	v_add_f32_e32 v108, v108, v28
	v_add_f32_e32 v109, v109, v29
	v_add_f32_e32 v110, v110, v30
	v_add_f32_e32 v111, v111, v31
	v_add_f32_e32 v112, v112, v32
	v_add_f32_e32 v113, v113, v33
	v_add_f32_e32 v114, v114, v34
	v_add_f32_e32 v115, v115, v35
	v_add_f32_e32 v116, v116, v36
	v_add_f32_e32 v117, v117, v37
	v_add_f32_e32 v118, v118, v38
	v_add_f32_e32 v119, v119, v39
	v_mul_f32_e32 v208, v104, v104
	v_fmac_f32_e32 v208, v105, v105
	v_fmac_f32_e32 v208, v106, v106
	v_fmac_f32_e32 v208, v107, v107
	v_fmac_f32_e32 v208, v108, v108
	v_fmac_f32_e32 v208, v109, v109
	v_fmac_f32_e32 v208, v110, v110
	v_fmac_f32_e32 v208, v111, v111
	v_fmac_f32_e32 v208, v112, v112
	v_fmac_f32_e32 v208, v113, v113
	v_fmac_f32_e32 v208, v114, v114
	v_fmac_f32_e32 v208, v115, v115
	v_fmac_f32_e32 v208, v116, v116
	v_fmac_f32_e32 v208, v117, v117
	v_fmac_f32_e32 v208, v118, v118
	v_fmac_f32_e32 v208, v119, v119
	v_mov_b32_e32 v209, v208
	s_nop 1
	v_permlane16_swap_b32_e32 v208, v209
	v_add_f32_e32 v208, v208, v209
	v_mov_b32_e32 v209, v208
	s_nop 1
	v_permlane32_swap_b32_e32 v208, v209
	v_add_f32_e32 v208, v208, v209
	v_mov_b32_e32 v210, 0x358637bd
	v_fmac_f32_e32 v210, 0x3c800000, v208
	v_rsq_f32_e32 v210, v210
	s_add_u32 s24, s29, 3
	s_lshr_b32 s8, s24, 1
	s_lshl_b32 s8, s8, 12
	s_and_b32 s24, s24, 1
	s_lshl_b32 s24, s24, 8
	s_add_u32 s8, s8, s24
	v_mul_f32_e32 v210, v211, v210
	v_add_u32_e32 v212, s8, v23
	v_mul_f32_e32 v104, v104, v210
	v_mul_f32_e32 v105, v105, v210
	v_mul_f32_e32 v106, v106, v210
	v_mul_f32_e32 v107, v107, v210
	v_mul_f32_e32 v104, v104, v40
	v_mul_f32_e32 v105, v105, v41
	v_mul_f32_e32 v106, v106, v42
	v_mul_f32_e32 v107, v107, v43
	v_cvt_pk_f16_f32 v104, v104, v105
	v_cvt_pk_f16_f32 v105, v106, v107
	global_store_dwordx2 v212, v[104:105], s[22:23] offset:0
	v_mul_f32_e32 v108, v108, v210
	v_mul_f32_e32 v109, v109, v210
	v_mul_f32_e32 v110, v110, v210
	v_mul_f32_e32 v111, v111, v210
	v_mul_f32_e32 v108, v108, v44
	v_mul_f32_e32 v109, v109, v45
	v_mul_f32_e32 v110, v110, v46
	v_mul_f32_e32 v111, v111, v47
	v_cvt_pk_f16_f32 v108, v108, v109
	v_cvt_pk_f16_f32 v109, v110, v111
	global_store_dwordx2 v212, v[108:109], s[22:23] offset:1024
	v_mul_f32_e32 v112, v112, v210
	v_mul_f32_e32 v113, v113, v210
	v_mul_f32_e32 v114, v114, v210
	v_mul_f32_e32 v115, v115, v210
	v_mul_f32_e32 v112, v112, v48
	v_mul_f32_e32 v113, v113, v49
	v_mul_f32_e32 v114, v114, v50
	v_mul_f32_e32 v115, v115, v51
	v_cvt_pk_f16_f32 v112, v112, v113
	v_cvt_pk_f16_f32 v113, v114, v115
	global_store_dwordx2 v212, v[112:113], s[22:23] offset:2048
	v_mul_f32_e32 v116, v116, v210
	v_mul_f32_e32 v117, v117, v210
	v_mul_f32_e32 v118, v118, v210
	v_mul_f32_e32 v119, v119, v210
	v_mul_f32_e32 v116, v116, v52
	v_mul_f32_e32 v117, v117, v53
	v_mul_f32_e32 v118, v118, v54
	v_mul_f32_e32 v119, v119, v55
	v_cvt_pk_f16_f32 v116, v116, v117
	v_cvt_pk_f16_f32 v117, v118, v119
	global_store_dwordx2 v212, v[116:117], s[22:23] offset:3072
	s_branch .Lpf_done
.Lpf_vKA:
	s_mul_i32 s25, s25, 0x50
	s_add_u32 s29, s10, s25
	s_lshr_b32 s29, s29, 4
	v_add_u32_e32 v5, s25, v3
	v_lshlrev_b32_e32 v5, 7, v5
	v_add_u32_e32 v15, v5, v6
	v_add_u32_e32 v16, v5, v7
	v_add_u32_e32 v5, 0x9000, v9
	v_add_u32_e32 v17, v5, v6
	v_add_u32_e32 v18, v5, v7
	v_add_u32_e32 v19, 0x1a000, v15
	v_add_u32_e32 v20, 0x1a000, v16
	v_add_u32_e32 v21, 0x1a000, v17
	v_add_u32_e32 v22, 0x1a000, v18
	v_lshlrev_b32_e32 v5, 4, v4
	global_load_dwordx4 v[24:27], v5, s[14:15] offset:0
	global_load_dwordx4 v[28:31], v5, s[14:15] offset:64
	global_load_dwordx4 v[32:35], v5, s[14:15] offset:128
	global_load_dwordx4 v[36:39], v5, s[14:15] offset:192
	global_load_dwordx4 v[40:43], v5, s[16:17] offset:0
	global_load_dwordx4 v[44:47], v5, s[16:17] offset:64
	global_load_dwordx4 v[48:51], v5, s[16:17] offset:128
	global_load_dwordx4 v[52:55], v5, s[16:17] offset:192
	s_add_u32 m0, s28, 0x0
	s_nop 0
	global_load_lds_dwordx4 v10, s[4:5]
	s_add_u32 m0, s28, 0x2000
	s_nop 0
	global_load_lds_dwordx4 v11, s[4:5]
	s_add_u32 m0, s28, 0x4000
	s_nop 0
	global_load_lds_dwordx4 v12, s[4:5]
	s_add_u32 m0, s28, 0x6000
	s_nop 0
	global_load_lds_dwordx4 v13, s[4:5]
	s_add_u32 m0, s28, 0x8000
	s_nop 0
	global_load_lds_dwordx4 v14, s[4:5]
	s_add_u32 s4, s4, s20
	s_addc_u32 s5, s5, 0
	s_add_u32 m0, s28, 0x9000
	s_nop 0
	global_load_lds_dwordx4 v10, s[6:7]
	s_add_u32 m0, s28, 0xb000
	s_nop 0
	global_load_lds_dwordx4 v11, s[6:7]
	s_add_u32 s6, s6, s20
	s_addc_u32 s7, s7, 0
	s_add_u32 m0, s28, 0xd000
	s_nop 0
	global_load_lds_dwordx4 v10, s[4:5]
	s_add_u32 m0, s28, 0xf000
	s_nop 0
	global_load_lds_dwordx4 v11, s[4:5]
	s_add_u32 m0, s28, 0x11000
	s_nop 0
	global_load_lds_dwordx4 v12, s[4:5]
	s_add_u32 m0, s28, 0x13000
	s_nop 0
	global_load_lds_dwordx4 v13, s[4:5]
	s_add_u32 m0, s28, 0x15000
	s_nop 0
	global_load_lds_dwordx4 v14, s[4:5]
	s_add_u32 s4, s4, s20
	s_addc_u32 s5, s5, 0
	s_add_u32 m0, s28, 0x16000
	s_nop 0
	global_load_lds_dwordx4 v10, s[6:7]
	s_add_u32 m0, s28, 0x18000
	s_nop 0
	global_load_lds_dwordx4 v11, s[6:7]
	s_add_u32 s6, s6, s20
	s_addc_u32 s7, s7, 0
	s_add_u32 m0, s28, 0x1a000
	s_nop 0
	global_load_lds_dwordx4 v10, s[4:5]
	s_add_u32 m0, s28, 0x1c000
	s_nop 0
	global_load_lds_dwordx4 v11, s[4:5]
	s_add_u32 m0, s28, 0x1e000
	s_nop 0
	global_load_lds_dwordx4 v12, s[4:5]
	s_add_u32 m0, s28, 0x20000
	s_nop 0
	global_load_lds_dwordx4 v13, s[4:5]
	s_add_u32 m0, s28, 0x22000
	s_nop 0
	global_load_lds_dwordx4 v14, s[4:5]
	s_add_u32 s4, s4, s20
	s_addc_u32 s5, s5, 0
	s_add_u32 m0, s28, 0x23000
	s_nop 0
	global_load_lds_dwordx4 v10, s[6:7]
	s_add_u32 m0, s28, 0x25000
	s_nop 0
	global_load_lds_dwordx4 v11, s[6:7]
	s_add_u32 s6, s6, s20
	s_addc_u32 s7, s7, 0
	s_waitcnt vmcnt(14) lgkmcnt(0)
	s_barrier
	s_waitcnt lgkmcnt(6)
	ds_read_b128 v[136:139], v15
	ds_read_b128 v[156:159], v17
	ds_read_b128 v[160:163], v17 offset:2048
	ds_read_b128 v[164:167], v17 offset:4096
	ds_read_b128 v[168:171], v17 offset:6144
	ds_read_b128 v[140:143], v15 offset:2048
	ds_read_b128 v[144:147], v15 offset:4096
	ds_read_b128 v[148:151], v15 offset:6144
	ds_read_b128 v[152:155], v15 offset:8192
	s_waitcnt lgkmcnt(6)
	ds_read_b128 v[172:175], v16
	ds_read_b128 v[192:195], v18
	ds_read_b128 v[196:199], v18 offset:2048
	ds_read_b128 v[200:203], v18 offset:4096
	ds_read_b128 v[204:207], v18 offset:6144
	ds_read_b128 v[176:179], v16 offset:2048
	ds_read_b128 v[180:183], v16 offset:4096
	ds_read_b128 v[184:187], v16 offset:6144
	ds_read_b128 v[188:191], v16 offset:8192
	v_mfma_f32_16x16x32_f16 v[56:59], v[156:159], v[136:139], 0
	s_waitcnt lgkmcnt(15)
	v_mfma_f32_16x16x32_f16 v[60:63], v[160:163], v[136:139], 0
	s_waitcnt lgkmcnt(14)
	v_mfma_f32_16x16x32_f16 v[64:67], v[164:167], v[136:139], 0
	s_waitcnt lgkmcnt(13)
	v_mfma_f32_16x16x32_f16 v[68:71], v[168:171], v[136:139], 0
	s_waitcnt lgkmcnt(12)
	v_mfma_f32_16x16x32_f16 v[72:75], v[156:159], v[140:143], 0
	v_mfma_f32_16x16x32_f16 v[76:79], v[160:163], v[140:143], 0
	v_mfma_f32_16x16x32_f16 v[80:83], v[164:167], v[140:143], 0
	v_mfma_f32_16x16x32_f16 v[84:87], v[168:171], v[140:143], 0
	s_waitcnt lgkmcnt(11)
	v_mfma_f32_16x16x32_f16 v[88:91], v[156:159], v[144:147], 0
	v_mfma_f32_16x16x32_f16 v[92:95], v[160:163], v[144:147], 0
	v_mfma_f32_16x16x32_f16 v[96:99], v[164:167], v[144:147], 0
	v_mfma_f32_16x16x32_f16 v[100:103], v[168:171], v[144:147], 0
	s_waitcnt lgkmcnt(10)
	v_mfma_f32_16x16x32_f16 v[104:107], v[156:159], v[148:151], 0
	v_mfma_f32_16x16x32_f16 v[108:111], v[160:163], v[148:151], 0
	v_mfma_f32_16x16x32_f16 v[112:115], v[164:167], v[148:151], 0
	v_mfma_f32_16x16x32_f16 v[116:119], v[168:171], v[148:151], 0
	s_waitcnt lgkmcnt(9)
	v_mfma_f32_16x16x32_f16 v[120:123], v[156:159], v[152:155], 0
	v_mfma_f32_16x16x32_f16 v[124:127], v[160:163], v[152:155], 0
	v_mfma_f32_16x16x32_f16 v[128:131], v[164:167], v[152:155], 0
	v_mfma_f32_16x16x32_f16 v[132:135], v[168:171], v[152:155], 0
	s_waitcnt vmcnt(7) lgkmcnt(0)
	s_barrier
	s_waitcnt lgkmcnt(6)
	ds_read_b128 v[136:139], v15 offset:53248
	ds_read_b128 v[156:159], v17 offset:53248
	ds_read_b128 v[160:163], v17 offset:55296
	ds_read_b128 v[164:167], v17 offset:57344
	ds_read_b128 v[168:171], v17 offset:59392
	ds_read_b128 v[140:143], v15 offset:55296
	ds_read_b128 v[144:147], v15 offset:57344
	ds_read_b128 v[148:151], v15 offset:59392
	ds_read_b128 v[152:155], v15 offset:61440
	v_mfma_f32_16x16x32_f16 v[56:59], v[192:195], v[172:175], v[56:59]
	s_add_u32 m0, s28, 0x0
	s_nop 0
	global_load_lds_dwordx4 v10, s[4:5]
	s_waitcnt lgkmcnt(15)
	v_mfma_f32_16x16x32_f16 v[60:63], v[196:199], v[172:175], v[60:63]
	s_waitcnt lgkmcnt(14)
	v_mfma_f32_16x16x32_f16 v[64:67], v[200:203], v[172:175], v[64:67]
	s_waitcnt lgkmcnt(13)
	v_mfma_f32_16x16x32_f16 v[68:71], v[204:207], v[172:175], v[68:71]
	s_waitcnt lgkmcnt(12)
	v_mfma_f32_16x16x32_f16 v[72:75], v[192:195], v[176:179], v[72:75]
	v_mfma_f32_16x16x32_f16 v[76:79], v[196:199], v[176:179], v[76:79]
	s_add_u32 m0, s28, 0x2000
	s_nop 0
	global_load_lds_dwordx4 v11, s[4:5]
	v_mfma_f32_16x16x32_f16 v[80:83], v[200:203], v[176:179], v[80:83]
	v_mfma_f32_16x16x32_f16 v[84:87], v[204:207], v[176:179], v[84:87]
	s_waitcnt lgkmcnt(11)
	v_mfma_f32_16x16x32_f16 v[88:91], v[192:195], v[180:183], v[88:91]
	v_mfma_f32_16x16x32_f16 v[92:95], v[196:199], v[180:183], v[92:95]
	v_mfma_f32_16x16x32_f16 v[96:99], v[200:203], v[180:183], v[96:99]
	s_add_u32 m0, s28, 0x4000
	s_nop 0
	global_load_lds_dwordx4 v12, s[4:5]
	v_mfma_f32_16x16x32_f16 v[100:103], v[204:207], v[180:183], v[100:103]
	s_waitcnt lgkmcnt(10)
	v_mfma_f32_16x16x32_f16 v[104:107], v[192:195], v[184:187], v[104:107]
	v_mfma_f32_16x16x32_f16 v[108:111], v[196:199], v[184:187], v[108:111]
	v_mfma_f32_16x16x32_f16 v[112:115], v[200:203], v[184:187], v[112:115]
	v_mfma_f32_16x16x32_f16 v[116:119], v[204:207], v[184:187], v[116:119]
	s_add_u32 m0, s28, 0x6000
	s_nop 0
	global_load_lds_dwordx4 v13, s[4:5]
	s_waitcnt lgkmcnt(9)
	v_mfma_f32_16x16x32_f16 v[120:123], v[192:195], v[188:191], v[120:123]
	v_mfma_f32_16x16x32_f16 v[124:127], v[196:199], v[188:191], v[124:127]
	v_mfma_f32_16x16x32_f16 v[128:131], v[200:203], v[188:191], v[128:131]
	v_mfma_f32_16x16x32_f16 v[132:135], v[204:207], v[188:191], v[132:135]
	s_waitcnt lgkmcnt(6)
	ds_read_b128 v[172:175], v16 offset:53248
	ds_read_b128 v[192:195], v18 offset:53248
	ds_read_b128 v[196:199], v18 offset:55296
	ds_read_b128 v[200:203], v18 offset:57344
	ds_read_b128 v[204:207], v18 offset:59392
	ds_read_b128 v[176:179], v16 offset:55296
	ds_read_b128 v[180:183], v16 offset:57344
	ds_read_b128 v[184:187], v16 offset:59392
	ds_read_b128 v[188:191], v16 offset:61440
	v_mfma_f32_16x16x32_f16 v[56:59], v[156:159], v[136:139], v[56:59]
	s_add_u32 m0, s28, 0x8000
	s_nop 0
	global_load_lds_dwordx4 v14, s[4:5]
	s_add_u32 s4, s4, s20
	s_addc_u32 s5, s5, 0
	s_waitcnt lgkmcnt(15)
	v_mfma_f32_16x16x32_f16 v[60:63], v[160:163], v[136:139], v[60:63]
	s_waitcnt lgkmcnt(14)
	v_mfma_f32_16x16x32_f16 v[64:67], v[164:167], v[136:139], v[64:67]
	s_waitcnt lgkmcnt(13)
	v_mfma_f32_16x16x32_f16 v[68:71], v[168:171], v[136:139], v[68:71]
	s_waitcnt lgkmcnt(12)
	v_mfma_f32_16x16x32_f16 v[72:75], v[156:159], v[140:143], v[72:75]
	v_mfma_f32_16x16x32_f16 v[76:79], v[160:163], v[140:143], v[76:79]
	v_mfma_f32_16x16x32_f16 v[80:83], v[164:167], v[140:143], v[80:83]
	s_add_u32 m0, s28, 0x9000
	s_nop 0
	global_load_lds_dwordx4 v10, s[6:7]
	v_mfma_f32_16x16x32_f16 v[84:87], v[168:171], v[140:143], v[84:87]
	s_waitcnt lgkmcnt(11)
	v_mfma_f32_16x16x32_f16 v[88:91], v[156:159], v[144:147], v[88:91]
	v_mfma_f32_16x16x32_f16 v[92:95], v[160:163], v[144:147], v[92:95]
	v_mfma_f32_16x16x32_f16 v[96:99], v[164:167], v[144:147], v[96:99]
	v_mfma_f32_16x16x32_f16 v[100:103], v[168:171], v[144:147], v[100:103]
	s_waitcnt lgkmcnt(10)
	v_mfma_f32_16x16x32_f16 v[104:107], v[156:159], v[148:151], v[104:107]
	v_mfma_f32_16x16x32_f16 v[108:111], v[160:163], v[148:151], v[108:111]
	s_add_u32 m0, s28, 0xb000
	s_nop 0
	global_load_lds_dwordx4 v11, s[6:7]
	s_add_u32 s6, s6, s20
	s_addc_u32 s7, s7, 0
	v_mfma_f32_16x16x32_f16 v[112:115], v[164:167], v[148:151], v[112:115]
	v_mfma_f32_16x16x32_f16 v[116:119], v[168:171], v[148:151], v[116:119]
	s_waitcnt lgkmcnt(9)
	v_mfma_f32_16x16x32_f16 v[120:123], v[156:159], v[152:155], v[120:123]
	v_mfma_f32_16x16x32_f16 v[124:127], v[160:163], v[152:155], v[124:127]
	v_mfma_f32_16x16x32_f16 v[128:131], v[164:167], v[152:155], v[128:131]
	v_mfma_f32_16x16x32_f16 v[132:135], v[168:171], v[152:155], v[132:135]
	s_waitcnt vmcnt(7) lgkmcnt(0)
	s_barrier
	s_waitcnt lgkmcnt(6)
	ds_read_b128 v[136:139], v19
	ds_read_b128 v[156:159], v21
	ds_read_b128 v[160:163], v21 offset:2048
	ds_read_b128 v[164:167], v21 offset:4096
	ds_read_b128 v[168:171], v21 offset:6144
	ds_read_b128 v[140:143], v19 offset:2048
	ds_read_b128 v[144:147], v19 offset:4096
	ds_read_b128 v[148:151], v19 offset:6144
	ds_read_b128 v[152:155], v19 offset:8192
	v_mfma_f32_16x16x32_f16 v[56:59], v[192:195], v[172:175], v[56:59]
	s_add_u32 m0, s28, 0xd000
	s_nop 0
	global_load_lds_dwordx4 v10, s[4:5]
	s_waitcnt lgkmcnt(15)
	v_mfma_f32_16x16x32_f16 v[60:63], v[196:199], v[172:175], v[60:63]
	s_waitcnt lgkmcnt(14)
	v_mfma_f32_16x16x32_f16 v[64:67], v[200:203], v[172:175], v[64:67]
	s_waitcnt lgkmcnt(13)
	v_mfma_f32_16x16x32_f16 v[68:71], v[204:207], v[172:175], v[68:71]
	s_waitcnt lgkmcnt(12)
	v_mfma_f32_16x16x32_f16 v[72:75], v[192:195], v[176:179], v[72:75]
	v_mfma_f32_16x16x32_f16 v[76:79], v[196:199], v[176:179], v[76:79]
	s_add_u32 m0, s28, 0xf000
	s_nop 0
	global_load_lds_dwordx4 v11, s[4:5]
	v_mfma_f32_16x16x32_f16 v[80:83], v[200:203], v[176:179], v[80:83]
	v_mfma_f32_16x16x32_f16 v[84:87], v[204:207], v[176:179], v[84:87]
	s_waitcnt lgkmcnt(11)
	v_mfma_f32_16x16x32_f16 v[88:91], v[192:195], v[180:183], v[88:91]
	v_mfma_f32_16x16x32_f16 v[92:95], v[196:199], v[180:183], v[92:95]
	v_mfma_f32_16x16x32_f16 v[96:99], v[200:203], v[180:183], v[96:99]
	s_add_u32 m0, s28, 0x11000
	s_nop 0
	global_load_lds_dwordx4 v12, s[4:5]
	v_mfma_f32_16x16x32_f16 v[100:103], v[204:207], v[180:183], v[100:103]
	s_waitcnt lgkmcnt(10)
	v_mfma_f32_16x16x32_f16 v[104:107], v[192:195], v[184:187], v[104:107]
	v_mfma_f32_16x16x32_f16 v[108:111], v[196:199], v[184:187], v[108:111]
	v_mfma_f32_16x16x32_f16 v[112:115], v[200:203], v[184:187], v[112:115]
	v_mfma_f32_16x16x32_f16 v[116:119], v[204:207], v[184:187], v[116:119]
	s_add_u32 m0, s28, 0x13000
	s_nop 0
	global_load_lds_dwordx4 v13, s[4:5]
	s_waitcnt lgkmcnt(9)
	v_mfma_f32_16x16x32_f16 v[120:123], v[192:195], v[188:191], v[120:123]
	v_mfma_f32_16x16x32_f16 v[124:127], v[196:199], v[188:191], v[124:127]
	v_mfma_f32_16x16x32_f16 v[128:131], v[200:203], v[188:191], v[128:131]
	v_mfma_f32_16x16x32_f16 v[132:135], v[204:207], v[188:191], v[132:135]
	s_waitcnt lgkmcnt(6)
	ds_read_b128 v[172:175], v20
	ds_read_b128 v[192:195], v22
	ds_read_b128 v[196:199], v22 offset:2048
	ds_read_b128 v[200:203], v22 offset:4096
	ds_read_b128 v[204:207], v22 offset:6144
	ds_read_b128 v[176:179], v20 offset:2048
	ds_read_b128 v[180:183], v20 offset:4096
	ds_read_b128 v[184:187], v20 offset:6144
	ds_read_b128 v[188:191], v20 offset:8192
	v_mfma_f32_16x16x32_f16 v[56:59], v[156:159], v[136:139], v[56:59]
	s_add_u32 m0, s28, 0x15000
	s_nop 0
	global_load_lds_dwordx4 v14, s[4:5]
	s_add_u32 s4, s4, s20
	s_addc_u32 s5, s5, 0
	s_waitcnt lgkmcnt(15)
	v_mfma_f32_16x16x32_f16 v[60:63], v[160:163], v[136:139], v[60:63]
	s_waitcnt lgkmcnt(14)
	v_mfma_f32_16x16x32_f16 v[64:67], v[164:167], v[136:139], v[64:67]
	s_waitcnt lgkmcnt(13)
	v_mfma_f32_16x16x32_f16 v[68:71], v[168:171], v[136:139], v[68:71]
	s_waitcnt lgkmcnt(12)
	v_mfma_f32_16x16x32_f16 v[72:75], v[156:159], v[140:143], v[72:75]
	v_mfma_f32_16x16x32_f16 v[76:79], v[160:163], v[140:143], v[76:79]
	v_mfma_f32_16x16x32_f16 v[80:83], v[164:167], v[140:143], v[80:83]
	s_add_u32 m0, s28, 0x16000
	s_nop 0
	global_load_lds_dwordx4 v10, s[6:7]
	v_mfma_f32_16x16x32_f16 v[84:87], v[168:171], v[140:143], v[84:87]
	s_waitcnt lgkmcnt(11)
	v_mfma_f32_16x16x32_f16 v[88:91], v[156:159], v[144:147], v[88:91]
	v_mfma_f32_16x16x32_f16 v[92:95], v[160:163], v[144:147], v[92:95]
	v_mfma_f32_16x16x32_f16 v[96:99], v[164:167], v[144:147], v[96:99]
	v_mfma_f32_16x16x32_f16 v[100:103], v[168:171], v[144:147], v[100:103]
	s_waitcnt lgkmcnt(10)
	v_mfma_f32_16x16x32_f16 v[104:107], v[156:159], v[148:151], v[104:107]
	v_mfma_f32_16x16x32_f16 v[108:111], v[160:163], v[148:151], v[108:111]
	s_add_u32 m0, s28, 0x18000
	s_nop 0
	global_load_lds_dwordx4 v11, s[6:7]
	s_add_u32 s6, s6, s20
	s_addc_u32 s7, s7, 0
	v_mfma_f32_16x16x32_f16 v[112:115], v[164:167], v[148:151], v[112:115]
	v_mfma_f32_16x16x32_f16 v[116:119], v[168:171], v[148:151], v[116:119]
	s_waitcnt lgkmcnt(9)
	v_mfma_f32_16x16x32_f16 v[120:123], v[156:159], v[152:155], v[120:123]
	v_mfma_f32_16x16x32_f16 v[124:127], v[160:163], v[152:155], v[124:127]
	v_mfma_f32_16x16x32_f16 v[128:131], v[164:167], v[152:155], v[128:131]
	v_mfma_f32_16x16x32_f16 v[132:135], v[168:171], v[152:155], v[132:135]
	s_waitcnt vmcnt(7) lgkmcnt(0)
	s_barrier
	s_waitcnt lgkmcnt(6)
	ds_read_b128 v[136:139], v15
	ds_read_b128 v[156:159], v17
	ds_read_b128 v[160:163], v17 offset:2048
	ds_read_b128 v[164:167], v17 offset:4096
	ds_read_b128 v[168:171], v17 offset:6144
	ds_read_b128 v[140:143], v15 offset:2048
	ds_read_b128 v[144:147], v15 offset:4096
	ds_read_b128 v[148:151], v15 offset:6144
	ds_read_b128 v[152:155], v15 offset:8192
	v_mfma_f32_16x16x32_f16 v[56:59], v[192:195], v[172:175], v[56:59]
	s_add_u32 m0, s28, 0x1a000
	s_nop 0
	global_load_lds_dwordx4 v10, s[4:5]
	s_waitcnt lgkmcnt(15)
	v_mfma_f32_16x16x32_f16 v[60:63], v[196:199], v[172:175], v[60:63]
	s_waitcnt lgkmcnt(14)
	v_mfma_f32_16x16x32_f16 v[64:67], v[200:203], v[172:175], v[64:67]
	s_waitcnt lgkmcnt(13)
	v_mfma_f32_16x16x32_f16 v[68:71], v[204:207], v[172:175], v[68:71]
	s_waitcnt lgkmcnt(12)
	v_mfma_f32_16x16x32_f16 v[72:75], v[192:195], v[176:179], v[72:75]
	v_mfma_f32_16x16x32_f16 v[76:79], v[196:199], v[176:179], v[76:79]
	s_add_u32 m0, s28, 0x1c000
	s_nop 0
	global_load_lds_dwordx4 v11, s[4:5]
	v_mfma_f32_16x16x32_f16 v[80:83], v[200:203], v[176:179], v[80:83]
	v_mfma_f32_16x16x32_f16 v[84:87], v[204:207], v[176:179], v[84:87]
	s_waitcnt lgkmcnt(11)
	v_mfma_f32_16x16x32_f16 v[88:91], v[192:195], v[180:183], v[88:91]
	v_mfma_f32_16x16x32_f16 v[92:95], v[196:199], v[180:183], v[92:95]
	v_mfma_f32_16x16x32_f16 v[96:99], v[200:203], v[180:183], v[96:99]
	s_add_u32 m0, s28, 0x1e000
	s_nop 0
	global_load_lds_dwordx4 v12, s[4:5]
	v_mfma_f32_16x16x32_f16 v[100:103], v[204:207], v[180:183], v[100:103]
	s_waitcnt lgkmcnt(10)
	v_mfma_f32_16x16x32_f16 v[104:107], v[192:195], v[184:187], v[104:107]
	v_mfma_f32_16x16x32_f16 v[108:111], v[196:199], v[184:187], v[108:111]
	v_mfma_f32_16x16x32_f16 v[112:115], v[200:203], v[184:187], v[112:115]
	v_mfma_f32_16x16x32_f16 v[116:119], v[204:207], v[184:187], v[116:119]
	s_add_u32 m0, s28, 0x20000
	s_nop 0
	global_load_lds_dwordx4 v13, s[4:5]
	s_waitcnt lgkmcnt(9)
	v_mfma_f32_16x16x32_f16 v[120:123], v[192:195], v[188:191], v[120:123]
	v_mfma_f32_16x16x32_f16 v[124:127], v[196:199], v[188:191], v[124:127]
	v_mfma_f32_16x16x32_f16 v[128:131], v[200:203], v[188:191], v[128:131]
	v_mfma_f32_16x16x32_f16 v[132:135], v[204:207], v[188:191], v[132:135]
	s_waitcnt lgkmcnt(6)
	ds_read_b128 v[172:175], v16
	ds_read_b128 v[192:195], v18
	ds_read_b128 v[196:199], v18 offset:2048
	ds_read_b128 v[200:203], v18 offset:4096
	ds_read_b128 v[204:207], v18 offset:6144
	ds_read_b128 v[176:179], v16 offset:2048
	ds_read_b128 v[180:183], v16 offset:4096
	ds_read_b128 v[184:187], v16 offset:6144
	ds_read_b128 v[188:191], v16 offset:8192
	v_mfma_f32_16x16x32_f16 v[56:59], v[156:159], v[136:139], v[56:59]
	s_add_u32 m0, s28, 0x22000
	s_nop 0
	global_load_lds_dwordx4 v14, s[4:5]
	s_add_u32 s4, s4, s20
	s_addc_u32 s5, s5, 0
	s_waitcnt lgkmcnt(15)
	v_mfma_f32_16x16x32_f16 v[60:63], v[160:163], v[136:139], v[60:63]
	s_waitcnt lgkmcnt(14)
	v_mfma_f32_16x16x32_f16 v[64:67], v[164:167], v[136:139], v[64:67]
	s_waitcnt lgkmcnt(13)
	v_mfma_f32_16x16x32_f16 v[68:71], v[168:171], v[136:139], v[68:71]
	s_waitcnt lgkmcnt(12)
	v_mfma_f32_16x16x32_f16 v[72:75], v[156:159], v[140:143], v[72:75]
	v_mfma_f32_16x16x32_f16 v[76:79], v[160:163], v[140:143], v[76:79]
	v_mfma_f32_16x16x32_f16 v[80:83], v[164:167], v[140:143], v[80:83]
	s_add_u32 m0, s28, 0x23000
	s_nop 0
	global_load_lds_dwordx4 v10, s[6:7]
	v_mfma_f32_16x16x32_f16 v[84:87], v[168:171], v[140:143], v[84:87]
	s_waitcnt lgkmcnt(11)
	v_mfma_f32_16x16x32_f16 v[88:91], v[156:159], v[144:147], v[88:91]
	v_mfma_f32_16x16x32_f16 v[92:95], v[160:163], v[144:147], v[92:95]
	v_mfma_f32_16x16x32_f16 v[96:99], v[164:167], v[144:147], v[96:99]
	v_mfma_f32_16x16x32_f16 v[100:103], v[168:171], v[144:147], v[100:103]
	s_waitcnt lgkmcnt(10)
	v_mfma_f32_16x16x32_f16 v[104:107], v[156:159], v[148:151], v[104:107]
	v_mfma_f32_16x16x32_f16 v[108:111], v[160:163], v[148:151], v[108:111]
	s_add_u32 m0, s28, 0x25000
	s_nop 0
	global_load_lds_dwordx4 v11, s[6:7]
	s_add_u32 s6, s6, s20
	s_addc_u32 s7, s7, 0
	v_mfma_f32_16x16x32_f16 v[112:115], v[164:167], v[148:151], v[112:115]
	v_mfma_f32_16x16x32_f16 v[116:119], v[168:171], v[148:151], v[116:119]
	s_waitcnt lgkmcnt(9)
	v_mfma_f32_16x16x32_f16 v[120:123], v[156:159], v[152:155], v[120:123]
	v_mfma_f32_16x16x32_f16 v[124:127], v[160:163], v[152:155], v[124:127]
	v_mfma_f32_16x16x32_f16 v[128:131], v[164:167], v[152:155], v[128:131]
	v_mfma_f32_16x16x32_f16 v[132:135], v[168:171], v[152:155], v[132:135]
	s_waitcnt vmcnt(7) lgkmcnt(0)
	s_barrier
	s_waitcnt lgkmcnt(6)
	ds_read_b128 v[136:139], v15 offset:53248
	ds_read_b128 v[156:159], v17 offset:53248
	ds_read_b128 v[160:163], v17 offset:55296
	ds_read_b128 v[164:167], v17 offset:57344
	ds_read_b128 v[168:171], v17 offset:59392
	ds_read_b128 v[140:143], v15 offset:55296
	ds_read_b128 v[144:147], v15 offset:57344
	ds_read_b128 v[148:151], v15 offset:59392
	ds_read_b128 v[152:155], v15 offset:61440
	v_mfma_f32_16x16x32_f16 v[56:59], v[192:195], v[172:175], v[56:59]
	s_add_u32 m0, s28, 0x0
	s_nop 0
	global_load_lds_dwordx4 v10, s[4:5]
	s_waitcnt lgkmcnt(15)
	v_mfma_f32_16x16x32_f16 v[60:63], v[196:199], v[172:175], v[60:63]
	s_waitcnt lgkmcnt(14)
	v_mfma_f32_16x16x32_f16 v[64:67], v[200:203], v[172:175], v[64:67]
	s_waitcnt lgkmcnt(13)
	v_mfma_f32_16x16x32_f16 v[68:71], v[204:207], v[172:175], v[68:71]
	s_waitcnt lgkmcnt(12)
	v_mfma_f32_16x16x32_f16 v[72:75], v[192:195], v[176:179], v[72:75]
	v_mfma_f32_16x16x32_f16 v[76:79], v[196:199], v[176:179], v[76:79]
	s_add_u32 m0, s28, 0x2000
	s_nop 0
	global_load_lds_dwordx4 v11, s[4:5]
	v_mfma_f32_16x16x32_f16 v[80:83], v[200:203], v[176:179], v[80:83]
	v_mfma_f32_16x16x32_f16 v[84:87], v[204:207], v[176:179], v[84:87]
	s_waitcnt lgkmcnt(11)
	v_mfma_f32_16x16x32_f16 v[88:91], v[192:195], v[180:183], v[88:91]
	v_mfma_f32_16x16x32_f16 v[92:95], v[196:199], v[180:183], v[92:95]
	v_mfma_f32_16x16x32_f16 v[96:99], v[200:203], v[180:183], v[96:99]
	s_add_u32 m0, s28, 0x4000
	s_nop 0
	global_load_lds_dwordx4 v12, s[4:5]
	v_mfma_f32_16x16x32_f16 v[100:103], v[204:207], v[180:183], v[100:103]
	s_waitcnt lgkmcnt(10)
	v_mfma_f32_16x16x32_f16 v[104:107], v[192:195], v[184:187], v[104:107]
	v_mfma_f32_16x16x32_f16 v[108:111], v[196:199], v[184:187], v[108:111]
	v_mfma_f32_16x16x32_f16 v[112:115], v[200:203], v[184:187], v[112:115]
	v_mfma_f32_16x16x32_f16 v[116:119], v[204:207], v[184:187], v[116:119]
	s_add_u32 m0, s28, 0x6000
	s_nop 0
	global_load_lds_dwordx4 v13, s[4:5]
	s_waitcnt lgkmcnt(9)
	v_mfma_f32_16x16x32_f16 v[120:123], v[192:195], v[188:191], v[120:123]
	v_mfma_f32_16x16x32_f16 v[124:127], v[196:199], v[188:191], v[124:127]
	v_mfma_f32_16x16x32_f16 v[128:131], v[200:203], v[188:191], v[128:131]
	v_mfma_f32_16x16x32_f16 v[132:135], v[204:207], v[188:191], v[132:135]
	s_waitcnt lgkmcnt(6)
	ds_read_b128 v[172:175], v16 offset:53248
	ds_read_b128 v[192:195], v18 offset:53248
	ds_read_b128 v[196:199], v18 offset:55296
	ds_read_b128 v[200:203], v18 offset:57344
	ds_read_b128 v[204:207], v18 offset:59392
	ds_read_b128 v[176:179], v16 offset:55296
	ds_read_b128 v[180:183], v16 offset:57344
	ds_read_b128 v[184:187], v16 offset:59392
	ds_read_b128 v[188:191], v16 offset:61440
	v_mfma_f32_16x16x32_f16 v[56:59], v[156:159], v[136:139], v[56:59]
	s_add_u32 m0, s28, 0x8000
	s_nop 0
	global_load_lds_dwordx4 v14, s[4:5]
	s_add_u32 s4, s4, s20
	s_addc_u32 s5, s5, 0
	s_waitcnt lgkmcnt(15)
	v_mfma_f32_16x16x32_f16 v[60:63], v[160:163], v[136:139], v[60:63]
	s_waitcnt lgkmcnt(14)
	v_mfma_f32_16x16x32_f16 v[64:67], v[164:167], v[136:139], v[64:67]
	s_waitcnt lgkmcnt(13)
	v_mfma_f32_16x16x32_f16 v[68:71], v[168:171], v[136:139], v[68:71]
	s_waitcnt lgkmcnt(12)
	v_mfma_f32_16x16x32_f16 v[72:75], v[156:159], v[140:143], v[72:75]
	v_mfma_f32_16x16x32_f16 v[76:79], v[160:163], v[140:143], v[76:79]
	v_mfma_f32_16x16x32_f16 v[80:83], v[164:167], v[140:143], v[80:83]
	s_add_u32 m0, s28, 0x9000
	s_nop 0
	global_load_lds_dwordx4 v10, s[6:7]
	v_mfma_f32_16x16x32_f16 v[84:87], v[168:171], v[140:143], v[84:87]
	s_waitcnt lgkmcnt(11)
	v_mfma_f32_16x16x32_f16 v[88:91], v[156:159], v[144:147], v[88:91]
	v_mfma_f32_16x16x32_f16 v[92:95], v[160:163], v[144:147], v[92:95]
	v_mfma_f32_16x16x32_f16 v[96:99], v[164:167], v[144:147], v[96:99]
	v_mfma_f32_16x16x32_f16 v[100:103], v[168:171], v[144:147], v[100:103]
	s_waitcnt lgkmcnt(10)
	v_mfma_f32_16x16x32_f16 v[104:107], v[156:159], v[148:151], v[104:107]
	v_mfma_f32_16x16x32_f16 v[108:111], v[160:163], v[148:151], v[108:111]
	s_add_u32 m0, s28, 0xb000
	s_nop 0
	global_load_lds_dwordx4 v11, s[6:7]
	s_add_u32 s6, s6, s20
	s_addc_u32 s7, s7, 0
	v_mfma_f32_16x16x32_f16 v[112:115], v[164:167], v[148:151], v[112:115]
	v_mfma_f32_16x16x32_f16 v[116:119], v[168:171], v[148:151], v[116:119]
	s_waitcnt lgkmcnt(9)
	v_mfma_f32_16x16x32_f16 v[120:123], v[156:159], v[152:155], v[120:123]
	v_mfma_f32_16x16x32_f16 v[124:127], v[160:163], v[152:155], v[124:127]
	v_mfma_f32_16x16x32_f16 v[128:131], v[164:167], v[152:155], v[128:131]
	v_mfma_f32_16x16x32_f16 v[132:135], v[168:171], v[152:155], v[132:135]
	s_waitcnt vmcnt(7) lgkmcnt(0)
	s_barrier
	s_waitcnt lgkmcnt(6)
	ds_read_b128 v[136:139], v19
	ds_read_b128 v[156:159], v21
	ds_read_b128 v[160:163], v21 offset:2048
	ds_read_b128 v[164:167], v21 offset:4096
	ds_read_b128 v[168:171], v21 offset:6144
	ds_read_b128 v[140:143], v19 offset:2048
	ds_read_b128 v[144:147], v19 offset:4096
	ds_read_b128 v[148:151], v19 offset:6144
	ds_read_b128 v[152:155], v19 offset:8192
	v_mfma_f32_16x16x32_f16 v[56:59], v[192:195], v[172:175], v[56:59]
	s_add_u32 m0, s28, 0xd000
	s_nop 0
	global_load_lds_dwordx4 v10, s[4:5]
	s_waitcnt lgkmcnt(15)
	v_mfma_f32_16x16x32_f16 v[60:63], v[196:199], v[172:175], v[60:63]
	s_waitcnt lgkmcnt(14)
	v_mfma_f32_16x16x32_f16 v[64:67], v[200:203], v[172:175], v[64:67]
	s_waitcnt lgkmcnt(13)
	v_mfma_f32_16x16x32_f16 v[68:71], v[204:207], v[172:175], v[68:71]
	s_waitcnt lgkmcnt(12)
	v_mfma_f32_16x16x32_f16 v[72:75], v[192:195], v[176:179], v[72:75]
	v_mfma_f32_16x16x32_f16 v[76:79], v[196:199], v[176:179], v[76:79]
	s_add_u32 m0, s28, 0xf000
	s_nop 0
	global_load_lds_dwordx4 v11, s[4:5]
	v_mfma_f32_16x16x32_f16 v[80:83], v[200:203], v[176:179], v[80:83]
	v_mfma_f32_16x16x32_f16 v[84:87], v[204:207], v[176:179], v[84:87]
	s_waitcnt lgkmcnt(11)
	v_mfma_f32_16x16x32_f16 v[88:91], v[192:195], v[180:183], v[88:91]
	v_mfma_f32_16x16x32_f16 v[92:95], v[196:199], v[180:183], v[92:95]
	v_mfma_f32_16x16x32_f16 v[96:99], v[200:203], v[180:183], v[96:99]
	s_add_u32 m0, s28, 0x11000
	s_nop 0
	global_load_lds_dwordx4 v12, s[4:5]
	v_mfma_f32_16x16x32_f16 v[100:103], v[204:207], v[180:183], v[100:103]
	s_waitcnt lgkmcnt(10)
	v_mfma_f32_16x16x32_f16 v[104:107], v[192:195], v[184:187], v[104:107]
	v_mfma_f32_16x16x32_f16 v[108:111], v[196:199], v[184:187], v[108:111]
	v_mfma_f32_16x16x32_f16 v[112:115], v[200:203], v[184:187], v[112:115]
	v_mfma_f32_16x16x32_f16 v[116:119], v[204:207], v[184:187], v[116:119]
	s_add_u32 m0, s28, 0x13000
	s_nop 0
	global_load_lds_dwordx4 v13, s[4:5]
	s_waitcnt lgkmcnt(9)
	v_mfma_f32_16x16x32_f16 v[120:123], v[192:195], v[188:191], v[120:123]
	v_mfma_f32_16x16x32_f16 v[124:127], v[196:199], v[188:191], v[124:127]
	v_mfma_f32_16x16x32_f16 v[128:131], v[200:203], v[188:191], v[128:131]
	v_mfma_f32_16x16x32_f16 v[132:135], v[204:207], v[188:191], v[132:135]
	s_waitcnt lgkmcnt(6)
	ds_read_b128 v[172:175], v20
	ds_read_b128 v[192:195], v22
	ds_read_b128 v[196:199], v22 offset:2048
	ds_read_b128 v[200:203], v22 offset:4096
	ds_read_b128 v[204:207], v22 offset:6144
	ds_read_b128 v[176:179], v20 offset:2048
	ds_read_b128 v[180:183], v20 offset:4096
	ds_read_b128 v[184:187], v20 offset:6144
	ds_read_b128 v[188:191], v20 offset:8192
	v_mfma_f32_16x16x32_f16 v[56:59], v[156:159], v[136:139], v[56:59]
	s_add_u32 m0, s28, 0x15000
	s_nop 0
	global_load_lds_dwordx4 v14, s[4:5]
	s_add_u32 s4, s4, s20
	s_addc_u32 s5, s5, 0
	s_waitcnt lgkmcnt(15)
	v_mfma_f32_16x16x32_f16 v[60:63], v[160:163], v[136:139], v[60:63]
	s_waitcnt lgkmcnt(14)
	v_mfma_f32_16x16x32_f16 v[64:67], v[164:167], v[136:139], v[64:67]
	s_waitcnt lgkmcnt(13)
	v_mfma_f32_16x16x32_f16 v[68:71], v[168:171], v[136:139], v[68:71]
	s_waitcnt lgkmcnt(12)
	v_mfma_f32_16x16x32_f16 v[72:75], v[156:159], v[140:143], v[72:75]
	v_mfma_f32_16x16x32_f16 v[76:79], v[160:163], v[140:143], v[76:79]
	v_mfma_f32_16x16x32_f16 v[80:83], v[164:167], v[140:143], v[80:83]
	s_add_u32 m0, s28, 0x16000
	s_nop 0
	global_load_lds_dwordx4 v10, s[6:7]
	v_mfma_f32_16x16x32_f16 v[84:87], v[168:171], v[140:143], v[84:87]
	s_waitcnt lgkmcnt(11)
	v_mfma_f32_16x16x32_f16 v[88:91], v[156:159], v[144:147], v[88:91]
	v_mfma_f32_16x16x32_f16 v[92:95], v[160:163], v[144:147], v[92:95]
	v_mfma_f32_16x16x32_f16 v[96:99], v[164:167], v[144:147], v[96:99]
	v_mfma_f32_16x16x32_f16 v[100:103], v[168:171], v[144:147], v[100:103]
	s_waitcnt lgkmcnt(10)
	v_mfma_f32_16x16x32_f16 v[104:107], v[156:159], v[148:151], v[104:107]
	v_mfma_f32_16x16x32_f16 v[108:111], v[160:163], v[148:151], v[108:111]
	s_add_u32 m0, s28, 0x18000
	s_nop 0
	global_load_lds_dwordx4 v11, s[6:7]
	s_add_u32 s6, s6, s20
	s_addc_u32 s7, s7, 0
	v_mfma_f32_16x16x32_f16 v[112:115], v[164:167], v[148:151], v[112:115]
	v_mfma_f32_16x16x32_f16 v[116:119], v[168:171], v[148:151], v[116:119]
	s_waitcnt lgkmcnt(9)
	v_mfma_f32_16x16x32_f16 v[120:123], v[156:159], v[152:155], v[120:123]
	v_mfma_f32_16x16x32_f16 v[124:127], v[160:163], v[152:155], v[124:127]
	v_mfma_f32_16x16x32_f16 v[128:131], v[164:167], v[152:155], v[128:131]
	v_mfma_f32_16x16x32_f16 v[132:135], v[168:171], v[152:155], v[132:135]
	s_waitcnt vmcnt(7) lgkmcnt(0)
	s_barrier
	s_waitcnt lgkmcnt(6)
	ds_read_b128 v[136:139], v15
	ds_read_b128 v[156:159], v17
	ds_read_b128 v[160:163], v17 offset:2048
	ds_read_b128 v[164:167], v17 offset:4096
	ds_read_b128 v[168:171], v17 offset:6144
	ds_read_b128 v[140:143], v15 offset:2048
	ds_read_b128 v[144:147], v15 offset:4096
	ds_read_b128 v[148:151], v15 offset:6144
	ds_read_b128 v[152:155], v15 offset:8192
	v_mfma_f32_16x16x32_f16 v[56:59], v[192:195], v[172:175], v[56:59]
	s_add_u32 m0, s28, 0x1a000
	s_nop 0
	global_load_lds_dwordx4 v10, s[4:5]
	s_waitcnt lgkmcnt(15)
	v_mfma_f32_16x16x32_f16 v[60:63], v[196:199], v[172:175], v[60:63]
	s_waitcnt lgkmcnt(14)
	v_mfma_f32_16x16x32_f16 v[64:67], v[200:203], v[172:175], v[64:67]
	s_waitcnt lgkmcnt(13)
	v_mfma_f32_16x16x32_f16 v[68:71], v[204:207], v[172:175], v[68:71]
	s_waitcnt lgkmcnt(12)
	v_mfma_f32_16x16x32_f16 v[72:75], v[192:195], v[176:179], v[72:75]
	v_mfma_f32_16x16x32_f16 v[76:79], v[196:199], v[176:179], v[76:79]
	s_add_u32 m0, s28, 0x1c000
	s_nop 0
	global_load_lds_dwordx4 v11, s[4:5]
	v_mfma_f32_16x16x32_f16 v[80:83], v[200:203], v[176:179], v[80:83]
	v_mfma_f32_16x16x32_f16 v[84:87], v[204:207], v[176:179], v[84:87]
	s_waitcnt lgkmcnt(11)
	v_mfma_f32_16x16x32_f16 v[88:91], v[192:195], v[180:183], v[88:91]
	v_mfma_f32_16x16x32_f16 v[92:95], v[196:199], v[180:183], v[92:95]
	v_mfma_f32_16x16x32_f16 v[96:99], v[200:203], v[180:183], v[96:99]
	s_add_u32 m0, s28, 0x1e000
	s_nop 0
	global_load_lds_dwordx4 v12, s[4:5]
	v_mfma_f32_16x16x32_f16 v[100:103], v[204:207], v[180:183], v[100:103]
	s_waitcnt lgkmcnt(10)
	v_mfma_f32_16x16x32_f16 v[104:107], v[192:195], v[184:187], v[104:107]
	v_mfma_f32_16x16x32_f16 v[108:111], v[196:199], v[184:187], v[108:111]
	v_mfma_f32_16x16x32_f16 v[112:115], v[200:203], v[184:187], v[112:115]
	v_mfma_f32_16x16x32_f16 v[116:119], v[204:207], v[184:187], v[116:119]
	s_add_u32 m0, s28, 0x20000
	s_nop 0
	global_load_lds_dwordx4 v13, s[4:5]
	s_waitcnt lgkmcnt(9)
	v_mfma_f32_16x16x32_f16 v[120:123], v[192:195], v[188:191], v[120:123]
	v_mfma_f32_16x16x32_f16 v[124:127], v[196:199], v[188:191], v[124:127]
	v_mfma_f32_16x16x32_f16 v[128:131], v[200:203], v[188:191], v[128:131]
	v_mfma_f32_16x16x32_f16 v[132:135], v[204:207], v[188:191], v[132:135]
	s_waitcnt lgkmcnt(6)
	ds_read_b128 v[172:175], v16
	ds_read_b128 v[192:195], v18
	ds_read_b128 v[196:199], v18 offset:2048
	ds_read_b128 v[200:203], v18 offset:4096
	ds_read_b128 v[204:207], v18 offset:6144
	ds_read_b128 v[176:179], v16 offset:2048
	ds_read_b128 v[180:183], v16 offset:4096
	ds_read_b128 v[184:187], v16 offset:6144
	ds_read_b128 v[188:191], v16 offset:8192
	v_mfma_f32_16x16x32_f16 v[56:59], v[156:159], v[136:139], v[56:59]
	s_add_u32 m0, s28, 0x22000
	s_nop 0
	global_load_lds_dwordx4 v14, s[4:5]
	s_add_u32 s4, s4, s20
	s_addc_u32 s5, s5, 0
	s_waitcnt lgkmcnt(15)
	v_mfma_f32_16x16x32_f16 v[60:63], v[160:163], v[136:139], v[60:63]
	s_waitcnt lgkmcnt(14)
	v_mfma_f32_16x16x32_f16 v[64:67], v[164:167], v[136:139], v[64:67]
	s_waitcnt lgkmcnt(13)
	v_mfma_f32_16x16x32_f16 v[68:71], v[168:171], v[136:139], v[68:71]
	s_waitcnt lgkmcnt(12)
	v_mfma_f32_16x16x32_f16 v[72:75], v[156:159], v[140:143], v[72:75]
	v_mfma_f32_16x16x32_f16 v[76:79], v[160:163], v[140:143], v[76:79]
	v_mfma_f32_16x16x32_f16 v[80:83], v[164:167], v[140:143], v[80:83]
	s_add_u32 m0, s28, 0x23000
	s_nop 0
	global_load_lds_dwordx4 v10, s[6:7]
	v_mfma_f32_16x16x32_f16 v[84:87], v[168:171], v[140:143], v[84:87]
	s_waitcnt lgkmcnt(11)
	v_mfma_f32_16x16x32_f16 v[88:91], v[156:159], v[144:147], v[88:91]
	v_mfma_f32_16x16x32_f16 v[92:95], v[160:163], v[144:147], v[92:95]
	v_mfma_f32_16x16x32_f16 v[96:99], v[164:167], v[144:147], v[96:99]
	v_mfma_f32_16x16x32_f16 v[100:103], v[168:171], v[144:147], v[100:103]
	s_waitcnt lgkmcnt(10)
	v_mfma_f32_16x16x32_f16 v[104:107], v[156:159], v[148:151], v[104:107]
	v_mfma_f32_16x16x32_f16 v[108:111], v[160:163], v[148:151], v[108:111]
	s_add_u32 m0, s28, 0x25000
	s_nop 0
	global_load_lds_dwordx4 v11, s[6:7]
	s_add_u32 s6, s6, s20
	s_addc_u32 s7, s7, 0
	v_mfma_f32_16x16x32_f16 v[112:115], v[164:167], v[148:151], v[112:115]
	v_mfma_f32_16x16x32_f16 v[116:119], v[168:171], v[148:151], v[116:119]
	s_waitcnt lgkmcnt(9)
	v_mfma_f32_16x16x32_f16 v[120:123], v[156:159], v[152:155], v[120:123]
	v_mfma_f32_16x16x32_f16 v[124:127], v[160:163], v[152:155], v[124:127]
	v_mfma_f32_16x16x32_f16 v[128:131], v[164:167], v[152:155], v[128:131]
	v_mfma_f32_16x16x32_f16 v[132:135], v[168:171], v[152:155], v[132:135]
	s_waitcnt vmcnt(7) lgkmcnt(0)
	s_barrier
	s_waitcnt lgkmcnt(6)
	ds_read_b128 v[136:139], v15 offset:53248
	ds_read_b128 v[156:159], v17 offset:53248
	ds_read_b128 v[160:163], v17 offset:55296
	ds_read_b128 v[164:167], v17 offset:57344
	ds_read_b128 v[168:171], v17 offset:59392
	ds_read_b128 v[140:143], v15 offset:55296
	ds_read_b128 v[144:147], v15 offset:57344
	ds_read_b128 v[148:151], v15 offset:59392
	ds_read_b128 v[152:155], v15 offset:61440
	v_mfma_f32_16x16x32_f16 v[56:59], v[192:195], v[172:175], v[56:59]
	s_add_u32 m0, s28, 0x0
	s_nop 0
	global_load_lds_dwordx4 v10, s[4:5]
	s_waitcnt lgkmcnt(15)
	v_mfma_f32_16x16x32_f16 v[60:63], v[196:199], v[172:175], v[60:63]
	s_waitcnt lgkmcnt(14)
	v_mfma_f32_16x16x32_f16 v[64:67], v[200:203], v[172:175], v[64:67]
	s_waitcnt lgkmcnt(13)
	v_mfma_f32_16x16x32_f16 v[68:71], v[204:207], v[172:175], v[68:71]
	s_waitcnt lgkmcnt(12)
	v_mfma_f32_16x16x32_f16 v[72:75], v[192:195], v[176:179], v[72:75]
	v_mfma_f32_16x16x32_f16 v[76:79], v[196:199], v[176:179], v[76:79]
	s_add_u32 m0, s28, 0x2000
	s_nop 0
	global_load_lds_dwordx4 v11, s[4:5]
	v_mfma_f32_16x16x32_f16 v[80:83], v[200:203], v[176:179], v[80:83]
	v_mfma_f32_16x16x32_f16 v[84:87], v[204:207], v[176:179], v[84:87]
	s_waitcnt lgkmcnt(11)
	v_mfma_f32_16x16x32_f16 v[88:91], v[192:195], v[180:183], v[88:91]
	v_mfma_f32_16x16x32_f16 v[92:95], v[196:199], v[180:183], v[92:95]
	v_mfma_f32_16x16x32_f16 v[96:99], v[200:203], v[180:183], v[96:99]
	s_add_u32 m0, s28, 0x4000
	s_nop 0
	global_load_lds_dwordx4 v12, s[4:5]
	v_mfma_f32_16x16x32_f16 v[100:103], v[204:207], v[180:183], v[100:103]
	s_waitcnt lgkmcnt(10)
	v_mfma_f32_16x16x32_f16 v[104:107], v[192:195], v[184:187], v[104:107]
	v_mfma_f32_16x16x32_f16 v[108:111], v[196:199], v[184:187], v[108:111]
	v_mfma_f32_16x16x32_f16 v[112:115], v[200:203], v[184:187], v[112:115]
	v_mfma_f32_16x16x32_f16 v[116:119], v[204:207], v[184:187], v[116:119]
	s_add_u32 m0, s28, 0x6000
	s_nop 0
	global_load_lds_dwordx4 v13, s[4:5]
	s_waitcnt lgkmcnt(9)
	v_mfma_f32_16x16x32_f16 v[120:123], v[192:195], v[188:191], v[120:123]
	v_mfma_f32_16x16x32_f16 v[124:127], v[196:199], v[188:191], v[124:127]
	v_mfma_f32_16x16x32_f16 v[128:131], v[200:203], v[188:191], v[128:131]
	v_mfma_f32_16x16x32_f16 v[132:135], v[204:207], v[188:191], v[132:135]
	s_waitcnt lgkmcnt(6)
	ds_read_b128 v[172:175], v16 offset:53248
	ds_read_b128 v[192:195], v18 offset:53248
	ds_read_b128 v[196:199], v18 offset:55296
	ds_read_b128 v[200:203], v18 offset:57344
	ds_read_b128 v[204:207], v18 offset:59392
	ds_read_b128 v[176:179], v16 offset:55296
	ds_read_b128 v[180:183], v16 offset:57344
	ds_read_b128 v[184:187], v16 offset:59392
	ds_read_b128 v[188:191], v16 offset:61440
	v_mfma_f32_16x16x32_f16 v[56:59], v[156:159], v[136:139], v[56:59]
	s_add_u32 m0, s28, 0x8000
	s_nop 0
	global_load_lds_dwordx4 v14, s[4:5]
	s_add_u32 s4, s4, s20
	s_addc_u32 s5, s5, 0
	s_waitcnt lgkmcnt(15)
	v_mfma_f32_16x16x32_f16 v[60:63], v[160:163], v[136:139], v[60:63]
	s_waitcnt lgkmcnt(14)
	v_mfma_f32_16x16x32_f16 v[64:67], v[164:167], v[136:139], v[64:67]
	s_waitcnt lgkmcnt(13)
	v_mfma_f32_16x16x32_f16 v[68:71], v[168:171], v[136:139], v[68:71]
	s_waitcnt lgkmcnt(12)
	v_mfma_f32_16x16x32_f16 v[72:75], v[156:159], v[140:143], v[72:75]
	v_mfma_f32_16x16x32_f16 v[76:79], v[160:163], v[140:143], v[76:79]
	v_mfma_f32_16x16x32_f16 v[80:83], v[164:167], v[140:143], v[80:83]
	s_add_u32 m0, s28, 0x9000
	s_nop 0
	global_load_lds_dwordx4 v10, s[6:7]
	v_mfma_f32_16x16x32_f16 v[84:87], v[168:171], v[140:143], v[84:87]
	s_waitcnt lgkmcnt(11)
	v_mfma_f32_16x16x32_f16 v[88:91], v[156:159], v[144:147], v[88:91]
	v_mfma_f32_16x16x32_f16 v[92:95], v[160:163], v[144:147], v[92:95]
	v_mfma_f32_16x16x32_f16 v[96:99], v[164:167], v[144:147], v[96:99]
	v_mfma_f32_16x16x32_f16 v[100:103], v[168:171], v[144:147], v[100:103]
	s_waitcnt lgkmcnt(10)
	v_mfma_f32_16x16x32_f16 v[104:107], v[156:159], v[148:151], v[104:107]
	v_mfma_f32_16x16x32_f16 v[108:111], v[160:163], v[148:151], v[108:111]
	s_add_u32 m0, s28, 0xb000
	s_nop 0
	global_load_lds_dwordx4 v11, s[6:7]
	s_add_u32 s6, s6, s20
	s_addc_u32 s7, s7, 0
	v_mfma_f32_16x16x32_f16 v[112:115], v[164:167], v[148:151], v[112:115]
	v_mfma_f32_16x16x32_f16 v[116:119], v[168:171], v[148:151], v[116:119]
	s_waitcnt lgkmcnt(9)
	v_mfma_f32_16x16x32_f16 v[120:123], v[156:159], v[152:155], v[120:123]
	v_mfma_f32_16x16x32_f16 v[124:127], v[160:163], v[152:155], v[124:127]
	v_mfma_f32_16x16x32_f16 v[128:131], v[164:167], v[152:155], v[128:131]
	v_mfma_f32_16x16x32_f16 v[132:135], v[168:171], v[152:155], v[132:135]
	s_waitcnt vmcnt(7) lgkmcnt(0)
	s_barrier
	s_waitcnt lgkmcnt(6)
	ds_read_b128 v[136:139], v19
	ds_read_b128 v[156:159], v21
	ds_read_b128 v[160:163], v21 offset:2048
	ds_read_b128 v[164:167], v21 offset:4096
	ds_read_b128 v[168:171], v21 offset:6144
	ds_read_b128 v[140:143], v19 offset:2048
	ds_read_b128 v[144:147], v19 offset:4096
	ds_read_b128 v[148:151], v19 offset:6144
	ds_read_b128 v[152:155], v19 offset:8192
	v_mfma_f32_16x16x32_f16 v[56:59], v[192:195], v[172:175], v[56:59]
	s_add_u32 m0, s28, 0xd000
	s_nop 0
	global_load_lds_dwordx4 v10, s[4:5]
	s_waitcnt lgkmcnt(15)
	v_mfma_f32_16x16x32_f16 v[60:63], v[196:199], v[172:175], v[60:63]
	s_waitcnt lgkmcnt(14)
	v_mfma_f32_16x16x32_f16 v[64:67], v[200:203], v[172:175], v[64:67]
	s_waitcnt lgkmcnt(13)
	v_mfma_f32_16x16x32_f16 v[68:71], v[204:207], v[172:175], v[68:71]
	s_waitcnt lgkmcnt(12)
	v_mfma_f32_16x16x32_f16 v[72:75], v[192:195], v[176:179], v[72:75]
	v_mfma_f32_16x16x32_f16 v[76:79], v[196:199], v[176:179], v[76:79]
	s_add_u32 m0, s28, 0xf000
	s_nop 0
	global_load_lds_dwordx4 v11, s[4:5]
	v_mfma_f32_16x16x32_f16 v[80:83], v[200:203], v[176:179], v[80:83]
	v_mfma_f32_16x16x32_f16 v[84:87], v[204:207], v[176:179], v[84:87]
	s_waitcnt lgkmcnt(11)
	v_mfma_f32_16x16x32_f16 v[88:91], v[192:195], v[180:183], v[88:91]
	v_mfma_f32_16x16x32_f16 v[92:95], v[196:199], v[180:183], v[92:95]
	v_mfma_f32_16x16x32_f16 v[96:99], v[200:203], v[180:183], v[96:99]
	s_add_u32 m0, s28, 0x11000
	s_nop 0
	global_load_lds_dwordx4 v12, s[4:5]
	v_mfma_f32_16x16x32_f16 v[100:103], v[204:207], v[180:183], v[100:103]
	s_waitcnt lgkmcnt(10)
	v_mfma_f32_16x16x32_f16 v[104:107], v[192:195], v[184:187], v[104:107]
	v_mfma_f32_16x16x32_f16 v[108:111], v[196:199], v[184:187], v[108:111]
	v_mfma_f32_16x16x32_f16 v[112:115], v[200:203], v[184:187], v[112:115]
	v_mfma_f32_16x16x32_f16 v[116:119], v[204:207], v[184:187], v[116:119]
	s_add_u32 m0, s28, 0x13000
	s_nop 0
	global_load_lds_dwordx4 v13, s[4:5]
	s_waitcnt lgkmcnt(9)
	v_mfma_f32_16x16x32_f16 v[120:123], v[192:195], v[188:191], v[120:123]
	v_mfma_f32_16x16x32_f16 v[124:127], v[196:199], v[188:191], v[124:127]
	v_mfma_f32_16x16x32_f16 v[128:131], v[200:203], v[188:191], v[128:131]
	v_mfma_f32_16x16x32_f16 v[132:135], v[204:207], v[188:191], v[132:135]
	s_waitcnt lgkmcnt(6)
	ds_read_b128 v[172:175], v20
	ds_read_b128 v[192:195], v22
	ds_read_b128 v[196:199], v22 offset:2048
	ds_read_b128 v[200:203], v22 offset:4096
	ds_read_b128 v[204:207], v22 offset:6144
	ds_read_b128 v[176:179], v20 offset:2048
	ds_read_b128 v[180:183], v20 offset:4096
	ds_read_b128 v[184:187], v20 offset:6144
	ds_read_b128 v[188:191], v20 offset:8192
	v_mfma_f32_16x16x32_f16 v[56:59], v[156:159], v[136:139], v[56:59]
	s_add_u32 m0, s28, 0x15000
	s_nop 0
	global_load_lds_dwordx4 v14, s[4:5]
	s_add_u32 s4, s4, s20
	s_addc_u32 s5, s5, 0
	s_waitcnt lgkmcnt(15)
	v_mfma_f32_16x16x32_f16 v[60:63], v[160:163], v[136:139], v[60:63]
	s_waitcnt lgkmcnt(14)
	v_mfma_f32_16x16x32_f16 v[64:67], v[164:167], v[136:139], v[64:67]
	s_waitcnt lgkmcnt(13)
	v_mfma_f32_16x16x32_f16 v[68:71], v[168:171], v[136:139], v[68:71]
	s_waitcnt lgkmcnt(12)
	v_mfma_f32_16x16x32_f16 v[72:75], v[156:159], v[140:143], v[72:75]
	v_mfma_f32_16x16x32_f16 v[76:79], v[160:163], v[140:143], v[76:79]
	v_mfma_f32_16x16x32_f16 v[80:83], v[164:167], v[140:143], v[80:83]
	s_add_u32 m0, s28, 0x16000
	s_nop 0
	global_load_lds_dwordx4 v10, s[6:7]
	v_mfma_f32_16x16x32_f16 v[84:87], v[168:171], v[140:143], v[84:87]
	s_waitcnt lgkmcnt(11)
	v_mfma_f32_16x16x32_f16 v[88:91], v[156:159], v[144:147], v[88:91]
	v_mfma_f32_16x16x32_f16 v[92:95], v[160:163], v[144:147], v[92:95]
	v_mfma_f32_16x16x32_f16 v[96:99], v[164:167], v[144:147], v[96:99]
	v_mfma_f32_16x16x32_f16 v[100:103], v[168:171], v[144:147], v[100:103]
	s_waitcnt lgkmcnt(10)
	v_mfma_f32_16x16x32_f16 v[104:107], v[156:159], v[148:151], v[104:107]
	v_mfma_f32_16x16x32_f16 v[108:111], v[160:163], v[148:151], v[108:111]
	s_add_u32 m0, s28, 0x18000
	s_nop 0
	global_load_lds_dwordx4 v11, s[6:7]
	s_add_u32 s6, s6, s20
	s_addc_u32 s7, s7, 0
	v_mfma_f32_16x16x32_f16 v[112:115], v[164:167], v[148:151], v[112:115]
	v_mfma_f32_16x16x32_f16 v[116:119], v[168:171], v[148:151], v[116:119]
	s_waitcnt lgkmcnt(9)
	v_mfma_f32_16x16x32_f16 v[120:123], v[156:159], v[152:155], v[120:123]
	v_mfma_f32_16x16x32_f16 v[124:127], v[160:163], v[152:155], v[124:127]
	v_mfma_f32_16x16x32_f16 v[128:131], v[164:167], v[152:155], v[128:131]
	v_mfma_f32_16x16x32_f16 v[132:135], v[168:171], v[152:155], v[132:135]
	s_waitcnt vmcnt(7) lgkmcnt(0)
	s_barrier
	s_waitcnt lgkmcnt(6)
	ds_read_b128 v[136:139], v15
	ds_read_b128 v[156:159], v17
	ds_read_b128 v[160:163], v17 offset:2048
	ds_read_b128 v[164:167], v17 offset:4096
	ds_read_b128 v[168:171], v17 offset:6144
	ds_read_b128 v[140:143], v15 offset:2048
	ds_read_b128 v[144:147], v15 offset:4096
	ds_read_b128 v[148:151], v15 offset:6144
	ds_read_b128 v[152:155], v15 offset:8192
	v_mfma_f32_16x16x32_f16 v[56:59], v[192:195], v[172:175], v[56:59]
	s_add_u32 m0, s28, 0x1a000
	s_nop 0
	global_load_lds_dwordx4 v10, s[4:5]
	s_waitcnt lgkmcnt(15)
	v_mfma_f32_16x16x32_f16 v[60:63], v[196:199], v[172:175], v[60:63]
	s_waitcnt lgkmcnt(14)
	v_mfma_f32_16x16x32_f16 v[64:67], v[200:203], v[172:175], v[64:67]
	s_waitcnt lgkmcnt(13)
	v_mfma_f32_16x16x32_f16 v[68:71], v[204:207], v[172:175], v[68:71]
	s_waitcnt lgkmcnt(12)
	v_mfma_f32_16x16x32_f16 v[72:75], v[192:195], v[176:179], v[72:75]
	v_mfma_f32_16x16x32_f16 v[76:79], v[196:199], v[176:179], v[76:79]
	s_add_u32 m0, s28, 0x1c000
	s_nop 0
	global_load_lds_dwordx4 v11, s[4:5]
	v_mfma_f32_16x16x32_f16 v[80:83], v[200:203], v[176:179], v[80:83]
	v_mfma_f32_16x16x32_f16 v[84:87], v[204:207], v[176:179], v[84:87]
	s_waitcnt lgkmcnt(11)
	v_mfma_f32_16x16x32_f16 v[88:91], v[192:195], v[180:183], v[88:91]
	v_mfma_f32_16x16x32_f16 v[92:95], v[196:199], v[180:183], v[92:95]
	v_mfma_f32_16x16x32_f16 v[96:99], v[200:203], v[180:183], v[96:99]
	s_add_u32 m0, s28, 0x1e000
	s_nop 0
	global_load_lds_dwordx4 v12, s[4:5]
	v_mfma_f32_16x16x32_f16 v[100:103], v[204:207], v[180:183], v[100:103]
	s_waitcnt lgkmcnt(10)
	v_mfma_f32_16x16x32_f16 v[104:107], v[192:195], v[184:187], v[104:107]
	v_mfma_f32_16x16x32_f16 v[108:111], v[196:199], v[184:187], v[108:111]
	v_mfma_f32_16x16x32_f16 v[112:115], v[200:203], v[184:187], v[112:115]
	v_mfma_f32_16x16x32_f16 v[116:119], v[204:207], v[184:187], v[116:119]
	s_add_u32 m0, s28, 0x20000
	s_nop 0
	global_load_lds_dwordx4 v13, s[4:5]
	s_waitcnt lgkmcnt(9)
	v_mfma_f32_16x16x32_f16 v[120:123], v[192:195], v[188:191], v[120:123]
	v_mfma_f32_16x16x32_f16 v[124:127], v[196:199], v[188:191], v[124:127]
	v_mfma_f32_16x16x32_f16 v[128:131], v[200:203], v[188:191], v[128:131]
	v_mfma_f32_16x16x32_f16 v[132:135], v[204:207], v[188:191], v[132:135]
	s_waitcnt lgkmcnt(6)
	ds_read_b128 v[172:175], v16
	ds_read_b128 v[192:195], v18
	ds_read_b128 v[196:199], v18 offset:2048
	ds_read_b128 v[200:203], v18 offset:4096
	ds_read_b128 v[204:207], v18 offset:6144
	ds_read_b128 v[176:179], v16 offset:2048
	ds_read_b128 v[180:183], v16 offset:4096
	ds_read_b128 v[184:187], v16 offset:6144
	ds_read_b128 v[188:191], v16 offset:8192
	v_mfma_f32_16x16x32_f16 v[56:59], v[156:159], v[136:139], v[56:59]
	s_add_u32 m0, s28, 0x22000
	s_nop 0
	global_load_lds_dwordx4 v14, s[4:5]
	s_add_u32 s4, s4, s20
	s_addc_u32 s5, s5, 0
	s_waitcnt lgkmcnt(15)
	v_mfma_f32_16x16x32_f16 v[60:63], v[160:163], v[136:139], v[60:63]
	s_waitcnt lgkmcnt(14)
	v_mfma_f32_16x16x32_f16 v[64:67], v[164:167], v[136:139], v[64:67]
	s_waitcnt lgkmcnt(13)
	v_mfma_f32_16x16x32_f16 v[68:71], v[168:171], v[136:139], v[68:71]
	s_waitcnt lgkmcnt(12)
	v_mfma_f32_16x16x32_f16 v[72:75], v[156:159], v[140:143], v[72:75]
	v_mfma_f32_16x16x32_f16 v[76:79], v[160:163], v[140:143], v[76:79]
	v_mfma_f32_16x16x32_f16 v[80:83], v[164:167], v[140:143], v[80:83]
	s_add_u32 m0, s28, 0x23000
	s_nop 0
	global_load_lds_dwordx4 v10, s[6:7]
	v_mfma_f32_16x16x32_f16 v[84:87], v[168:171], v[140:143], v[84:87]
	s_waitcnt lgkmcnt(11)
	v_mfma_f32_16x16x32_f16 v[88:91], v[156:159], v[144:147], v[88:91]
	v_mfma_f32_16x16x32_f16 v[92:95], v[160:163], v[144:147], v[92:95]
	v_mfma_f32_16x16x32_f16 v[96:99], v[164:167], v[144:147], v[96:99]
	v_mfma_f32_16x16x32_f16 v[100:103], v[168:171], v[144:147], v[100:103]
	s_waitcnt lgkmcnt(10)
	v_mfma_f32_16x16x32_f16 v[104:107], v[156:159], v[148:151], v[104:107]
	v_mfma_f32_16x16x32_f16 v[108:111], v[160:163], v[148:151], v[108:111]
	s_add_u32 m0, s28, 0x25000
	s_nop 0
	global_load_lds_dwordx4 v11, s[6:7]
	s_add_u32 s6, s6, s20
	s_addc_u32 s7, s7, 0
	v_mfma_f32_16x16x32_f16 v[112:115], v[164:167], v[148:151], v[112:115]
	v_mfma_f32_16x16x32_f16 v[116:119], v[168:171], v[148:151], v[116:119]
	s_waitcnt lgkmcnt(9)
	v_mfma_f32_16x16x32_f16 v[120:123], v[156:159], v[152:155], v[120:123]
	v_mfma_f32_16x16x32_f16 v[124:127], v[160:163], v[152:155], v[124:127]
	v_mfma_f32_16x16x32_f16 v[128:131], v[164:167], v[152:155], v[128:131]
	v_mfma_f32_16x16x32_f16 v[132:135], v[168:171], v[152:155], v[132:135]
	s_waitcnt vmcnt(7) lgkmcnt(0)
	s_barrier
	s_waitcnt lgkmcnt(6)
	ds_read_b128 v[136:139], v15 offset:53248
	ds_read_b128 v[156:159], v17 offset:53248
	ds_read_b128 v[160:163], v17 offset:55296
	ds_read_b128 v[164:167], v17 offset:57344
	ds_read_b128 v[168:171], v17 offset:59392
	ds_read_b128 v[140:143], v15 offset:55296
	ds_read_b128 v[144:147], v15 offset:57344
	ds_read_b128 v[148:151], v15 offset:59392
	ds_read_b128 v[152:155], v15 offset:61440
	v_mfma_f32_16x16x32_f16 v[56:59], v[192:195], v[172:175], v[56:59]
	s_add_u32 m0, s28, 0x0
	s_nop 0
	global_load_lds_dwordx4 v10, s[4:5]
	s_waitcnt lgkmcnt(15)
	v_mfma_f32_16x16x32_f16 v[60:63], v[196:199], v[172:175], v[60:63]
	s_waitcnt lgkmcnt(14)
	v_mfma_f32_16x16x32_f16 v[64:67], v[200:203], v[172:175], v[64:67]
	s_waitcnt lgkmcnt(13)
	v_mfma_f32_16x16x32_f16 v[68:71], v[204:207], v[172:175], v[68:71]
	s_waitcnt lgkmcnt(12)
	v_mfma_f32_16x16x32_f16 v[72:75], v[192:195], v[176:179], v[72:75]
	v_mfma_f32_16x16x32_f16 v[76:79], v[196:199], v[176:179], v[76:79]
	s_add_u32 m0, s28, 0x2000
	s_nop 0
	global_load_lds_dwordx4 v11, s[4:5]
	v_mfma_f32_16x16x32_f16 v[80:83], v[200:203], v[176:179], v[80:83]
	v_mfma_f32_16x16x32_f16 v[84:87], v[204:207], v[176:179], v[84:87]
	s_waitcnt lgkmcnt(11)
	v_mfma_f32_16x16x32_f16 v[88:91], v[192:195], v[180:183], v[88:91]
	v_mfma_f32_16x16x32_f16 v[92:95], v[196:199], v[180:183], v[92:95]
	v_mfma_f32_16x16x32_f16 v[96:99], v[200:203], v[180:183], v[96:99]
	s_add_u32 m0, s28, 0x4000
	s_nop 0
	global_load_lds_dwordx4 v12, s[4:5]
	v_mfma_f32_16x16x32_f16 v[100:103], v[204:207], v[180:183], v[100:103]
	s_waitcnt lgkmcnt(10)
	v_mfma_f32_16x16x32_f16 v[104:107], v[192:195], v[184:187], v[104:107]
	v_mfma_f32_16x16x32_f16 v[108:111], v[196:199], v[184:187], v[108:111]
	v_mfma_f32_16x16x32_f16 v[112:115], v[200:203], v[184:187], v[112:115]
	v_mfma_f32_16x16x32_f16 v[116:119], v[204:207], v[184:187], v[116:119]
	s_add_u32 m0, s28, 0x6000
	s_nop 0
	global_load_lds_dwordx4 v13, s[4:5]
	s_waitcnt lgkmcnt(9)
	v_mfma_f32_16x16x32_f16 v[120:123], v[192:195], v[188:191], v[120:123]
	v_mfma_f32_16x16x32_f16 v[124:127], v[196:199], v[188:191], v[124:127]
	v_mfma_f32_16x16x32_f16 v[128:131], v[200:203], v[188:191], v[128:131]
	v_mfma_f32_16x16x32_f16 v[132:135], v[204:207], v[188:191], v[132:135]
	s_waitcnt lgkmcnt(6)
	ds_read_b128 v[172:175], v16 offset:53248
	ds_read_b128 v[192:195], v18 offset:53248
	ds_read_b128 v[196:199], v18 offset:55296
	ds_read_b128 v[200:203], v18 offset:57344
	ds_read_b128 v[204:207], v18 offset:59392
	ds_read_b128 v[176:179], v16 offset:55296
	ds_read_b128 v[180:183], v16 offset:57344
	ds_read_b128 v[184:187], v16 offset:59392
	ds_read_b128 v[188:191], v16 offset:61440
	v_mfma_f32_16x16x32_f16 v[56:59], v[156:159], v[136:139], v[56:59]
	s_add_u32 m0, s28, 0x8000
	s_nop 0
	global_load_lds_dwordx4 v14, s[4:5]
	s_add_u32 s4, s4, s20
	s_addc_u32 s5, s5, 0
	s_waitcnt lgkmcnt(15)
	v_mfma_f32_16x16x32_f16 v[60:63], v[160:163], v[136:139], v[60:63]
	s_waitcnt lgkmcnt(14)
	v_mfma_f32_16x16x32_f16 v[64:67], v[164:167], v[136:139], v[64:67]
	s_waitcnt lgkmcnt(13)
	v_mfma_f32_16x16x32_f16 v[68:71], v[168:171], v[136:139], v[68:71]
	s_waitcnt lgkmcnt(12)
	v_mfma_f32_16x16x32_f16 v[72:75], v[156:159], v[140:143], v[72:75]
	v_mfma_f32_16x16x32_f16 v[76:79], v[160:163], v[140:143], v[76:79]
	v_mfma_f32_16x16x32_f16 v[80:83], v[164:167], v[140:143], v[80:83]
	s_add_u32 m0, s28, 0x9000
	s_nop 0
	global_load_lds_dwordx4 v10, s[6:7]
	v_mfma_f32_16x16x32_f16 v[84:87], v[168:171], v[140:143], v[84:87]
	s_waitcnt lgkmcnt(11)
	v_mfma_f32_16x16x32_f16 v[88:91], v[156:159], v[144:147], v[88:91]
	v_mfma_f32_16x16x32_f16 v[92:95], v[160:163], v[144:147], v[92:95]
	v_mfma_f32_16x16x32_f16 v[96:99], v[164:167], v[144:147], v[96:99]
	v_mfma_f32_16x16x32_f16 v[100:103], v[168:171], v[144:147], v[100:103]
	s_waitcnt lgkmcnt(10)
	v_mfma_f32_16x16x32_f16 v[104:107], v[156:159], v[148:151], v[104:107]
	v_mfma_f32_16x16x32_f16 v[108:111], v[160:163], v[148:151], v[108:111]
	s_add_u32 m0, s28, 0xb000
	s_nop 0
	global_load_lds_dwordx4 v11, s[6:7]
	s_add_u32 s6, s6, s20
	s_addc_u32 s7, s7, 0
	v_mfma_f32_16x16x32_f16 v[112:115], v[164:167], v[148:151], v[112:115]
	v_mfma_f32_16x16x32_f16 v[116:119], v[168:171], v[148:151], v[116:119]
	s_waitcnt lgkmcnt(9)
	v_mfma_f32_16x16x32_f16 v[120:123], v[156:159], v[152:155], v[120:123]
	v_mfma_f32_16x16x32_f16 v[124:127], v[160:163], v[152:155], v[124:127]
	v_mfma_f32_16x16x32_f16 v[128:131], v[164:167], v[152:155], v[128:131]
	v_mfma_f32_16x16x32_f16 v[132:135], v[168:171], v[152:155], v[132:135]
	s_waitcnt vmcnt(7) lgkmcnt(0)
	s_barrier
	s_waitcnt lgkmcnt(6)
	ds_read_b128 v[136:139], v19
	ds_read_b128 v[156:159], v21
	ds_read_b128 v[160:163], v21 offset:2048
	ds_read_b128 v[164:167], v21 offset:4096
	ds_read_b128 v[168:171], v21 offset:6144
	ds_read_b128 v[140:143], v19 offset:2048
	ds_read_b128 v[144:147], v19 offset:4096
	ds_read_b128 v[148:151], v19 offset:6144
	ds_read_b128 v[152:155], v19 offset:8192
	v_mfma_f32_16x16x32_f16 v[56:59], v[192:195], v[172:175], v[56:59]
	s_add_u32 m0, s28, 0xd000
	s_nop 0
	global_load_lds_dwordx4 v10, s[4:5]
	s_waitcnt lgkmcnt(15)
	v_mfma_f32_16x16x32_f16 v[60:63], v[196:199], v[172:175], v[60:63]
	s_waitcnt lgkmcnt(14)
	v_mfma_f32_16x16x32_f16 v[64:67], v[200:203], v[172:175], v[64:67]
	s_waitcnt lgkmcnt(13)
	v_mfma_f32_16x16x32_f16 v[68:71], v[204:207], v[172:175], v[68:71]
	s_waitcnt lgkmcnt(12)
	v_mfma_f32_16x16x32_f16 v[72:75], v[192:195], v[176:179], v[72:75]
	v_mfma_f32_16x16x32_f16 v[76:79], v[196:199], v[176:179], v[76:79]
	s_add_u32 m0, s28, 0xf000
	s_nop 0
	global_load_lds_dwordx4 v11, s[4:5]
	v_mfma_f32_16x16x32_f16 v[80:83], v[200:203], v[176:179], v[80:83]
	v_mfma_f32_16x16x32_f16 v[84:87], v[204:207], v[176:179], v[84:87]
	s_waitcnt lgkmcnt(11)
	v_mfma_f32_16x16x32_f16 v[88:91], v[192:195], v[180:183], v[88:91]
	v_mfma_f32_16x16x32_f16 v[92:95], v[196:199], v[180:183], v[92:95]
	v_mfma_f32_16x16x32_f16 v[96:99], v[200:203], v[180:183], v[96:99]
	s_add_u32 m0, s28, 0x11000
	s_nop 0
	global_load_lds_dwordx4 v12, s[4:5]
	v_mfma_f32_16x16x32_f16 v[100:103], v[204:207], v[180:183], v[100:103]
	s_waitcnt lgkmcnt(10)
	v_mfma_f32_16x16x32_f16 v[104:107], v[192:195], v[184:187], v[104:107]
	v_mfma_f32_16x16x32_f16 v[108:111], v[196:199], v[184:187], v[108:111]
	v_mfma_f32_16x16x32_f16 v[112:115], v[200:203], v[184:187], v[112:115]
	v_mfma_f32_16x16x32_f16 v[116:119], v[204:207], v[184:187], v[116:119]
	s_add_u32 m0, s28, 0x13000
	s_nop 0
	global_load_lds_dwordx4 v13, s[4:5]
	s_waitcnt lgkmcnt(9)
	v_mfma_f32_16x16x32_f16 v[120:123], v[192:195], v[188:191], v[120:123]
	v_mfma_f32_16x16x32_f16 v[124:127], v[196:199], v[188:191], v[124:127]
	v_mfma_f32_16x16x32_f16 v[128:131], v[200:203], v[188:191], v[128:131]
	v_mfma_f32_16x16x32_f16 v[132:135], v[204:207], v[188:191], v[132:135]
	s_waitcnt lgkmcnt(6)
	ds_read_b128 v[172:175], v20
	ds_read_b128 v[192:195], v22
	ds_read_b128 v[196:199], v22 offset:2048
	ds_read_b128 v[200:203], v22 offset:4096
	ds_read_b128 v[204:207], v22 offset:6144
	ds_read_b128 v[176:179], v20 offset:2048
	ds_read_b128 v[180:183], v20 offset:4096
	ds_read_b128 v[184:187], v20 offset:6144
	ds_read_b128 v[188:191], v20 offset:8192
	v_mfma_f32_16x16x32_f16 v[56:59], v[156:159], v[136:139], v[56:59]
	s_add_u32 m0, s28, 0x15000
	s_nop 0
	global_load_lds_dwordx4 v14, s[4:5]
	s_add_u32 s4, s4, s20
	s_addc_u32 s5, s5, 0
	s_waitcnt lgkmcnt(15)
	v_mfma_f32_16x16x32_f16 v[60:63], v[160:163], v[136:139], v[60:63]
	s_waitcnt lgkmcnt(14)
	v_mfma_f32_16x16x32_f16 v[64:67], v[164:167], v[136:139], v[64:67]
	s_waitcnt lgkmcnt(13)
	v_mfma_f32_16x16x32_f16 v[68:71], v[168:171], v[136:139], v[68:71]
	s_waitcnt lgkmcnt(12)
	v_mfma_f32_16x16x32_f16 v[72:75], v[156:159], v[140:143], v[72:75]
	v_mfma_f32_16x16x32_f16 v[76:79], v[160:163], v[140:143], v[76:79]
	v_mfma_f32_16x16x32_f16 v[80:83], v[164:167], v[140:143], v[80:83]
	s_add_u32 m0, s28, 0x16000
	s_nop 0
	global_load_lds_dwordx4 v10, s[6:7]
	v_mfma_f32_16x16x32_f16 v[84:87], v[168:171], v[140:143], v[84:87]
	s_waitcnt lgkmcnt(11)
	v_mfma_f32_16x16x32_f16 v[88:91], v[156:159], v[144:147], v[88:91]
	v_mfma_f32_16x16x32_f16 v[92:95], v[160:163], v[144:147], v[92:95]
	v_mfma_f32_16x16x32_f16 v[96:99], v[164:167], v[144:147], v[96:99]
	v_mfma_f32_16x16x32_f16 v[100:103], v[168:171], v[144:147], v[100:103]
	s_waitcnt lgkmcnt(10)
	v_mfma_f32_16x16x32_f16 v[104:107], v[156:159], v[148:151], v[104:107]
	v_mfma_f32_16x16x32_f16 v[108:111], v[160:163], v[148:151], v[108:111]
	s_add_u32 m0, s28, 0x18000
	s_nop 0
	global_load_lds_dwordx4 v11, s[6:7]
	s_add_u32 s6, s6, s20
	s_addc_u32 s7, s7, 0
	v_mfma_f32_16x16x32_f16 v[112:115], v[164:167], v[148:151], v[112:115]
	v_mfma_f32_16x16x32_f16 v[116:119], v[168:171], v[148:151], v[116:119]
	s_waitcnt lgkmcnt(9)
	v_mfma_f32_16x16x32_f16 v[120:123], v[156:159], v[152:155], v[120:123]
	v_mfma_f32_16x16x32_f16 v[124:127], v[160:163], v[152:155], v[124:127]
	v_mfma_f32_16x16x32_f16 v[128:131], v[164:167], v[152:155], v[128:131]
	v_mfma_f32_16x16x32_f16 v[132:135], v[168:171], v[152:155], v[132:135]
	s_waitcnt vmcnt(7) lgkmcnt(0)
	s_barrier
	s_waitcnt lgkmcnt(6)
	ds_read_b128 v[136:139], v15
	ds_read_b128 v[156:159], v17
	ds_read_b128 v[160:163], v17 offset:2048
	ds_read_b128 v[164:167], v17 offset:4096
	ds_read_b128 v[168:171], v17 offset:6144
	ds_read_b128 v[140:143], v15 offset:2048
	ds_read_b128 v[144:147], v15 offset:4096
	ds_read_b128 v[148:151], v15 offset:6144
	ds_read_b128 v[152:155], v15 offset:8192
	v_mfma_f32_16x16x32_f16 v[56:59], v[192:195], v[172:175], v[56:59]
	s_add_u32 m0, s28, 0x1a000
	s_nop 0
	global_load_lds_dwordx4 v10, s[4:5]
	s_waitcnt lgkmcnt(15)
	v_mfma_f32_16x16x32_f16 v[60:63], v[196:199], v[172:175], v[60:63]
	s_waitcnt lgkmcnt(14)
	v_mfma_f32_16x16x32_f16 v[64:67], v[200:203], v[172:175], v[64:67]
	s_waitcnt lgkmcnt(13)
	v_mfma_f32_16x16x32_f16 v[68:71], v[204:207], v[172:175], v[68:71]
	s_waitcnt lgkmcnt(12)
	v_mfma_f32_16x16x32_f16 v[72:75], v[192:195], v[176:179], v[72:75]
	v_mfma_f32_16x16x32_f16 v[76:79], v[196:199], v[176:179], v[76:79]
	s_add_u32 m0, s28, 0x1c000
	s_nop 0
	global_load_lds_dwordx4 v11, s[4:5]
	v_mfma_f32_16x16x32_f16 v[80:83], v[200:203], v[176:179], v[80:83]
	v_mfma_f32_16x16x32_f16 v[84:87], v[204:207], v[176:179], v[84:87]
	s_waitcnt lgkmcnt(11)
	v_mfma_f32_16x16x32_f16 v[88:91], v[192:195], v[180:183], v[88:91]
	v_mfma_f32_16x16x32_f16 v[92:95], v[196:199], v[180:183], v[92:95]
	v_mfma_f32_16x16x32_f16 v[96:99], v[200:203], v[180:183], v[96:99]
	s_add_u32 m0, s28, 0x1e000
	s_nop 0
	global_load_lds_dwordx4 v12, s[4:5]
	v_mfma_f32_16x16x32_f16 v[100:103], v[204:207], v[180:183], v[100:103]
	s_waitcnt lgkmcnt(10)
	v_mfma_f32_16x16x32_f16 v[104:107], v[192:195], v[184:187], v[104:107]
	v_mfma_f32_16x16x32_f16 v[108:111], v[196:199], v[184:187], v[108:111]
	v_mfma_f32_16x16x32_f16 v[112:115], v[200:203], v[184:187], v[112:115]
	v_mfma_f32_16x16x32_f16 v[116:119], v[204:207], v[184:187], v[116:119]
	s_add_u32 m0, s28, 0x20000
	s_nop 0
	global_load_lds_dwordx4 v13, s[4:5]
	s_waitcnt lgkmcnt(9)
	v_mfma_f32_16x16x32_f16 v[120:123], v[192:195], v[188:191], v[120:123]
	v_mfma_f32_16x16x32_f16 v[124:127], v[196:199], v[188:191], v[124:127]
	v_mfma_f32_16x16x32_f16 v[128:131], v[200:203], v[188:191], v[128:131]
	v_mfma_f32_16x16x32_f16 v[132:135], v[204:207], v[188:191], v[132:135]
	s_waitcnt lgkmcnt(6)
	ds_read_b128 v[172:175], v16
	ds_read_b128 v[192:195], v18
	ds_read_b128 v[196:199], v18 offset:2048
	ds_read_b128 v[200:203], v18 offset:4096
	ds_read_b128 v[204:207], v18 offset:6144
	ds_read_b128 v[176:179], v16 offset:2048
	ds_read_b128 v[180:183], v16 offset:4096
	ds_read_b128 v[184:187], v16 offset:6144
	ds_read_b128 v[188:191], v16 offset:8192
	v_mfma_f32_16x16x32_f16 v[56:59], v[156:159], v[136:139], v[56:59]
	s_add_u32 m0, s28, 0x22000
	s_nop 0
	global_load_lds_dwordx4 v14, s[4:5]
	s_add_u32 s4, s4, s20
	s_addc_u32 s5, s5, 0
	s_waitcnt lgkmcnt(15)
	v_mfma_f32_16x16x32_f16 v[60:63], v[160:163], v[136:139], v[60:63]
	s_waitcnt lgkmcnt(14)
	v_mfma_f32_16x16x32_f16 v[64:67], v[164:167], v[136:139], v[64:67]
	s_waitcnt lgkmcnt(13)
	v_mfma_f32_16x16x32_f16 v[68:71], v[168:171], v[136:139], v[68:71]
	s_waitcnt lgkmcnt(12)
	v_mfma_f32_16x16x32_f16 v[72:75], v[156:159], v[140:143], v[72:75]
	v_mfma_f32_16x16x32_f16 v[76:79], v[160:163], v[140:143], v[76:79]
	v_mfma_f32_16x16x32_f16 v[80:83], v[164:167], v[140:143], v[80:83]
	s_add_u32 m0, s28, 0x23000
	s_nop 0
	global_load_lds_dwordx4 v10, s[6:7]
	v_mfma_f32_16x16x32_f16 v[84:87], v[168:171], v[140:143], v[84:87]
	s_waitcnt lgkmcnt(11)
	v_mfma_f32_16x16x32_f16 v[88:91], v[156:159], v[144:147], v[88:91]
	v_mfma_f32_16x16x32_f16 v[92:95], v[160:163], v[144:147], v[92:95]
	v_mfma_f32_16x16x32_f16 v[96:99], v[164:167], v[144:147], v[96:99]
	v_mfma_f32_16x16x32_f16 v[100:103], v[168:171], v[144:147], v[100:103]
	s_waitcnt lgkmcnt(10)
	v_mfma_f32_16x16x32_f16 v[104:107], v[156:159], v[148:151], v[104:107]
	v_mfma_f32_16x16x32_f16 v[108:111], v[160:163], v[148:151], v[108:111]
	s_add_u32 m0, s28, 0x25000
	s_nop 0
	global_load_lds_dwordx4 v11, s[6:7]
	s_add_u32 s6, s6, s20
	s_addc_u32 s7, s7, 0
	v_mfma_f32_16x16x32_f16 v[112:115], v[164:167], v[148:151], v[112:115]
	v_mfma_f32_16x16x32_f16 v[116:119], v[168:171], v[148:151], v[116:119]
	s_waitcnt lgkmcnt(9)
	v_mfma_f32_16x16x32_f16 v[120:123], v[156:159], v[152:155], v[120:123]
	v_mfma_f32_16x16x32_f16 v[124:127], v[160:163], v[152:155], v[124:127]
	v_mfma_f32_16x16x32_f16 v[128:131], v[164:167], v[152:155], v[128:131]
	v_mfma_f32_16x16x32_f16 v[132:135], v[168:171], v[152:155], v[132:135]
	s_waitcnt vmcnt(7) lgkmcnt(0)
	s_barrier
	s_waitcnt lgkmcnt(6)
	ds_read_b128 v[136:139], v15 offset:53248
	ds_read_b128 v[156:159], v17 offset:53248
	ds_read_b128 v[160:163], v17 offset:55296
	ds_read_b128 v[164:167], v17 offset:57344
	ds_read_b128 v[168:171], v17 offset:59392
	ds_read_b128 v[140:143], v15 offset:55296
	ds_read_b128 v[144:147], v15 offset:57344
	ds_read_b128 v[148:151], v15 offset:59392
	ds_read_b128 v[152:155], v15 offset:61440
	v_mfma_f32_16x16x32_f16 v[56:59], v[192:195], v[172:175], v[56:59]
	s_add_u32 m0, s28, 0x0
	s_nop 0
	global_load_lds_dwordx4 v10, s[4:5]
	s_waitcnt lgkmcnt(15)
	v_mfma_f32_16x16x32_f16 v[60:63], v[196:199], v[172:175], v[60:63]
	s_waitcnt lgkmcnt(14)
	v_mfma_f32_16x16x32_f16 v[64:67], v[200:203], v[172:175], v[64:67]
	s_waitcnt lgkmcnt(13)
	v_mfma_f32_16x16x32_f16 v[68:71], v[204:207], v[172:175], v[68:71]
	s_waitcnt lgkmcnt(12)
	v_mfma_f32_16x16x32_f16 v[72:75], v[192:195], v[176:179], v[72:75]
	v_mfma_f32_16x16x32_f16 v[76:79], v[196:199], v[176:179], v[76:79]
	s_add_u32 m0, s28, 0x2000
	s_nop 0
	global_load_lds_dwordx4 v11, s[4:5]
	v_mfma_f32_16x16x32_f16 v[80:83], v[200:203], v[176:179], v[80:83]
	v_mfma_f32_16x16x32_f16 v[84:87], v[204:207], v[176:179], v[84:87]
	s_waitcnt lgkmcnt(11)
	v_mfma_f32_16x16x32_f16 v[88:91], v[192:195], v[180:183], v[88:91]
	v_mfma_f32_16x16x32_f16 v[92:95], v[196:199], v[180:183], v[92:95]
	v_mfma_f32_16x16x32_f16 v[96:99], v[200:203], v[180:183], v[96:99]
	s_add_u32 m0, s28, 0x4000
	s_nop 0
	global_load_lds_dwordx4 v12, s[4:5]
	v_mfma_f32_16x16x32_f16 v[100:103], v[204:207], v[180:183], v[100:103]
	s_waitcnt lgkmcnt(10)
	v_mfma_f32_16x16x32_f16 v[104:107], v[192:195], v[184:187], v[104:107]
	v_mfma_f32_16x16x32_f16 v[108:111], v[196:199], v[184:187], v[108:111]
	v_mfma_f32_16x16x32_f16 v[112:115], v[200:203], v[184:187], v[112:115]
	v_mfma_f32_16x16x32_f16 v[116:119], v[204:207], v[184:187], v[116:119]
	s_add_u32 m0, s28, 0x6000
	s_nop 0
	global_load_lds_dwordx4 v13, s[4:5]
	s_waitcnt lgkmcnt(9)
	v_mfma_f32_16x16x32_f16 v[120:123], v[192:195], v[188:191], v[120:123]
	v_mfma_f32_16x16x32_f16 v[124:127], v[196:199], v[188:191], v[124:127]
	v_mfma_f32_16x16x32_f16 v[128:131], v[200:203], v[188:191], v[128:131]
	v_mfma_f32_16x16x32_f16 v[132:135], v[204:207], v[188:191], v[132:135]
	s_waitcnt lgkmcnt(6)
	ds_read_b128 v[172:175], v16 offset:53248
	ds_read_b128 v[192:195], v18 offset:53248
	ds_read_b128 v[196:199], v18 offset:55296
	ds_read_b128 v[200:203], v18 offset:57344
	ds_read_b128 v[204:207], v18 offset:59392
	ds_read_b128 v[176:179], v16 offset:55296
	ds_read_b128 v[180:183], v16 offset:57344
	ds_read_b128 v[184:187], v16 offset:59392
	ds_read_b128 v[188:191], v16 offset:61440
	v_mfma_f32_16x16x32_f16 v[56:59], v[156:159], v[136:139], v[56:59]
	s_add_u32 m0, s28, 0x8000
	s_nop 0
	global_load_lds_dwordx4 v14, s[4:5]
	s_add_u32 s4, s4, s20
	s_addc_u32 s5, s5, 0
	s_waitcnt lgkmcnt(15)
	v_mfma_f32_16x16x32_f16 v[60:63], v[160:163], v[136:139], v[60:63]
	s_waitcnt lgkmcnt(14)
	v_mfma_f32_16x16x32_f16 v[64:67], v[164:167], v[136:139], v[64:67]
	s_waitcnt lgkmcnt(13)
	v_mfma_f32_16x16x32_f16 v[68:71], v[168:171], v[136:139], v[68:71]
	s_waitcnt lgkmcnt(12)
	v_mfma_f32_16x16x32_f16 v[72:75], v[156:159], v[140:143], v[72:75]
	v_mfma_f32_16x16x32_f16 v[76:79], v[160:163], v[140:143], v[76:79]
	v_mfma_f32_16x16x32_f16 v[80:83], v[164:167], v[140:143], v[80:83]
	s_add_u32 m0, s28, 0x9000
	s_nop 0
	global_load_lds_dwordx4 v10, s[6:7]
	v_mfma_f32_16x16x32_f16 v[84:87], v[168:171], v[140:143], v[84:87]
	s_waitcnt lgkmcnt(11)
	v_mfma_f32_16x16x32_f16 v[88:91], v[156:159], v[144:147], v[88:91]
	v_mfma_f32_16x16x32_f16 v[92:95], v[160:163], v[144:147], v[92:95]
	v_mfma_f32_16x16x32_f16 v[96:99], v[164:167], v[144:147], v[96:99]
	v_mfma_f32_16x16x32_f16 v[100:103], v[168:171], v[144:147], v[100:103]
	s_waitcnt lgkmcnt(10)
	v_mfma_f32_16x16x32_f16 v[104:107], v[156:159], v[148:151], v[104:107]
	v_mfma_f32_16x16x32_f16 v[108:111], v[160:163], v[148:151], v[108:111]
	s_add_u32 m0, s28, 0xb000
	s_nop 0
	global_load_lds_dwordx4 v11, s[6:7]
	s_add_u32 s6, s6, s20
	s_addc_u32 s7, s7, 0
	v_mfma_f32_16x16x32_f16 v[112:115], v[164:167], v[148:151], v[112:115]
	v_mfma_f32_16x16x32_f16 v[116:119], v[168:171], v[148:151], v[116:119]
	s_waitcnt lgkmcnt(9)
	v_mfma_f32_16x16x32_f16 v[120:123], v[156:159], v[152:155], v[120:123]
	v_mfma_f32_16x16x32_f16 v[124:127], v[160:163], v[152:155], v[124:127]
	v_mfma_f32_16x16x32_f16 v[128:131], v[164:167], v[152:155], v[128:131]
	v_mfma_f32_16x16x32_f16 v[132:135], v[168:171], v[152:155], v[132:135]
	s_waitcnt vmcnt(7) lgkmcnt(0)
	s_barrier
	s_waitcnt lgkmcnt(6)
	ds_read_b128 v[136:139], v19
	ds_read_b128 v[156:159], v21
	ds_read_b128 v[160:163], v21 offset:2048
	ds_read_b128 v[164:167], v21 offset:4096
	ds_read_b128 v[168:171], v21 offset:6144
	ds_read_b128 v[140:143], v19 offset:2048
	ds_read_b128 v[144:147], v19 offset:4096
	ds_read_b128 v[148:151], v19 offset:6144
	ds_read_b128 v[152:155], v19 offset:8192
	v_mfma_f32_16x16x32_f16 v[56:59], v[192:195], v[172:175], v[56:59]
	s_waitcnt lgkmcnt(15)
	v_mfma_f32_16x16x32_f16 v[60:63], v[196:199], v[172:175], v[60:63]
	s_waitcnt lgkmcnt(14)
	v_mfma_f32_16x16x32_f16 v[64:67], v[200:203], v[172:175], v[64:67]
	s_waitcnt lgkmcnt(13)
	v_mfma_f32_16x16x32_f16 v[68:71], v[204:207], v[172:175], v[68:71]
	s_waitcnt lgkmcnt(12)
	v_mfma_f32_16x16x32_f16 v[72:75], v[192:195], v[176:179], v[72:75]
	v_mfma_f32_16x16x32_f16 v[76:79], v[196:199], v[176:179], v[76:79]
	v_mfma_f32_16x16x32_f16 v[80:83], v[200:203], v[176:179], v[80:83]
	v_mfma_f32_16x16x32_f16 v[84:87], v[204:207], v[176:179], v[84:87]
	s_waitcnt lgkmcnt(11)
	v_mfma_f32_16x16x32_f16 v[88:91], v[192:195], v[180:183], v[88:91]
	v_mfma_f32_16x16x32_f16 v[92:95], v[196:199], v[180:183], v[92:95]
	v_mfma_f32_16x16x32_f16 v[96:99], v[200:203], v[180:183], v[96:99]
	v_mfma_f32_16x16x32_f16 v[100:103], v[204:207], v[180:183], v[100:103]
	s_waitcnt lgkmcnt(10)
	v_mfma_f32_16x16x32_f16 v[104:107], v[192:195], v[184:187], v[104:107]
	v_mfma_f32_16x16x32_f16 v[108:111], v[196:199], v[184:187], v[108:111]
	v_mfma_f32_16x16x32_f16 v[112:115], v[200:203], v[184:187], v[112:115]
	v_mfma_f32_16x16x32_f16 v[116:119], v[204:207], v[184:187], v[116:119]
	s_waitcnt lgkmcnt(9)
	v_mfma_f32_16x16x32_f16 v[120:123], v[192:195], v[188:191], v[120:123]
	v_mfma_f32_16x16x32_f16 v[124:127], v[196:199], v[188:191], v[124:127]
	v_mfma_f32_16x16x32_f16 v[128:131], v[200:203], v[188:191], v[128:131]
	v_mfma_f32_16x16x32_f16 v[132:135], v[204:207], v[188:191], v[132:135]
	s_waitcnt lgkmcnt(6)
	ds_read_b128 v[172:175], v20
	ds_read_b128 v[192:195], v22
	ds_read_b128 v[196:199], v22 offset:2048
	ds_read_b128 v[200:203], v22 offset:4096
	ds_read_b128 v[204:207], v22 offset:6144
	ds_read_b128 v[176:179], v20 offset:2048
	ds_read_b128 v[180:183], v20 offset:4096
	ds_read_b128 v[184:187], v20 offset:6144
	ds_read_b128 v[188:191], v20 offset:8192
	v_mfma_f32_16x16x32_f16 v[56:59], v[156:159], v[136:139], v[56:59]
	s_waitcnt lgkmcnt(15)
	v_mfma_f32_16x16x32_f16 v[60:63], v[160:163], v[136:139], v[60:63]
	s_waitcnt lgkmcnt(14)
	v_mfma_f32_16x16x32_f16 v[64:67], v[164:167], v[136:139], v[64:67]
	s_waitcnt lgkmcnt(13)
	v_mfma_f32_16x16x32_f16 v[68:71], v[168:171], v[136:139], v[68:71]
	s_waitcnt lgkmcnt(12)
	v_mfma_f32_16x16x32_f16 v[72:75], v[156:159], v[140:143], v[72:75]
	v_mfma_f32_16x16x32_f16 v[76:79], v[160:163], v[140:143], v[76:79]
	v_mfma_f32_16x16x32_f16 v[80:83], v[164:167], v[140:143], v[80:83]
	v_mfma_f32_16x16x32_f16 v[84:87], v[168:171], v[140:143], v[84:87]
	s_waitcnt lgkmcnt(11)
	v_mfma_f32_16x16x32_f16 v[88:91], v[156:159], v[144:147], v[88:91]
	v_mfma_f32_16x16x32_f16 v[92:95], v[160:163], v[144:147], v[92:95]
	v_mfma_f32_16x16x32_f16 v[96:99], v[164:167], v[144:147], v[96:99]
	v_mfma_f32_16x16x32_f16 v[100:103], v[168:171], v[144:147], v[100:103]
	s_waitcnt lgkmcnt(10)
	v_mfma_f32_16x16x32_f16 v[104:107], v[156:159], v[148:151], v[104:107]
	v_mfma_f32_16x16x32_f16 v[108:111], v[160:163], v[148:151], v[108:111]
	v_mfma_f32_16x16x32_f16 v[112:115], v[164:167], v[148:151], v[112:115]
	v_mfma_f32_16x16x32_f16 v[116:119], v[168:171], v[148:151], v[116:119]
	s_waitcnt lgkmcnt(9)
	v_mfma_f32_16x16x32_f16 v[120:123], v[156:159], v[152:155], v[120:123]
	v_mfma_f32_16x16x32_f16 v[124:127], v[160:163], v[152:155], v[124:127]
	v_mfma_f32_16x16x32_f16 v[128:131], v[164:167], v[152:155], v[128:131]
	v_mfma_f32_16x16x32_f16 v[132:135], v[168:171], v[152:155], v[132:135]
	s_waitcnt vmcnt(0) lgkmcnt(0)
	s_barrier
	s_waitcnt lgkmcnt(6)
	ds_read_b128 v[136:139], v15
	ds_read_b128 v[156:159], v17
	ds_read_b128 v[160:163], v17 offset:2048
	ds_read_b128 v[164:167], v17 offset:4096
	ds_read_b128 v[168:171], v17 offset:6144
	ds_read_b128 v[140:143], v15 offset:2048
	ds_read_b128 v[144:147], v15 offset:4096
	ds_read_b128 v[148:151], v15 offset:6144
	ds_read_b128 v[152:155], v15 offset:8192
	v_mfma_f32_16x16x32_f16 v[56:59], v[192:195], v[172:175], v[56:59]
	s_waitcnt lgkmcnt(15)
	v_mfma_f32_16x16x32_f16 v[60:63], v[196:199], v[172:175], v[60:63]
	s_waitcnt lgkmcnt(14)
	v_mfma_f32_16x16x32_f16 v[64:67], v[200:203], v[172:175], v[64:67]
	s_waitcnt lgkmcnt(13)
	v_mfma_f32_16x16x32_f16 v[68:71], v[204:207], v[172:175], v[68:71]
	s_waitcnt lgkmcnt(12)
	v_mfma_f32_16x16x32_f16 v[72:75], v[192:195], v[176:179], v[72:75]
	v_mfma_f32_16x16x32_f16 v[76:79], v[196:199], v[176:179], v[76:79]
	v_mfma_f32_16x16x32_f16 v[80:83], v[200:203], v[176:179], v[80:83]
	v_mfma_f32_16x16x32_f16 v[84:87], v[204:207], v[176:179], v[84:87]
	s_waitcnt lgkmcnt(11)
	v_mfma_f32_16x16x32_f16 v[88:91], v[192:195], v[180:183], v[88:91]
	v_mfma_f32_16x16x32_f16 v[92:95], v[196:199], v[180:183], v[92:95]
	v_mfma_f32_16x16x32_f16 v[96:99], v[200:203], v[180:183], v[96:99]
	v_mfma_f32_16x16x32_f16 v[100:103], v[204:207], v[180:183], v[100:103]
	s_waitcnt lgkmcnt(10)
	v_mfma_f32_16x16x32_f16 v[104:107], v[192:195], v[184:187], v[104:107]
	v_mfma_f32_16x16x32_f16 v[108:111], v[196:199], v[184:187], v[108:111]
	v_mfma_f32_16x16x32_f16 v[112:115], v[200:203], v[184:187], v[112:115]
	v_mfma_f32_16x16x32_f16 v[116:119], v[204:207], v[184:187], v[116:119]
	s_waitcnt lgkmcnt(9)
	v_mfma_f32_16x16x32_f16 v[120:123], v[192:195], v[188:191], v[120:123]
	v_mfma_f32_16x16x32_f16 v[124:127], v[196:199], v[188:191], v[124:127]
	v_mfma_f32_16x16x32_f16 v[128:131], v[200:203], v[188:191], v[128:131]
	v_mfma_f32_16x16x32_f16 v[132:135], v[204:207], v[188:191], v[132:135]
	s_waitcnt lgkmcnt(6)
	ds_read_b128 v[172:175], v16
	ds_read_b128 v[192:195], v18
	ds_read_b128 v[196:199], v18 offset:2048
	ds_read_b128 v[200:203], v18 offset:4096
	ds_read_b128 v[204:207], v18 offset:6144
	ds_read_b128 v[176:179], v16 offset:2048
	ds_read_b128 v[180:183], v16 offset:4096
	ds_read_b128 v[184:187], v16 offset:6144
	ds_read_b128 v[188:191], v16 offset:8192
	v_mfma_f32_16x16x32_f16 v[56:59], v[156:159], v[136:139], v[56:59]
	s_waitcnt lgkmcnt(15)
	v_mfma_f32_16x16x32_f16 v[60:63], v[160:163], v[136:139], v[60:63]
	s_waitcnt lgkmcnt(14)
	v_mfma_f32_16x16x32_f16 v[64:67], v[164:167], v[136:139], v[64:67]
	s_waitcnt lgkmcnt(13)
	v_mfma_f32_16x16x32_f16 v[68:71], v[168:171], v[136:139], v[68:71]
	s_waitcnt lgkmcnt(12)
	v_mfma_f32_16x16x32_f16 v[72:75], v[156:159], v[140:143], v[72:75]
	v_mfma_f32_16x16x32_f16 v[76:79], v[160:163], v[140:143], v[76:79]
	v_mfma_f32_16x16x32_f16 v[80:83], v[164:167], v[140:143], v[80:83]
	v_mfma_f32_16x16x32_f16 v[84:87], v[168:171], v[140:143], v[84:87]
	s_waitcnt lgkmcnt(11)
	v_mfma_f32_16x16x32_f16 v[88:91], v[156:159], v[144:147], v[88:91]
	v_mfma_f32_16x16x32_f16 v[92:95], v[160:163], v[144:147], v[92:95]
	v_mfma_f32_16x16x32_f16 v[96:99], v[164:167], v[144:147], v[96:99]
	v_mfma_f32_16x16x32_f16 v[100:103], v[168:171], v[144:147], v[100:103]
	s_waitcnt lgkmcnt(10)
	v_mfma_f32_16x16x32_f16 v[104:107], v[156:159], v[148:151], v[104:107]
	v_mfma_f32_16x16x32_f16 v[108:111], v[160:163], v[148:151], v[108:111]
	v_mfma_f32_16x16x32_f16 v[112:115], v[164:167], v[148:151], v[112:115]
	v_mfma_f32_16x16x32_f16 v[116:119], v[168:171], v[148:151], v[116:119]
	s_waitcnt lgkmcnt(9)
	v_mfma_f32_16x16x32_f16 v[120:123], v[156:159], v[152:155], v[120:123]
	v_mfma_f32_16x16x32_f16 v[124:127], v[160:163], v[152:155], v[124:127]
	v_mfma_f32_16x16x32_f16 v[128:131], v[164:167], v[152:155], v[128:131]
	v_mfma_f32_16x16x32_f16 v[132:135], v[168:171], v[152:155], v[132:135]
	s_waitcnt lgkmcnt(7)
	v_mfma_f32_16x16x32_f16 v[56:59], v[192:195], v[172:175], v[56:59]
	s_waitcnt lgkmcnt(6)
	v_mfma_f32_16x16x32_f16 v[60:63], v[196:199], v[172:175], v[60:63]
	s_waitcnt lgkmcnt(5)
	v_mfma_f32_16x16x32_f16 v[64:67], v[200:203], v[172:175], v[64:67]
	s_waitcnt lgkmcnt(4)
	v_mfma_f32_16x16x32_f16 v[68:71], v[204:207], v[172:175], v[68:71]
	s_waitcnt lgkmcnt(3)
	v_mfma_f32_16x16x32_f16 v[72:75], v[192:195], v[176:179], v[72:75]
	v_mfma_f32_16x16x32_f16 v[76:79], v[196:199], v[176:179], v[76:79]
	v_mfma_f32_16x16x32_f16 v[80:83], v[200:203], v[176:179], v[80:83]
	v_mfma_f32_16x16x32_f16 v[84:87], v[204:207], v[176:179], v[84:87]
	s_waitcnt lgkmcnt(2)
	v_mfma_f32_16x16x32_f16 v[88:91], v[192:195], v[180:183], v[88:91]
	v_mfma_f32_16x16x32_f16 v[92:95], v[196:199], v[180:183], v[92:95]
	v_mfma_f32_16x16x32_f16 v[96:99], v[200:203], v[180:183], v[96:99]
	v_mfma_f32_16x16x32_f16 v[100:103], v[204:207], v[180:183], v[100:103]
	s_waitcnt lgkmcnt(1)
	v_mfma_f32_16x16x32_f16 v[104:107], v[192:195], v[184:187], v[104:107]
	v_mfma_f32_16x16x32_f16 v[108:111], v[196:199], v[184:187], v[108:111]
	v_mfma_f32_16x16x32_f16 v[112:115], v[200:203], v[184:187], v[112:115]
	v_mfma_f32_16x16x32_f16 v[116:119], v[204:207], v[184:187], v[116:119]
	s_waitcnt lgkmcnt(0)
	v_mfma_f32_16x16x32_f16 v[120:123], v[192:195], v[188:191], v[120:123]
	v_mfma_f32_16x16x32_f16 v[124:127], v[196:199], v[188:191], v[124:127]
	v_mfma_f32_16x16x32_f16 v[128:131], v[200:203], v[188:191], v[128:131]
	v_mfma_f32_16x16x32_f16 v[132:135], v[204:207], v[188:191], v[132:135]
	s_nop 7
	s_nop 1
	v_mov_b32_e32 v211, s19
	v_add_f32_e32 v56, v56, v24
	v_add_f32_e32 v57, v57, v25
	v_add_f32_e32 v58, v58, v26
	v_add_f32_e32 v59, v59, v27
	v_add_f32_e32 v60, v60, v28
	v_add_f32_e32 v61, v61, v29
	v_add_f32_e32 v62, v62, v30
	v_add_f32_e32 v63, v63, v31
	v_add_f32_e32 v64, v64, v32
	v_add_f32_e32 v65, v65, v33
	v_add_f32_e32 v66, v66, v34
	v_add_f32_e32 v67, v67, v35
	v_add_f32_e32 v68, v68, v36
	v_add_f32_e32 v69, v69, v37
	v_add_f32_e32 v70, v70, v38
	v_add_f32_e32 v71, v71, v39
	v_mul_f32_e32 v208, v56, v56
	v_fmac_f32_e32 v208, v57, v57
	v_fmac_f32_e32 v208, v58, v58
	v_fmac_f32_e32 v208, v59, v59
	v_fmac_f32_e32 v208, v60, v60
	v_fmac_f32_e32 v208, v61, v61
	v_fmac_f32_e32 v208, v62, v62
	v_fmac_f32_e32 v208, v63, v63
	v_fmac_f32_e32 v208, v64, v64
	v_fmac_f32_e32 v208, v65, v65
	v_fmac_f32_e32 v208, v66, v66
	v_fmac_f32_e32 v208, v67, v67
	v_fmac_f32_e32 v208, v68, v68
	v_fmac_f32_e32 v208, v69, v69
	v_fmac_f32_e32 v208, v70, v70
	v_fmac_f32_e32 v208, v71, v71
	v_mov_b32_e32 v209, v208
	s_nop 1
	v_permlane16_swap_b32_e32 v208, v209
	v_add_f32_e32 v208, v208, v209
	v_mov_b32_e32 v209, v208
	s_nop 1
	v_permlane32_swap_b32_e32 v208, v209
	v_add_f32_e32 v208, v208, v209
	v_mov_b32_e32 v210, 0x358637bd
	v_fmac_f32_e32 v210, 0x3c800000, v208
	v_rsq_f32_e32 v210, v210
	s_add_u32 s24, s29, 0
	s_lshr_b32 s8, s24, 1
	s_lshl_b32 s8, s8, 12
	s_and_b32 s24, s24, 1
	s_lshl_b32 s24, s24, 8
	s_add_u32 s8, s8, s24
	v_mul_f32_e32 v210, v211, v210
	v_add_u32_e32 v212, s8, v23
	v_mul_f32_e32 v56, v56, v210
	v_mul_f32_e32 v57, v57, v210
	v_mul_f32_e32 v58, v58, v210
	v_mul_f32_e32 v59, v59, v210
	v_mul_f32_e32 v56, v56, v40
	v_mul_f32_e32 v57, v57, v41
	v_mul_f32_e32 v58, v58, v42
	v_mul_f32_e32 v59, v59, v43
	v_cvt_pk_f16_f32 v56, v56, v57
	v_cvt_pk_f16_f32 v57, v58, v59
	global_store_dwordx2 v212, v[56:57], s[22:23] offset:0
	v_mul_f32_e32 v60, v60, v210
	v_mul_f32_e32 v61, v61, v210
	v_mul_f32_e32 v62, v62, v210
	v_mul_f32_e32 v63, v63, v210
	v_mul_f32_e32 v60, v60, v44
	v_mul_f32_e32 v61, v61, v45
	v_mul_f32_e32 v62, v62, v46
	v_mul_f32_e32 v63, v63, v47
	v_cvt_pk_f16_f32 v60, v60, v61
	v_cvt_pk_f16_f32 v61, v62, v63
	global_store_dwordx2 v212, v[60:61], s[22:23] offset:1024
	v_mul_f32_e32 v64, v64, v210
	v_mul_f32_e32 v65, v65, v210
	v_mul_f32_e32 v66, v66, v210
	v_mul_f32_e32 v67, v67, v210
	v_mul_f32_e32 v64, v64, v48
	v_mul_f32_e32 v65, v65, v49
	v_mul_f32_e32 v66, v66, v50
	v_mul_f32_e32 v67, v67, v51
	v_cvt_pk_f16_f32 v64, v64, v65
	v_cvt_pk_f16_f32 v65, v66, v67
	global_store_dwordx2 v212, v[64:65], s[22:23] offset:2048
	v_mul_f32_e32 v68, v68, v210
	v_mul_f32_e32 v69, v69, v210
	v_mul_f32_e32 v70, v70, v210
	v_mul_f32_e32 v71, v71, v210
	v_mul_f32_e32 v68, v68, v52
	v_mul_f32_e32 v69, v69, v53
	v_mul_f32_e32 v70, v70, v54
	v_mul_f32_e32 v71, v71, v55
	v_cvt_pk_f16_f32 v68, v68, v69
	v_cvt_pk_f16_f32 v69, v70, v71
	global_store_dwordx2 v212, v[68:69], s[22:23] offset:3072
	v_add_f32_e32 v72, v72, v24
	v_add_f32_e32 v73, v73, v25
	v_add_f32_e32 v74, v74, v26
	v_add_f32_e32 v75, v75, v27
	v_add_f32_e32 v76, v76, v28
	v_add_f32_e32 v77, v77, v29
	v_add_f32_e32 v78, v78, v30
	v_add_f32_e32 v79, v79, v31
	v_add_f32_e32 v80, v80, v32
	v_add_f32_e32 v81, v81, v33
	v_add_f32_e32 v82, v82, v34
	v_add_f32_e32 v83, v83, v35
	v_add_f32_e32 v84, v84, v36
	v_add_f32_e32 v85, v85, v37
	v_add_f32_e32 v86, v86, v38
	v_add_f32_e32 v87, v87, v39
	v_mul_f32_e32 v208, v72, v72
	v_fmac_f32_e32 v208, v73, v73
	v_fmac_f32_e32 v208, v74, v74
	v_fmac_f32_e32 v208, v75, v75
	v_fmac_f32_e32 v208, v76, v76
	v_fmac_f32_e32 v208, v77, v77
	v_fmac_f32_e32 v208, v78, v78
	v_fmac_f32_e32 v208, v79, v79
	v_fmac_f32_e32 v208, v80, v80
	v_fmac_f32_e32 v208, v81, v81
	v_fmac_f32_e32 v208, v82, v82
	v_fmac_f32_e32 v208, v83, v83
	v_fmac_f32_e32 v208, v84, v84
	v_fmac_f32_e32 v208, v85, v85
	v_fmac_f32_e32 v208, v86, v86
	v_fmac_f32_e32 v208, v87, v87
	v_mov_b32_e32 v209, v208
	s_nop 1
	v_permlane16_swap_b32_e32 v208, v209
	v_add_f32_e32 v208, v208, v209
	v_mov_b32_e32 v209, v208
	s_nop 1
	v_permlane32_swap_b32_e32 v208, v209
	v_add_f32_e32 v208, v208, v209
	v_mov_b32_e32 v210, 0x358637bd
	v_fmac_f32_e32 v210, 0x3c800000, v208
	v_rsq_f32_e32 v210, v210
	s_add_u32 s24, s29, 1
	s_lshr_b32 s8, s24, 1
	s_lshl_b32 s8, s8, 12
	s_and_b32 s24, s24, 1
	s_lshl_b32 s24, s24, 8
	s_add_u32 s8, s8, s24
	v_mul_f32_e32 v210, v211, v210
	v_add_u32_e32 v212, s8, v23
	v_mul_f32_e32 v72, v72, v210
	v_mul_f32_e32 v73, v73, v210
	v_mul_f32_e32 v74, v74, v210
	v_mul_f32_e32 v75, v75, v210
	v_mul_f32_e32 v72, v72, v40
	v_mul_f32_e32 v73, v73, v41
	v_mul_f32_e32 v74, v74, v42
	v_mul_f32_e32 v75, v75, v43
	v_cvt_pk_f16_f32 v72, v72, v73
	v_cvt_pk_f16_f32 v73, v74, v75
	global_store_dwordx2 v212, v[72:73], s[22:23] offset:0
	v_mul_f32_e32 v76, v76, v210
	v_mul_f32_e32 v77, v77, v210
	v_mul_f32_e32 v78, v78, v210
	v_mul_f32_e32 v79, v79, v210
	v_mul_f32_e32 v76, v76, v44
	v_mul_f32_e32 v77, v77, v45
	v_mul_f32_e32 v78, v78, v46
	v_mul_f32_e32 v79, v79, v47
	v_cvt_pk_f16_f32 v76, v76, v77
	v_cvt_pk_f16_f32 v77, v78, v79
	global_store_dwordx2 v212, v[76:77], s[22:23] offset:1024
	v_mul_f32_e32 v80, v80, v210
	v_mul_f32_e32 v81, v81, v210
	v_mul_f32_e32 v82, v82, v210
	v_mul_f32_e32 v83, v83, v210
	v_mul_f32_e32 v80, v80, v48
	v_mul_f32_e32 v81, v81, v49
	v_mul_f32_e32 v82, v82, v50
	v_mul_f32_e32 v83, v83, v51
	v_cvt_pk_f16_f32 v80, v80, v81
	v_cvt_pk_f16_f32 v81, v82, v83
	global_store_dwordx2 v212, v[80:81], s[22:23] offset:2048
	v_mul_f32_e32 v84, v84, v210
	v_mul_f32_e32 v85, v85, v210
	v_mul_f32_e32 v86, v86, v210
	v_mul_f32_e32 v87, v87, v210
	v_mul_f32_e32 v84, v84, v52
	v_mul_f32_e32 v85, v85, v53
	v_mul_f32_e32 v86, v86, v54
	v_mul_f32_e32 v87, v87, v55
	v_cvt_pk_f16_f32 v84, v84, v85
	v_cvt_pk_f16_f32 v85, v86, v87
	global_store_dwordx2 v212, v[84:85], s[22:23] offset:3072
	v_add_f32_e32 v88, v88, v24
	v_add_f32_e32 v89, v89, v25
	v_add_f32_e32 v90, v90, v26
	v_add_f32_e32 v91, v91, v27
	v_add_f32_e32 v92, v92, v28
	v_add_f32_e32 v93, v93, v29
	v_add_f32_e32 v94, v94, v30
	v_add_f32_e32 v95, v95, v31
	v_add_f32_e32 v96, v96, v32
	v_add_f32_e32 v97, v97, v33
	v_add_f32_e32 v98, v98, v34
	v_add_f32_e32 v99, v99, v35
	v_add_f32_e32 v100, v100, v36
	v_add_f32_e32 v101, v101, v37
	v_add_f32_e32 v102, v102, v38
	v_add_f32_e32 v103, v103, v39
	v_mul_f32_e32 v208, v88, v88
	v_fmac_f32_e32 v208, v89, v89
	v_fmac_f32_e32 v208, v90, v90
	v_fmac_f32_e32 v208, v91, v91
	v_fmac_f32_e32 v208, v92, v92
	v_fmac_f32_e32 v208, v93, v93
	v_fmac_f32_e32 v208, v94, v94
	v_fmac_f32_e32 v208, v95, v95
	v_fmac_f32_e32 v208, v96, v96
	v_fmac_f32_e32 v208, v97, v97
	v_fmac_f32_e32 v208, v98, v98
	v_fmac_f32_e32 v208, v99, v99
	v_fmac_f32_e32 v208, v100, v100
	v_fmac_f32_e32 v208, v101, v101
	v_fmac_f32_e32 v208, v102, v102
	v_fmac_f32_e32 v208, v103, v103
	v_mov_b32_e32 v209, v208
	s_nop 1
	v_permlane16_swap_b32_e32 v208, v209
	v_add_f32_e32 v208, v208, v209
	v_mov_b32_e32 v209, v208
	s_nop 1
	v_permlane32_swap_b32_e32 v208, v209
	v_add_f32_e32 v208, v208, v209
	v_mov_b32_e32 v210, 0x358637bd
	v_fmac_f32_e32 v210, 0x3c800000, v208
	v_rsq_f32_e32 v210, v210
	s_add_u32 s24, s29, 2
	s_lshr_b32 s8, s24, 1
	s_lshl_b32 s8, s8, 12
	s_and_b32 s24, s24, 1
	s_lshl_b32 s24, s24, 8
	s_add_u32 s8, s8, s24
	v_mul_f32_e32 v210, v211, v210
	v_add_u32_e32 v212, s8, v23
	v_mul_f32_e32 v88, v88, v210
	v_mul_f32_e32 v89, v89, v210
	v_mul_f32_e32 v90, v90, v210
	v_mul_f32_e32 v91, v91, v210
	v_mul_f32_e32 v88, v88, v40
	v_mul_f32_e32 v89, v89, v41
	v_mul_f32_e32 v90, v90, v42
	v_mul_f32_e32 v91, v91, v43
	v_cvt_pk_f16_f32 v88, v88, v89
	v_cvt_pk_f16_f32 v89, v90, v91
	global_store_dwordx2 v212, v[88:89], s[22:23] offset:0
	v_mul_f32_e32 v92, v92, v210
	v_mul_f32_e32 v93, v93, v210
	v_mul_f32_e32 v94, v94, v210
	v_mul_f32_e32 v95, v95, v210
	v_mul_f32_e32 v92, v92, v44
	v_mul_f32_e32 v93, v93, v45
	v_mul_f32_e32 v94, v94, v46
	v_mul_f32_e32 v95, v95, v47
	v_cvt_pk_f16_f32 v92, v92, v93
	v_cvt_pk_f16_f32 v93, v94, v95
	global_store_dwordx2 v212, v[92:93], s[22:23] offset:1024
	v_mul_f32_e32 v96, v96, v210
	v_mul_f32_e32 v97, v97, v210
	v_mul_f32_e32 v98, v98, v210
	v_mul_f32_e32 v99, v99, v210
	v_mul_f32_e32 v96, v96, v48
	v_mul_f32_e32 v97, v97, v49
	v_mul_f32_e32 v98, v98, v50
	v_mul_f32_e32 v99, v99, v51
	v_cvt_pk_f16_f32 v96, v96, v97
	v_cvt_pk_f16_f32 v97, v98, v99
	global_store_dwordx2 v212, v[96:97], s[22:23] offset:2048
	v_mul_f32_e32 v100, v100, v210
	v_mul_f32_e32 v101, v101, v210
	v_mul_f32_e32 v102, v102, v210
	v_mul_f32_e32 v103, v103, v210
	v_mul_f32_e32 v100, v100, v52
	v_mul_f32_e32 v101, v101, v53
	v_mul_f32_e32 v102, v102, v54
	v_mul_f32_e32 v103, v103, v55
	v_cvt_pk_f16_f32 v100, v100, v101
	v_cvt_pk_f16_f32 v101, v102, v103
	global_store_dwordx2 v212, v[100:101], s[22:23] offset:3072
	v_add_f32_e32 v104, v104, v24
	v_add_f32_e32 v105, v105, v25
	v_add_f32_e32 v106, v106, v26
	v_add_f32_e32 v107, v107, v27
	v_add_f32_e32 v108, v108, v28
	v_add_f32_e32 v109, v109, v29
	v_add_f32_e32 v110, v110, v30
	v_add_f32_e32 v111, v111, v31
	v_add_f32_e32 v112, v112, v32
	v_add_f32_e32 v113, v113, v33
	v_add_f32_e32 v114, v114, v34
	v_add_f32_e32 v115, v115, v35
	v_add_f32_e32 v116, v116, v36
	v_add_f32_e32 v117, v117, v37
	v_add_f32_e32 v118, v118, v38
	v_add_f32_e32 v119, v119, v39
	v_mul_f32_e32 v208, v104, v104
	v_fmac_f32_e32 v208, v105, v105
	v_fmac_f32_e32 v208, v106, v106
	v_fmac_f32_e32 v208, v107, v107
	v_fmac_f32_e32 v208, v108, v108
	v_fmac_f32_e32 v208, v109, v109
	v_fmac_f32_e32 v208, v110, v110
	v_fmac_f32_e32 v208, v111, v111
	v_fmac_f32_e32 v208, v112, v112
	v_fmac_f32_e32 v208, v113, v113
	v_fmac_f32_e32 v208, v114, v114
	v_fmac_f32_e32 v208, v115, v115
	v_fmac_f32_e32 v208, v116, v116
	v_fmac_f32_e32 v208, v117, v117
	v_fmac_f32_e32 v208, v118, v118
	v_fmac_f32_e32 v208, v119, v119
	v_mov_b32_e32 v209, v208
	s_nop 1
	v_permlane16_swap_b32_e32 v208, v209
	v_add_f32_e32 v208, v208, v209
	v_mov_b32_e32 v209, v208
	s_nop 1
	v_permlane32_swap_b32_e32 v208, v209
	v_add_f32_e32 v208, v208, v209
	v_mov_b32_e32 v210, 0x358637bd
	v_fmac_f32_e32 v210, 0x3c800000, v208
	v_rsq_f32_e32 v210, v210
	s_add_u32 s24, s29, 3
	s_lshr_b32 s8, s24, 1
	s_lshl_b32 s8, s8, 12
	s_and_b32 s24, s24, 1
	s_lshl_b32 s24, s24, 8
	s_add_u32 s8, s8, s24
	v_mul_f32_e32 v210, v211, v210
	v_add_u32_e32 v212, s8, v23
	v_mul_f32_e32 v104, v104, v210
	v_mul_f32_e32 v105, v105, v210
	v_mul_f32_e32 v106, v106, v210
	v_mul_f32_e32 v107, v107, v210
	v_mul_f32_e32 v104, v104, v40
	v_mul_f32_e32 v105, v105, v41
	v_mul_f32_e32 v106, v106, v42
	v_mul_f32_e32 v107, v107, v43
	v_cvt_pk_f16_f32 v104, v104, v105
	v_cvt_pk_f16_f32 v105, v106, v107
	global_store_dwordx2 v212, v[104:105], s[22:23] offset:0
	v_mul_f32_e32 v108, v108, v210
	v_mul_f32_e32 v109, v109, v210
	v_mul_f32_e32 v110, v110, v210
	v_mul_f32_e32 v111, v111, v210
	v_mul_f32_e32 v108, v108, v44
	v_mul_f32_e32 v109, v109, v45
	v_mul_f32_e32 v110, v110, v46
	v_mul_f32_e32 v111, v111, v47
	v_cvt_pk_f16_f32 v108, v108, v109
	v_cvt_pk_f16_f32 v109, v110, v111
	global_store_dwordx2 v212, v[108:109], s[22:23] offset:1024
	v_mul_f32_e32 v112, v112, v210
	v_mul_f32_e32 v113, v113, v210
	v_mul_f32_e32 v114, v114, v210
	v_mul_f32_e32 v115, v115, v210
	v_mul_f32_e32 v112, v112, v48
	v_mul_f32_e32 v113, v113, v49
	v_mul_f32_e32 v114, v114, v50
	v_mul_f32_e32 v115, v115, v51
	v_cvt_pk_f16_f32 v112, v112, v113
	v_cvt_pk_f16_f32 v113, v114, v115
	global_store_dwordx2 v212, v[112:113], s[22:23] offset:2048
	v_mul_f32_e32 v116, v116, v210
	v_mul_f32_e32 v117, v117, v210
	v_mul_f32_e32 v118, v118, v210
	v_mul_f32_e32 v119, v119, v210
	v_mul_f32_e32 v116, v116, v52
	v_mul_f32_e32 v117, v117, v53
	v_mul_f32_e32 v118, v118, v54
	v_mul_f32_e32 v119, v119, v55
	v_cvt_pk_f16_f32 v116, v116, v117
	v_cvt_pk_f16_f32 v117, v118, v119
	global_store_dwordx2 v212, v[116:117], s[22:23] offset:3072
	v_add_f32_e32 v120, v120, v24
	v_add_f32_e32 v121, v121, v25
	v_add_f32_e32 v122, v122, v26
	v_add_f32_e32 v123, v123, v27
	v_add_f32_e32 v124, v124, v28
	v_add_f32_e32 v125, v125, v29
	v_add_f32_e32 v126, v126, v30
	v_add_f32_e32 v127, v127, v31
	v_add_f32_e32 v128, v128, v32
	v_add_f32_e32 v129, v129, v33
	v_add_f32_e32 v130, v130, v34
	v_add_f32_e32 v131, v131, v35
	v_add_f32_e32 v132, v132, v36
	v_add_f32_e32 v133, v133, v37
	v_add_f32_e32 v134, v134, v38
	v_add_f32_e32 v135, v135, v39
	v_mul_f32_e32 v208, v120, v120
	v_fmac_f32_e32 v208, v121, v121
	v_fmac_f32_e32 v208, v122, v122
	v_fmac_f32_e32 v208, v123, v123
	v_fmac_f32_e32 v208, v124, v124
	v_fmac_f32_e32 v208, v125, v125
	v_fmac_f32_e32 v208, v126, v126
	v_fmac_f32_e32 v208, v127, v127
	v_fmac_f32_e32 v208, v128, v128
	v_fmac_f32_e32 v208, v129, v129
	v_fmac_f32_e32 v208, v130, v130
	v_fmac_f32_e32 v208, v131, v131
	v_fmac_f32_e32 v208, v132, v132
	v_fmac_f32_e32 v208, v133, v133
	v_fmac_f32_e32 v208, v134, v134
	v_fmac_f32_e32 v208, v135, v135
	v_mov_b32_e32 v209, v208
	s_nop 1
	v_permlane16_swap_b32_e32 v208, v209
	v_add_f32_e32 v208, v208, v209
	v_mov_b32_e32 v209, v208
	s_nop 1
	v_permlane32_swap_b32_e32 v208, v209
	v_add_f32_e32 v208, v208, v209
	v_mov_b32_e32 v210, 0x358637bd
	v_fmac_f32_e32 v210, 0x3c800000, v208
	v_rsq_f32_e32 v210, v210
	s_add_u32 s24, s29, 4
	s_lshr_b32 s8, s24, 1
	s_lshl_b32 s8, s8, 12
	s_and_b32 s24, s24, 1
	s_lshl_b32 s24, s24, 8
	s_add_u32 s8, s8, s24
	v_mul_f32_e32 v210, v211, v210
	v_add_u32_e32 v212, s8, v23
	v_mul_f32_e32 v120, v120, v210
	v_mul_f32_e32 v121, v121, v210
	v_mul_f32_e32 v122, v122, v210
	v_mul_f32_e32 v123, v123, v210
	v_mul_f32_e32 v120, v120, v40
	v_mul_f32_e32 v121, v121, v41
	v_mul_f32_e32 v122, v122, v42
	v_mul_f32_e32 v123, v123, v43
	v_cvt_pk_f16_f32 v120, v120, v121
	v_cvt_pk_f16_f32 v121, v122, v123
	global_store_dwordx2 v212, v[120:121], s[22:23] offset:0
	v_mul_f32_e32 v124, v124, v210
	v_mul_f32_e32 v125, v125, v210
	v_mul_f32_e32 v126, v126, v210
	v_mul_f32_e32 v127, v127, v210
	v_mul_f32_e32 v124, v124, v44
	v_mul_f32_e32 v125, v125, v45
	v_mul_f32_e32 v126, v126, v46
	v_mul_f32_e32 v127, v127, v47
	v_cvt_pk_f16_f32 v124, v124, v125
	v_cvt_pk_f16_f32 v125, v126, v127
	global_store_dwordx2 v212, v[124:125], s[22:23] offset:1024
	v_mul_f32_e32 v128, v128, v210
	v_mul_f32_e32 v129, v129, v210
	v_mul_f32_e32 v130, v130, v210
	v_mul_f32_e32 v131, v131, v210
	v_mul_f32_e32 v128, v128, v48
	v_mul_f32_e32 v129, v129, v49
	v_mul_f32_e32 v130, v130, v50
	v_mul_f32_e32 v131, v131, v51
	v_cvt_pk_f16_f32 v128, v128, v129
	v_cvt_pk_f16_f32 v129, v130, v131
	global_store_dwordx2 v212, v[128:129], s[22:23] offset:2048
	v_mul_f32_e32 v132, v132, v210
	v_mul_f32_e32 v133, v133, v210
	v_mul_f32_e32 v134, v134, v210
	v_mul_f32_e32 v135, v135, v210
	v_mul_f32_e32 v132, v132, v52
	v_mul_f32_e32 v133, v133, v53
	v_mul_f32_e32 v134, v134, v54
	v_mul_f32_e32 v135, v135, v55
	v_cvt_pk_f16_f32 v132, v132, v133
	v_cvt_pk_f16_f32 v133, v134, v135
	global_store_dwordx2 v212, v[132:133], s[22:23] offset:3072
	s_branch .Lpf_done
.Lpf_vKB:
	s_lshl_b32 s25, s25, 6
	s_add_u32 s25, s25, 32
	s_add_u32 s29, s10, s25
	s_lshr_b32 s29, s29, 4
	v_add_u32_e32 v5, s25, v3
	v_lshlrev_b32_e32 v5, 7, v5
	v_add_u32_e32 v15, v5, v6
	v_add_u32_e32 v16, v5, v7
	v_add_u32_e32 v5, 0x9000, v9
	v_add_u32_e32 v17, v5, v6
	v_add_u32_e32 v18, v5, v7
	v_add_u32_e32 v19, 0x1a000, v15
	v_add_u32_e32 v20, 0x1a000, v16
	v_add_u32_e32 v21, 0x1a000, v17
	v_add_u32_e32 v22, 0x1a000, v18
	v_lshlrev_b32_e32 v5, 4, v4
	global_load_dwordx4 v[24:27], v5, s[14:15] offset:0
	global_load_dwordx4 v[28:31], v5, s[14:15] offset:64
	global_load_dwordx4 v[32:35], v5, s[14:15] offset:128
	global_load_dwordx4 v[36:39], v5, s[14:15] offset:192
	global_load_dwordx4 v[40:43], v5, s[16:17] offset:0
	global_load_dwordx4 v[44:47], v5, s[16:17] offset:64
	global_load_dwordx4 v[48:51], v5, s[16:17] offset:128
	global_load_dwordx4 v[52:55], v5, s[16:17] offset:192
	s_add_u32 m0, s28, 0x0
	s_nop 0
	global_load_lds_dwordx4 v10, s[4:5]
	s_add_u32 m0, s28, 0x2000
	s_nop 0
	global_load_lds_dwordx4 v11, s[4:5]
	s_add_u32 m0, s28, 0x4000
	s_nop 0
	global_load_lds_dwordx4 v12, s[4:5]
	s_add_u32 m0, s28, 0x6000
	s_nop 0
	global_load_lds_dwordx4 v13, s[4:5]
	s_add_u32 s4, s4, s20
	s_addc_u32 s5, s5, 0
	s_add_u32 m0, s28, 0x9000
	s_nop 0
	global_load_lds_dwordx4 v10, s[6:7]
	s_add_u32 m0, s28, 0xb000
	s_nop 0
	global_load_lds_dwordx4 v11, s[6:7]
	s_add_u32 s6, s6, s20
	s_addc_u32 s7, s7, 0
	s_add_u32 m0, s28, 0xd000
	s_nop 0
	global_load_lds_dwordx4 v10, s[4:5]
	s_add_u32 m0, s28, 0xf000
	s_nop 0
	global_load_lds_dwordx4 v11, s[4:5]
	s_add_u32 m0, s28, 0x11000
	s_nop 0
	global_load_lds_dwordx4 v12, s[4:5]
	s_add_u32 m0, s28, 0x13000
	s_nop 0
	global_load_lds_dwordx4 v13, s[4:5]
	s_add_u32 s4, s4, s20
	s_addc_u32 s5, s5, 0
	s_add_u32 m0, s28, 0x16000
	s_nop 0
	global_load_lds_dwordx4 v10, s[6:7]
	s_add_u32 m0, s28, 0x18000
	s_nop 0
	global_load_lds_dwordx4 v11, s[6:7]
	s_add_u32 s6, s6, s20
	s_addc_u32 s7, s7, 0
	s_add_u32 m0, s28, 0x1a000
	s_nop 0
	global_load_lds_dwordx4 v10, s[4:5]
	s_add_u32 m0, s28, 0x1c000
	s_nop 0
	global_load_lds_dwordx4 v11, s[4:5]
	s_add_u32 m0, s28, 0x1e000
	s_nop 0
	global_load_lds_dwordx4 v12, s[4:5]
	s_add_u32 m0, s28, 0x20000
	s_nop 0
	global_load_lds_dwordx4 v13, s[4:5]
	s_add_u32 s4, s4, s20
	s_addc_u32 s5, s5, 0
	s_add_u32 m0, s28, 0x23000
	s_nop 0
	global_load_lds_dwordx4 v10, s[6:7]
	s_add_u32 m0, s28, 0x25000
	s_nop 0
	global_load_lds_dwordx4 v11, s[6:7]
	s_add_u32 s6, s6, s20
	s_addc_u32 s7, s7, 0
	s_waitcnt vmcnt(12) lgkmcnt(0)
	s_barrier
	s_waitcnt lgkmcnt(7)
	ds_read_b128 v[136:139], v15
	ds_read_b128 v[156:159], v17
	ds_read_b128 v[160:163], v17 offset:2048
	ds_read_b128 v[164:167], v17 offset:4096
	ds_read_b128 v[168:171], v17 offset:6144
	ds_read_b128 v[140:143], v15 offset:2048
	ds_read_b128 v[144:147], v15 offset:4096
	ds_read_b128 v[148:151], v15 offset:6144
	s_waitcnt lgkmcnt(7)
	ds_read_b128 v[172:175], v16
	ds_read_b128 v[192:195], v18
	ds_read_b128 v[196:199], v18 offset:2048
	ds_read_b128 v[200:203], v18 offset:4096
	ds_read_b128 v[204:207], v18 offset:6144
	ds_read_b128 v[176:179], v16 offset:2048
	ds_read_b128 v[180:183], v16 offset:4096
	ds_read_b128 v[184:187], v16 offset:6144
	s_waitcnt lgkmcnt(14)
	v_mfma_f32_16x16x32_f16 v[56:59], v[156:159], v[136:139], 0
	s_waitcnt lgkmcnt(13)
	v_mfma_f32_16x16x32_f16 v[60:63], v[160:163], v[136:139], 0
	s_waitcnt lgkmcnt(12)
	v_mfma_f32_16x16x32_f16 v[64:67], v[164:167], v[136:139], 0
	s_waitcnt lgkmcnt(11)
	v_mfma_f32_16x16x32_f16 v[68:71], v[168:171], v[136:139], 0
	s_waitcnt lgkmcnt(10)
	v_mfma_f32_16x16x32_f16 v[72:75], v[156:159], v[140:143], 0
	v_mfma_f32_16x16x32_f16 v[76:79], v[160:163], v[140:143], 0
	v_mfma_f32_16x16x32_f16 v[80:83], v[164:167], v[140:143], 0
	v_mfma_f32_16x16x32_f16 v[84:87], v[168:171], v[140:143], 0
	s_waitcnt lgkmcnt(9)
	v_mfma_f32_16x16x32_f16 v[88:91], v[156:159], v[144:147], 0
	v_mfma_f32_16x16x32_f16 v[92:95], v[160:163], v[144:147], 0
	v_mfma_f32_16x16x32_f16 v[96:99], v[164:167], v[144:147], 0
	v_mfma_f32_16x16x32_f16 v[100:103], v[168:171], v[144:147], 0
	s_waitcnt lgkmcnt(8)
	v_mfma_f32_16x16x32_f16 v[104:107], v[156:159], v[148:151], 0
	v_mfma_f32_16x16x32_f16 v[108:111], v[160:163], v[148:151], 0
	v_mfma_f32_16x16x32_f16 v[112:115], v[164:167], v[148:151], 0
	v_mfma_f32_16x16x32_f16 v[116:119], v[168:171], v[148:151], 0
	s_waitcnt vmcnt(6) lgkmcnt(0)
	s_barrier
	s_waitcnt lgkmcnt(7)
	ds_read_b128 v[136:139], v15 offset:53248
	ds_read_b128 v[156:159], v17 offset:53248
	ds_read_b128 v[160:163], v17 offset:55296
	ds_read_b128 v[164:167], v17 offset:57344
	ds_read_b128 v[168:171], v17 offset:59392
	ds_read_b128 v[140:143], v15 offset:55296
	ds_read_b128 v[144:147], v15 offset:57344
	ds_read_b128 v[148:151], v15 offset:59392
	s_waitcnt lgkmcnt(14)
	v_mfma_f32_16x16x32_f16 v[56:59], v[192:195], v[172:175], v[56:59]
	s_add_u32 m0, s28, 0x0
	s_nop 0
	global_load_lds_dwordx4 v10, s[4:5]
	s_waitcnt lgkmcnt(13)
	v_mfma_f32_16x16x32_f16 v[60:63], v[196:199], v[172:175], v[60:63]
	s_waitcnt lgkmcnt(12)
	v_mfma_f32_16x16x32_f16 v[64:67], v[200:203], v[172:175], v[64:67]
	s_waitcnt lgkmcnt(11)
	v_mfma_f32_16x16x32_f16 v[68:71], v[204:207], v[172:175], v[68:71]
	s_waitcnt lgkmcnt(10)
	v_mfma_f32_16x16x32_f16 v[72:75], v[192:195], v[176:179], v[72:75]
	v_mfma_f32_16x16x32_f16 v[76:79], v[196:199], v[176:179], v[76:79]
	s_add_u32 m0, s28, 0x2000
	s_nop 0
	global_load_lds_dwordx4 v11, s[4:5]
	v_mfma_f32_16x16x32_f16 v[80:83], v[200:203], v[176:179], v[80:83]
	v_mfma_f32_16x16x32_f16 v[84:87], v[204:207], v[176:179], v[84:87]
	s_waitcnt lgkmcnt(9)
	v_mfma_f32_16x16x32_f16 v[88:91], v[192:195], v[180:183], v[88:91]
	v_mfma_f32_16x16x32_f16 v[92:95], v[196:199], v[180:183], v[92:95]
	v_mfma_f32_16x16x32_f16 v[96:99], v[200:203], v[180:183], v[96:99]
	s_add_u32 m0, s28, 0x4000
	s_nop 0
	global_load_lds_dwordx4 v12, s[4:5]
	v_mfma_f32_16x16x32_f16 v[100:103], v[204:207], v[180:183], v[100:103]
	s_waitcnt lgkmcnt(8)
	v_mfma_f32_16x16x32_f16 v[104:107], v[192:195], v[184:187], v[104:107]
	v_mfma_f32_16x16x32_f16 v[108:111], v[196:199], v[184:187], v[108:111]
	v_mfma_f32_16x16x32_f16 v[112:115], v[200:203], v[184:187], v[112:115]
	v_mfma_f32_16x16x32_f16 v[116:119], v[204:207], v[184:187], v[116:119]
	s_waitcnt lgkmcnt(7)
	ds_read_b128 v[172:175], v16 offset:53248
	ds_read_b128 v[192:195], v18 offset:53248
	ds_read_b128 v[196:199], v18 offset:55296
	ds_read_b128 v[200:203], v18 offset:57344
	ds_read_b128 v[204:207], v18 offset:59392
	ds_read_b128 v[176:179], v16 offset:55296
	ds_read_b128 v[180:183], v16 offset:57344
	ds_read_b128 v[184:187], v16 offset:59392
	s_waitcnt lgkmcnt(14)
	v_mfma_f32_16x16x32_f16 v[56:59], v[156:159], v[136:139], v[56:59]
	s_add_u32 m0, s28, 0x6000
	s_nop 0
	global_load_lds_dwordx4 v13, s[4:5]
	s_add_u32 s4, s4, s20
	s_addc_u32 s5, s5, 0
	s_waitcnt lgkmcnt(13)
	v_mfma_f32_16x16x32_f16 v[60:63], v[160:163], v[136:139], v[60:63]
	s_waitcnt lgkmcnt(12)
	v_mfma_f32_16x16x32_f16 v[64:67], v[164:167], v[136:139], v[64:67]
	s_waitcnt lgkmcnt(11)
	v_mfma_f32_16x16x32_f16 v[68:71], v[168:171], v[136:139], v[68:71]
	s_waitcnt lgkmcnt(10)
	v_mfma_f32_16x16x32_f16 v[72:75], v[156:159], v[140:143], v[72:75]
	v_mfma_f32_16x16x32_f16 v[76:79], v[160:163], v[140:143], v[76:79]
	s_add_u32 m0, s28, 0x9000
	s_nop 0
	global_load_lds_dwordx4 v10, s[6:7]
	v_mfma_f32_16x16x32_f16 v[80:83], v[164:167], v[140:143], v[80:83]
	v_mfma_f32_16x16x32_f16 v[84:87], v[168:171], v[140:143], v[84:87]
	s_waitcnt lgkmcnt(9)
	v_mfma_f32_16x16x32_f16 v[88:91], v[156:159], v[144:147], v[88:91]
	v_mfma_f32_16x16x32_f16 v[92:95], v[160:163], v[144:147], v[92:95]
	v_mfma_f32_16x16x32_f16 v[96:99], v[164:167], v[144:147], v[96:99]
	s_add_u32 m0, s28, 0xb000
	s_nop 0
	global_load_lds_dwordx4 v11, s[6:7]
	s_add_u32 s6, s6, s20
	s_addc_u32 s7, s7, 0
	v_mfma_f32_16x16x32_f16 v[100:103], v[168:171], v[144:147], v[100:103]
	s_waitcnt lgkmcnt(8)
	v_mfma_f32_16x16x32_f16 v[104:107], v[156:159], v[148:151], v[104:107]
	v_mfma_f32_16x16x32_f16 v[108:111], v[160:163], v[148:151], v[108:111]
	v_mfma_f32_16x16x32_f16 v[112:115], v[164:167], v[148:151], v[112:115]
	v_mfma_f32_16x16x32_f16 v[116:119], v[168:171], v[148:151], v[116:119]
	s_waitcnt vmcnt(6) lgkmcnt(0)
	s_barrier
	s_waitcnt lgkmcnt(7)
	ds_read_b128 v[136:139], v19
	ds_read_b128 v[156:159], v21
	ds_read_b128 v[160:163], v21 offset:2048
	ds_read_b128 v[164:167], v21 offset:4096
	ds_read_b128 v[168:171], v21 offset:6144
	ds_read_b128 v[140:143], v19 offset:2048
	ds_read_b128 v[144:147], v19 offset:4096
	ds_read_b128 v[148:151], v19 offset:6144
	s_waitcnt lgkmcnt(14)
	v_mfma_f32_16x16x32_f16 v[56:59], v[192:195], v[172:175], v[56:59]
	s_add_u32 m0, s28, 0xd000
	s_nop 0
	global_load_lds_dwordx4 v10, s[4:5]
	s_waitcnt lgkmcnt(13)
	v_mfma_f32_16x16x32_f16 v[60:63], v[196:199], v[172:175], v[60:63]
	s_waitcnt lgkmcnt(12)
	v_mfma_f32_16x16x32_f16 v[64:67], v[200:203], v[172:175], v[64:67]
	s_waitcnt lgkmcnt(11)
	v_mfma_f32_16x16x32_f16 v[68:71], v[204:207], v[172:175], v[68:71]
	s_waitcnt lgkmcnt(10)
	v_mfma_f32_16x16x32_f16 v[72:75], v[192:195], v[176:179], v[72:75]
	v_mfma_f32_16x16x32_f16 v[76:79], v[196:199], v[176:179], v[76:79]
	s_add_u32 m0, s28, 0xf000
	s_nop 0
	global_load_lds_dwordx4 v11, s[4:5]
	v_mfma_f32_16x16x32_f16 v[80:83], v[200:203], v[176:179], v[80:83]
	v_mfma_f32_16x16x32_f16 v[84:87], v[204:207], v[176:179], v[84:87]
	s_waitcnt lgkmcnt(9)
	v_mfma_f32_16x16x32_f16 v[88:91], v[192:195], v[180:183], v[88:91]
	v_mfma_f32_16x16x32_f16 v[92:95], v[196:199], v[180:183], v[92:95]
	v_mfma_f32_16x16x32_f16 v[96:99], v[200:203], v[180:183], v[96:99]
	s_add_u32 m0, s28, 0x11000
	s_nop 0
	global_load_lds_dwordx4 v12, s[4:5]
	v_mfma_f32_16x16x32_f16 v[100:103], v[204:207], v[180:183], v[100:103]
	s_waitcnt lgkmcnt(8)
	v_mfma_f32_16x16x32_f16 v[104:107], v[192:195], v[184:187], v[104:107]
	v_mfma_f32_16x16x32_f16 v[108:111], v[196:199], v[184:187], v[108:111]
	v_mfma_f32_16x16x32_f16 v[112:115], v[200:203], v[184:187], v[112:115]
	v_mfma_f32_16x16x32_f16 v[116:119], v[204:207], v[184:187], v[116:119]
	s_waitcnt lgkmcnt(7)
	ds_read_b128 v[172:175], v20
	ds_read_b128 v[192:195], v22
	ds_read_b128 v[196:199], v22 offset:2048
	ds_read_b128 v[200:203], v22 offset:4096
	ds_read_b128 v[204:207], v22 offset:6144
	ds_read_b128 v[176:179], v20 offset:2048
	ds_read_b128 v[180:183], v20 offset:4096
	ds_read_b128 v[184:187], v20 offset:6144
	s_waitcnt lgkmcnt(14)
	v_mfma_f32_16x16x32_f16 v[56:59], v[156:159], v[136:139], v[56:59]
	s_add_u32 m0, s28, 0x13000
	s_nop 0
	global_load_lds_dwordx4 v13, s[4:5]
	s_add_u32 s4, s4, s20
	s_addc_u32 s5, s5, 0
	s_waitcnt lgkmcnt(13)
	v_mfma_f32_16x16x32_f16 v[60:63], v[160:163], v[136:139], v[60:63]
	s_waitcnt lgkmcnt(12)
	v_mfma_f32_16x16x32_f16 v[64:67], v[164:167], v[136:139], v[64:67]
	s_waitcnt lgkmcnt(11)
	v_mfma_f32_16x16x32_f16 v[68:71], v[168:171], v[136:139], v[68:71]
	s_waitcnt lgkmcnt(10)
	v_mfma_f32_16x16x32_f16 v[72:75], v[156:159], v[140:143], v[72:75]
	v_mfma_f32_16x16x32_f16 v[76:79], v[160:163], v[140:143], v[76:79]
	s_add_u32 m0, s28, 0x16000
	s_nop 0
	global_load_lds_dwordx4 v10, s[6:7]
	v_mfma_f32_16x16x32_f16 v[80:83], v[164:167], v[140:143], v[80:83]
	v_mfma_f32_16x16x32_f16 v[84:87], v[168:171], v[140:143], v[84:87]
	s_waitcnt lgkmcnt(9)
	v_mfma_f32_16x16x32_f16 v[88:91], v[156:159], v[144:147], v[88:91]
	v_mfma_f32_16x16x32_f16 v[92:95], v[160:163], v[144:147], v[92:95]
	v_mfma_f32_16x16x32_f16 v[96:99], v[164:167], v[144:147], v[96:99]
	s_add_u32 m0, s28, 0x18000
	s_nop 0
	global_load_lds_dwordx4 v11, s[6:7]
	s_add_u32 s6, s6, s20
	s_addc_u32 s7, s7, 0
	v_mfma_f32_16x16x32_f16 v[100:103], v[168:171], v[144:147], v[100:103]
	s_waitcnt lgkmcnt(8)
	v_mfma_f32_16x16x32_f16 v[104:107], v[156:159], v[148:151], v[104:107]
	v_mfma_f32_16x16x32_f16 v[108:111], v[160:163], v[148:151], v[108:111]
	v_mfma_f32_16x16x32_f16 v[112:115], v[164:167], v[148:151], v[112:115]
	v_mfma_f32_16x16x32_f16 v[116:119], v[168:171], v[148:151], v[116:119]
	s_waitcnt vmcnt(6) lgkmcnt(0)
	s_barrier
	s_waitcnt lgkmcnt(7)
	ds_read_b128 v[136:139], v15
	ds_read_b128 v[156:159], v17
	ds_read_b128 v[160:163], v17 offset:2048
	ds_read_b128 v[164:167], v17 offset:4096
	ds_read_b128 v[168:171], v17 offset:6144
	ds_read_b128 v[140:143], v15 offset:2048
	ds_read_b128 v[144:147], v15 offset:4096
	ds_read_b128 v[148:151], v15 offset:6144
	s_waitcnt lgkmcnt(14)
	v_mfma_f32_16x16x32_f16 v[56:59], v[192:195], v[172:175], v[56:59]
	s_add_u32 m0, s28, 0x1a000
	s_nop 0
	global_load_lds_dwordx4 v10, s[4:5]
	s_waitcnt lgkmcnt(13)
	v_mfma_f32_16x16x32_f16 v[60:63], v[196:199], v[172:175], v[60:63]
	s_waitcnt lgkmcnt(12)
	v_mfma_f32_16x16x32_f16 v[64:67], v[200:203], v[172:175], v[64:67]
	s_waitcnt lgkmcnt(11)
	v_mfma_f32_16x16x32_f16 v[68:71], v[204:207], v[172:175], v[68:71]
	s_waitcnt lgkmcnt(10)
	v_mfma_f32_16x16x32_f16 v[72:75], v[192:195], v[176:179], v[72:75]
	v_mfma_f32_16x16x32_f16 v[76:79], v[196:199], v[176:179], v[76:79]
	s_add_u32 m0, s28, 0x1c000
	s_nop 0
	global_load_lds_dwordx4 v11, s[4:5]
	v_mfma_f32_16x16x32_f16 v[80:83], v[200:203], v[176:179], v[80:83]
	v_mfma_f32_16x16x32_f16 v[84:87], v[204:207], v[176:179], v[84:87]
	s_waitcnt lgkmcnt(9)
	v_mfma_f32_16x16x32_f16 v[88:91], v[192:195], v[180:183], v[88:91]
	v_mfma_f32_16x16x32_f16 v[92:95], v[196:199], v[180:183], v[92:95]
	v_mfma_f32_16x16x32_f16 v[96:99], v[200:203], v[180:183], v[96:99]
	s_add_u32 m0, s28, 0x1e000
	s_nop 0
	global_load_lds_dwordx4 v12, s[4:5]
	v_mfma_f32_16x16x32_f16 v[100:103], v[204:207], v[180:183], v[100:103]
	s_waitcnt lgkmcnt(8)
	v_mfma_f32_16x16x32_f16 v[104:107], v[192:195], v[184:187], v[104:107]
	v_mfma_f32_16x16x32_f16 v[108:111], v[196:199], v[184:187], v[108:111]
	v_mfma_f32_16x16x32_f16 v[112:115], v[200:203], v[184:187], v[112:115]
	v_mfma_f32_16x16x32_f16 v[116:119], v[204:207], v[184:187], v[116:119]
	s_waitcnt lgkmcnt(7)
	ds_read_b128 v[172:175], v16
	ds_read_b128 v[192:195], v18
	ds_read_b128 v[196:199], v18 offset:2048
	ds_read_b128 v[200:203], v18 offset:4096
	ds_read_b128 v[204:207], v18 offset:6144
	ds_read_b128 v[176:179], v16 offset:2048
	ds_read_b128 v[180:183], v16 offset:4096
	ds_read_b128 v[184:187], v16 offset:6144
	s_waitcnt lgkmcnt(14)
	v_mfma_f32_16x16x32_f16 v[56:59], v[156:159], v[136:139], v[56:59]
	s_add_u32 m0, s28, 0x20000
	s_nop 0
	global_load_lds_dwordx4 v13, s[4:5]
	s_add_u32 s4, s4, s20
	s_addc_u32 s5, s5, 0
	s_waitcnt lgkmcnt(13)
	v_mfma_f32_16x16x32_f16 v[60:63], v[160:163], v[136:139], v[60:63]
	s_waitcnt lgkmcnt(12)
	v_mfma_f32_16x16x32_f16 v[64:67], v[164:167], v[136:139], v[64:67]
	s_waitcnt lgkmcnt(11)
	v_mfma_f32_16x16x32_f16 v[68:71], v[168:171], v[136:139], v[68:71]
	s_waitcnt lgkmcnt(10)
	v_mfma_f32_16x16x32_f16 v[72:75], v[156:159], v[140:143], v[72:75]
	v_mfma_f32_16x16x32_f16 v[76:79], v[160:163], v[140:143], v[76:79]
	s_add_u32 m0, s28, 0x23000
	s_nop 0
	global_load_lds_dwordx4 v10, s[6:7]
	v_mfma_f32_16x16x32_f16 v[80:83], v[164:167], v[140:143], v[80:83]
	v_mfma_f32_16x16x32_f16 v[84:87], v[168:171], v[140:143], v[84:87]
	s_waitcnt lgkmcnt(9)
	v_mfma_f32_16x16x32_f16 v[88:91], v[156:159], v[144:147], v[88:91]
	v_mfma_f32_16x16x32_f16 v[92:95], v[160:163], v[144:147], v[92:95]
	v_mfma_f32_16x16x32_f16 v[96:99], v[164:167], v[144:147], v[96:99]
	s_add_u32 m0, s28, 0x25000
	s_nop 0
	global_load_lds_dwordx4 v11, s[6:7]
	s_add_u32 s6, s6, s20
	s_addc_u32 s7, s7, 0
	v_mfma_f32_16x16x32_f16 v[100:103], v[168:171], v[144:147], v[100:103]
	s_waitcnt lgkmcnt(8)
	v_mfma_f32_16x16x32_f16 v[104:107], v[156:159], v[148:151], v[104:107]
	v_mfma_f32_16x16x32_f16 v[108:111], v[160:163], v[148:151], v[108:111]
	v_mfma_f32_16x16x32_f16 v[112:115], v[164:167], v[148:151], v[112:115]
	v_mfma_f32_16x16x32_f16 v[116:119], v[168:171], v[148:151], v[116:119]
	s_waitcnt vmcnt(6) lgkmcnt(0)
	s_barrier
	s_waitcnt lgkmcnt(7)
	ds_read_b128 v[136:139], v15 offset:53248
	ds_read_b128 v[156:159], v17 offset:53248
	ds_read_b128 v[160:163], v17 offset:55296
	ds_read_b128 v[164:167], v17 offset:57344
	ds_read_b128 v[168:171], v17 offset:59392
	ds_read_b128 v[140:143], v15 offset:55296
	ds_read_b128 v[144:147], v15 offset:57344
	ds_read_b128 v[148:151], v15 offset:59392
	s_waitcnt lgkmcnt(14)
	v_mfma_f32_16x16x32_f16 v[56:59], v[192:195], v[172:175], v[56:59]
	s_add_u32 m0, s28, 0x0
	s_nop 0
	global_load_lds_dwordx4 v10, s[4:5]
	s_waitcnt lgkmcnt(13)
	v_mfma_f32_16x16x32_f16 v[60:63], v[196:199], v[172:175], v[60:63]
	s_waitcnt lgkmcnt(12)
	v_mfma_f32_16x16x32_f16 v[64:67], v[200:203], v[172:175], v[64:67]
	s_waitcnt lgkmcnt(11)
	v_mfma_f32_16x16x32_f16 v[68:71], v[204:207], v[172:175], v[68:71]
	s_waitcnt lgkmcnt(10)
	v_mfma_f32_16x16x32_f16 v[72:75], v[192:195], v[176:179], v[72:75]
	v_mfma_f32_16x16x32_f16 v[76:79], v[196:199], v[176:179], v[76:79]
	s_add_u32 m0, s28, 0x2000
	s_nop 0
	global_load_lds_dwordx4 v11, s[4:5]
	v_mfma_f32_16x16x32_f16 v[80:83], v[200:203], v[176:179], v[80:83]
	v_mfma_f32_16x16x32_f16 v[84:87], v[204:207], v[176:179], v[84:87]
	s_waitcnt lgkmcnt(9)
	v_mfma_f32_16x16x32_f16 v[88:91], v[192:195], v[180:183], v[88:91]
	v_mfma_f32_16x16x32_f16 v[92:95], v[196:199], v[180:183], v[92:95]
	v_mfma_f32_16x16x32_f16 v[96:99], v[200:203], v[180:183], v[96:99]
	s_add_u32 m0, s28, 0x4000
	s_nop 0
	global_load_lds_dwordx4 v12, s[4:5]
	v_mfma_f32_16x16x32_f16 v[100:103], v[204:207], v[180:183], v[100:103]
	s_waitcnt lgkmcnt(8)
	v_mfma_f32_16x16x32_f16 v[104:107], v[192:195], v[184:187], v[104:107]
	v_mfma_f32_16x16x32_f16 v[108:111], v[196:199], v[184:187], v[108:111]
	v_mfma_f32_16x16x32_f16 v[112:115], v[200:203], v[184:187], v[112:115]
	v_mfma_f32_16x16x32_f16 v[116:119], v[204:207], v[184:187], v[116:119]
	s_waitcnt lgkmcnt(7)
	ds_read_b128 v[172:175], v16 offset:53248
	ds_read_b128 v[192:195], v18 offset:53248
	ds_read_b128 v[196:199], v18 offset:55296
	ds_read_b128 v[200:203], v18 offset:57344
	ds_read_b128 v[204:207], v18 offset:59392
	ds_read_b128 v[176:179], v16 offset:55296
	ds_read_b128 v[180:183], v16 offset:57344
	ds_read_b128 v[184:187], v16 offset:59392
	s_waitcnt lgkmcnt(14)
	v_mfma_f32_16x16x32_f16 v[56:59], v[156:159], v[136:139], v[56:59]
	s_add_u32 m0, s28, 0x6000
	s_nop 0
	global_load_lds_dwordx4 v13, s[4:5]
	s_add_u32 s4, s4, s20
	s_addc_u32 s5, s5, 0
	s_waitcnt lgkmcnt(13)
	v_mfma_f32_16x16x32_f16 v[60:63], v[160:163], v[136:139], v[60:63]
	s_waitcnt lgkmcnt(12)
	v_mfma_f32_16x16x32_f16 v[64:67], v[164:167], v[136:139], v[64:67]
	s_waitcnt lgkmcnt(11)
	v_mfma_f32_16x16x32_f16 v[68:71], v[168:171], v[136:139], v[68:71]
	s_waitcnt lgkmcnt(10)
	v_mfma_f32_16x16x32_f16 v[72:75], v[156:159], v[140:143], v[72:75]
	v_mfma_f32_16x16x32_f16 v[76:79], v[160:163], v[140:143], v[76:79]
	s_add_u32 m0, s28, 0x9000
	s_nop 0
	global_load_lds_dwordx4 v10, s[6:7]
	v_mfma_f32_16x16x32_f16 v[80:83], v[164:167], v[140:143], v[80:83]
	v_mfma_f32_16x16x32_f16 v[84:87], v[168:171], v[140:143], v[84:87]
	s_waitcnt lgkmcnt(9)
	v_mfma_f32_16x16x32_f16 v[88:91], v[156:159], v[144:147], v[88:91]
	v_mfma_f32_16x16x32_f16 v[92:95], v[160:163], v[144:147], v[92:95]
	v_mfma_f32_16x16x32_f16 v[96:99], v[164:167], v[144:147], v[96:99]
	s_add_u32 m0, s28, 0xb000
	s_nop 0
	global_load_lds_dwordx4 v11, s[6:7]
	s_add_u32 s6, s6, s20
	s_addc_u32 s7, s7, 0
	v_mfma_f32_16x16x32_f16 v[100:103], v[168:171], v[144:147], v[100:103]
	s_waitcnt lgkmcnt(8)
	v_mfma_f32_16x16x32_f16 v[104:107], v[156:159], v[148:151], v[104:107]
	v_mfma_f32_16x16x32_f16 v[108:111], v[160:163], v[148:151], v[108:111]
	v_mfma_f32_16x16x32_f16 v[112:115], v[164:167], v[148:151], v[112:115]
	v_mfma_f32_16x16x32_f16 v[116:119], v[168:171], v[148:151], v[116:119]
	s_waitcnt vmcnt(6) lgkmcnt(0)
	s_barrier
	s_waitcnt lgkmcnt(7)
	ds_read_b128 v[136:139], v19
	ds_read_b128 v[156:159], v21
	ds_read_b128 v[160:163], v21 offset:2048
	ds_read_b128 v[164:167], v21 offset:4096
	ds_read_b128 v[168:171], v21 offset:6144
	ds_read_b128 v[140:143], v19 offset:2048
	ds_read_b128 v[144:147], v19 offset:4096
	ds_read_b128 v[148:151], v19 offset:6144
	s_waitcnt lgkmcnt(14)
	v_mfma_f32_16x16x32_f16 v[56:59], v[192:195], v[172:175], v[56:59]
	s_add_u32 m0, s28, 0xd000
	s_nop 0
	global_load_lds_dwordx4 v10, s[4:5]
	s_waitcnt lgkmcnt(13)
	v_mfma_f32_16x16x32_f16 v[60:63], v[196:199], v[172:175], v[60:63]
	s_waitcnt lgkmcnt(12)
	v_mfma_f32_16x16x32_f16 v[64:67], v[200:203], v[172:175], v[64:67]
	s_waitcnt lgkmcnt(11)
	v_mfma_f32_16x16x32_f16 v[68:71], v[204:207], v[172:175], v[68:71]
	s_waitcnt lgkmcnt(10)
	v_mfma_f32_16x16x32_f16 v[72:75], v[192:195], v[176:179], v[72:75]
	v_mfma_f32_16x16x32_f16 v[76:79], v[196:199], v[176:179], v[76:79]
	s_add_u32 m0, s28, 0xf000
	s_nop 0
	global_load_lds_dwordx4 v11, s[4:5]
	v_mfma_f32_16x16x32_f16 v[80:83], v[200:203], v[176:179], v[80:83]
	v_mfma_f32_16x16x32_f16 v[84:87], v[204:207], v[176:179], v[84:87]
	s_waitcnt lgkmcnt(9)
	v_mfma_f32_16x16x32_f16 v[88:91], v[192:195], v[180:183], v[88:91]
	v_mfma_f32_16x16x32_f16 v[92:95], v[196:199], v[180:183], v[92:95]
	v_mfma_f32_16x16x32_f16 v[96:99], v[200:203], v[180:183], v[96:99]
	s_add_u32 m0, s28, 0x11000
	s_nop 0
	global_load_lds_dwordx4 v12, s[4:5]
	v_mfma_f32_16x16x32_f16 v[100:103], v[204:207], v[180:183], v[100:103]
	s_waitcnt lgkmcnt(8)
	v_mfma_f32_16x16x32_f16 v[104:107], v[192:195], v[184:187], v[104:107]
	v_mfma_f32_16x16x32_f16 v[108:111], v[196:199], v[184:187], v[108:111]
	v_mfma_f32_16x16x32_f16 v[112:115], v[200:203], v[184:187], v[112:115]
	v_mfma_f32_16x16x32_f16 v[116:119], v[204:207], v[184:187], v[116:119]
	s_waitcnt lgkmcnt(7)
	ds_read_b128 v[172:175], v20
	ds_read_b128 v[192:195], v22
	ds_read_b128 v[196:199], v22 offset:2048
	ds_read_b128 v[200:203], v22 offset:4096
	ds_read_b128 v[204:207], v22 offset:6144
	ds_read_b128 v[176:179], v20 offset:2048
	ds_read_b128 v[180:183], v20 offset:4096
	ds_read_b128 v[184:187], v20 offset:6144
	s_waitcnt lgkmcnt(14)
	v_mfma_f32_16x16x32_f16 v[56:59], v[156:159], v[136:139], v[56:59]
	s_add_u32 m0, s28, 0x13000
	s_nop 0
	global_load_lds_dwordx4 v13, s[4:5]
	s_add_u32 s4, s4, s20
	s_addc_u32 s5, s5, 0
	s_waitcnt lgkmcnt(13)
	v_mfma_f32_16x16x32_f16 v[60:63], v[160:163], v[136:139], v[60:63]
	s_waitcnt lgkmcnt(12)
	v_mfma_f32_16x16x32_f16 v[64:67], v[164:167], v[136:139], v[64:67]
	s_waitcnt lgkmcnt(11)
	v_mfma_f32_16x16x32_f16 v[68:71], v[168:171], v[136:139], v[68:71]
	s_waitcnt lgkmcnt(10)
	v_mfma_f32_16x16x32_f16 v[72:75], v[156:159], v[140:143], v[72:75]
	v_mfma_f32_16x16x32_f16 v[76:79], v[160:163], v[140:143], v[76:79]
	s_add_u32 m0, s28, 0x16000
	s_nop 0
	global_load_lds_dwordx4 v10, s[6:7]
	v_mfma_f32_16x16x32_f16 v[80:83], v[164:167], v[140:143], v[80:83]
	v_mfma_f32_16x16x32_f16 v[84:87], v[168:171], v[140:143], v[84:87]
	s_waitcnt lgkmcnt(9)
	v_mfma_f32_16x16x32_f16 v[88:91], v[156:159], v[144:147], v[88:91]
	v_mfma_f32_16x16x32_f16 v[92:95], v[160:163], v[144:147], v[92:95]
	v_mfma_f32_16x16x32_f16 v[96:99], v[164:167], v[144:147], v[96:99]
	s_add_u32 m0, s28, 0x18000
	s_nop 0
	global_load_lds_dwordx4 v11, s[6:7]
	s_add_u32 s6, s6, s20
	s_addc_u32 s7, s7, 0
	v_mfma_f32_16x16x32_f16 v[100:103], v[168:171], v[144:147], v[100:103]
	s_waitcnt lgkmcnt(8)
	v_mfma_f32_16x16x32_f16 v[104:107], v[156:159], v[148:151], v[104:107]
	v_mfma_f32_16x16x32_f16 v[108:111], v[160:163], v[148:151], v[108:111]
	v_mfma_f32_16x16x32_f16 v[112:115], v[164:167], v[148:151], v[112:115]
	v_mfma_f32_16x16x32_f16 v[116:119], v[168:171], v[148:151], v[116:119]
	s_waitcnt vmcnt(6) lgkmcnt(0)
	s_barrier
	s_waitcnt lgkmcnt(7)
	ds_read_b128 v[136:139], v15
	ds_read_b128 v[156:159], v17
	ds_read_b128 v[160:163], v17 offset:2048
	ds_read_b128 v[164:167], v17 offset:4096
	ds_read_b128 v[168:171], v17 offset:6144
	ds_read_b128 v[140:143], v15 offset:2048
	ds_read_b128 v[144:147], v15 offset:4096
	ds_read_b128 v[148:151], v15 offset:6144
	s_waitcnt lgkmcnt(14)
	v_mfma_f32_16x16x32_f16 v[56:59], v[192:195], v[172:175], v[56:59]
	s_add_u32 m0, s28, 0x1a000
	s_nop 0
	global_load_lds_dwordx4 v10, s[4:5]
	s_waitcnt lgkmcnt(13)
	v_mfma_f32_16x16x32_f16 v[60:63], v[196:199], v[172:175], v[60:63]
	s_waitcnt lgkmcnt(12)
	v_mfma_f32_16x16x32_f16 v[64:67], v[200:203], v[172:175], v[64:67]
	s_waitcnt lgkmcnt(11)
	v_mfma_f32_16x16x32_f16 v[68:71], v[204:207], v[172:175], v[68:71]
	s_waitcnt lgkmcnt(10)
	v_mfma_f32_16x16x32_f16 v[72:75], v[192:195], v[176:179], v[72:75]
	v_mfma_f32_16x16x32_f16 v[76:79], v[196:199], v[176:179], v[76:79]
	s_add_u32 m0, s28, 0x1c000
	s_nop 0
	global_load_lds_dwordx4 v11, s[4:5]
	v_mfma_f32_16x16x32_f16 v[80:83], v[200:203], v[176:179], v[80:83]
	v_mfma_f32_16x16x32_f16 v[84:87], v[204:207], v[176:179], v[84:87]
	s_waitcnt lgkmcnt(9)
	v_mfma_f32_16x16x32_f16 v[88:91], v[192:195], v[180:183], v[88:91]
	v_mfma_f32_16x16x32_f16 v[92:95], v[196:199], v[180:183], v[92:95]
	v_mfma_f32_16x16x32_f16 v[96:99], v[200:203], v[180:183], v[96:99]
	s_add_u32 m0, s28, 0x1e000
	s_nop 0
	global_load_lds_dwordx4 v12, s[4:5]
	v_mfma_f32_16x16x32_f16 v[100:103], v[204:207], v[180:183], v[100:103]
	s_waitcnt lgkmcnt(8)
	v_mfma_f32_16x16x32_f16 v[104:107], v[192:195], v[184:187], v[104:107]
	v_mfma_f32_16x16x32_f16 v[108:111], v[196:199], v[184:187], v[108:111]
	v_mfma_f32_16x16x32_f16 v[112:115], v[200:203], v[184:187], v[112:115]
	v_mfma_f32_16x16x32_f16 v[116:119], v[204:207], v[184:187], v[116:119]
	s_waitcnt lgkmcnt(7)
	ds_read_b128 v[172:175], v16
	ds_read_b128 v[192:195], v18
	ds_read_b128 v[196:199], v18 offset:2048
	ds_read_b128 v[200:203], v18 offset:4096
	ds_read_b128 v[204:207], v18 offset:6144
	ds_read_b128 v[176:179], v16 offset:2048
	ds_read_b128 v[180:183], v16 offset:4096
	ds_read_b128 v[184:187], v16 offset:6144
	s_waitcnt lgkmcnt(14)
	v_mfma_f32_16x16x32_f16 v[56:59], v[156:159], v[136:139], v[56:59]
	s_add_u32 m0, s28, 0x20000
	s_nop 0
	global_load_lds_dwordx4 v13, s[4:5]
	s_add_u32 s4, s4, s20
	s_addc_u32 s5, s5, 0
	s_waitcnt lgkmcnt(13)
	v_mfma_f32_16x16x32_f16 v[60:63], v[160:163], v[136:139], v[60:63]
	s_waitcnt lgkmcnt(12)
	v_mfma_f32_16x16x32_f16 v[64:67], v[164:167], v[136:139], v[64:67]
	s_waitcnt lgkmcnt(11)
	v_mfma_f32_16x16x32_f16 v[68:71], v[168:171], v[136:139], v[68:71]
	s_waitcnt lgkmcnt(10)
	v_mfma_f32_16x16x32_f16 v[72:75], v[156:159], v[140:143], v[72:75]
	v_mfma_f32_16x16x32_f16 v[76:79], v[160:163], v[140:143], v[76:79]
	s_add_u32 m0, s28, 0x23000
	s_nop 0
	global_load_lds_dwordx4 v10, s[6:7]
	v_mfma_f32_16x16x32_f16 v[80:83], v[164:167], v[140:143], v[80:83]
	v_mfma_f32_16x16x32_f16 v[84:87], v[168:171], v[140:143], v[84:87]
	s_waitcnt lgkmcnt(9)
	v_mfma_f32_16x16x32_f16 v[88:91], v[156:159], v[144:147], v[88:91]
	v_mfma_f32_16x16x32_f16 v[92:95], v[160:163], v[144:147], v[92:95]
	v_mfma_f32_16x16x32_f16 v[96:99], v[164:167], v[144:147], v[96:99]
	s_add_u32 m0, s28, 0x25000
	s_nop 0
	global_load_lds_dwordx4 v11, s[6:7]
	s_add_u32 s6, s6, s20
	s_addc_u32 s7, s7, 0
	v_mfma_f32_16x16x32_f16 v[100:103], v[168:171], v[144:147], v[100:103]
	s_waitcnt lgkmcnt(8)
	v_mfma_f32_16x16x32_f16 v[104:107], v[156:159], v[148:151], v[104:107]
	v_mfma_f32_16x16x32_f16 v[108:111], v[160:163], v[148:151], v[108:111]
	v_mfma_f32_16x16x32_f16 v[112:115], v[164:167], v[148:151], v[112:115]
	v_mfma_f32_16x16x32_f16 v[116:119], v[168:171], v[148:151], v[116:119]
	s_waitcnt vmcnt(6) lgkmcnt(0)
	s_barrier
	s_waitcnt lgkmcnt(7)
	ds_read_b128 v[136:139], v15 offset:53248
	ds_read_b128 v[156:159], v17 offset:53248
	ds_read_b128 v[160:163], v17 offset:55296
	ds_read_b128 v[164:167], v17 offset:57344
	ds_read_b128 v[168:171], v17 offset:59392
	ds_read_b128 v[140:143], v15 offset:55296
	ds_read_b128 v[144:147], v15 offset:57344
	ds_read_b128 v[148:151], v15 offset:59392
	s_waitcnt lgkmcnt(14)
	v_mfma_f32_16x16x32_f16 v[56:59], v[192:195], v[172:175], v[56:59]
	s_add_u32 m0, s28, 0x0
	s_nop 0
	global_load_lds_dwordx4 v10, s[4:5]
	s_waitcnt lgkmcnt(13)
	v_mfma_f32_16x16x32_f16 v[60:63], v[196:199], v[172:175], v[60:63]
	s_waitcnt lgkmcnt(12)
	v_mfma_f32_16x16x32_f16 v[64:67], v[200:203], v[172:175], v[64:67]
	s_waitcnt lgkmcnt(11)
	v_mfma_f32_16x16x32_f16 v[68:71], v[204:207], v[172:175], v[68:71]
	s_waitcnt lgkmcnt(10)
	v_mfma_f32_16x16x32_f16 v[72:75], v[192:195], v[176:179], v[72:75]
	v_mfma_f32_16x16x32_f16 v[76:79], v[196:199], v[176:179], v[76:79]
	s_add_u32 m0, s28, 0x2000
	s_nop 0
	global_load_lds_dwordx4 v11, s[4:5]
	v_mfma_f32_16x16x32_f16 v[80:83], v[200:203], v[176:179], v[80:83]
	v_mfma_f32_16x16x32_f16 v[84:87], v[204:207], v[176:179], v[84:87]
	s_waitcnt lgkmcnt(9)
	v_mfma_f32_16x16x32_f16 v[88:91], v[192:195], v[180:183], v[88:91]
	v_mfma_f32_16x16x32_f16 v[92:95], v[196:199], v[180:183], v[92:95]
	v_mfma_f32_16x16x32_f16 v[96:99], v[200:203], v[180:183], v[96:99]
	s_add_u32 m0, s28, 0x4000
	s_nop 0
	global_load_lds_dwordx4 v12, s[4:5]
	v_mfma_f32_16x16x32_f16 v[100:103], v[204:207], v[180:183], v[100:103]
	s_waitcnt lgkmcnt(8)
	v_mfma_f32_16x16x32_f16 v[104:107], v[192:195], v[184:187], v[104:107]
	v_mfma_f32_16x16x32_f16 v[108:111], v[196:199], v[184:187], v[108:111]
	v_mfma_f32_16x16x32_f16 v[112:115], v[200:203], v[184:187], v[112:115]
	v_mfma_f32_16x16x32_f16 v[116:119], v[204:207], v[184:187], v[116:119]
	s_waitcnt lgkmcnt(7)
	ds_read_b128 v[172:175], v16 offset:53248
	ds_read_b128 v[192:195], v18 offset:53248
	ds_read_b128 v[196:199], v18 offset:55296
	ds_read_b128 v[200:203], v18 offset:57344
	ds_read_b128 v[204:207], v18 offset:59392
	ds_read_b128 v[176:179], v16 offset:55296
	ds_read_b128 v[180:183], v16 offset:57344
	ds_read_b128 v[184:187], v16 offset:59392
	s_waitcnt lgkmcnt(14)
	v_mfma_f32_16x16x32_f16 v[56:59], v[156:159], v[136:139], v[56:59]
	s_add_u32 m0, s28, 0x6000
	s_nop 0
	global_load_lds_dwordx4 v13, s[4:5]
	s_add_u32 s4, s4, s20
	s_addc_u32 s5, s5, 0
	s_waitcnt lgkmcnt(13)
	v_mfma_f32_16x16x32_f16 v[60:63], v[160:163], v[136:139], v[60:63]
	s_waitcnt lgkmcnt(12)
	v_mfma_f32_16x16x32_f16 v[64:67], v[164:167], v[136:139], v[64:67]
	s_waitcnt lgkmcnt(11)
	v_mfma_f32_16x16x32_f16 v[68:71], v[168:171], v[136:139], v[68:71]
	s_waitcnt lgkmcnt(10)
	v_mfma_f32_16x16x32_f16 v[72:75], v[156:159], v[140:143], v[72:75]
	v_mfma_f32_16x16x32_f16 v[76:79], v[160:163], v[140:143], v[76:79]
	s_add_u32 m0, s28, 0x9000
	s_nop 0
	global_load_lds_dwordx4 v10, s[6:7]
	v_mfma_f32_16x16x32_f16 v[80:83], v[164:167], v[140:143], v[80:83]
	v_mfma_f32_16x16x32_f16 v[84:87], v[168:171], v[140:143], v[84:87]
	s_waitcnt lgkmcnt(9)
	v_mfma_f32_16x16x32_f16 v[88:91], v[156:159], v[144:147], v[88:91]
	v_mfma_f32_16x16x32_f16 v[92:95], v[160:163], v[144:147], v[92:95]
	v_mfma_f32_16x16x32_f16 v[96:99], v[164:167], v[144:147], v[96:99]
	s_add_u32 m0, s28, 0xb000
	s_nop 0
	global_load_lds_dwordx4 v11, s[6:7]
	s_add_u32 s6, s6, s20
	s_addc_u32 s7, s7, 0
	v_mfma_f32_16x16x32_f16 v[100:103], v[168:171], v[144:147], v[100:103]
	s_waitcnt lgkmcnt(8)
	v_mfma_f32_16x16x32_f16 v[104:107], v[156:159], v[148:151], v[104:107]
	v_mfma_f32_16x16x32_f16 v[108:111], v[160:163], v[148:151], v[108:111]
	v_mfma_f32_16x16x32_f16 v[112:115], v[164:167], v[148:151], v[112:115]
	v_mfma_f32_16x16x32_f16 v[116:119], v[168:171], v[148:151], v[116:119]
	s_waitcnt vmcnt(6) lgkmcnt(0)
	s_barrier
	s_waitcnt lgkmcnt(7)
	ds_read_b128 v[136:139], v19
	ds_read_b128 v[156:159], v21
	ds_read_b128 v[160:163], v21 offset:2048
	ds_read_b128 v[164:167], v21 offset:4096
	ds_read_b128 v[168:171], v21 offset:6144
	ds_read_b128 v[140:143], v19 offset:2048
	ds_read_b128 v[144:147], v19 offset:4096
	ds_read_b128 v[148:151], v19 offset:6144
	s_waitcnt lgkmcnt(14)
	v_mfma_f32_16x16x32_f16 v[56:59], v[192:195], v[172:175], v[56:59]
	s_add_u32 m0, s28, 0xd000
	s_nop 0
	global_load_lds_dwordx4 v10, s[4:5]
	s_waitcnt lgkmcnt(13)
	v_mfma_f32_16x16x32_f16 v[60:63], v[196:199], v[172:175], v[60:63]
	s_waitcnt lgkmcnt(12)
	v_mfma_f32_16x16x32_f16 v[64:67], v[200:203], v[172:175], v[64:67]
	s_waitcnt lgkmcnt(11)
	v_mfma_f32_16x16x32_f16 v[68:71], v[204:207], v[172:175], v[68:71]
	s_waitcnt lgkmcnt(10)
	v_mfma_f32_16x16x32_f16 v[72:75], v[192:195], v[176:179], v[72:75]
	v_mfma_f32_16x16x32_f16 v[76:79], v[196:199], v[176:179], v[76:79]
	s_add_u32 m0, s28, 0xf000
	s_nop 0
	global_load_lds_dwordx4 v11, s[4:5]
	v_mfma_f32_16x16x32_f16 v[80:83], v[200:203], v[176:179], v[80:83]
	v_mfma_f32_16x16x32_f16 v[84:87], v[204:207], v[176:179], v[84:87]
	s_waitcnt lgkmcnt(9)
	v_mfma_f32_16x16x32_f16 v[88:91], v[192:195], v[180:183], v[88:91]
	v_mfma_f32_16x16x32_f16 v[92:95], v[196:199], v[180:183], v[92:95]
	v_mfma_f32_16x16x32_f16 v[96:99], v[200:203], v[180:183], v[96:99]
	s_add_u32 m0, s28, 0x11000
	s_nop 0
	global_load_lds_dwordx4 v12, s[4:5]
	v_mfma_f32_16x16x32_f16 v[100:103], v[204:207], v[180:183], v[100:103]
	s_waitcnt lgkmcnt(8)
	v_mfma_f32_16x16x32_f16 v[104:107], v[192:195], v[184:187], v[104:107]
	v_mfma_f32_16x16x32_f16 v[108:111], v[196:199], v[184:187], v[108:111]
	v_mfma_f32_16x16x32_f16 v[112:115], v[200:203], v[184:187], v[112:115]
	v_mfma_f32_16x16x32_f16 v[116:119], v[204:207], v[184:187], v[116:119]
	s_waitcnt lgkmcnt(7)
	ds_read_b128 v[172:175], v20
	ds_read_b128 v[192:195], v22
	ds_read_b128 v[196:199], v22 offset:2048
	ds_read_b128 v[200:203], v22 offset:4096
	ds_read_b128 v[204:207], v22 offset:6144
	ds_read_b128 v[176:179], v20 offset:2048
	ds_read_b128 v[180:183], v20 offset:4096
	ds_read_b128 v[184:187], v20 offset:6144
	s_waitcnt lgkmcnt(14)
	v_mfma_f32_16x16x32_f16 v[56:59], v[156:159], v[136:139], v[56:59]
	s_add_u32 m0, s28, 0x13000
	s_nop 0
	global_load_lds_dwordx4 v13, s[4:5]
	s_add_u32 s4, s4, s20
	s_addc_u32 s5, s5, 0
	s_waitcnt lgkmcnt(13)
	v_mfma_f32_16x16x32_f16 v[60:63], v[160:163], v[136:139], v[60:63]
	s_waitcnt lgkmcnt(12)
	v_mfma_f32_16x16x32_f16 v[64:67], v[164:167], v[136:139], v[64:67]
	s_waitcnt lgkmcnt(11)
	v_mfma_f32_16x16x32_f16 v[68:71], v[168:171], v[136:139], v[68:71]
	s_waitcnt lgkmcnt(10)
	v_mfma_f32_16x16x32_f16 v[72:75], v[156:159], v[140:143], v[72:75]
	v_mfma_f32_16x16x32_f16 v[76:79], v[160:163], v[140:143], v[76:79]
	s_add_u32 m0, s28, 0x16000
	s_nop 0
	global_load_lds_dwordx4 v10, s[6:7]
	v_mfma_f32_16x16x32_f16 v[80:83], v[164:167], v[140:143], v[80:83]
	v_mfma_f32_16x16x32_f16 v[84:87], v[168:171], v[140:143], v[84:87]
	s_waitcnt lgkmcnt(9)
	v_mfma_f32_16x16x32_f16 v[88:91], v[156:159], v[144:147], v[88:91]
	v_mfma_f32_16x16x32_f16 v[92:95], v[160:163], v[144:147], v[92:95]
	v_mfma_f32_16x16x32_f16 v[96:99], v[164:167], v[144:147], v[96:99]
	s_add_u32 m0, s28, 0x18000
	s_nop 0
	global_load_lds_dwordx4 v11, s[6:7]
	s_add_u32 s6, s6, s20
	s_addc_u32 s7, s7, 0
	v_mfma_f32_16x16x32_f16 v[100:103], v[168:171], v[144:147], v[100:103]
	s_waitcnt lgkmcnt(8)
	v_mfma_f32_16x16x32_f16 v[104:107], v[156:159], v[148:151], v[104:107]
	v_mfma_f32_16x16x32_f16 v[108:111], v[160:163], v[148:151], v[108:111]
	v_mfma_f32_16x16x32_f16 v[112:115], v[164:167], v[148:151], v[112:115]
	v_mfma_f32_16x16x32_f16 v[116:119], v[168:171], v[148:151], v[116:119]
	s_waitcnt vmcnt(6) lgkmcnt(0)
	s_barrier
	s_waitcnt lgkmcnt(7)
	ds_read_b128 v[136:139], v15
	ds_read_b128 v[156:159], v17
	ds_read_b128 v[160:163], v17 offset:2048
	ds_read_b128 v[164:167], v17 offset:4096
	ds_read_b128 v[168:171], v17 offset:6144
	ds_read_b128 v[140:143], v15 offset:2048
	ds_read_b128 v[144:147], v15 offset:4096
	ds_read_b128 v[148:151], v15 offset:6144
	s_waitcnt lgkmcnt(14)
	v_mfma_f32_16x16x32_f16 v[56:59], v[192:195], v[172:175], v[56:59]
	s_add_u32 m0, s28, 0x1a000
	s_nop 0
	global_load_lds_dwordx4 v10, s[4:5]
	s_waitcnt lgkmcnt(13)
	v_mfma_f32_16x16x32_f16 v[60:63], v[196:199], v[172:175], v[60:63]
	s_waitcnt lgkmcnt(12)
	v_mfma_f32_16x16x32_f16 v[64:67], v[200:203], v[172:175], v[64:67]
	s_waitcnt lgkmcnt(11)
	v_mfma_f32_16x16x32_f16 v[68:71], v[204:207], v[172:175], v[68:71]
	s_waitcnt lgkmcnt(10)
	v_mfma_f32_16x16x32_f16 v[72:75], v[192:195], v[176:179], v[72:75]
	v_mfma_f32_16x16x32_f16 v[76:79], v[196:199], v[176:179], v[76:79]
	s_add_u32 m0, s28, 0x1c000
	s_nop 0
	global_load_lds_dwordx4 v11, s[4:5]
	v_mfma_f32_16x16x32_f16 v[80:83], v[200:203], v[176:179], v[80:83]
	v_mfma_f32_16x16x32_f16 v[84:87], v[204:207], v[176:179], v[84:87]
	s_waitcnt lgkmcnt(9)
	v_mfma_f32_16x16x32_f16 v[88:91], v[192:195], v[180:183], v[88:91]
	v_mfma_f32_16x16x32_f16 v[92:95], v[196:199], v[180:183], v[92:95]
	v_mfma_f32_16x16x32_f16 v[96:99], v[200:203], v[180:183], v[96:99]
	s_add_u32 m0, s28, 0x1e000
	s_nop 0
	global_load_lds_dwordx4 v12, s[4:5]
	v_mfma_f32_16x16x32_f16 v[100:103], v[204:207], v[180:183], v[100:103]
	s_waitcnt lgkmcnt(8)
	v_mfma_f32_16x16x32_f16 v[104:107], v[192:195], v[184:187], v[104:107]
	v_mfma_f32_16x16x32_f16 v[108:111], v[196:199], v[184:187], v[108:111]
	v_mfma_f32_16x16x32_f16 v[112:115], v[200:203], v[184:187], v[112:115]
	v_mfma_f32_16x16x32_f16 v[116:119], v[204:207], v[184:187], v[116:119]
	s_waitcnt lgkmcnt(7)
	ds_read_b128 v[172:175], v16
	ds_read_b128 v[192:195], v18
	ds_read_b128 v[196:199], v18 offset:2048
	ds_read_b128 v[200:203], v18 offset:4096
	ds_read_b128 v[204:207], v18 offset:6144
	ds_read_b128 v[176:179], v16 offset:2048
	ds_read_b128 v[180:183], v16 offset:4096
	ds_read_b128 v[184:187], v16 offset:6144
	s_waitcnt lgkmcnt(14)
	v_mfma_f32_16x16x32_f16 v[56:59], v[156:159], v[136:139], v[56:59]
	s_add_u32 m0, s28, 0x20000
	s_nop 0
	global_load_lds_dwordx4 v13, s[4:5]
	s_add_u32 s4, s4, s20
	s_addc_u32 s5, s5, 0
	s_waitcnt lgkmcnt(13)
	v_mfma_f32_16x16x32_f16 v[60:63], v[160:163], v[136:139], v[60:63]
	s_waitcnt lgkmcnt(12)
	v_mfma_f32_16x16x32_f16 v[64:67], v[164:167], v[136:139], v[64:67]
	s_waitcnt lgkmcnt(11)
	v_mfma_f32_16x16x32_f16 v[68:71], v[168:171], v[136:139], v[68:71]
	s_waitcnt lgkmcnt(10)
	v_mfma_f32_16x16x32_f16 v[72:75], v[156:159], v[140:143], v[72:75]
	v_mfma_f32_16x16x32_f16 v[76:79], v[160:163], v[140:143], v[76:79]
	s_add_u32 m0, s28, 0x23000
	s_nop 0
	global_load_lds_dwordx4 v10, s[6:7]
	v_mfma_f32_16x16x32_f16 v[80:83], v[164:167], v[140:143], v[80:83]
	v_mfma_f32_16x16x32_f16 v[84:87], v[168:171], v[140:143], v[84:87]
	s_waitcnt lgkmcnt(9)
	v_mfma_f32_16x16x32_f16 v[88:91], v[156:159], v[144:147], v[88:91]
	v_mfma_f32_16x16x32_f16 v[92:95], v[160:163], v[144:147], v[92:95]
	v_mfma_f32_16x16x32_f16 v[96:99], v[164:167], v[144:147], v[96:99]
	s_add_u32 m0, s28, 0x25000
	s_nop 0
	global_load_lds_dwordx4 v11, s[6:7]
	s_add_u32 s6, s6, s20
	s_addc_u32 s7, s7, 0
	v_mfma_f32_16x16x32_f16 v[100:103], v[168:171], v[144:147], v[100:103]
	s_waitcnt lgkmcnt(8)
	v_mfma_f32_16x16x32_f16 v[104:107], v[156:159], v[148:151], v[104:107]
	v_mfma_f32_16x16x32_f16 v[108:111], v[160:163], v[148:151], v[108:111]
	v_mfma_f32_16x16x32_f16 v[112:115], v[164:167], v[148:151], v[112:115]
	v_mfma_f32_16x16x32_f16 v[116:119], v[168:171], v[148:151], v[116:119]
	s_waitcnt vmcnt(6) lgkmcnt(0)
	s_barrier
	s_waitcnt lgkmcnt(7)
	ds_read_b128 v[136:139], v15 offset:53248
	ds_read_b128 v[156:159], v17 offset:53248
	ds_read_b128 v[160:163], v17 offset:55296
	ds_read_b128 v[164:167], v17 offset:57344
	ds_read_b128 v[168:171], v17 offset:59392
	ds_read_b128 v[140:143], v15 offset:55296
	ds_read_b128 v[144:147], v15 offset:57344
	ds_read_b128 v[148:151], v15 offset:59392
	s_waitcnt lgkmcnt(14)
	v_mfma_f32_16x16x32_f16 v[56:59], v[192:195], v[172:175], v[56:59]
	s_add_u32 m0, s28, 0x0
	s_nop 0
	global_load_lds_dwordx4 v10, s[4:5]
	s_waitcnt lgkmcnt(13)
	v_mfma_f32_16x16x32_f16 v[60:63], v[196:199], v[172:175], v[60:63]
	s_waitcnt lgkmcnt(12)
	v_mfma_f32_16x16x32_f16 v[64:67], v[200:203], v[172:175], v[64:67]
	s_waitcnt lgkmcnt(11)
	v_mfma_f32_16x16x32_f16 v[68:71], v[204:207], v[172:175], v[68:71]
	s_waitcnt lgkmcnt(10)
	v_mfma_f32_16x16x32_f16 v[72:75], v[192:195], v[176:179], v[72:75]
	v_mfma_f32_16x16x32_f16 v[76:79], v[196:199], v[176:179], v[76:79]
	s_add_u32 m0, s28, 0x2000
	s_nop 0
	global_load_lds_dwordx4 v11, s[4:5]
	v_mfma_f32_16x16x32_f16 v[80:83], v[200:203], v[176:179], v[80:83]
	v_mfma_f32_16x16x32_f16 v[84:87], v[204:207], v[176:179], v[84:87]
	s_waitcnt lgkmcnt(9)
	v_mfma_f32_16x16x32_f16 v[88:91], v[192:195], v[180:183], v[88:91]
	v_mfma_f32_16x16x32_f16 v[92:95], v[196:199], v[180:183], v[92:95]
	v_mfma_f32_16x16x32_f16 v[96:99], v[200:203], v[180:183], v[96:99]
	s_add_u32 m0, s28, 0x4000
	s_nop 0
	global_load_lds_dwordx4 v12, s[4:5]
	v_mfma_f32_16x16x32_f16 v[100:103], v[204:207], v[180:183], v[100:103]
	s_waitcnt lgkmcnt(8)
	v_mfma_f32_16x16x32_f16 v[104:107], v[192:195], v[184:187], v[104:107]
	v_mfma_f32_16x16x32_f16 v[108:111], v[196:199], v[184:187], v[108:111]
	v_mfma_f32_16x16x32_f16 v[112:115], v[200:203], v[184:187], v[112:115]
	v_mfma_f32_16x16x32_f16 v[116:119], v[204:207], v[184:187], v[116:119]
	s_waitcnt lgkmcnt(7)
	ds_read_b128 v[172:175], v16 offset:53248
	ds_read_b128 v[192:195], v18 offset:53248
	ds_read_b128 v[196:199], v18 offset:55296
	ds_read_b128 v[200:203], v18 offset:57344
	ds_read_b128 v[204:207], v18 offset:59392
	ds_read_b128 v[176:179], v16 offset:55296
	ds_read_b128 v[180:183], v16 offset:57344
	ds_read_b128 v[184:187], v16 offset:59392
	s_waitcnt lgkmcnt(14)
	v_mfma_f32_16x16x32_f16 v[56:59], v[156:159], v[136:139], v[56:59]
	s_add_u32 m0, s28, 0x6000
	s_nop 0
	global_load_lds_dwordx4 v13, s[4:5]
	s_add_u32 s4, s4, s20
	s_addc_u32 s5, s5, 0
	s_waitcnt lgkmcnt(13)
	v_mfma_f32_16x16x32_f16 v[60:63], v[160:163], v[136:139], v[60:63]
	s_waitcnt lgkmcnt(12)
	v_mfma_f32_16x16x32_f16 v[64:67], v[164:167], v[136:139], v[64:67]
	s_waitcnt lgkmcnt(11)
	v_mfma_f32_16x16x32_f16 v[68:71], v[168:171], v[136:139], v[68:71]
	s_waitcnt lgkmcnt(10)
	v_mfma_f32_16x16x32_f16 v[72:75], v[156:159], v[140:143], v[72:75]
	v_mfma_f32_16x16x32_f16 v[76:79], v[160:163], v[140:143], v[76:79]
	s_add_u32 m0, s28, 0x9000
	s_nop 0
	global_load_lds_dwordx4 v10, s[6:7]
	v_mfma_f32_16x16x32_f16 v[80:83], v[164:167], v[140:143], v[80:83]
	v_mfma_f32_16x16x32_f16 v[84:87], v[168:171], v[140:143], v[84:87]
	s_waitcnt lgkmcnt(9)
	v_mfma_f32_16x16x32_f16 v[88:91], v[156:159], v[144:147], v[88:91]
	v_mfma_f32_16x16x32_f16 v[92:95], v[160:163], v[144:147], v[92:95]
	v_mfma_f32_16x16x32_f16 v[96:99], v[164:167], v[144:147], v[96:99]
	s_add_u32 m0, s28, 0xb000
	s_nop 0
	global_load_lds_dwordx4 v11, s[6:7]
	s_add_u32 s6, s6, s20
	s_addc_u32 s7, s7, 0
	v_mfma_f32_16x16x32_f16 v[100:103], v[168:171], v[144:147], v[100:103]
	s_waitcnt lgkmcnt(8)
	v_mfma_f32_16x16x32_f16 v[104:107], v[156:159], v[148:151], v[104:107]
	v_mfma_f32_16x16x32_f16 v[108:111], v[160:163], v[148:151], v[108:111]
	v_mfma_f32_16x16x32_f16 v[112:115], v[164:167], v[148:151], v[112:115]
	v_mfma_f32_16x16x32_f16 v[116:119], v[168:171], v[148:151], v[116:119]
	s_waitcnt vmcnt(6) lgkmcnt(0)
	s_barrier
	s_waitcnt lgkmcnt(7)
	ds_read_b128 v[136:139], v19
	ds_read_b128 v[156:159], v21
	ds_read_b128 v[160:163], v21 offset:2048
	ds_read_b128 v[164:167], v21 offset:4096
	ds_read_b128 v[168:171], v21 offset:6144
	ds_read_b128 v[140:143], v19 offset:2048
	ds_read_b128 v[144:147], v19 offset:4096
	ds_read_b128 v[148:151], v19 offset:6144
	s_waitcnt lgkmcnt(14)
	v_mfma_f32_16x16x32_f16 v[56:59], v[192:195], v[172:175], v[56:59]
	s_add_u32 m0, s28, 0xd000
	s_nop 0
	global_load_lds_dwordx4 v10, s[4:5]
	s_waitcnt lgkmcnt(13)
	v_mfma_f32_16x16x32_f16 v[60:63], v[196:199], v[172:175], v[60:63]
	s_waitcnt lgkmcnt(12)
	v_mfma_f32_16x16x32_f16 v[64:67], v[200:203], v[172:175], v[64:67]
	s_waitcnt lgkmcnt(11)
	v_mfma_f32_16x16x32_f16 v[68:71], v[204:207], v[172:175], v[68:71]
	s_waitcnt lgkmcnt(10)
	v_mfma_f32_16x16x32_f16 v[72:75], v[192:195], v[176:179], v[72:75]
	v_mfma_f32_16x16x32_f16 v[76:79], v[196:199], v[176:179], v[76:79]
	s_add_u32 m0, s28, 0xf000
	s_nop 0
	global_load_lds_dwordx4 v11, s[4:5]
	v_mfma_f32_16x16x32_f16 v[80:83], v[200:203], v[176:179], v[80:83]
	v_mfma_f32_16x16x32_f16 v[84:87], v[204:207], v[176:179], v[84:87]
	s_waitcnt lgkmcnt(9)
	v_mfma_f32_16x16x32_f16 v[88:91], v[192:195], v[180:183], v[88:91]
	v_mfma_f32_16x16x32_f16 v[92:95], v[196:199], v[180:183], v[92:95]
	v_mfma_f32_16x16x32_f16 v[96:99], v[200:203], v[180:183], v[96:99]
	s_add_u32 m0, s28, 0x11000
	s_nop 0
	global_load_lds_dwordx4 v12, s[4:5]
	v_mfma_f32_16x16x32_f16 v[100:103], v[204:207], v[180:183], v[100:103]
	s_waitcnt lgkmcnt(8)
	v_mfma_f32_16x16x32_f16 v[104:107], v[192:195], v[184:187], v[104:107]
	v_mfma_f32_16x16x32_f16 v[108:111], v[196:199], v[184:187], v[108:111]
	v_mfma_f32_16x16x32_f16 v[112:115], v[200:203], v[184:187], v[112:115]
	v_mfma_f32_16x16x32_f16 v[116:119], v[204:207], v[184:187], v[116:119]
	s_waitcnt lgkmcnt(7)
	ds_read_b128 v[172:175], v20
	ds_read_b128 v[192:195], v22
	ds_read_b128 v[196:199], v22 offset:2048
	ds_read_b128 v[200:203], v22 offset:4096
	ds_read_b128 v[204:207], v22 offset:6144
	ds_read_b128 v[176:179], v20 offset:2048
	ds_read_b128 v[180:183], v20 offset:4096
	ds_read_b128 v[184:187], v20 offset:6144
	s_waitcnt lgkmcnt(14)
	v_mfma_f32_16x16x32_f16 v[56:59], v[156:159], v[136:139], v[56:59]
	s_add_u32 m0, s28, 0x13000
	s_nop 0
	global_load_lds_dwordx4 v13, s[4:5]
	s_add_u32 s4, s4, s20
	s_addc_u32 s5, s5, 0
	s_waitcnt lgkmcnt(13)
	v_mfma_f32_16x16x32_f16 v[60:63], v[160:163], v[136:139], v[60:63]
	s_waitcnt lgkmcnt(12)
	v_mfma_f32_16x16x32_f16 v[64:67], v[164:167], v[136:139], v[64:67]
	s_waitcnt lgkmcnt(11)
	v_mfma_f32_16x16x32_f16 v[68:71], v[168:171], v[136:139], v[68:71]
	s_waitcnt lgkmcnt(10)
	v_mfma_f32_16x16x32_f16 v[72:75], v[156:159], v[140:143], v[72:75]
	v_mfma_f32_16x16x32_f16 v[76:79], v[160:163], v[140:143], v[76:79]
	s_add_u32 m0, s28, 0x16000
	s_nop 0
	global_load_lds_dwordx4 v10, s[6:7]
	v_mfma_f32_16x16x32_f16 v[80:83], v[164:167], v[140:143], v[80:83]
	v_mfma_f32_16x16x32_f16 v[84:87], v[168:171], v[140:143], v[84:87]
	s_waitcnt lgkmcnt(9)
	v_mfma_f32_16x16x32_f16 v[88:91], v[156:159], v[144:147], v[88:91]
	v_mfma_f32_16x16x32_f16 v[92:95], v[160:163], v[144:147], v[92:95]
	v_mfma_f32_16x16x32_f16 v[96:99], v[164:167], v[144:147], v[96:99]
	s_add_u32 m0, s28, 0x18000
	s_nop 0
	global_load_lds_dwordx4 v11, s[6:7]
	s_add_u32 s6, s6, s20
	s_addc_u32 s7, s7, 0
	v_mfma_f32_16x16x32_f16 v[100:103], v[168:171], v[144:147], v[100:103]
	s_waitcnt lgkmcnt(8)
	v_mfma_f32_16x16x32_f16 v[104:107], v[156:159], v[148:151], v[104:107]
	v_mfma_f32_16x16x32_f16 v[108:111], v[160:163], v[148:151], v[108:111]
	v_mfma_f32_16x16x32_f16 v[112:115], v[164:167], v[148:151], v[112:115]
	v_mfma_f32_16x16x32_f16 v[116:119], v[168:171], v[148:151], v[116:119]
	s_waitcnt vmcnt(6) lgkmcnt(0)
	s_barrier
	s_waitcnt lgkmcnt(7)
	ds_read_b128 v[136:139], v15
	ds_read_b128 v[156:159], v17
	ds_read_b128 v[160:163], v17 offset:2048
	ds_read_b128 v[164:167], v17 offset:4096
	ds_read_b128 v[168:171], v17 offset:6144
	ds_read_b128 v[140:143], v15 offset:2048
	ds_read_b128 v[144:147], v15 offset:4096
	ds_read_b128 v[148:151], v15 offset:6144
	s_waitcnt lgkmcnt(14)
	v_mfma_f32_16x16x32_f16 v[56:59], v[192:195], v[172:175], v[56:59]
	s_add_u32 m0, s28, 0x1a000
	s_nop 0
	global_load_lds_dwordx4 v10, s[4:5]
	s_waitcnt lgkmcnt(13)
	v_mfma_f32_16x16x32_f16 v[60:63], v[196:199], v[172:175], v[60:63]
	s_waitcnt lgkmcnt(12)
	v_mfma_f32_16x16x32_f16 v[64:67], v[200:203], v[172:175], v[64:67]
	s_waitcnt lgkmcnt(11)
	v_mfma_f32_16x16x32_f16 v[68:71], v[204:207], v[172:175], v[68:71]
	s_waitcnt lgkmcnt(10)
	v_mfma_f32_16x16x32_f16 v[72:75], v[192:195], v[176:179], v[72:75]
	v_mfma_f32_16x16x32_f16 v[76:79], v[196:199], v[176:179], v[76:79]
	s_add_u32 m0, s28, 0x1c000
	s_nop 0
	global_load_lds_dwordx4 v11, s[4:5]
	v_mfma_f32_16x16x32_f16 v[80:83], v[200:203], v[176:179], v[80:83]
	v_mfma_f32_16x16x32_f16 v[84:87], v[204:207], v[176:179], v[84:87]
	s_waitcnt lgkmcnt(9)
	v_mfma_f32_16x16x32_f16 v[88:91], v[192:195], v[180:183], v[88:91]
	v_mfma_f32_16x16x32_f16 v[92:95], v[196:199], v[180:183], v[92:95]
	v_mfma_f32_16x16x32_f16 v[96:99], v[200:203], v[180:183], v[96:99]
	s_add_u32 m0, s28, 0x1e000
	s_nop 0
	global_load_lds_dwordx4 v12, s[4:5]
	v_mfma_f32_16x16x32_f16 v[100:103], v[204:207], v[180:183], v[100:103]
	s_waitcnt lgkmcnt(8)
	v_mfma_f32_16x16x32_f16 v[104:107], v[192:195], v[184:187], v[104:107]
	v_mfma_f32_16x16x32_f16 v[108:111], v[196:199], v[184:187], v[108:111]
	v_mfma_f32_16x16x32_f16 v[112:115], v[200:203], v[184:187], v[112:115]
	v_mfma_f32_16x16x32_f16 v[116:119], v[204:207], v[184:187], v[116:119]
	s_waitcnt lgkmcnt(7)
	ds_read_b128 v[172:175], v16
	ds_read_b128 v[192:195], v18
	ds_read_b128 v[196:199], v18 offset:2048
	ds_read_b128 v[200:203], v18 offset:4096
	ds_read_b128 v[204:207], v18 offset:6144
	ds_read_b128 v[176:179], v16 offset:2048
	ds_read_b128 v[180:183], v16 offset:4096
	ds_read_b128 v[184:187], v16 offset:6144
	s_waitcnt lgkmcnt(14)
	v_mfma_f32_16x16x32_f16 v[56:59], v[156:159], v[136:139], v[56:59]
	s_add_u32 m0, s28, 0x20000
	s_nop 0
	global_load_lds_dwordx4 v13, s[4:5]
	s_add_u32 s4, s4, s20
	s_addc_u32 s5, s5, 0
	s_waitcnt lgkmcnt(13)
	v_mfma_f32_16x16x32_f16 v[60:63], v[160:163], v[136:139], v[60:63]
	s_waitcnt lgkmcnt(12)
	v_mfma_f32_16x16x32_f16 v[64:67], v[164:167], v[136:139], v[64:67]
	s_waitcnt lgkmcnt(11)
	v_mfma_f32_16x16x32_f16 v[68:71], v[168:171], v[136:139], v[68:71]
	s_waitcnt lgkmcnt(10)
	v_mfma_f32_16x16x32_f16 v[72:75], v[156:159], v[140:143], v[72:75]
	v_mfma_f32_16x16x32_f16 v[76:79], v[160:163], v[140:143], v[76:79]
	s_add_u32 m0, s28, 0x23000
	s_nop 0
	global_load_lds_dwordx4 v10, s[6:7]
	v_mfma_f32_16x16x32_f16 v[80:83], v[164:167], v[140:143], v[80:83]
	v_mfma_f32_16x16x32_f16 v[84:87], v[168:171], v[140:143], v[84:87]
	s_waitcnt lgkmcnt(9)
	v_mfma_f32_16x16x32_f16 v[88:91], v[156:159], v[144:147], v[88:91]
	v_mfma_f32_16x16x32_f16 v[92:95], v[160:163], v[144:147], v[92:95]
	v_mfma_f32_16x16x32_f16 v[96:99], v[164:167], v[144:147], v[96:99]
	s_add_u32 m0, s28, 0x25000
	s_nop 0
	global_load_lds_dwordx4 v11, s[6:7]
	s_add_u32 s6, s6, s20
	s_addc_u32 s7, s7, 0
	v_mfma_f32_16x16x32_f16 v[100:103], v[168:171], v[144:147], v[100:103]
	s_waitcnt lgkmcnt(8)
	v_mfma_f32_16x16x32_f16 v[104:107], v[156:159], v[148:151], v[104:107]
	v_mfma_f32_16x16x32_f16 v[108:111], v[160:163], v[148:151], v[108:111]
	v_mfma_f32_16x16x32_f16 v[112:115], v[164:167], v[148:151], v[112:115]
	v_mfma_f32_16x16x32_f16 v[116:119], v[168:171], v[148:151], v[116:119]
	s_waitcnt vmcnt(6) lgkmcnt(0)
	s_barrier
	s_waitcnt lgkmcnt(7)
	ds_read_b128 v[136:139], v15 offset:53248
	ds_read_b128 v[156:159], v17 offset:53248
	ds_read_b128 v[160:163], v17 offset:55296
	ds_read_b128 v[164:167], v17 offset:57344
	ds_read_b128 v[168:171], v17 offset:59392
	ds_read_b128 v[140:143], v15 offset:55296
	ds_read_b128 v[144:147], v15 offset:57344
	ds_read_b128 v[148:151], v15 offset:59392
	s_waitcnt lgkmcnt(14)
	v_mfma_f32_16x16x32_f16 v[56:59], v[192:195], v[172:175], v[56:59]
	s_add_u32 m0, s28, 0x0
	s_nop 0
	global_load_lds_dwordx4 v10, s[4:5]
	s_waitcnt lgkmcnt(13)
	v_mfma_f32_16x16x32_f16 v[60:63], v[196:199], v[172:175], v[60:63]
	s_waitcnt lgkmcnt(12)
	v_mfma_f32_16x16x32_f16 v[64:67], v[200:203], v[172:175], v[64:67]
	s_waitcnt lgkmcnt(11)
	v_mfma_f32_16x16x32_f16 v[68:71], v[204:207], v[172:175], v[68:71]
	s_waitcnt lgkmcnt(10)
	v_mfma_f32_16x16x32_f16 v[72:75], v[192:195], v[176:179], v[72:75]
	v_mfma_f32_16x16x32_f16 v[76:79], v[196:199], v[176:179], v[76:79]
	s_add_u32 m0, s28, 0x2000
	s_nop 0
	global_load_lds_dwordx4 v11, s[4:5]
	v_mfma_f32_16x16x32_f16 v[80:83], v[200:203], v[176:179], v[80:83]
	v_mfma_f32_16x16x32_f16 v[84:87], v[204:207], v[176:179], v[84:87]
	s_waitcnt lgkmcnt(9)
	v_mfma_f32_16x16x32_f16 v[88:91], v[192:195], v[180:183], v[88:91]
	v_mfma_f32_16x16x32_f16 v[92:95], v[196:199], v[180:183], v[92:95]
	v_mfma_f32_16x16x32_f16 v[96:99], v[200:203], v[180:183], v[96:99]
	s_add_u32 m0, s28, 0x4000
	s_nop 0
	global_load_lds_dwordx4 v12, s[4:5]
	v_mfma_f32_16x16x32_f16 v[100:103], v[204:207], v[180:183], v[100:103]
	s_waitcnt lgkmcnt(8)
	v_mfma_f32_16x16x32_f16 v[104:107], v[192:195], v[184:187], v[104:107]
	v_mfma_f32_16x16x32_f16 v[108:111], v[196:199], v[184:187], v[108:111]
	v_mfma_f32_16x16x32_f16 v[112:115], v[200:203], v[184:187], v[112:115]
	v_mfma_f32_16x16x32_f16 v[116:119], v[204:207], v[184:187], v[116:119]
	s_waitcnt lgkmcnt(7)
	ds_read_b128 v[172:175], v16 offset:53248
	ds_read_b128 v[192:195], v18 offset:53248
	ds_read_b128 v[196:199], v18 offset:55296
	ds_read_b128 v[200:203], v18 offset:57344
	ds_read_b128 v[204:207], v18 offset:59392
	ds_read_b128 v[176:179], v16 offset:55296
	ds_read_b128 v[180:183], v16 offset:57344
	ds_read_b128 v[184:187], v16 offset:59392
	s_waitcnt lgkmcnt(14)
	v_mfma_f32_16x16x32_f16 v[56:59], v[156:159], v[136:139], v[56:59]
	s_add_u32 m0, s28, 0x6000
	s_nop 0
	global_load_lds_dwordx4 v13, s[4:5]
	s_add_u32 s4, s4, s20
	s_addc_u32 s5, s5, 0
	s_waitcnt lgkmcnt(13)
	v_mfma_f32_16x16x32_f16 v[60:63], v[160:163], v[136:139], v[60:63]
	s_waitcnt lgkmcnt(12)
	v_mfma_f32_16x16x32_f16 v[64:67], v[164:167], v[136:139], v[64:67]
	s_waitcnt lgkmcnt(11)
	v_mfma_f32_16x16x32_f16 v[68:71], v[168:171], v[136:139], v[68:71]
	s_waitcnt lgkmcnt(10)
	v_mfma_f32_16x16x32_f16 v[72:75], v[156:159], v[140:143], v[72:75]
	v_mfma_f32_16x16x32_f16 v[76:79], v[160:163], v[140:143], v[76:79]
	s_add_u32 m0, s28, 0x9000
	s_nop 0
	global_load_lds_dwordx4 v10, s[6:7]
	v_mfma_f32_16x16x32_f16 v[80:83], v[164:167], v[140:143], v[80:83]
	v_mfma_f32_16x16x32_f16 v[84:87], v[168:171], v[140:143], v[84:87]
	s_waitcnt lgkmcnt(9)
	v_mfma_f32_16x16x32_f16 v[88:91], v[156:159], v[144:147], v[88:91]
	v_mfma_f32_16x16x32_f16 v[92:95], v[160:163], v[144:147], v[92:95]
	v_mfma_f32_16x16x32_f16 v[96:99], v[164:167], v[144:147], v[96:99]
	s_add_u32 m0, s28, 0xb000
	s_nop 0
	global_load_lds_dwordx4 v11, s[6:7]
	s_add_u32 s6, s6, s20
	s_addc_u32 s7, s7, 0
	v_mfma_f32_16x16x32_f16 v[100:103], v[168:171], v[144:147], v[100:103]
	s_waitcnt lgkmcnt(8)
	v_mfma_f32_16x16x32_f16 v[104:107], v[156:159], v[148:151], v[104:107]
	v_mfma_f32_16x16x32_f16 v[108:111], v[160:163], v[148:151], v[108:111]
	v_mfma_f32_16x16x32_f16 v[112:115], v[164:167], v[148:151], v[112:115]
	v_mfma_f32_16x16x32_f16 v[116:119], v[168:171], v[148:151], v[116:119]
	s_waitcnt vmcnt(6) lgkmcnt(0)
	s_barrier
	s_waitcnt lgkmcnt(7)
	ds_read_b128 v[136:139], v19
	ds_read_b128 v[156:159], v21
	ds_read_b128 v[160:163], v21 offset:2048
	ds_read_b128 v[164:167], v21 offset:4096
	ds_read_b128 v[168:171], v21 offset:6144
	ds_read_b128 v[140:143], v19 offset:2048
	ds_read_b128 v[144:147], v19 offset:4096
	ds_read_b128 v[148:151], v19 offset:6144
	s_waitcnt lgkmcnt(14)
	v_mfma_f32_16x16x32_f16 v[56:59], v[192:195], v[172:175], v[56:59]
	s_waitcnt lgkmcnt(13)
	v_mfma_f32_16x16x32_f16 v[60:63], v[196:199], v[172:175], v[60:63]
	s_waitcnt lgkmcnt(12)
	v_mfma_f32_16x16x32_f16 v[64:67], v[200:203], v[172:175], v[64:67]
	s_waitcnt lgkmcnt(11)
	v_mfma_f32_16x16x32_f16 v[68:71], v[204:207], v[172:175], v[68:71]
	s_waitcnt lgkmcnt(10)
	v_mfma_f32_16x16x32_f16 v[72:75], v[192:195], v[176:179], v[72:75]
	v_mfma_f32_16x16x32_f16 v[76:79], v[196:199], v[176:179], v[76:79]
	v_mfma_f32_16x16x32_f16 v[80:83], v[200:203], v[176:179], v[80:83]
	v_mfma_f32_16x16x32_f16 v[84:87], v[204:207], v[176:179], v[84:87]
	s_waitcnt lgkmcnt(9)
	v_mfma_f32_16x16x32_f16 v[88:91], v[192:195], v[180:183], v[88:91]
	v_mfma_f32_16x16x32_f16 v[92:95], v[196:199], v[180:183], v[92:95]
	v_mfma_f32_16x16x32_f16 v[96:99], v[200:203], v[180:183], v[96:99]
	v_mfma_f32_16x16x32_f16 v[100:103], v[204:207], v[180:183], v[100:103]
	s_waitcnt lgkmcnt(8)
	v_mfma_f32_16x16x32_f16 v[104:107], v[192:195], v[184:187], v[104:107]
	v_mfma_f32_16x16x32_f16 v[108:111], v[196:199], v[184:187], v[108:111]
	v_mfma_f32_16x16x32_f16 v[112:115], v[200:203], v[184:187], v[112:115]
	v_mfma_f32_16x16x32_f16 v[116:119], v[204:207], v[184:187], v[116:119]
	s_waitcnt lgkmcnt(7)
	ds_read_b128 v[172:175], v20
	ds_read_b128 v[192:195], v22
	ds_read_b128 v[196:199], v22 offset:2048
	ds_read_b128 v[200:203], v22 offset:4096
	ds_read_b128 v[204:207], v22 offset:6144
	ds_read_b128 v[176:179], v20 offset:2048
	ds_read_b128 v[180:183], v20 offset:4096
	ds_read_b128 v[184:187], v20 offset:6144
	s_waitcnt lgkmcnt(14)
	v_mfma_f32_16x16x32_f16 v[56:59], v[156:159], v[136:139], v[56:59]
	s_waitcnt lgkmcnt(13)
	v_mfma_f32_16x16x32_f16 v[60:63], v[160:163], v[136:139], v[60:63]
	s_waitcnt lgkmcnt(12)
	v_mfma_f32_16x16x32_f16 v[64:67], v[164:167], v[136:139], v[64:67]
	s_waitcnt lgkmcnt(11)
	v_mfma_f32_16x16x32_f16 v[68:71], v[168:171], v[136:139], v[68:71]
	s_waitcnt lgkmcnt(10)
	v_mfma_f32_16x16x32_f16 v[72:75], v[156:159], v[140:143], v[72:75]
	v_mfma_f32_16x16x32_f16 v[76:79], v[160:163], v[140:143], v[76:79]
	v_mfma_f32_16x16x32_f16 v[80:83], v[164:167], v[140:143], v[80:83]
	v_mfma_f32_16x16x32_f16 v[84:87], v[168:171], v[140:143], v[84:87]
	s_waitcnt lgkmcnt(9)
	v_mfma_f32_16x16x32_f16 v[88:91], v[156:159], v[144:147], v[88:91]
	v_mfma_f32_16x16x32_f16 v[92:95], v[160:163], v[144:147], v[92:95]
	v_mfma_f32_16x16x32_f16 v[96:99], v[164:167], v[144:147], v[96:99]
	v_mfma_f32_16x16x32_f16 v[100:103], v[168:171], v[144:147], v[100:103]
	s_waitcnt lgkmcnt(8)
	v_mfma_f32_16x16x32_f16 v[104:107], v[156:159], v[148:151], v[104:107]
	v_mfma_f32_16x16x32_f16 v[108:111], v[160:163], v[148:151], v[108:111]
	v_mfma_f32_16x16x32_f16 v[112:115], v[164:167], v[148:151], v[112:115]
	v_mfma_f32_16x16x32_f16 v[116:119], v[168:171], v[148:151], v[116:119]
	s_waitcnt vmcnt(0) lgkmcnt(0)
	s_barrier
	s_waitcnt lgkmcnt(7)
	ds_read_b128 v[136:139], v15
	ds_read_b128 v[156:159], v17
	ds_read_b128 v[160:163], v17 offset:2048
	ds_read_b128 v[164:167], v17 offset:4096
	ds_read_b128 v[168:171], v17 offset:6144
	ds_read_b128 v[140:143], v15 offset:2048
	ds_read_b128 v[144:147], v15 offset:4096
	ds_read_b128 v[148:151], v15 offset:6144
	s_waitcnt lgkmcnt(14)
	v_mfma_f32_16x16x32_f16 v[56:59], v[192:195], v[172:175], v[56:59]
	s_waitcnt lgkmcnt(13)
	v_mfma_f32_16x16x32_f16 v[60:63], v[196:199], v[172:175], v[60:63]
	s_waitcnt lgkmcnt(12)
	v_mfma_f32_16x16x32_f16 v[64:67], v[200:203], v[172:175], v[64:67]
	s_waitcnt lgkmcnt(11)
	v_mfma_f32_16x16x32_f16 v[68:71], v[204:207], v[172:175], v[68:71]
	s_waitcnt lgkmcnt(10)
	v_mfma_f32_16x16x32_f16 v[72:75], v[192:195], v[176:179], v[72:75]
	v_mfma_f32_16x16x32_f16 v[76:79], v[196:199], v[176:179], v[76:79]
	v_mfma_f32_16x16x32_f16 v[80:83], v[200:203], v[176:179], v[80:83]
	v_mfma_f32_16x16x32_f16 v[84:87], v[204:207], v[176:179], v[84:87]
	s_waitcnt lgkmcnt(9)
	v_mfma_f32_16x16x32_f16 v[88:91], v[192:195], v[180:183], v[88:91]
	v_mfma_f32_16x16x32_f16 v[92:95], v[196:199], v[180:183], v[92:95]
	v_mfma_f32_16x16x32_f16 v[96:99], v[200:203], v[180:183], v[96:99]
	v_mfma_f32_16x16x32_f16 v[100:103], v[204:207], v[180:183], v[100:103]
	s_waitcnt lgkmcnt(8)
	v_mfma_f32_16x16x32_f16 v[104:107], v[192:195], v[184:187], v[104:107]
	v_mfma_f32_16x16x32_f16 v[108:111], v[196:199], v[184:187], v[108:111]
	v_mfma_f32_16x16x32_f16 v[112:115], v[200:203], v[184:187], v[112:115]
	v_mfma_f32_16x16x32_f16 v[116:119], v[204:207], v[184:187], v[116:119]
	s_waitcnt lgkmcnt(7)
	ds_read_b128 v[172:175], v16
	ds_read_b128 v[192:195], v18
	ds_read_b128 v[196:199], v18 offset:2048
	ds_read_b128 v[200:203], v18 offset:4096
	ds_read_b128 v[204:207], v18 offset:6144
	ds_read_b128 v[176:179], v16 offset:2048
	ds_read_b128 v[180:183], v16 offset:4096
	ds_read_b128 v[184:187], v16 offset:6144
	s_waitcnt lgkmcnt(14)
	v_mfma_f32_16x16x32_f16 v[56:59], v[156:159], v[136:139], v[56:59]
	s_waitcnt lgkmcnt(13)
	v_mfma_f32_16x16x32_f16 v[60:63], v[160:163], v[136:139], v[60:63]
	s_waitcnt lgkmcnt(12)
	v_mfma_f32_16x16x32_f16 v[64:67], v[164:167], v[136:139], v[64:67]
	s_waitcnt lgkmcnt(11)
	v_mfma_f32_16x16x32_f16 v[68:71], v[168:171], v[136:139], v[68:71]
	s_waitcnt lgkmcnt(10)
	v_mfma_f32_16x16x32_f16 v[72:75], v[156:159], v[140:143], v[72:75]
	v_mfma_f32_16x16x32_f16 v[76:79], v[160:163], v[140:143], v[76:79]
	v_mfma_f32_16x16x32_f16 v[80:83], v[164:167], v[140:143], v[80:83]
	v_mfma_f32_16x16x32_f16 v[84:87], v[168:171], v[140:143], v[84:87]
	s_waitcnt lgkmcnt(9)
	v_mfma_f32_16x16x32_f16 v[88:91], v[156:159], v[144:147], v[88:91]
	v_mfma_f32_16x16x32_f16 v[92:95], v[160:163], v[144:147], v[92:95]
	v_mfma_f32_16x16x32_f16 v[96:99], v[164:167], v[144:147], v[96:99]
	v_mfma_f32_16x16x32_f16 v[100:103], v[168:171], v[144:147], v[100:103]
	s_waitcnt lgkmcnt(8)
	v_mfma_f32_16x16x32_f16 v[104:107], v[156:159], v[148:151], v[104:107]
	v_mfma_f32_16x16x32_f16 v[108:111], v[160:163], v[148:151], v[108:111]
	v_mfma_f32_16x16x32_f16 v[112:115], v[164:167], v[148:151], v[112:115]
	v_mfma_f32_16x16x32_f16 v[116:119], v[168:171], v[148:151], v[116:119]
	s_waitcnt lgkmcnt(6)
	v_mfma_f32_16x16x32_f16 v[56:59], v[192:195], v[172:175], v[56:59]
	s_waitcnt lgkmcnt(5)
	v_mfma_f32_16x16x32_f16 v[60:63], v[196:199], v[172:175], v[60:63]
	s_waitcnt lgkmcnt(4)
	v_mfma_f32_16x16x32_f16 v[64:67], v[200:203], v[172:175], v[64:67]
	s_waitcnt lgkmcnt(3)
	v_mfma_f32_16x16x32_f16 v[68:71], v[204:207], v[172:175], v[68:71]
	s_waitcnt lgkmcnt(2)
	v_mfma_f32_16x16x32_f16 v[72:75], v[192:195], v[176:179], v[72:75]
	v_mfma_f32_16x16x32_f16 v[76:79], v[196:199], v[176:179], v[76:79]
	v_mfma_f32_16x16x32_f16 v[80:83], v[200:203], v[176:179], v[80:83]
	v_mfma_f32_16x16x32_f16 v[84:87], v[204:207], v[176:179], v[84:87]
	s_waitcnt lgkmcnt(1)
	v_mfma_f32_16x16x32_f16 v[88:91], v[192:195], v[180:183], v[88:91]
	v_mfma_f32_16x16x32_f16 v[92:95], v[196:199], v[180:183], v[92:95]
	v_mfma_f32_16x16x32_f16 v[96:99], v[200:203], v[180:183], v[96:99]
	v_mfma_f32_16x16x32_f16 v[100:103], v[204:207], v[180:183], v[100:103]
	s_waitcnt lgkmcnt(0)
	v_mfma_f32_16x16x32_f16 v[104:107], v[192:195], v[184:187], v[104:107]
	v_mfma_f32_16x16x32_f16 v[108:111], v[196:199], v[184:187], v[108:111]
	v_mfma_f32_16x16x32_f16 v[112:115], v[200:203], v[184:187], v[112:115]
	v_mfma_f32_16x16x32_f16 v[116:119], v[204:207], v[184:187], v[116:119]
	s_nop 7
	s_nop 1
	v_mov_b32_e32 v211, s19
	v_add_f32_e32 v56, v56, v24
	v_add_f32_e32 v57, v57, v25
	v_add_f32_e32 v58, v58, v26
	v_add_f32_e32 v59, v59, v27
	v_add_f32_e32 v60, v60, v28
	v_add_f32_e32 v61, v61, v29
	v_add_f32_e32 v62, v62, v30
	v_add_f32_e32 v63, v63, v31
	v_add_f32_e32 v64, v64, v32
	v_add_f32_e32 v65, v65, v33
	v_add_f32_e32 v66, v66, v34
	v_add_f32_e32 v67, v67, v35
	v_add_f32_e32 v68, v68, v36
	v_add_f32_e32 v69, v69, v37
	v_add_f32_e32 v70, v70, v38
	v_add_f32_e32 v71, v71, v39
	v_mul_f32_e32 v208, v56, v56
	v_fmac_f32_e32 v208, v57, v57
	v_fmac_f32_e32 v208, v58, v58
	v_fmac_f32_e32 v208, v59, v59
	v_fmac_f32_e32 v208, v60, v60
	v_fmac_f32_e32 v208, v61, v61
	v_fmac_f32_e32 v208, v62, v62
	v_fmac_f32_e32 v208, v63, v63
	v_fmac_f32_e32 v208, v64, v64
	v_fmac_f32_e32 v208, v65, v65
	v_fmac_f32_e32 v208, v66, v66
	v_fmac_f32_e32 v208, v67, v67
	v_fmac_f32_e32 v208, v68, v68
	v_fmac_f32_e32 v208, v69, v69
	v_fmac_f32_e32 v208, v70, v70
	v_fmac_f32_e32 v208, v71, v71
	v_mov_b32_e32 v209, v208
	s_nop 1
	v_permlane16_swap_b32_e32 v208, v209
	v_add_f32_e32 v208, v208, v209
	v_mov_b32_e32 v209, v208
	s_nop 1
	v_permlane32_swap_b32_e32 v208, v209
	v_add_f32_e32 v208, v208, v209
	v_mov_b32_e32 v210, 0x358637bd
	v_fmac_f32_e32 v210, 0x3c800000, v208
	v_rsq_f32_e32 v210, v210
	s_add_u32 s24, s29, 0
	s_lshr_b32 s8, s24, 1
	s_lshl_b32 s8, s8, 12
	s_and_b32 s24, s24, 1
	s_lshl_b32 s24, s24, 8
	s_add_u32 s8, s8, s24
	v_mul_f32_e32 v210, v211, v210
	v_add_u32_e32 v212, s8, v23
	v_mul_f32_e32 v56, v56, v210
	v_mul_f32_e32 v57, v57, v210
	v_mul_f32_e32 v58, v58, v210
	v_mul_f32_e32 v59, v59, v210
	v_mul_f32_e32 v56, v56, v40
	v_mul_f32_e32 v57, v57, v41
	v_mul_f32_e32 v58, v58, v42
	v_mul_f32_e32 v59, v59, v43
	v_cvt_pk_f16_f32 v56, v56, v57
	v_cvt_pk_f16_f32 v57, v58, v59
	global_store_dwordx2 v212, v[56:57], s[22:23] offset:0
	v_mul_f32_e32 v60, v60, v210
	v_mul_f32_e32 v61, v61, v210
	v_mul_f32_e32 v62, v62, v210
	v_mul_f32_e32 v63, v63, v210
	v_mul_f32_e32 v60, v60, v44
	v_mul_f32_e32 v61, v61, v45
	v_mul_f32_e32 v62, v62, v46
	v_mul_f32_e32 v63, v63, v47
	v_cvt_pk_f16_f32 v60, v60, v61
	v_cvt_pk_f16_f32 v61, v62, v63
	global_store_dwordx2 v212, v[60:61], s[22:23] offset:1024
	v_mul_f32_e32 v64, v64, v210
	v_mul_f32_e32 v65, v65, v210
	v_mul_f32_e32 v66, v66, v210
	v_mul_f32_e32 v67, v67, v210
	v_mul_f32_e32 v64, v64, v48
	v_mul_f32_e32 v65, v65, v49
	v_mul_f32_e32 v66, v66, v50
	v_mul_f32_e32 v67, v67, v51
	v_cvt_pk_f16_f32 v64, v64, v65
	v_cvt_pk_f16_f32 v65, v66, v67
	global_store_dwordx2 v212, v[64:65], s[22:23] offset:2048
	v_mul_f32_e32 v68, v68, v210
	v_mul_f32_e32 v69, v69, v210
	v_mul_f32_e32 v70, v70, v210
	v_mul_f32_e32 v71, v71, v210
	v_mul_f32_e32 v68, v68, v52
	v_mul_f32_e32 v69, v69, v53
	v_mul_f32_e32 v70, v70, v54
	v_mul_f32_e32 v71, v71, v55
	v_cvt_pk_f16_f32 v68, v68, v69
	v_cvt_pk_f16_f32 v69, v70, v71
	global_store_dwordx2 v212, v[68:69], s[22:23] offset:3072
	v_add_f32_e32 v72, v72, v24
	v_add_f32_e32 v73, v73, v25
	v_add_f32_e32 v74, v74, v26
	v_add_f32_e32 v75, v75, v27
	v_add_f32_e32 v76, v76, v28
	v_add_f32_e32 v77, v77, v29
	v_add_f32_e32 v78, v78, v30
	v_add_f32_e32 v79, v79, v31
	v_add_f32_e32 v80, v80, v32
	v_add_f32_e32 v81, v81, v33
	v_add_f32_e32 v82, v82, v34
	v_add_f32_e32 v83, v83, v35
	v_add_f32_e32 v84, v84, v36
	v_add_f32_e32 v85, v85, v37
	v_add_f32_e32 v86, v86, v38
	v_add_f32_e32 v87, v87, v39
	v_mul_f32_e32 v208, v72, v72
	v_fmac_f32_e32 v208, v73, v73
	v_fmac_f32_e32 v208, v74, v74
	v_fmac_f32_e32 v208, v75, v75
	v_fmac_f32_e32 v208, v76, v76
	v_fmac_f32_e32 v208, v77, v77
	v_fmac_f32_e32 v208, v78, v78
	v_fmac_f32_e32 v208, v79, v79
	v_fmac_f32_e32 v208, v80, v80
	v_fmac_f32_e32 v208, v81, v81
	v_fmac_f32_e32 v208, v82, v82
	v_fmac_f32_e32 v208, v83, v83
	v_fmac_f32_e32 v208, v84, v84
	v_fmac_f32_e32 v208, v85, v85
	v_fmac_f32_e32 v208, v86, v86
	v_fmac_f32_e32 v208, v87, v87
	v_mov_b32_e32 v209, v208
	s_nop 1
	v_permlane16_swap_b32_e32 v208, v209
	v_add_f32_e32 v208, v208, v209
	v_mov_b32_e32 v209, v208
	s_nop 1
	v_permlane32_swap_b32_e32 v208, v209
	v_add_f32_e32 v208, v208, v209
	v_mov_b32_e32 v210, 0x358637bd
	v_fmac_f32_e32 v210, 0x3c800000, v208
	v_rsq_f32_e32 v210, v210
	s_add_u32 s24, s29, 1
	s_lshr_b32 s8, s24, 1
	s_lshl_b32 s8, s8, 12
	s_and_b32 s24, s24, 1
	s_lshl_b32 s24, s24, 8
	s_add_u32 s8, s8, s24
	v_mul_f32_e32 v210, v211, v210
	v_add_u32_e32 v212, s8, v23
	v_mul_f32_e32 v72, v72, v210
	v_mul_f32_e32 v73, v73, v210
	v_mul_f32_e32 v74, v74, v210
	v_mul_f32_e32 v75, v75, v210
	v_mul_f32_e32 v72, v72, v40
	v_mul_f32_e32 v73, v73, v41
	v_mul_f32_e32 v74, v74, v42
	v_mul_f32_e32 v75, v75, v43
	v_cvt_pk_f16_f32 v72, v72, v73
	v_cvt_pk_f16_f32 v73, v74, v75
	global_store_dwordx2 v212, v[72:73], s[22:23] offset:0
	v_mul_f32_e32 v76, v76, v210
	v_mul_f32_e32 v77, v77, v210
	v_mul_f32_e32 v78, v78, v210
	v_mul_f32_e32 v79, v79, v210
	v_mul_f32_e32 v76, v76, v44
	v_mul_f32_e32 v77, v77, v45
	v_mul_f32_e32 v78, v78, v46
	v_mul_f32_e32 v79, v79, v47
	v_cvt_pk_f16_f32 v76, v76, v77
	v_cvt_pk_f16_f32 v77, v78, v79
	global_store_dwordx2 v212, v[76:77], s[22:23] offset:1024
	v_mul_f32_e32 v80, v80, v210
	v_mul_f32_e32 v81, v81, v210
	v_mul_f32_e32 v82, v82, v210
	v_mul_f32_e32 v83, v83, v210
	v_mul_f32_e32 v80, v80, v48
	v_mul_f32_e32 v81, v81, v49
	v_mul_f32_e32 v82, v82, v50
	v_mul_f32_e32 v83, v83, v51
	v_cvt_pk_f16_f32 v80, v80, v81
	v_cvt_pk_f16_f32 v81, v82, v83
	global_store_dwordx2 v212, v[80:81], s[22:23] offset:2048
	v_mul_f32_e32 v84, v84, v210
	v_mul_f32_e32 v85, v85, v210
	v_mul_f32_e32 v86, v86, v210
	v_mul_f32_e32 v87, v87, v210
	v_mul_f32_e32 v84, v84, v52
	v_mul_f32_e32 v85, v85, v53
	v_mul_f32_e32 v86, v86, v54
	v_mul_f32_e32 v87, v87, v55
	v_cvt_pk_f16_f32 v84, v84, v85
	v_cvt_pk_f16_f32 v85, v86, v87
	global_store_dwordx2 v212, v[84:85], s[22:23] offset:3072
	v_add_f32_e32 v88, v88, v24
	v_add_f32_e32 v89, v89, v25
	v_add_f32_e32 v90, v90, v26
	v_add_f32_e32 v91, v91, v27
	v_add_f32_e32 v92, v92, v28
	v_add_f32_e32 v93, v93, v29
	v_add_f32_e32 v94, v94, v30
	v_add_f32_e32 v95, v95, v31
	v_add_f32_e32 v96, v96, v32
	v_add_f32_e32 v97, v97, v33
	v_add_f32_e32 v98, v98, v34
	v_add_f32_e32 v99, v99, v35
	v_add_f32_e32 v100, v100, v36
	v_add_f32_e32 v101, v101, v37
	v_add_f32_e32 v102, v102, v38
	v_add_f32_e32 v103, v103, v39
	v_mul_f32_e32 v208, v88, v88
	v_fmac_f32_e32 v208, v89, v89
	v_fmac_f32_e32 v208, v90, v90
	v_fmac_f32_e32 v208, v91, v91
	v_fmac_f32_e32 v208, v92, v92
	v_fmac_f32_e32 v208, v93, v93
	v_fmac_f32_e32 v208, v94, v94
	v_fmac_f32_e32 v208, v95, v95
	v_fmac_f32_e32 v208, v96, v96
	v_fmac_f32_e32 v208, v97, v97
	v_fmac_f32_e32 v208, v98, v98
	v_fmac_f32_e32 v208, v99, v99
	v_fmac_f32_e32 v208, v100, v100
	v_fmac_f32_e32 v208, v101, v101
	v_fmac_f32_e32 v208, v102, v102
	v_fmac_f32_e32 v208, v103, v103
	v_mov_b32_e32 v209, v208
	s_nop 1
	v_permlane16_swap_b32_e32 v208, v209
	v_add_f32_e32 v208, v208, v209
	v_mov_b32_e32 v209, v208
	s_nop 1
	v_permlane32_swap_b32_e32 v208, v209
	v_add_f32_e32 v208, v208, v209
	v_mov_b32_e32 v210, 0x358637bd
	v_fmac_f32_e32 v210, 0x3c800000, v208
	v_rsq_f32_e32 v210, v210
	s_add_u32 s24, s29, 2
	s_lshr_b32 s8, s24, 1
	s_lshl_b32 s8, s8, 12
	s_and_b32 s24, s24, 1
	s_lshl_b32 s24, s24, 8
	s_add_u32 s8, s8, s24
	v_mul_f32_e32 v210, v211, v210
	v_add_u32_e32 v212, s8, v23
	v_mul_f32_e32 v88, v88, v210
	v_mul_f32_e32 v89, v89, v210
	v_mul_f32_e32 v90, v90, v210
	v_mul_f32_e32 v91, v91, v210
	v_mul_f32_e32 v88, v88, v40
	v_mul_f32_e32 v89, v89, v41
	v_mul_f32_e32 v90, v90, v42
	v_mul_f32_e32 v91, v91, v43
	v_cvt_pk_f16_f32 v88, v88, v89
	v_cvt_pk_f16_f32 v89, v90, v91
	global_store_dwordx2 v212, v[88:89], s[22:23] offset:0
	v_mul_f32_e32 v92, v92, v210
	v_mul_f32_e32 v93, v93, v210
	v_mul_f32_e32 v94, v94, v210
	v_mul_f32_e32 v95, v95, v210
	v_mul_f32_e32 v92, v92, v44
	v_mul_f32_e32 v93, v93, v45
	v_mul_f32_e32 v94, v94, v46
	v_mul_f32_e32 v95, v95, v47
	v_cvt_pk_f16_f32 v92, v92, v93
	v_cvt_pk_f16_f32 v93, v94, v95
	global_store_dwordx2 v212, v[92:93], s[22:23] offset:1024
	v_mul_f32_e32 v96, v96, v210
	v_mul_f32_e32 v97, v97, v210
	v_mul_f32_e32 v98, v98, v210
	v_mul_f32_e32 v99, v99, v210
	v_mul_f32_e32 v96, v96, v48
	v_mul_f32_e32 v97, v97, v49
	v_mul_f32_e32 v98, v98, v50
	v_mul_f32_e32 v99, v99, v51
	v_cvt_pk_f16_f32 v96, v96, v97
	v_cvt_pk_f16_f32 v97, v98, v99
	global_store_dwordx2 v212, v[96:97], s[22:23] offset:2048
	v_mul_f32_e32 v100, v100, v210
	v_mul_f32_e32 v101, v101, v210
	v_mul_f32_e32 v102, v102, v210
	v_mul_f32_e32 v103, v103, v210
	v_mul_f32_e32 v100, v100, v52
	v_mul_f32_e32 v101, v101, v53
	v_mul_f32_e32 v102, v102, v54
	v_mul_f32_e32 v103, v103, v55
	v_cvt_pk_f16_f32 v100, v100, v101
	v_cvt_pk_f16_f32 v101, v102, v103
	global_store_dwordx2 v212, v[100:101], s[22:23] offset:3072
	v_add_f32_e32 v104, v104, v24
	v_add_f32_e32 v105, v105, v25
	v_add_f32_e32 v106, v106, v26
	v_add_f32_e32 v107, v107, v27
	v_add_f32_e32 v108, v108, v28
	v_add_f32_e32 v109, v109, v29
	v_add_f32_e32 v110, v110, v30
	v_add_f32_e32 v111, v111, v31
	v_add_f32_e32 v112, v112, v32
	v_add_f32_e32 v113, v113, v33
	v_add_f32_e32 v114, v114, v34
	v_add_f32_e32 v115, v115, v35
	v_add_f32_e32 v116, v116, v36
	v_add_f32_e32 v117, v117, v37
	v_add_f32_e32 v118, v118, v38
	v_add_f32_e32 v119, v119, v39
	v_mul_f32_e32 v208, v104, v104
	v_fmac_f32_e32 v208, v105, v105
	v_fmac_f32_e32 v208, v106, v106
	v_fmac_f32_e32 v208, v107, v107
	v_fmac_f32_e32 v208, v108, v108
	v_fmac_f32_e32 v208, v109, v109
	v_fmac_f32_e32 v208, v110, v110
	v_fmac_f32_e32 v208, v111, v111
	v_fmac_f32_e32 v208, v112, v112
	v_fmac_f32_e32 v208, v113, v113
	v_fmac_f32_e32 v208, v114, v114
	v_fmac_f32_e32 v208, v115, v115
	v_fmac_f32_e32 v208, v116, v116
	v_fmac_f32_e32 v208, v117, v117
	v_fmac_f32_e32 v208, v118, v118
	v_fmac_f32_e32 v208, v119, v119
	v_mov_b32_e32 v209, v208
	s_nop 1
	v_permlane16_swap_b32_e32 v208, v209
	v_add_f32_e32 v208, v208, v209
	v_mov_b32_e32 v209, v208
	s_nop 1
	v_permlane32_swap_b32_e32 v208, v209
	v_add_f32_e32 v208, v208, v209
	v_mov_b32_e32 v210, 0x358637bd
	v_fmac_f32_e32 v210, 0x3c800000, v208
	v_rsq_f32_e32 v210, v210
	s_add_u32 s24, s29, 3
	s_lshr_b32 s8, s24, 1
	s_lshl_b32 s8, s8, 12
	s_and_b32 s24, s24, 1
	s_lshl_b32 s24, s24, 8
	s_add_u32 s8, s8, s24
	v_mul_f32_e32 v210, v211, v210
	v_add_u32_e32 v212, s8, v23
	v_mul_f32_e32 v104, v104, v210
	v_mul_f32_e32 v105, v105, v210
	v_mul_f32_e32 v106, v106, v210
	v_mul_f32_e32 v107, v107, v210
	v_mul_f32_e32 v104, v104, v40
	v_mul_f32_e32 v105, v105, v41
	v_mul_f32_e32 v106, v106, v42
	v_mul_f32_e32 v107, v107, v43
	v_cvt_pk_f16_f32 v104, v104, v105
	v_cvt_pk_f16_f32 v105, v106, v107
	global_store_dwordx2 v212, v[104:105], s[22:23] offset:0
	v_mul_f32_e32 v108, v108, v210
	v_mul_f32_e32 v109, v109, v210
	v_mul_f32_e32 v110, v110, v210
	v_mul_f32_e32 v111, v111, v210
	v_mul_f32_e32 v108, v108, v44
	v_mul_f32_e32 v109, v109, v45
	v_mul_f32_e32 v110, v110, v46
	v_mul_f32_e32 v111, v111, v47
	v_cvt_pk_f16_f32 v108, v108, v109
	v_cvt_pk_f16_f32 v109, v110, v111
	global_store_dwordx2 v212, v[108:109], s[22:23] offset:1024
	v_mul_f32_e32 v112, v112, v210
	v_mul_f32_e32 v113, v113, v210
	v_mul_f32_e32 v114, v114, v210
	v_mul_f32_e32 v115, v115, v210
	v_mul_f32_e32 v112, v112, v48
	v_mul_f32_e32 v113, v113, v49
	v_mul_f32_e32 v114, v114, v50
	v_mul_f32_e32 v115, v115, v51
	v_cvt_pk_f16_f32 v112, v112, v113
	v_cvt_pk_f16_f32 v113, v114, v115
	global_store_dwordx2 v212, v[112:113], s[22:23] offset:2048
	v_mul_f32_e32 v116, v116, v210
	v_mul_f32_e32 v117, v117, v210
	v_mul_f32_e32 v118, v118, v210
	v_mul_f32_e32 v119, v119, v210
	v_mul_f32_e32 v116, v116, v52
	v_mul_f32_e32 v117, v117, v53
	v_mul_f32_e32 v118, v118, v54
	v_mul_f32_e32 v119, v119, v55
	v_cvt_pk_f16_f32 v116, v116, v117
	v_cvt_pk_f16_f32 v117, v118, v119
	global_store_dwordx2 v212, v[116:117], s[22:23] offset:3072
	s_branch .Lpf_done
.Lpf_vVA:
	s_mul_i32 s25, s25, 0x50
	s_add_u32 s29, s10, s25
	s_lshr_b32 s29, s29, 4
	v_add_u32_e32 v5, s25, v3
	v_lshlrev_b32_e32 v5, 7, v5
	v_add_u32_e32 v15, v5, v6
	v_add_u32_e32 v16, v5, v7
	v_add_u32_e32 v5, 0x9000, v9
	v_add_u32_e32 v17, v5, v6
	v_add_u32_e32 v18, v5, v7
	v_add_u32_e32 v19, 0x1a000, v15
	v_add_u32_e32 v20, 0x1a000, v16
	v_add_u32_e32 v21, 0x1a000, v17
	v_add_u32_e32 v22, 0x1a000, v18
	v_lshlrev_b32_e32 v5, 2, v3
	global_load_dword v24, v5, s[14:15] offset:0
	global_load_dword v25, v5, s[14:15] offset:64
	global_load_dword v26, v5, s[14:15] offset:128
	global_load_dword v27, v5, s[14:15] offset:192
	s_add_u32 m0, s28, 0x0
	s_nop 0
	global_load_lds_dwordx4 v10, s[4:5]
	s_add_u32 m0, s28, 0x2000
	s_nop 0
	global_load_lds_dwordx4 v11, s[4:5]
	s_add_u32 m0, s28, 0x4000
	s_nop 0
	global_load_lds_dwordx4 v12, s[4:5]
	s_add_u32 m0, s28, 0x6000
	s_nop 0
	global_load_lds_dwordx4 v13, s[4:5]
	s_add_u32 m0, s28, 0x8000
	s_nop 0
	global_load_lds_dwordx4 v14, s[4:5]
	s_add_u32 s4, s4, s20
	s_addc_u32 s5, s5, 0
	s_add_u32 m0, s28, 0x9000
	s_nop 0
	global_load_lds_dwordx4 v10, s[6:7]
	s_add_u32 m0, s28, 0xb000
	s_nop 0
	global_load_lds_dwordx4 v11, s[6:7]
	s_add_u32 s6, s6, s20
	s_addc_u32 s7, s7, 0
	s_add_u32 m0, s28, 0xd000
	s_nop 0
	global_load_lds_dwordx4 v10, s[4:5]
	s_add_u32 m0, s28, 0xf000
	s_nop 0
	global_load_lds_dwordx4 v11, s[4:5]
	s_add_u32 m0, s28, 0x11000
	s_nop 0
	global_load_lds_dwordx4 v12, s[4:5]
	s_add_u32 m0, s28, 0x13000
	s_nop 0
	global_load_lds_dwordx4 v13, s[4:5]
	s_add_u32 m0, s28, 0x15000
	s_nop 0
	global_load_lds_dwordx4 v14, s[4:5]
	s_add_u32 s4, s4, s20
	s_addc_u32 s5, s5, 0
	s_add_u32 m0, s28, 0x16000
	s_nop 0
	global_load_lds_dwordx4 v10, s[6:7]
	s_add_u32 m0, s28, 0x18000
	s_nop 0
	global_load_lds_dwordx4 v11, s[6:7]
	s_add_u32 s6, s6, s20
	s_addc_u32 s7, s7, 0
	s_add_u32 m0, s28, 0x1a000
	s_nop 0
	global_load_lds_dwordx4 v10, s[4:5]
	s_add_u32 m0, s28, 0x1c000
	s_nop 0
	global_load_lds_dwordx4 v11, s[4:5]
	s_add_u32 m0, s28, 0x1e000
	s_nop 0
	global_load_lds_dwordx4 v12, s[4:5]
	s_add_u32 m0, s28, 0x20000
	s_nop 0
	global_load_lds_dwordx4 v13, s[4:5]
	s_add_u32 m0, s28, 0x22000
	s_nop 0
	global_load_lds_dwordx4 v14, s[4:5]
	s_add_u32 s4, s4, s20
	s_addc_u32 s5, s5, 0
	s_add_u32 m0, s28, 0x23000
	s_nop 0
	global_load_lds_dwordx4 v10, s[6:7]
	s_add_u32 m0, s28, 0x25000
	s_nop 0
	global_load_lds_dwordx4 v11, s[6:7]
	s_add_u32 s6, s6, s20
	s_addc_u32 s7, s7, 0
	s_waitcnt vmcnt(14) lgkmcnt(0)
	s_barrier
	s_waitcnt lgkmcnt(6)
	ds_read_b128 v[136:139], v15
	ds_read_b128 v[156:159], v17
	ds_read_b128 v[160:163], v17 offset:2048
	ds_read_b128 v[164:167], v17 offset:4096
	ds_read_b128 v[168:171], v17 offset:6144
	ds_read_b128 v[140:143], v15 offset:2048
	ds_read_b128 v[144:147], v15 offset:4096
	ds_read_b128 v[148:151], v15 offset:6144
	ds_read_b128 v[152:155], v15 offset:8192
	s_waitcnt lgkmcnt(6)
	ds_read_b128 v[172:175], v16
	ds_read_b128 v[192:195], v18
	ds_read_b128 v[196:199], v18 offset:2048
	ds_read_b128 v[200:203], v18 offset:4096
	ds_read_b128 v[204:207], v18 offset:6144
	ds_read_b128 v[176:179], v16 offset:2048
	ds_read_b128 v[180:183], v16 offset:4096
	ds_read_b128 v[184:187], v16 offset:6144
	ds_read_b128 v[188:191], v16 offset:8192
	v_mfma_f32_16x16x32_f16 v[56:59], v[136:139], v[156:159], 0
	s_waitcnt lgkmcnt(15)
	v_mfma_f32_16x16x32_f16 v[60:63], v[136:139], v[160:163], 0
	s_waitcnt lgkmcnt(14)
	v_mfma_f32_16x16x32_f16 v[64:67], v[136:139], v[164:167], 0
	s_waitcnt lgkmcnt(13)
	v_mfma_f32_16x16x32_f16 v[68:71], v[136:139], v[168:171], 0
	s_waitcnt lgkmcnt(12)
	v_mfma_f32_16x16x32_f16 v[72:75], v[140:143], v[156:159], 0
	v_mfma_f32_16x16x32_f16 v[76:79], v[140:143], v[160:163], 0
	v_mfma_f32_16x16x32_f16 v[80:83], v[140:143], v[164:167], 0
	v_mfma_f32_16x16x32_f16 v[84:87], v[140:143], v[168:171], 0
	s_waitcnt lgkmcnt(11)
	v_mfma_f32_16x16x32_f16 v[88:91], v[144:147], v[156:159], 0
	v_mfma_f32_16x16x32_f16 v[92:95], v[144:147], v[160:163], 0
	v_mfma_f32_16x16x32_f16 v[96:99], v[144:147], v[164:167], 0
	v_mfma_f32_16x16x32_f16 v[100:103], v[144:147], v[168:171], 0
	s_waitcnt lgkmcnt(10)
	v_mfma_f32_16x16x32_f16 v[104:107], v[148:151], v[156:159], 0
	v_mfma_f32_16x16x32_f16 v[108:111], v[148:151], v[160:163], 0
	v_mfma_f32_16x16x32_f16 v[112:115], v[148:151], v[164:167], 0
	v_mfma_f32_16x16x32_f16 v[116:119], v[148:151], v[168:171], 0
	s_waitcnt lgkmcnt(9)
	v_mfma_f32_16x16x32_f16 v[120:123], v[152:155], v[156:159], 0
	v_mfma_f32_16x16x32_f16 v[124:127], v[152:155], v[160:163], 0
	v_mfma_f32_16x16x32_f16 v[128:131], v[152:155], v[164:167], 0
	v_mfma_f32_16x16x32_f16 v[132:135], v[152:155], v[168:171], 0
	s_waitcnt vmcnt(7) lgkmcnt(0)
	s_barrier
	s_waitcnt lgkmcnt(6)
	ds_read_b128 v[136:139], v15 offset:53248
	ds_read_b128 v[156:159], v17 offset:53248
	ds_read_b128 v[160:163], v17 offset:55296
	ds_read_b128 v[164:167], v17 offset:57344
	ds_read_b128 v[168:171], v17 offset:59392
	ds_read_b128 v[140:143], v15 offset:55296
	ds_read_b128 v[144:147], v15 offset:57344
	ds_read_b128 v[148:151], v15 offset:59392
	ds_read_b128 v[152:155], v15 offset:61440
	v_mfma_f32_16x16x32_f16 v[56:59], v[172:175], v[192:195], v[56:59]
	s_add_u32 m0, s28, 0x0
	s_nop 0
	global_load_lds_dwordx4 v10, s[4:5]
	s_waitcnt lgkmcnt(15)
	v_mfma_f32_16x16x32_f16 v[60:63], v[172:175], v[196:199], v[60:63]
	s_waitcnt lgkmcnt(14)
	v_mfma_f32_16x16x32_f16 v[64:67], v[172:175], v[200:203], v[64:67]
	s_waitcnt lgkmcnt(13)
	v_mfma_f32_16x16x32_f16 v[68:71], v[172:175], v[204:207], v[68:71]
	s_waitcnt lgkmcnt(12)
	v_mfma_f32_16x16x32_f16 v[72:75], v[176:179], v[192:195], v[72:75]
	v_mfma_f32_16x16x32_f16 v[76:79], v[176:179], v[196:199], v[76:79]
	s_add_u32 m0, s28, 0x2000
	s_nop 0
	global_load_lds_dwordx4 v11, s[4:5]
	v_mfma_f32_16x16x32_f16 v[80:83], v[176:179], v[200:203], v[80:83]
	v_mfma_f32_16x16x32_f16 v[84:87], v[176:179], v[204:207], v[84:87]
	s_waitcnt lgkmcnt(11)
	v_mfma_f32_16x16x32_f16 v[88:91], v[180:183], v[192:195], v[88:91]
	v_mfma_f32_16x16x32_f16 v[92:95], v[180:183], v[196:199], v[92:95]
	v_mfma_f32_16x16x32_f16 v[96:99], v[180:183], v[200:203], v[96:99]
	s_add_u32 m0, s28, 0x4000
	s_nop 0
	global_load_lds_dwordx4 v12, s[4:5]
	v_mfma_f32_16x16x32_f16 v[100:103], v[180:183], v[204:207], v[100:103]
	s_waitcnt lgkmcnt(10)
	v_mfma_f32_16x16x32_f16 v[104:107], v[184:187], v[192:195], v[104:107]
	v_mfma_f32_16x16x32_f16 v[108:111], v[184:187], v[196:199], v[108:111]
	v_mfma_f32_16x16x32_f16 v[112:115], v[184:187], v[200:203], v[112:115]
	v_mfma_f32_16x16x32_f16 v[116:119], v[184:187], v[204:207], v[116:119]
	s_add_u32 m0, s28, 0x6000
	s_nop 0
	global_load_lds_dwordx4 v13, s[4:5]
	s_waitcnt lgkmcnt(9)
	v_mfma_f32_16x16x32_f16 v[120:123], v[188:191], v[192:195], v[120:123]
	v_mfma_f32_16x16x32_f16 v[124:127], v[188:191], v[196:199], v[124:127]
	v_mfma_f32_16x16x32_f16 v[128:131], v[188:191], v[200:203], v[128:131]
	v_mfma_f32_16x16x32_f16 v[132:135], v[188:191], v[204:207], v[132:135]
	s_waitcnt lgkmcnt(6)
	ds_read_b128 v[172:175], v16 offset:53248
	ds_read_b128 v[192:195], v18 offset:53248
	ds_read_b128 v[196:199], v18 offset:55296
	ds_read_b128 v[200:203], v18 offset:57344
	ds_read_b128 v[204:207], v18 offset:59392
	ds_read_b128 v[176:179], v16 offset:55296
	ds_read_b128 v[180:183], v16 offset:57344
	ds_read_b128 v[184:187], v16 offset:59392
	ds_read_b128 v[188:191], v16 offset:61440
	v_mfma_f32_16x16x32_f16 v[56:59], v[136:139], v[156:159], v[56:59]
	s_add_u32 m0, s28, 0x8000
	s_nop 0
	global_load_lds_dwordx4 v14, s[4:5]
	s_add_u32 s4, s4, s20
	s_addc_u32 s5, s5, 0
	s_waitcnt lgkmcnt(15)
	v_mfma_f32_16x16x32_f16 v[60:63], v[136:139], v[160:163], v[60:63]
	s_waitcnt lgkmcnt(14)
	v_mfma_f32_16x16x32_f16 v[64:67], v[136:139], v[164:167], v[64:67]
	s_waitcnt lgkmcnt(13)
	v_mfma_f32_16x16x32_f16 v[68:71], v[136:139], v[168:171], v[68:71]
	s_waitcnt lgkmcnt(12)
	v_mfma_f32_16x16x32_f16 v[72:75], v[140:143], v[156:159], v[72:75]
	v_mfma_f32_16x16x32_f16 v[76:79], v[140:143], v[160:163], v[76:79]
	v_mfma_f32_16x16x32_f16 v[80:83], v[140:143], v[164:167], v[80:83]
	s_add_u32 m0, s28, 0x9000
	s_nop 0
	global_load_lds_dwordx4 v10, s[6:7]
	v_mfma_f32_16x16x32_f16 v[84:87], v[140:143], v[168:171], v[84:87]
	s_waitcnt lgkmcnt(11)
	v_mfma_f32_16x16x32_f16 v[88:91], v[144:147], v[156:159], v[88:91]
	v_mfma_f32_16x16x32_f16 v[92:95], v[144:147], v[160:163], v[92:95]
	v_mfma_f32_16x16x32_f16 v[96:99], v[144:147], v[164:167], v[96:99]
	v_mfma_f32_16x16x32_f16 v[100:103], v[144:147], v[168:171], v[100:103]
	s_waitcnt lgkmcnt(10)
	v_mfma_f32_16x16x32_f16 v[104:107], v[148:151], v[156:159], v[104:107]
	v_mfma_f32_16x16x32_f16 v[108:111], v[148:151], v[160:163], v[108:111]
	s_add_u32 m0, s28, 0xb000
	s_nop 0
	global_load_lds_dwordx4 v11, s[6:7]
	s_add_u32 s6, s6, s20
	s_addc_u32 s7, s7, 0
	v_mfma_f32_16x16x32_f16 v[112:115], v[148:151], v[164:167], v[112:115]
	v_mfma_f32_16x16x32_f16 v[116:119], v[148:151], v[168:171], v[116:119]
	s_waitcnt lgkmcnt(9)
	v_mfma_f32_16x16x32_f16 v[120:123], v[152:155], v[156:159], v[120:123]
	v_mfma_f32_16x16x32_f16 v[124:127], v[152:155], v[160:163], v[124:127]
	v_mfma_f32_16x16x32_f16 v[128:131], v[152:155], v[164:167], v[128:131]
	v_mfma_f32_16x16x32_f16 v[132:135], v[152:155], v[168:171], v[132:135]
	s_waitcnt vmcnt(7) lgkmcnt(0)
	s_barrier
	s_waitcnt lgkmcnt(6)
	ds_read_b128 v[136:139], v19
	ds_read_b128 v[156:159], v21
	ds_read_b128 v[160:163], v21 offset:2048
	ds_read_b128 v[164:167], v21 offset:4096
	ds_read_b128 v[168:171], v21 offset:6144
	ds_read_b128 v[140:143], v19 offset:2048
	ds_read_b128 v[144:147], v19 offset:4096
	ds_read_b128 v[148:151], v19 offset:6144
	ds_read_b128 v[152:155], v19 offset:8192
	v_mfma_f32_16x16x32_f16 v[56:59], v[172:175], v[192:195], v[56:59]
	s_add_u32 m0, s28, 0xd000
	s_nop 0
	global_load_lds_dwordx4 v10, s[4:5]
	s_waitcnt lgkmcnt(15)
	v_mfma_f32_16x16x32_f16 v[60:63], v[172:175], v[196:199], v[60:63]
	s_waitcnt lgkmcnt(14)
	v_mfma_f32_16x16x32_f16 v[64:67], v[172:175], v[200:203], v[64:67]
	s_waitcnt lgkmcnt(13)
	v_mfma_f32_16x16x32_f16 v[68:71], v[172:175], v[204:207], v[68:71]
	s_waitcnt lgkmcnt(12)
	v_mfma_f32_16x16x32_f16 v[72:75], v[176:179], v[192:195], v[72:75]
	v_mfma_f32_16x16x32_f16 v[76:79], v[176:179], v[196:199], v[76:79]
	s_add_u32 m0, s28, 0xf000
	s_nop 0
	global_load_lds_dwordx4 v11, s[4:5]
	v_mfma_f32_16x16x32_f16 v[80:83], v[176:179], v[200:203], v[80:83]
	v_mfma_f32_16x16x32_f16 v[84:87], v[176:179], v[204:207], v[84:87]
	s_waitcnt lgkmcnt(11)
	v_mfma_f32_16x16x32_f16 v[88:91], v[180:183], v[192:195], v[88:91]
	v_mfma_f32_16x16x32_f16 v[92:95], v[180:183], v[196:199], v[92:95]
	v_mfma_f32_16x16x32_f16 v[96:99], v[180:183], v[200:203], v[96:99]
	s_add_u32 m0, s28, 0x11000
	s_nop 0
	global_load_lds_dwordx4 v12, s[4:5]
	v_mfma_f32_16x16x32_f16 v[100:103], v[180:183], v[204:207], v[100:103]
	s_waitcnt lgkmcnt(10)
	v_mfma_f32_16x16x32_f16 v[104:107], v[184:187], v[192:195], v[104:107]
	v_mfma_f32_16x16x32_f16 v[108:111], v[184:187], v[196:199], v[108:111]
	v_mfma_f32_16x16x32_f16 v[112:115], v[184:187], v[200:203], v[112:115]
	v_mfma_f32_16x16x32_f16 v[116:119], v[184:187], v[204:207], v[116:119]
	s_add_u32 m0, s28, 0x13000
	s_nop 0
	global_load_lds_dwordx4 v13, s[4:5]
	s_waitcnt lgkmcnt(9)
	v_mfma_f32_16x16x32_f16 v[120:123], v[188:191], v[192:195], v[120:123]
	v_mfma_f32_16x16x32_f16 v[124:127], v[188:191], v[196:199], v[124:127]
	v_mfma_f32_16x16x32_f16 v[128:131], v[188:191], v[200:203], v[128:131]
	v_mfma_f32_16x16x32_f16 v[132:135], v[188:191], v[204:207], v[132:135]
	s_waitcnt lgkmcnt(6)
	ds_read_b128 v[172:175], v20
	ds_read_b128 v[192:195], v22
	ds_read_b128 v[196:199], v22 offset:2048
	ds_read_b128 v[200:203], v22 offset:4096
	ds_read_b128 v[204:207], v22 offset:6144
	ds_read_b128 v[176:179], v20 offset:2048
	ds_read_b128 v[180:183], v20 offset:4096
	ds_read_b128 v[184:187], v20 offset:6144
	ds_read_b128 v[188:191], v20 offset:8192
	v_mfma_f32_16x16x32_f16 v[56:59], v[136:139], v[156:159], v[56:59]
	s_add_u32 m0, s28, 0x15000
	s_nop 0
	global_load_lds_dwordx4 v14, s[4:5]
	s_add_u32 s4, s4, s20
	s_addc_u32 s5, s5, 0
	s_waitcnt lgkmcnt(15)
	v_mfma_f32_16x16x32_f16 v[60:63], v[136:139], v[160:163], v[60:63]
	s_waitcnt lgkmcnt(14)
	v_mfma_f32_16x16x32_f16 v[64:67], v[136:139], v[164:167], v[64:67]
	s_waitcnt lgkmcnt(13)
	v_mfma_f32_16x16x32_f16 v[68:71], v[136:139], v[168:171], v[68:71]
	s_waitcnt lgkmcnt(12)
	v_mfma_f32_16x16x32_f16 v[72:75], v[140:143], v[156:159], v[72:75]
	v_mfma_f32_16x16x32_f16 v[76:79], v[140:143], v[160:163], v[76:79]
	v_mfma_f32_16x16x32_f16 v[80:83], v[140:143], v[164:167], v[80:83]
	s_add_u32 m0, s28, 0x16000
	s_nop 0
	global_load_lds_dwordx4 v10, s[6:7]
	v_mfma_f32_16x16x32_f16 v[84:87], v[140:143], v[168:171], v[84:87]
	s_waitcnt lgkmcnt(11)
	v_mfma_f32_16x16x32_f16 v[88:91], v[144:147], v[156:159], v[88:91]
	v_mfma_f32_16x16x32_f16 v[92:95], v[144:147], v[160:163], v[92:95]
	v_mfma_f32_16x16x32_f16 v[96:99], v[144:147], v[164:167], v[96:99]
	v_mfma_f32_16x16x32_f16 v[100:103], v[144:147], v[168:171], v[100:103]
	s_waitcnt lgkmcnt(10)
	v_mfma_f32_16x16x32_f16 v[104:107], v[148:151], v[156:159], v[104:107]
	v_mfma_f32_16x16x32_f16 v[108:111], v[148:151], v[160:163], v[108:111]
	s_add_u32 m0, s28, 0x18000
	s_nop 0
	global_load_lds_dwordx4 v11, s[6:7]
	s_add_u32 s6, s6, s20
	s_addc_u32 s7, s7, 0
	v_mfma_f32_16x16x32_f16 v[112:115], v[148:151], v[164:167], v[112:115]
	v_mfma_f32_16x16x32_f16 v[116:119], v[148:151], v[168:171], v[116:119]
	s_waitcnt lgkmcnt(9)
	v_mfma_f32_16x16x32_f16 v[120:123], v[152:155], v[156:159], v[120:123]
	v_mfma_f32_16x16x32_f16 v[124:127], v[152:155], v[160:163], v[124:127]
	v_mfma_f32_16x16x32_f16 v[128:131], v[152:155], v[164:167], v[128:131]
	v_mfma_f32_16x16x32_f16 v[132:135], v[152:155], v[168:171], v[132:135]
	s_waitcnt vmcnt(7) lgkmcnt(0)
	s_barrier
	s_waitcnt lgkmcnt(6)
	ds_read_b128 v[136:139], v15
	ds_read_b128 v[156:159], v17
	ds_read_b128 v[160:163], v17 offset:2048
	ds_read_b128 v[164:167], v17 offset:4096
	ds_read_b128 v[168:171], v17 offset:6144
	ds_read_b128 v[140:143], v15 offset:2048
	ds_read_b128 v[144:147], v15 offset:4096
	ds_read_b128 v[148:151], v15 offset:6144
	ds_read_b128 v[152:155], v15 offset:8192
	v_mfma_f32_16x16x32_f16 v[56:59], v[172:175], v[192:195], v[56:59]
	s_add_u32 m0, s28, 0x1a000
	s_nop 0
	global_load_lds_dwordx4 v10, s[4:5]
	s_waitcnt lgkmcnt(15)
	v_mfma_f32_16x16x32_f16 v[60:63], v[172:175], v[196:199], v[60:63]
	s_waitcnt lgkmcnt(14)
	v_mfma_f32_16x16x32_f16 v[64:67], v[172:175], v[200:203], v[64:67]
	s_waitcnt lgkmcnt(13)
	v_mfma_f32_16x16x32_f16 v[68:71], v[172:175], v[204:207], v[68:71]
	s_waitcnt lgkmcnt(12)
	v_mfma_f32_16x16x32_f16 v[72:75], v[176:179], v[192:195], v[72:75]
	v_mfma_f32_16x16x32_f16 v[76:79], v[176:179], v[196:199], v[76:79]
	s_add_u32 m0, s28, 0x1c000
	s_nop 0
	global_load_lds_dwordx4 v11, s[4:5]
	v_mfma_f32_16x16x32_f16 v[80:83], v[176:179], v[200:203], v[80:83]
	v_mfma_f32_16x16x32_f16 v[84:87], v[176:179], v[204:207], v[84:87]
	s_waitcnt lgkmcnt(11)
	v_mfma_f32_16x16x32_f16 v[88:91], v[180:183], v[192:195], v[88:91]
	v_mfma_f32_16x16x32_f16 v[92:95], v[180:183], v[196:199], v[92:95]
	v_mfma_f32_16x16x32_f16 v[96:99], v[180:183], v[200:203], v[96:99]
	s_add_u32 m0, s28, 0x1e000
	s_nop 0
	global_load_lds_dwordx4 v12, s[4:5]
	v_mfma_f32_16x16x32_f16 v[100:103], v[180:183], v[204:207], v[100:103]
	s_waitcnt lgkmcnt(10)
	v_mfma_f32_16x16x32_f16 v[104:107], v[184:187], v[192:195], v[104:107]
	v_mfma_f32_16x16x32_f16 v[108:111], v[184:187], v[196:199], v[108:111]
	v_mfma_f32_16x16x32_f16 v[112:115], v[184:187], v[200:203], v[112:115]
	v_mfma_f32_16x16x32_f16 v[116:119], v[184:187], v[204:207], v[116:119]
	s_add_u32 m0, s28, 0x20000
	s_nop 0
	global_load_lds_dwordx4 v13, s[4:5]
	s_waitcnt lgkmcnt(9)
	v_mfma_f32_16x16x32_f16 v[120:123], v[188:191], v[192:195], v[120:123]
	v_mfma_f32_16x16x32_f16 v[124:127], v[188:191], v[196:199], v[124:127]
	v_mfma_f32_16x16x32_f16 v[128:131], v[188:191], v[200:203], v[128:131]
	v_mfma_f32_16x16x32_f16 v[132:135], v[188:191], v[204:207], v[132:135]
	s_waitcnt lgkmcnt(6)
	ds_read_b128 v[172:175], v16
	ds_read_b128 v[192:195], v18
	ds_read_b128 v[196:199], v18 offset:2048
	ds_read_b128 v[200:203], v18 offset:4096
	ds_read_b128 v[204:207], v18 offset:6144
	ds_read_b128 v[176:179], v16 offset:2048
	ds_read_b128 v[180:183], v16 offset:4096
	ds_read_b128 v[184:187], v16 offset:6144
	ds_read_b128 v[188:191], v16 offset:8192
	v_mfma_f32_16x16x32_f16 v[56:59], v[136:139], v[156:159], v[56:59]
	s_add_u32 m0, s28, 0x22000
	s_nop 0
	global_load_lds_dwordx4 v14, s[4:5]
	s_add_u32 s4, s4, s20
	s_addc_u32 s5, s5, 0
	s_waitcnt lgkmcnt(15)
	v_mfma_f32_16x16x32_f16 v[60:63], v[136:139], v[160:163], v[60:63]
	s_waitcnt lgkmcnt(14)
	v_mfma_f32_16x16x32_f16 v[64:67], v[136:139], v[164:167], v[64:67]
	s_waitcnt lgkmcnt(13)
	v_mfma_f32_16x16x32_f16 v[68:71], v[136:139], v[168:171], v[68:71]
	s_waitcnt lgkmcnt(12)
	v_mfma_f32_16x16x32_f16 v[72:75], v[140:143], v[156:159], v[72:75]
	v_mfma_f32_16x16x32_f16 v[76:79], v[140:143], v[160:163], v[76:79]
	v_mfma_f32_16x16x32_f16 v[80:83], v[140:143], v[164:167], v[80:83]
	s_add_u32 m0, s28, 0x23000
	s_nop 0
	global_load_lds_dwordx4 v10, s[6:7]
	v_mfma_f32_16x16x32_f16 v[84:87], v[140:143], v[168:171], v[84:87]
	s_waitcnt lgkmcnt(11)
	v_mfma_f32_16x16x32_f16 v[88:91], v[144:147], v[156:159], v[88:91]
	v_mfma_f32_16x16x32_f16 v[92:95], v[144:147], v[160:163], v[92:95]
	v_mfma_f32_16x16x32_f16 v[96:99], v[144:147], v[164:167], v[96:99]
	v_mfma_f32_16x16x32_f16 v[100:103], v[144:147], v[168:171], v[100:103]
	s_waitcnt lgkmcnt(10)
	v_mfma_f32_16x16x32_f16 v[104:107], v[148:151], v[156:159], v[104:107]
	v_mfma_f32_16x16x32_f16 v[108:111], v[148:151], v[160:163], v[108:111]
	s_add_u32 m0, s28, 0x25000
	s_nop 0
	global_load_lds_dwordx4 v11, s[6:7]
	s_add_u32 s6, s6, s20
	s_addc_u32 s7, s7, 0
	v_mfma_f32_16x16x32_f16 v[112:115], v[148:151], v[164:167], v[112:115]
	v_mfma_f32_16x16x32_f16 v[116:119], v[148:151], v[168:171], v[116:119]
	s_waitcnt lgkmcnt(9)
	v_mfma_f32_16x16x32_f16 v[120:123], v[152:155], v[156:159], v[120:123]
	v_mfma_f32_16x16x32_f16 v[124:127], v[152:155], v[160:163], v[124:127]
	v_mfma_f32_16x16x32_f16 v[128:131], v[152:155], v[164:167], v[128:131]
	v_mfma_f32_16x16x32_f16 v[132:135], v[152:155], v[168:171], v[132:135]
	s_waitcnt vmcnt(7) lgkmcnt(0)
	s_barrier
	s_waitcnt lgkmcnt(6)
	ds_read_b128 v[136:139], v15 offset:53248
	ds_read_b128 v[156:159], v17 offset:53248
	ds_read_b128 v[160:163], v17 offset:55296
	ds_read_b128 v[164:167], v17 offset:57344
	ds_read_b128 v[168:171], v17 offset:59392
	ds_read_b128 v[140:143], v15 offset:55296
	ds_read_b128 v[144:147], v15 offset:57344
	ds_read_b128 v[148:151], v15 offset:59392
	ds_read_b128 v[152:155], v15 offset:61440
	v_mfma_f32_16x16x32_f16 v[56:59], v[172:175], v[192:195], v[56:59]
	s_add_u32 m0, s28, 0x0
	s_nop 0
	global_load_lds_dwordx4 v10, s[4:5]
	s_waitcnt lgkmcnt(15)
	v_mfma_f32_16x16x32_f16 v[60:63], v[172:175], v[196:199], v[60:63]
	s_waitcnt lgkmcnt(14)
	v_mfma_f32_16x16x32_f16 v[64:67], v[172:175], v[200:203], v[64:67]
	s_waitcnt lgkmcnt(13)
	v_mfma_f32_16x16x32_f16 v[68:71], v[172:175], v[204:207], v[68:71]
	s_waitcnt lgkmcnt(12)
	v_mfma_f32_16x16x32_f16 v[72:75], v[176:179], v[192:195], v[72:75]
	v_mfma_f32_16x16x32_f16 v[76:79], v[176:179], v[196:199], v[76:79]
	s_add_u32 m0, s28, 0x2000
	s_nop 0
	global_load_lds_dwordx4 v11, s[4:5]
	v_mfma_f32_16x16x32_f16 v[80:83], v[176:179], v[200:203], v[80:83]
	v_mfma_f32_16x16x32_f16 v[84:87], v[176:179], v[204:207], v[84:87]
	s_waitcnt lgkmcnt(11)
	v_mfma_f32_16x16x32_f16 v[88:91], v[180:183], v[192:195], v[88:91]
	v_mfma_f32_16x16x32_f16 v[92:95], v[180:183], v[196:199], v[92:95]
	v_mfma_f32_16x16x32_f16 v[96:99], v[180:183], v[200:203], v[96:99]
	s_add_u32 m0, s28, 0x4000
	s_nop 0
	global_load_lds_dwordx4 v12, s[4:5]
	v_mfma_f32_16x16x32_f16 v[100:103], v[180:183], v[204:207], v[100:103]
	s_waitcnt lgkmcnt(10)
	v_mfma_f32_16x16x32_f16 v[104:107], v[184:187], v[192:195], v[104:107]
	v_mfma_f32_16x16x32_f16 v[108:111], v[184:187], v[196:199], v[108:111]
	v_mfma_f32_16x16x32_f16 v[112:115], v[184:187], v[200:203], v[112:115]
	v_mfma_f32_16x16x32_f16 v[116:119], v[184:187], v[204:207], v[116:119]
	s_add_u32 m0, s28, 0x6000
	s_nop 0
	global_load_lds_dwordx4 v13, s[4:5]
	s_waitcnt lgkmcnt(9)
	v_mfma_f32_16x16x32_f16 v[120:123], v[188:191], v[192:195], v[120:123]
	v_mfma_f32_16x16x32_f16 v[124:127], v[188:191], v[196:199], v[124:127]
	v_mfma_f32_16x16x32_f16 v[128:131], v[188:191], v[200:203], v[128:131]
	v_mfma_f32_16x16x32_f16 v[132:135], v[188:191], v[204:207], v[132:135]
	s_waitcnt lgkmcnt(6)
	ds_read_b128 v[172:175], v16 offset:53248
	ds_read_b128 v[192:195], v18 offset:53248
	ds_read_b128 v[196:199], v18 offset:55296
	ds_read_b128 v[200:203], v18 offset:57344
	ds_read_b128 v[204:207], v18 offset:59392
	ds_read_b128 v[176:179], v16 offset:55296
	ds_read_b128 v[180:183], v16 offset:57344
	ds_read_b128 v[184:187], v16 offset:59392
	ds_read_b128 v[188:191], v16 offset:61440
	v_mfma_f32_16x16x32_f16 v[56:59], v[136:139], v[156:159], v[56:59]
	s_add_u32 m0, s28, 0x8000
	s_nop 0
	global_load_lds_dwordx4 v14, s[4:5]
	s_add_u32 s4, s4, s20
	s_addc_u32 s5, s5, 0
	s_waitcnt lgkmcnt(15)
	v_mfma_f32_16x16x32_f16 v[60:63], v[136:139], v[160:163], v[60:63]
	s_waitcnt lgkmcnt(14)
	v_mfma_f32_16x16x32_f16 v[64:67], v[136:139], v[164:167], v[64:67]
	s_waitcnt lgkmcnt(13)
	v_mfma_f32_16x16x32_f16 v[68:71], v[136:139], v[168:171], v[68:71]
	s_waitcnt lgkmcnt(12)
	v_mfma_f32_16x16x32_f16 v[72:75], v[140:143], v[156:159], v[72:75]
	v_mfma_f32_16x16x32_f16 v[76:79], v[140:143], v[160:163], v[76:79]
	v_mfma_f32_16x16x32_f16 v[80:83], v[140:143], v[164:167], v[80:83]
	s_add_u32 m0, s28, 0x9000
	s_nop 0
	global_load_lds_dwordx4 v10, s[6:7]
	v_mfma_f32_16x16x32_f16 v[84:87], v[140:143], v[168:171], v[84:87]
	s_waitcnt lgkmcnt(11)
	v_mfma_f32_16x16x32_f16 v[88:91], v[144:147], v[156:159], v[88:91]
	v_mfma_f32_16x16x32_f16 v[92:95], v[144:147], v[160:163], v[92:95]
	v_mfma_f32_16x16x32_f16 v[96:99], v[144:147], v[164:167], v[96:99]
	v_mfma_f32_16x16x32_f16 v[100:103], v[144:147], v[168:171], v[100:103]
	s_waitcnt lgkmcnt(10)
	v_mfma_f32_16x16x32_f16 v[104:107], v[148:151], v[156:159], v[104:107]
	v_mfma_f32_16x16x32_f16 v[108:111], v[148:151], v[160:163], v[108:111]
	s_add_u32 m0, s28, 0xb000
	s_nop 0
	global_load_lds_dwordx4 v11, s[6:7]
	s_add_u32 s6, s6, s20
	s_addc_u32 s7, s7, 0
	v_mfma_f32_16x16x32_f16 v[112:115], v[148:151], v[164:167], v[112:115]
	v_mfma_f32_16x16x32_f16 v[116:119], v[148:151], v[168:171], v[116:119]
	s_waitcnt lgkmcnt(9)
	v_mfma_f32_16x16x32_f16 v[120:123], v[152:155], v[156:159], v[120:123]
	v_mfma_f32_16x16x32_f16 v[124:127], v[152:155], v[160:163], v[124:127]
	v_mfma_f32_16x16x32_f16 v[128:131], v[152:155], v[164:167], v[128:131]
	v_mfma_f32_16x16x32_f16 v[132:135], v[152:155], v[168:171], v[132:135]
	s_waitcnt vmcnt(7) lgkmcnt(0)
	s_barrier
	s_waitcnt lgkmcnt(6)
	ds_read_b128 v[136:139], v19
	ds_read_b128 v[156:159], v21
	ds_read_b128 v[160:163], v21 offset:2048
	ds_read_b128 v[164:167], v21 offset:4096
	ds_read_b128 v[168:171], v21 offset:6144
	ds_read_b128 v[140:143], v19 offset:2048
	ds_read_b128 v[144:147], v19 offset:4096
	ds_read_b128 v[148:151], v19 offset:6144
	ds_read_b128 v[152:155], v19 offset:8192
	v_mfma_f32_16x16x32_f16 v[56:59], v[172:175], v[192:195], v[56:59]
	s_add_u32 m0, s28, 0xd000
	s_nop 0
	global_load_lds_dwordx4 v10, s[4:5]
	s_waitcnt lgkmcnt(15)
	v_mfma_f32_16x16x32_f16 v[60:63], v[172:175], v[196:199], v[60:63]
	s_waitcnt lgkmcnt(14)
	v_mfma_f32_16x16x32_f16 v[64:67], v[172:175], v[200:203], v[64:67]
	s_waitcnt lgkmcnt(13)
	v_mfma_f32_16x16x32_f16 v[68:71], v[172:175], v[204:207], v[68:71]
	s_waitcnt lgkmcnt(12)
	v_mfma_f32_16x16x32_f16 v[72:75], v[176:179], v[192:195], v[72:75]
	v_mfma_f32_16x16x32_f16 v[76:79], v[176:179], v[196:199], v[76:79]
	s_add_u32 m0, s28, 0xf000
	s_nop 0
	global_load_lds_dwordx4 v11, s[4:5]
	v_mfma_f32_16x16x32_f16 v[80:83], v[176:179], v[200:203], v[80:83]
	v_mfma_f32_16x16x32_f16 v[84:87], v[176:179], v[204:207], v[84:87]
	s_waitcnt lgkmcnt(11)
	v_mfma_f32_16x16x32_f16 v[88:91], v[180:183], v[192:195], v[88:91]
	v_mfma_f32_16x16x32_f16 v[92:95], v[180:183], v[196:199], v[92:95]
	v_mfma_f32_16x16x32_f16 v[96:99], v[180:183], v[200:203], v[96:99]
	s_add_u32 m0, s28, 0x11000
	s_nop 0
	global_load_lds_dwordx4 v12, s[4:5]
	v_mfma_f32_16x16x32_f16 v[100:103], v[180:183], v[204:207], v[100:103]
	s_waitcnt lgkmcnt(10)
	v_mfma_f32_16x16x32_f16 v[104:107], v[184:187], v[192:195], v[104:107]
	v_mfma_f32_16x16x32_f16 v[108:111], v[184:187], v[196:199], v[108:111]
	v_mfma_f32_16x16x32_f16 v[112:115], v[184:187], v[200:203], v[112:115]
	v_mfma_f32_16x16x32_f16 v[116:119], v[184:187], v[204:207], v[116:119]
	s_add_u32 m0, s28, 0x13000
	s_nop 0
	global_load_lds_dwordx4 v13, s[4:5]
	s_waitcnt lgkmcnt(9)
	v_mfma_f32_16x16x32_f16 v[120:123], v[188:191], v[192:195], v[120:123]
	v_mfma_f32_16x16x32_f16 v[124:127], v[188:191], v[196:199], v[124:127]
	v_mfma_f32_16x16x32_f16 v[128:131], v[188:191], v[200:203], v[128:131]
	v_mfma_f32_16x16x32_f16 v[132:135], v[188:191], v[204:207], v[132:135]
	s_waitcnt lgkmcnt(6)
	ds_read_b128 v[172:175], v20
	ds_read_b128 v[192:195], v22
	ds_read_b128 v[196:199], v22 offset:2048
	ds_read_b128 v[200:203], v22 offset:4096
	ds_read_b128 v[204:207], v22 offset:6144
	ds_read_b128 v[176:179], v20 offset:2048
	ds_read_b128 v[180:183], v20 offset:4096
	ds_read_b128 v[184:187], v20 offset:6144
	ds_read_b128 v[188:191], v20 offset:8192
	v_mfma_f32_16x16x32_f16 v[56:59], v[136:139], v[156:159], v[56:59]
	s_add_u32 m0, s28, 0x15000
	s_nop 0
	global_load_lds_dwordx4 v14, s[4:5]
	s_add_u32 s4, s4, s20
	s_addc_u32 s5, s5, 0
	s_waitcnt lgkmcnt(15)
	v_mfma_f32_16x16x32_f16 v[60:63], v[136:139], v[160:163], v[60:63]
	s_waitcnt lgkmcnt(14)
	v_mfma_f32_16x16x32_f16 v[64:67], v[136:139], v[164:167], v[64:67]
	s_waitcnt lgkmcnt(13)
	v_mfma_f32_16x16x32_f16 v[68:71], v[136:139], v[168:171], v[68:71]
	s_waitcnt lgkmcnt(12)
	v_mfma_f32_16x16x32_f16 v[72:75], v[140:143], v[156:159], v[72:75]
	v_mfma_f32_16x16x32_f16 v[76:79], v[140:143], v[160:163], v[76:79]
	v_mfma_f32_16x16x32_f16 v[80:83], v[140:143], v[164:167], v[80:83]
	s_add_u32 m0, s28, 0x16000
	s_nop 0
	global_load_lds_dwordx4 v10, s[6:7]
	v_mfma_f32_16x16x32_f16 v[84:87], v[140:143], v[168:171], v[84:87]
	s_waitcnt lgkmcnt(11)
	v_mfma_f32_16x16x32_f16 v[88:91], v[144:147], v[156:159], v[88:91]
	v_mfma_f32_16x16x32_f16 v[92:95], v[144:147], v[160:163], v[92:95]
	v_mfma_f32_16x16x32_f16 v[96:99], v[144:147], v[164:167], v[96:99]
	v_mfma_f32_16x16x32_f16 v[100:103], v[144:147], v[168:171], v[100:103]
	s_waitcnt lgkmcnt(10)
	v_mfma_f32_16x16x32_f16 v[104:107], v[148:151], v[156:159], v[104:107]
	v_mfma_f32_16x16x32_f16 v[108:111], v[148:151], v[160:163], v[108:111]
	s_add_u32 m0, s28, 0x18000
	s_nop 0
	global_load_lds_dwordx4 v11, s[6:7]
	s_add_u32 s6, s6, s20
	s_addc_u32 s7, s7, 0
	v_mfma_f32_16x16x32_f16 v[112:115], v[148:151], v[164:167], v[112:115]
	v_mfma_f32_16x16x32_f16 v[116:119], v[148:151], v[168:171], v[116:119]
	s_waitcnt lgkmcnt(9)
	v_mfma_f32_16x16x32_f16 v[120:123], v[152:155], v[156:159], v[120:123]
	v_mfma_f32_16x16x32_f16 v[124:127], v[152:155], v[160:163], v[124:127]
	v_mfma_f32_16x16x32_f16 v[128:131], v[152:155], v[164:167], v[128:131]
	v_mfma_f32_16x16x32_f16 v[132:135], v[152:155], v[168:171], v[132:135]
	s_waitcnt vmcnt(7) lgkmcnt(0)
	s_barrier
	s_waitcnt lgkmcnt(6)
	ds_read_b128 v[136:139], v15
	ds_read_b128 v[156:159], v17
	ds_read_b128 v[160:163], v17 offset:2048
	ds_read_b128 v[164:167], v17 offset:4096
	ds_read_b128 v[168:171], v17 offset:6144
	ds_read_b128 v[140:143], v15 offset:2048
	ds_read_b128 v[144:147], v15 offset:4096
	ds_read_b128 v[148:151], v15 offset:6144
	ds_read_b128 v[152:155], v15 offset:8192
	v_mfma_f32_16x16x32_f16 v[56:59], v[172:175], v[192:195], v[56:59]
	s_add_u32 m0, s28, 0x1a000
	s_nop 0
	global_load_lds_dwordx4 v10, s[4:5]
	s_waitcnt lgkmcnt(15)
	v_mfma_f32_16x16x32_f16 v[60:63], v[172:175], v[196:199], v[60:63]
	s_waitcnt lgkmcnt(14)
	v_mfma_f32_16x16x32_f16 v[64:67], v[172:175], v[200:203], v[64:67]
	s_waitcnt lgkmcnt(13)
	v_mfma_f32_16x16x32_f16 v[68:71], v[172:175], v[204:207], v[68:71]
	s_waitcnt lgkmcnt(12)
	v_mfma_f32_16x16x32_f16 v[72:75], v[176:179], v[192:195], v[72:75]
	v_mfma_f32_16x16x32_f16 v[76:79], v[176:179], v[196:199], v[76:79]
	s_add_u32 m0, s28, 0x1c000
	s_nop 0
	global_load_lds_dwordx4 v11, s[4:5]
	v_mfma_f32_16x16x32_f16 v[80:83], v[176:179], v[200:203], v[80:83]
	v_mfma_f32_16x16x32_f16 v[84:87], v[176:179], v[204:207], v[84:87]
	s_waitcnt lgkmcnt(11)
	v_mfma_f32_16x16x32_f16 v[88:91], v[180:183], v[192:195], v[88:91]
	v_mfma_f32_16x16x32_f16 v[92:95], v[180:183], v[196:199], v[92:95]
	v_mfma_f32_16x16x32_f16 v[96:99], v[180:183], v[200:203], v[96:99]
	s_add_u32 m0, s28, 0x1e000
	s_nop 0
	global_load_lds_dwordx4 v12, s[4:5]
	v_mfma_f32_16x16x32_f16 v[100:103], v[180:183], v[204:207], v[100:103]
	s_waitcnt lgkmcnt(10)
	v_mfma_f32_16x16x32_f16 v[104:107], v[184:187], v[192:195], v[104:107]
	v_mfma_f32_16x16x32_f16 v[108:111], v[184:187], v[196:199], v[108:111]
	v_mfma_f32_16x16x32_f16 v[112:115], v[184:187], v[200:203], v[112:115]
	v_mfma_f32_16x16x32_f16 v[116:119], v[184:187], v[204:207], v[116:119]
	s_add_u32 m0, s28, 0x20000
	s_nop 0
	global_load_lds_dwordx4 v13, s[4:5]
	s_waitcnt lgkmcnt(9)
	v_mfma_f32_16x16x32_f16 v[120:123], v[188:191], v[192:195], v[120:123]
	v_mfma_f32_16x16x32_f16 v[124:127], v[188:191], v[196:199], v[124:127]
	v_mfma_f32_16x16x32_f16 v[128:131], v[188:191], v[200:203], v[128:131]
	v_mfma_f32_16x16x32_f16 v[132:135], v[188:191], v[204:207], v[132:135]
	s_waitcnt lgkmcnt(6)
	ds_read_b128 v[172:175], v16
	ds_read_b128 v[192:195], v18
	ds_read_b128 v[196:199], v18 offset:2048
	ds_read_b128 v[200:203], v18 offset:4096
	ds_read_b128 v[204:207], v18 offset:6144
	ds_read_b128 v[176:179], v16 offset:2048
	ds_read_b128 v[180:183], v16 offset:4096
	ds_read_b128 v[184:187], v16 offset:6144
	ds_read_b128 v[188:191], v16 offset:8192
	v_mfma_f32_16x16x32_f16 v[56:59], v[136:139], v[156:159], v[56:59]
	s_add_u32 m0, s28, 0x22000
	s_nop 0
	global_load_lds_dwordx4 v14, s[4:5]
	s_add_u32 s4, s4, s20
	s_addc_u32 s5, s5, 0
	s_waitcnt lgkmcnt(15)
	v_mfma_f32_16x16x32_f16 v[60:63], v[136:139], v[160:163], v[60:63]
	s_waitcnt lgkmcnt(14)
	v_mfma_f32_16x16x32_f16 v[64:67], v[136:139], v[164:167], v[64:67]
	s_waitcnt lgkmcnt(13)
	v_mfma_f32_16x16x32_f16 v[68:71], v[136:139], v[168:171], v[68:71]
	s_waitcnt lgkmcnt(12)
	v_mfma_f32_16x16x32_f16 v[72:75], v[140:143], v[156:159], v[72:75]
	v_mfma_f32_16x16x32_f16 v[76:79], v[140:143], v[160:163], v[76:79]
	v_mfma_f32_16x16x32_f16 v[80:83], v[140:143], v[164:167], v[80:83]
	s_add_u32 m0, s28, 0x23000
	s_nop 0
	global_load_lds_dwordx4 v10, s[6:7]
	v_mfma_f32_16x16x32_f16 v[84:87], v[140:143], v[168:171], v[84:87]
	s_waitcnt lgkmcnt(11)
	v_mfma_f32_16x16x32_f16 v[88:91], v[144:147], v[156:159], v[88:91]
	v_mfma_f32_16x16x32_f16 v[92:95], v[144:147], v[160:163], v[92:95]
	v_mfma_f32_16x16x32_f16 v[96:99], v[144:147], v[164:167], v[96:99]
	v_mfma_f32_16x16x32_f16 v[100:103], v[144:147], v[168:171], v[100:103]
	s_waitcnt lgkmcnt(10)
	v_mfma_f32_16x16x32_f16 v[104:107], v[148:151], v[156:159], v[104:107]
	v_mfma_f32_16x16x32_f16 v[108:111], v[148:151], v[160:163], v[108:111]
	s_add_u32 m0, s28, 0x25000
	s_nop 0
	global_load_lds_dwordx4 v11, s[6:7]
	s_add_u32 s6, s6, s20
	s_addc_u32 s7, s7, 0
	v_mfma_f32_16x16x32_f16 v[112:115], v[148:151], v[164:167], v[112:115]
	v_mfma_f32_16x16x32_f16 v[116:119], v[148:151], v[168:171], v[116:119]
	s_waitcnt lgkmcnt(9)
	v_mfma_f32_16x16x32_f16 v[120:123], v[152:155], v[156:159], v[120:123]
	v_mfma_f32_16x16x32_f16 v[124:127], v[152:155], v[160:163], v[124:127]
	v_mfma_f32_16x16x32_f16 v[128:131], v[152:155], v[164:167], v[128:131]
	v_mfma_f32_16x16x32_f16 v[132:135], v[152:155], v[168:171], v[132:135]
	s_waitcnt vmcnt(7) lgkmcnt(0)
	s_barrier
	s_waitcnt lgkmcnt(6)
	ds_read_b128 v[136:139], v15 offset:53248
	ds_read_b128 v[156:159], v17 offset:53248
	ds_read_b128 v[160:163], v17 offset:55296
	ds_read_b128 v[164:167], v17 offset:57344
	ds_read_b128 v[168:171], v17 offset:59392
	ds_read_b128 v[140:143], v15 offset:55296
	ds_read_b128 v[144:147], v15 offset:57344
	ds_read_b128 v[148:151], v15 offset:59392
	ds_read_b128 v[152:155], v15 offset:61440
	v_mfma_f32_16x16x32_f16 v[56:59], v[172:175], v[192:195], v[56:59]
	s_add_u32 m0, s28, 0x0
	s_nop 0
	global_load_lds_dwordx4 v10, s[4:5]
	s_waitcnt lgkmcnt(15)
	v_mfma_f32_16x16x32_f16 v[60:63], v[172:175], v[196:199], v[60:63]
	s_waitcnt lgkmcnt(14)
	v_mfma_f32_16x16x32_f16 v[64:67], v[172:175], v[200:203], v[64:67]
	s_waitcnt lgkmcnt(13)
	v_mfma_f32_16x16x32_f16 v[68:71], v[172:175], v[204:207], v[68:71]
	s_waitcnt lgkmcnt(12)
	v_mfma_f32_16x16x32_f16 v[72:75], v[176:179], v[192:195], v[72:75]
	v_mfma_f32_16x16x32_f16 v[76:79], v[176:179], v[196:199], v[76:79]
	s_add_u32 m0, s28, 0x2000
	s_nop 0
	global_load_lds_dwordx4 v11, s[4:5]
	v_mfma_f32_16x16x32_f16 v[80:83], v[176:179], v[200:203], v[80:83]
	v_mfma_f32_16x16x32_f16 v[84:87], v[176:179], v[204:207], v[84:87]
	s_waitcnt lgkmcnt(11)
	v_mfma_f32_16x16x32_f16 v[88:91], v[180:183], v[192:195], v[88:91]
	v_mfma_f32_16x16x32_f16 v[92:95], v[180:183], v[196:199], v[92:95]
	v_mfma_f32_16x16x32_f16 v[96:99], v[180:183], v[200:203], v[96:99]
	s_add_u32 m0, s28, 0x4000
	s_nop 0
	global_load_lds_dwordx4 v12, s[4:5]
	v_mfma_f32_16x16x32_f16 v[100:103], v[180:183], v[204:207], v[100:103]
	s_waitcnt lgkmcnt(10)
	v_mfma_f32_16x16x32_f16 v[104:107], v[184:187], v[192:195], v[104:107]
	v_mfma_f32_16x16x32_f16 v[108:111], v[184:187], v[196:199], v[108:111]
	v_mfma_f32_16x16x32_f16 v[112:115], v[184:187], v[200:203], v[112:115]
	v_mfma_f32_16x16x32_f16 v[116:119], v[184:187], v[204:207], v[116:119]
	s_add_u32 m0, s28, 0x6000
	s_nop 0
	global_load_lds_dwordx4 v13, s[4:5]
	s_waitcnt lgkmcnt(9)
	v_mfma_f32_16x16x32_f16 v[120:123], v[188:191], v[192:195], v[120:123]
	v_mfma_f32_16x16x32_f16 v[124:127], v[188:191], v[196:199], v[124:127]
	v_mfma_f32_16x16x32_f16 v[128:131], v[188:191], v[200:203], v[128:131]
	v_mfma_f32_16x16x32_f16 v[132:135], v[188:191], v[204:207], v[132:135]
	s_waitcnt lgkmcnt(6)
	ds_read_b128 v[172:175], v16 offset:53248
	ds_read_b128 v[192:195], v18 offset:53248
	ds_read_b128 v[196:199], v18 offset:55296
	ds_read_b128 v[200:203], v18 offset:57344
	ds_read_b128 v[204:207], v18 offset:59392
	ds_read_b128 v[176:179], v16 offset:55296
	ds_read_b128 v[180:183], v16 offset:57344
	ds_read_b128 v[184:187], v16 offset:59392
	ds_read_b128 v[188:191], v16 offset:61440
	v_mfma_f32_16x16x32_f16 v[56:59], v[136:139], v[156:159], v[56:59]
	s_add_u32 m0, s28, 0x8000
	s_nop 0
	global_load_lds_dwordx4 v14, s[4:5]
	s_add_u32 s4, s4, s20
	s_addc_u32 s5, s5, 0
	s_waitcnt lgkmcnt(15)
	v_mfma_f32_16x16x32_f16 v[60:63], v[136:139], v[160:163], v[60:63]
	s_waitcnt lgkmcnt(14)
	v_mfma_f32_16x16x32_f16 v[64:67], v[136:139], v[164:167], v[64:67]
	s_waitcnt lgkmcnt(13)
	v_mfma_f32_16x16x32_f16 v[68:71], v[136:139], v[168:171], v[68:71]
	s_waitcnt lgkmcnt(12)
	v_mfma_f32_16x16x32_f16 v[72:75], v[140:143], v[156:159], v[72:75]
	v_mfma_f32_16x16x32_f16 v[76:79], v[140:143], v[160:163], v[76:79]
	v_mfma_f32_16x16x32_f16 v[80:83], v[140:143], v[164:167], v[80:83]
	s_add_u32 m0, s28, 0x9000
	s_nop 0
	global_load_lds_dwordx4 v10, s[6:7]
	v_mfma_f32_16x16x32_f16 v[84:87], v[140:143], v[168:171], v[84:87]
	s_waitcnt lgkmcnt(11)
	v_mfma_f32_16x16x32_f16 v[88:91], v[144:147], v[156:159], v[88:91]
	v_mfma_f32_16x16x32_f16 v[92:95], v[144:147], v[160:163], v[92:95]
	v_mfma_f32_16x16x32_f16 v[96:99], v[144:147], v[164:167], v[96:99]
	v_mfma_f32_16x16x32_f16 v[100:103], v[144:147], v[168:171], v[100:103]
	s_waitcnt lgkmcnt(10)
	v_mfma_f32_16x16x32_f16 v[104:107], v[148:151], v[156:159], v[104:107]
	v_mfma_f32_16x16x32_f16 v[108:111], v[148:151], v[160:163], v[108:111]
	s_add_u32 m0, s28, 0xb000
	s_nop 0
	global_load_lds_dwordx4 v11, s[6:7]
	s_add_u32 s6, s6, s20
	s_addc_u32 s7, s7, 0
	v_mfma_f32_16x16x32_f16 v[112:115], v[148:151], v[164:167], v[112:115]
	v_mfma_f32_16x16x32_f16 v[116:119], v[148:151], v[168:171], v[116:119]
	s_waitcnt lgkmcnt(9)
	v_mfma_f32_16x16x32_f16 v[120:123], v[152:155], v[156:159], v[120:123]
	v_mfma_f32_16x16x32_f16 v[124:127], v[152:155], v[160:163], v[124:127]
	v_mfma_f32_16x16x32_f16 v[128:131], v[152:155], v[164:167], v[128:131]
	v_mfma_f32_16x16x32_f16 v[132:135], v[152:155], v[168:171], v[132:135]
	s_waitcnt vmcnt(7) lgkmcnt(0)
	s_barrier
	s_waitcnt lgkmcnt(6)
	ds_read_b128 v[136:139], v19
	ds_read_b128 v[156:159], v21
	ds_read_b128 v[160:163], v21 offset:2048
	ds_read_b128 v[164:167], v21 offset:4096
	ds_read_b128 v[168:171], v21 offset:6144
	ds_read_b128 v[140:143], v19 offset:2048
	ds_read_b128 v[144:147], v19 offset:4096
	ds_read_b128 v[148:151], v19 offset:6144
	ds_read_b128 v[152:155], v19 offset:8192
	v_mfma_f32_16x16x32_f16 v[56:59], v[172:175], v[192:195], v[56:59]
	s_add_u32 m0, s28, 0xd000
	s_nop 0
	global_load_lds_dwordx4 v10, s[4:5]
	s_waitcnt lgkmcnt(15)
	v_mfma_f32_16x16x32_f16 v[60:63], v[172:175], v[196:199], v[60:63]
	s_waitcnt lgkmcnt(14)
	v_mfma_f32_16x16x32_f16 v[64:67], v[172:175], v[200:203], v[64:67]
	s_waitcnt lgkmcnt(13)
	v_mfma_f32_16x16x32_f16 v[68:71], v[172:175], v[204:207], v[68:71]
	s_waitcnt lgkmcnt(12)
	v_mfma_f32_16x16x32_f16 v[72:75], v[176:179], v[192:195], v[72:75]
	v_mfma_f32_16x16x32_f16 v[76:79], v[176:179], v[196:199], v[76:79]
	s_add_u32 m0, s28, 0xf000
	s_nop 0
	global_load_lds_dwordx4 v11, s[4:5]
	v_mfma_f32_16x16x32_f16 v[80:83], v[176:179], v[200:203], v[80:83]
	v_mfma_f32_16x16x32_f16 v[84:87], v[176:179], v[204:207], v[84:87]
	s_waitcnt lgkmcnt(11)
	v_mfma_f32_16x16x32_f16 v[88:91], v[180:183], v[192:195], v[88:91]
	v_mfma_f32_16x16x32_f16 v[92:95], v[180:183], v[196:199], v[92:95]
	v_mfma_f32_16x16x32_f16 v[96:99], v[180:183], v[200:203], v[96:99]
	s_add_u32 m0, s28, 0x11000
	s_nop 0
	global_load_lds_dwordx4 v12, s[4:5]
	v_mfma_f32_16x16x32_f16 v[100:103], v[180:183], v[204:207], v[100:103]
	s_waitcnt lgkmcnt(10)
	v_mfma_f32_16x16x32_f16 v[104:107], v[184:187], v[192:195], v[104:107]
	v_mfma_f32_16x16x32_f16 v[108:111], v[184:187], v[196:199], v[108:111]
	v_mfma_f32_16x16x32_f16 v[112:115], v[184:187], v[200:203], v[112:115]
	v_mfma_f32_16x16x32_f16 v[116:119], v[184:187], v[204:207], v[116:119]
	s_add_u32 m0, s28, 0x13000
	s_nop 0
	global_load_lds_dwordx4 v13, s[4:5]
	s_waitcnt lgkmcnt(9)
	v_mfma_f32_16x16x32_f16 v[120:123], v[188:191], v[192:195], v[120:123]
	v_mfma_f32_16x16x32_f16 v[124:127], v[188:191], v[196:199], v[124:127]
	v_mfma_f32_16x16x32_f16 v[128:131], v[188:191], v[200:203], v[128:131]
	v_mfma_f32_16x16x32_f16 v[132:135], v[188:191], v[204:207], v[132:135]
	s_waitcnt lgkmcnt(6)
	ds_read_b128 v[172:175], v20
	ds_read_b128 v[192:195], v22
	ds_read_b128 v[196:199], v22 offset:2048
	ds_read_b128 v[200:203], v22 offset:4096
	ds_read_b128 v[204:207], v22 offset:6144
	ds_read_b128 v[176:179], v20 offset:2048
	ds_read_b128 v[180:183], v20 offset:4096
	ds_read_b128 v[184:187], v20 offset:6144
	ds_read_b128 v[188:191], v20 offset:8192
	v_mfma_f32_16x16x32_f16 v[56:59], v[136:139], v[156:159], v[56:59]
	s_add_u32 m0, s28, 0x15000
	s_nop 0
	global_load_lds_dwordx4 v14, s[4:5]
	s_add_u32 s4, s4, s20
	s_addc_u32 s5, s5, 0
	s_waitcnt lgkmcnt(15)
	v_mfma_f32_16x16x32_f16 v[60:63], v[136:139], v[160:163], v[60:63]
	s_waitcnt lgkmcnt(14)
	v_mfma_f32_16x16x32_f16 v[64:67], v[136:139], v[164:167], v[64:67]
	s_waitcnt lgkmcnt(13)
	v_mfma_f32_16x16x32_f16 v[68:71], v[136:139], v[168:171], v[68:71]
	s_waitcnt lgkmcnt(12)
	v_mfma_f32_16x16x32_f16 v[72:75], v[140:143], v[156:159], v[72:75]
	v_mfma_f32_16x16x32_f16 v[76:79], v[140:143], v[160:163], v[76:79]
	v_mfma_f32_16x16x32_f16 v[80:83], v[140:143], v[164:167], v[80:83]
	s_add_u32 m0, s28, 0x16000
	s_nop 0
	global_load_lds_dwordx4 v10, s[6:7]
	v_mfma_f32_16x16x32_f16 v[84:87], v[140:143], v[168:171], v[84:87]
	s_waitcnt lgkmcnt(11)
	v_mfma_f32_16x16x32_f16 v[88:91], v[144:147], v[156:159], v[88:91]
	v_mfma_f32_16x16x32_f16 v[92:95], v[144:147], v[160:163], v[92:95]
	v_mfma_f32_16x16x32_f16 v[96:99], v[144:147], v[164:167], v[96:99]
	v_mfma_f32_16x16x32_f16 v[100:103], v[144:147], v[168:171], v[100:103]
	s_waitcnt lgkmcnt(10)
	v_mfma_f32_16x16x32_f16 v[104:107], v[148:151], v[156:159], v[104:107]
	v_mfma_f32_16x16x32_f16 v[108:111], v[148:151], v[160:163], v[108:111]
	s_add_u32 m0, s28, 0x18000
	s_nop 0
	global_load_lds_dwordx4 v11, s[6:7]
	s_add_u32 s6, s6, s20
	s_addc_u32 s7, s7, 0
	v_mfma_f32_16x16x32_f16 v[112:115], v[148:151], v[164:167], v[112:115]
	v_mfma_f32_16x16x32_f16 v[116:119], v[148:151], v[168:171], v[116:119]
	s_waitcnt lgkmcnt(9)
	v_mfma_f32_16x16x32_f16 v[120:123], v[152:155], v[156:159], v[120:123]
	v_mfma_f32_16x16x32_f16 v[124:127], v[152:155], v[160:163], v[124:127]
	v_mfma_f32_16x16x32_f16 v[128:131], v[152:155], v[164:167], v[128:131]
	v_mfma_f32_16x16x32_f16 v[132:135], v[152:155], v[168:171], v[132:135]
	s_waitcnt vmcnt(7) lgkmcnt(0)
	s_barrier
	s_waitcnt lgkmcnt(6)
	ds_read_b128 v[136:139], v15
	ds_read_b128 v[156:159], v17
	ds_read_b128 v[160:163], v17 offset:2048
	ds_read_b128 v[164:167], v17 offset:4096
	ds_read_b128 v[168:171], v17 offset:6144
	ds_read_b128 v[140:143], v15 offset:2048
	ds_read_b128 v[144:147], v15 offset:4096
	ds_read_b128 v[148:151], v15 offset:6144
	ds_read_b128 v[152:155], v15 offset:8192
	v_mfma_f32_16x16x32_f16 v[56:59], v[172:175], v[192:195], v[56:59]
	s_add_u32 m0, s28, 0x1a000
	s_nop 0
	global_load_lds_dwordx4 v10, s[4:5]
	s_waitcnt lgkmcnt(15)
	v_mfma_f32_16x16x32_f16 v[60:63], v[172:175], v[196:199], v[60:63]
	s_waitcnt lgkmcnt(14)
	v_mfma_f32_16x16x32_f16 v[64:67], v[172:175], v[200:203], v[64:67]
	s_waitcnt lgkmcnt(13)
	v_mfma_f32_16x16x32_f16 v[68:71], v[172:175], v[204:207], v[68:71]
	s_waitcnt lgkmcnt(12)
	v_mfma_f32_16x16x32_f16 v[72:75], v[176:179], v[192:195], v[72:75]
	v_mfma_f32_16x16x32_f16 v[76:79], v[176:179], v[196:199], v[76:79]
	s_add_u32 m0, s28, 0x1c000
	s_nop 0
	global_load_lds_dwordx4 v11, s[4:5]
	v_mfma_f32_16x16x32_f16 v[80:83], v[176:179], v[200:203], v[80:83]
	v_mfma_f32_16x16x32_f16 v[84:87], v[176:179], v[204:207], v[84:87]
	s_waitcnt lgkmcnt(11)
	v_mfma_f32_16x16x32_f16 v[88:91], v[180:183], v[192:195], v[88:91]
	v_mfma_f32_16x16x32_f16 v[92:95], v[180:183], v[196:199], v[92:95]
	v_mfma_f32_16x16x32_f16 v[96:99], v[180:183], v[200:203], v[96:99]
	s_add_u32 m0, s28, 0x1e000
	s_nop 0
	global_load_lds_dwordx4 v12, s[4:5]
	v_mfma_f32_16x16x32_f16 v[100:103], v[180:183], v[204:207], v[100:103]
	s_waitcnt lgkmcnt(10)
	v_mfma_f32_16x16x32_f16 v[104:107], v[184:187], v[192:195], v[104:107]
	v_mfma_f32_16x16x32_f16 v[108:111], v[184:187], v[196:199], v[108:111]
	v_mfma_f32_16x16x32_f16 v[112:115], v[184:187], v[200:203], v[112:115]
	v_mfma_f32_16x16x32_f16 v[116:119], v[184:187], v[204:207], v[116:119]
	s_add_u32 m0, s28, 0x20000
	s_nop 0
	global_load_lds_dwordx4 v13, s[4:5]
	s_waitcnt lgkmcnt(9)
	v_mfma_f32_16x16x32_f16 v[120:123], v[188:191], v[192:195], v[120:123]
	v_mfma_f32_16x16x32_f16 v[124:127], v[188:191], v[196:199], v[124:127]
	v_mfma_f32_16x16x32_f16 v[128:131], v[188:191], v[200:203], v[128:131]
	v_mfma_f32_16x16x32_f16 v[132:135], v[188:191], v[204:207], v[132:135]
	s_waitcnt lgkmcnt(6)
	ds_read_b128 v[172:175], v16
	ds_read_b128 v[192:195], v18
	ds_read_b128 v[196:199], v18 offset:2048
	ds_read_b128 v[200:203], v18 offset:4096
	ds_read_b128 v[204:207], v18 offset:6144
	ds_read_b128 v[176:179], v16 offset:2048
	ds_read_b128 v[180:183], v16 offset:4096
	ds_read_b128 v[184:187], v16 offset:6144
	ds_read_b128 v[188:191], v16 offset:8192
	v_mfma_f32_16x16x32_f16 v[56:59], v[136:139], v[156:159], v[56:59]
	s_add_u32 m0, s28, 0x22000
	s_nop 0
	global_load_lds_dwordx4 v14, s[4:5]
	s_add_u32 s4, s4, s20
	s_addc_u32 s5, s5, 0
	s_waitcnt lgkmcnt(15)
	v_mfma_f32_16x16x32_f16 v[60:63], v[136:139], v[160:163], v[60:63]
	s_waitcnt lgkmcnt(14)
	v_mfma_f32_16x16x32_f16 v[64:67], v[136:139], v[164:167], v[64:67]
	s_waitcnt lgkmcnt(13)
	v_mfma_f32_16x16x32_f16 v[68:71], v[136:139], v[168:171], v[68:71]
	s_waitcnt lgkmcnt(12)
	v_mfma_f32_16x16x32_f16 v[72:75], v[140:143], v[156:159], v[72:75]
	v_mfma_f32_16x16x32_f16 v[76:79], v[140:143], v[160:163], v[76:79]
	v_mfma_f32_16x16x32_f16 v[80:83], v[140:143], v[164:167], v[80:83]
	s_add_u32 m0, s28, 0x23000
	s_nop 0
	global_load_lds_dwordx4 v10, s[6:7]
	v_mfma_f32_16x16x32_f16 v[84:87], v[140:143], v[168:171], v[84:87]
	s_waitcnt lgkmcnt(11)
	v_mfma_f32_16x16x32_f16 v[88:91], v[144:147], v[156:159], v[88:91]
	v_mfma_f32_16x16x32_f16 v[92:95], v[144:147], v[160:163], v[92:95]
	v_mfma_f32_16x16x32_f16 v[96:99], v[144:147], v[164:167], v[96:99]
	v_mfma_f32_16x16x32_f16 v[100:103], v[144:147], v[168:171], v[100:103]
	s_waitcnt lgkmcnt(10)
	v_mfma_f32_16x16x32_f16 v[104:107], v[148:151], v[156:159], v[104:107]
	v_mfma_f32_16x16x32_f16 v[108:111], v[148:151], v[160:163], v[108:111]
	s_add_u32 m0, s28, 0x25000
	s_nop 0
	global_load_lds_dwordx4 v11, s[6:7]
	s_add_u32 s6, s6, s20
	s_addc_u32 s7, s7, 0
	v_mfma_f32_16x16x32_f16 v[112:115], v[148:151], v[164:167], v[112:115]
	v_mfma_f32_16x16x32_f16 v[116:119], v[148:151], v[168:171], v[116:119]
	s_waitcnt lgkmcnt(9)
	v_mfma_f32_16x16x32_f16 v[120:123], v[152:155], v[156:159], v[120:123]
	v_mfma_f32_16x16x32_f16 v[124:127], v[152:155], v[160:163], v[124:127]
	v_mfma_f32_16x16x32_f16 v[128:131], v[152:155], v[164:167], v[128:131]
	v_mfma_f32_16x16x32_f16 v[132:135], v[152:155], v[168:171], v[132:135]
	s_waitcnt vmcnt(7) lgkmcnt(0)
	s_barrier
	s_waitcnt lgkmcnt(6)
	ds_read_b128 v[136:139], v15 offset:53248
	ds_read_b128 v[156:159], v17 offset:53248
	ds_read_b128 v[160:163], v17 offset:55296
	ds_read_b128 v[164:167], v17 offset:57344
	ds_read_b128 v[168:171], v17 offset:59392
	ds_read_b128 v[140:143], v15 offset:55296
	ds_read_b128 v[144:147], v15 offset:57344
	ds_read_b128 v[148:151], v15 offset:59392
	ds_read_b128 v[152:155], v15 offset:61440
	v_mfma_f32_16x16x32_f16 v[56:59], v[172:175], v[192:195], v[56:59]
	s_add_u32 m0, s28, 0x0
	s_nop 0
	global_load_lds_dwordx4 v10, s[4:5]
	s_waitcnt lgkmcnt(15)
	v_mfma_f32_16x16x32_f16 v[60:63], v[172:175], v[196:199], v[60:63]
	s_waitcnt lgkmcnt(14)
	v_mfma_f32_16x16x32_f16 v[64:67], v[172:175], v[200:203], v[64:67]
	s_waitcnt lgkmcnt(13)
	v_mfma_f32_16x16x32_f16 v[68:71], v[172:175], v[204:207], v[68:71]
	s_waitcnt lgkmcnt(12)
	v_mfma_f32_16x16x32_f16 v[72:75], v[176:179], v[192:195], v[72:75]
	v_mfma_f32_16x16x32_f16 v[76:79], v[176:179], v[196:199], v[76:79]
	s_add_u32 m0, s28, 0x2000
	s_nop 0
	global_load_lds_dwordx4 v11, s[4:5]
	v_mfma_f32_16x16x32_f16 v[80:83], v[176:179], v[200:203], v[80:83]
	v_mfma_f32_16x16x32_f16 v[84:87], v[176:179], v[204:207], v[84:87]
	s_waitcnt lgkmcnt(11)
	v_mfma_f32_16x16x32_f16 v[88:91], v[180:183], v[192:195], v[88:91]
	v_mfma_f32_16x16x32_f16 v[92:95], v[180:183], v[196:199], v[92:95]
	v_mfma_f32_16x16x32_f16 v[96:99], v[180:183], v[200:203], v[96:99]
	s_add_u32 m0, s28, 0x4000
	s_nop 0
	global_load_lds_dwordx4 v12, s[4:5]
	v_mfma_f32_16x16x32_f16 v[100:103], v[180:183], v[204:207], v[100:103]
	s_waitcnt lgkmcnt(10)
	v_mfma_f32_16x16x32_f16 v[104:107], v[184:187], v[192:195], v[104:107]
	v_mfma_f32_16x16x32_f16 v[108:111], v[184:187], v[196:199], v[108:111]
	v_mfma_f32_16x16x32_f16 v[112:115], v[184:187], v[200:203], v[112:115]
	v_mfma_f32_16x16x32_f16 v[116:119], v[184:187], v[204:207], v[116:119]
	s_add_u32 m0, s28, 0x6000
	s_nop 0
	global_load_lds_dwordx4 v13, s[4:5]
	s_waitcnt lgkmcnt(9)
	v_mfma_f32_16x16x32_f16 v[120:123], v[188:191], v[192:195], v[120:123]
	v_mfma_f32_16x16x32_f16 v[124:127], v[188:191], v[196:199], v[124:127]
	v_mfma_f32_16x16x32_f16 v[128:131], v[188:191], v[200:203], v[128:131]
	v_mfma_f32_16x16x32_f16 v[132:135], v[188:191], v[204:207], v[132:135]
	s_waitcnt lgkmcnt(6)
	ds_read_b128 v[172:175], v16 offset:53248
	ds_read_b128 v[192:195], v18 offset:53248
	ds_read_b128 v[196:199], v18 offset:55296
	ds_read_b128 v[200:203], v18 offset:57344
	ds_read_b128 v[204:207], v18 offset:59392
	ds_read_b128 v[176:179], v16 offset:55296
	ds_read_b128 v[180:183], v16 offset:57344
	ds_read_b128 v[184:187], v16 offset:59392
	ds_read_b128 v[188:191], v16 offset:61440
	v_mfma_f32_16x16x32_f16 v[56:59], v[136:139], v[156:159], v[56:59]
	s_add_u32 m0, s28, 0x8000
	s_nop 0
	global_load_lds_dwordx4 v14, s[4:5]
	s_add_u32 s4, s4, s20
	s_addc_u32 s5, s5, 0
	s_waitcnt lgkmcnt(15)
	v_mfma_f32_16x16x32_f16 v[60:63], v[136:139], v[160:163], v[60:63]
	s_waitcnt lgkmcnt(14)
	v_mfma_f32_16x16x32_f16 v[64:67], v[136:139], v[164:167], v[64:67]
	s_waitcnt lgkmcnt(13)
	v_mfma_f32_16x16x32_f16 v[68:71], v[136:139], v[168:171], v[68:71]
	s_waitcnt lgkmcnt(12)
	v_mfma_f32_16x16x32_f16 v[72:75], v[140:143], v[156:159], v[72:75]
	v_mfma_f32_16x16x32_f16 v[76:79], v[140:143], v[160:163], v[76:79]
	v_mfma_f32_16x16x32_f16 v[80:83], v[140:143], v[164:167], v[80:83]
	s_add_u32 m0, s28, 0x9000
	s_nop 0
	global_load_lds_dwordx4 v10, s[6:7]
	v_mfma_f32_16x16x32_f16 v[84:87], v[140:143], v[168:171], v[84:87]
	s_waitcnt lgkmcnt(11)
	v_mfma_f32_16x16x32_f16 v[88:91], v[144:147], v[156:159], v[88:91]
	v_mfma_f32_16x16x32_f16 v[92:95], v[144:147], v[160:163], v[92:95]
	v_mfma_f32_16x16x32_f16 v[96:99], v[144:147], v[164:167], v[96:99]
	v_mfma_f32_16x16x32_f16 v[100:103], v[144:147], v[168:171], v[100:103]
	s_waitcnt lgkmcnt(10)
	v_mfma_f32_16x16x32_f16 v[104:107], v[148:151], v[156:159], v[104:107]
	v_mfma_f32_16x16x32_f16 v[108:111], v[148:151], v[160:163], v[108:111]
	s_add_u32 m0, s28, 0xb000
	s_nop 0
	global_load_lds_dwordx4 v11, s[6:7]
	s_add_u32 s6, s6, s20
	s_addc_u32 s7, s7, 0
	v_mfma_f32_16x16x32_f16 v[112:115], v[148:151], v[164:167], v[112:115]
	v_mfma_f32_16x16x32_f16 v[116:119], v[148:151], v[168:171], v[116:119]
	s_waitcnt lgkmcnt(9)
	v_mfma_f32_16x16x32_f16 v[120:123], v[152:155], v[156:159], v[120:123]
	v_mfma_f32_16x16x32_f16 v[124:127], v[152:155], v[160:163], v[124:127]
	v_mfma_f32_16x16x32_f16 v[128:131], v[152:155], v[164:167], v[128:131]
	v_mfma_f32_16x16x32_f16 v[132:135], v[152:155], v[168:171], v[132:135]
	s_waitcnt vmcnt(7) lgkmcnt(0)
	s_barrier
	s_waitcnt lgkmcnt(6)
	ds_read_b128 v[136:139], v19
	ds_read_b128 v[156:159], v21
	ds_read_b128 v[160:163], v21 offset:2048
	ds_read_b128 v[164:167], v21 offset:4096
	ds_read_b128 v[168:171], v21 offset:6144
	ds_read_b128 v[140:143], v19 offset:2048
	ds_read_b128 v[144:147], v19 offset:4096
	ds_read_b128 v[148:151], v19 offset:6144
	ds_read_b128 v[152:155], v19 offset:8192
	v_mfma_f32_16x16x32_f16 v[56:59], v[172:175], v[192:195], v[56:59]
	s_add_u32 m0, s28, 0xd000
	s_nop 0
	global_load_lds_dwordx4 v10, s[4:5]
	s_waitcnt lgkmcnt(15)
	v_mfma_f32_16x16x32_f16 v[60:63], v[172:175], v[196:199], v[60:63]
	s_waitcnt lgkmcnt(14)
	v_mfma_f32_16x16x32_f16 v[64:67], v[172:175], v[200:203], v[64:67]
	s_waitcnt lgkmcnt(13)
	v_mfma_f32_16x16x32_f16 v[68:71], v[172:175], v[204:207], v[68:71]
	s_waitcnt lgkmcnt(12)
	v_mfma_f32_16x16x32_f16 v[72:75], v[176:179], v[192:195], v[72:75]
	v_mfma_f32_16x16x32_f16 v[76:79], v[176:179], v[196:199], v[76:79]
	s_add_u32 m0, s28, 0xf000
	s_nop 0
	global_load_lds_dwordx4 v11, s[4:5]
	v_mfma_f32_16x16x32_f16 v[80:83], v[176:179], v[200:203], v[80:83]
	v_mfma_f32_16x16x32_f16 v[84:87], v[176:179], v[204:207], v[84:87]
	s_waitcnt lgkmcnt(11)
	v_mfma_f32_16x16x32_f16 v[88:91], v[180:183], v[192:195], v[88:91]
	v_mfma_f32_16x16x32_f16 v[92:95], v[180:183], v[196:199], v[92:95]
	v_mfma_f32_16x16x32_f16 v[96:99], v[180:183], v[200:203], v[96:99]
	s_add_u32 m0, s28, 0x11000
	s_nop 0
	global_load_lds_dwordx4 v12, s[4:5]
	v_mfma_f32_16x16x32_f16 v[100:103], v[180:183], v[204:207], v[100:103]
	s_waitcnt lgkmcnt(10)
	v_mfma_f32_16x16x32_f16 v[104:107], v[184:187], v[192:195], v[104:107]
	v_mfma_f32_16x16x32_f16 v[108:111], v[184:187], v[196:199], v[108:111]
	v_mfma_f32_16x16x32_f16 v[112:115], v[184:187], v[200:203], v[112:115]
	v_mfma_f32_16x16x32_f16 v[116:119], v[184:187], v[204:207], v[116:119]
	s_add_u32 m0, s28, 0x13000
	s_nop 0
	global_load_lds_dwordx4 v13, s[4:5]
	s_waitcnt lgkmcnt(9)
	v_mfma_f32_16x16x32_f16 v[120:123], v[188:191], v[192:195], v[120:123]
	v_mfma_f32_16x16x32_f16 v[124:127], v[188:191], v[196:199], v[124:127]
	v_mfma_f32_16x16x32_f16 v[128:131], v[188:191], v[200:203], v[128:131]
	v_mfma_f32_16x16x32_f16 v[132:135], v[188:191], v[204:207], v[132:135]
	s_waitcnt lgkmcnt(6)
	ds_read_b128 v[172:175], v20
	ds_read_b128 v[192:195], v22
	ds_read_b128 v[196:199], v22 offset:2048
	ds_read_b128 v[200:203], v22 offset:4096
	ds_read_b128 v[204:207], v22 offset:6144
	ds_read_b128 v[176:179], v20 offset:2048
	ds_read_b128 v[180:183], v20 offset:4096
	ds_read_b128 v[184:187], v20 offset:6144
	ds_read_b128 v[188:191], v20 offset:8192
	v_mfma_f32_16x16x32_f16 v[56:59], v[136:139], v[156:159], v[56:59]
	s_add_u32 m0, s28, 0x15000
	s_nop 0
	global_load_lds_dwordx4 v14, s[4:5]
	s_add_u32 s4, s4, s20
	s_addc_u32 s5, s5, 0
	s_waitcnt lgkmcnt(15)
	v_mfma_f32_16x16x32_f16 v[60:63], v[136:139], v[160:163], v[60:63]
	s_waitcnt lgkmcnt(14)
	v_mfma_f32_16x16x32_f16 v[64:67], v[136:139], v[164:167], v[64:67]
	s_waitcnt lgkmcnt(13)
	v_mfma_f32_16x16x32_f16 v[68:71], v[136:139], v[168:171], v[68:71]
	s_waitcnt lgkmcnt(12)
	v_mfma_f32_16x16x32_f16 v[72:75], v[140:143], v[156:159], v[72:75]
	v_mfma_f32_16x16x32_f16 v[76:79], v[140:143], v[160:163], v[76:79]
	v_mfma_f32_16x16x32_f16 v[80:83], v[140:143], v[164:167], v[80:83]
	s_add_u32 m0, s28, 0x16000
	s_nop 0
	global_load_lds_dwordx4 v10, s[6:7]
	v_mfma_f32_16x16x32_f16 v[84:87], v[140:143], v[168:171], v[84:87]
	s_waitcnt lgkmcnt(11)
	v_mfma_f32_16x16x32_f16 v[88:91], v[144:147], v[156:159], v[88:91]
	v_mfma_f32_16x16x32_f16 v[92:95], v[144:147], v[160:163], v[92:95]
	v_mfma_f32_16x16x32_f16 v[96:99], v[144:147], v[164:167], v[96:99]
	v_mfma_f32_16x16x32_f16 v[100:103], v[144:147], v[168:171], v[100:103]
	s_waitcnt lgkmcnt(10)
	v_mfma_f32_16x16x32_f16 v[104:107], v[148:151], v[156:159], v[104:107]
	v_mfma_f32_16x16x32_f16 v[108:111], v[148:151], v[160:163], v[108:111]
	s_add_u32 m0, s28, 0x18000
	s_nop 0
	global_load_lds_dwordx4 v11, s[6:7]
	s_add_u32 s6, s6, s20
	s_addc_u32 s7, s7, 0
	v_mfma_f32_16x16x32_f16 v[112:115], v[148:151], v[164:167], v[112:115]
	v_mfma_f32_16x16x32_f16 v[116:119], v[148:151], v[168:171], v[116:119]
	s_waitcnt lgkmcnt(9)
	v_mfma_f32_16x16x32_f16 v[120:123], v[152:155], v[156:159], v[120:123]
	v_mfma_f32_16x16x32_f16 v[124:127], v[152:155], v[160:163], v[124:127]
	v_mfma_f32_16x16x32_f16 v[128:131], v[152:155], v[164:167], v[128:131]
	v_mfma_f32_16x16x32_f16 v[132:135], v[152:155], v[168:171], v[132:135]
	s_waitcnt vmcnt(7) lgkmcnt(0)
	s_barrier
	s_waitcnt lgkmcnt(6)
	ds_read_b128 v[136:139], v15
	ds_read_b128 v[156:159], v17
	ds_read_b128 v[160:163], v17 offset:2048
	ds_read_b128 v[164:167], v17 offset:4096
	ds_read_b128 v[168:171], v17 offset:6144
	ds_read_b128 v[140:143], v15 offset:2048
	ds_read_b128 v[144:147], v15 offset:4096
	ds_read_b128 v[148:151], v15 offset:6144
	ds_read_b128 v[152:155], v15 offset:8192
	v_mfma_f32_16x16x32_f16 v[56:59], v[172:175], v[192:195], v[56:59]
	s_add_u32 m0, s28, 0x1a000
	s_nop 0
	global_load_lds_dwordx4 v10, s[4:5]
	s_waitcnt lgkmcnt(15)
	v_mfma_f32_16x16x32_f16 v[60:63], v[172:175], v[196:199], v[60:63]
	s_waitcnt lgkmcnt(14)
	v_mfma_f32_16x16x32_f16 v[64:67], v[172:175], v[200:203], v[64:67]
	s_waitcnt lgkmcnt(13)
	v_mfma_f32_16x16x32_f16 v[68:71], v[172:175], v[204:207], v[68:71]
	s_waitcnt lgkmcnt(12)
	v_mfma_f32_16x16x32_f16 v[72:75], v[176:179], v[192:195], v[72:75]
	v_mfma_f32_16x16x32_f16 v[76:79], v[176:179], v[196:199], v[76:79]
	s_add_u32 m0, s28, 0x1c000
	s_nop 0
	global_load_lds_dwordx4 v11, s[4:5]
	v_mfma_f32_16x16x32_f16 v[80:83], v[176:179], v[200:203], v[80:83]
	v_mfma_f32_16x16x32_f16 v[84:87], v[176:179], v[204:207], v[84:87]
	s_waitcnt lgkmcnt(11)
	v_mfma_f32_16x16x32_f16 v[88:91], v[180:183], v[192:195], v[88:91]
	v_mfma_f32_16x16x32_f16 v[92:95], v[180:183], v[196:199], v[92:95]
	v_mfma_f32_16x16x32_f16 v[96:99], v[180:183], v[200:203], v[96:99]
	s_add_u32 m0, s28, 0x1e000
	s_nop 0
	global_load_lds_dwordx4 v12, s[4:5]
	v_mfma_f32_16x16x32_f16 v[100:103], v[180:183], v[204:207], v[100:103]
	s_waitcnt lgkmcnt(10)
	v_mfma_f32_16x16x32_f16 v[104:107], v[184:187], v[192:195], v[104:107]
	v_mfma_f32_16x16x32_f16 v[108:111], v[184:187], v[196:199], v[108:111]
	v_mfma_f32_16x16x32_f16 v[112:115], v[184:187], v[200:203], v[112:115]
	v_mfma_f32_16x16x32_f16 v[116:119], v[184:187], v[204:207], v[116:119]
	s_add_u32 m0, s28, 0x20000
	s_nop 0
	global_load_lds_dwordx4 v13, s[4:5]
	s_waitcnt lgkmcnt(9)
	v_mfma_f32_16x16x32_f16 v[120:123], v[188:191], v[192:195], v[120:123]
	v_mfma_f32_16x16x32_f16 v[124:127], v[188:191], v[196:199], v[124:127]
	v_mfma_f32_16x16x32_f16 v[128:131], v[188:191], v[200:203], v[128:131]
	v_mfma_f32_16x16x32_f16 v[132:135], v[188:191], v[204:207], v[132:135]
	s_waitcnt lgkmcnt(6)
	ds_read_b128 v[172:175], v16
	ds_read_b128 v[192:195], v18
	ds_read_b128 v[196:199], v18 offset:2048
	ds_read_b128 v[200:203], v18 offset:4096
	ds_read_b128 v[204:207], v18 offset:6144
	ds_read_b128 v[176:179], v16 offset:2048
	ds_read_b128 v[180:183], v16 offset:4096
	ds_read_b128 v[184:187], v16 offset:6144
	ds_read_b128 v[188:191], v16 offset:8192
	v_mfma_f32_16x16x32_f16 v[56:59], v[136:139], v[156:159], v[56:59]
	s_add_u32 m0, s28, 0x22000
	s_nop 0
	global_load_lds_dwordx4 v14, s[4:5]
	s_add_u32 s4, s4, s20
	s_addc_u32 s5, s5, 0
	s_waitcnt lgkmcnt(15)
	v_mfma_f32_16x16x32_f16 v[60:63], v[136:139], v[160:163], v[60:63]
	s_waitcnt lgkmcnt(14)
	v_mfma_f32_16x16x32_f16 v[64:67], v[136:139], v[164:167], v[64:67]
	s_waitcnt lgkmcnt(13)
	v_mfma_f32_16x16x32_f16 v[68:71], v[136:139], v[168:171], v[68:71]
	s_waitcnt lgkmcnt(12)
	v_mfma_f32_16x16x32_f16 v[72:75], v[140:143], v[156:159], v[72:75]
	v_mfma_f32_16x16x32_f16 v[76:79], v[140:143], v[160:163], v[76:79]
	v_mfma_f32_16x16x32_f16 v[80:83], v[140:143], v[164:167], v[80:83]
	s_add_u32 m0, s28, 0x23000
	s_nop 0
	global_load_lds_dwordx4 v10, s[6:7]
	v_mfma_f32_16x16x32_f16 v[84:87], v[140:143], v[168:171], v[84:87]
	s_waitcnt lgkmcnt(11)
	v_mfma_f32_16x16x32_f16 v[88:91], v[144:147], v[156:159], v[88:91]
	v_mfma_f32_16x16x32_f16 v[92:95], v[144:147], v[160:163], v[92:95]
	v_mfma_f32_16x16x32_f16 v[96:99], v[144:147], v[164:167], v[96:99]
	v_mfma_f32_16x16x32_f16 v[100:103], v[144:147], v[168:171], v[100:103]
	s_waitcnt lgkmcnt(10)
	v_mfma_f32_16x16x32_f16 v[104:107], v[148:151], v[156:159], v[104:107]
	v_mfma_f32_16x16x32_f16 v[108:111], v[148:151], v[160:163], v[108:111]
	s_add_u32 m0, s28, 0x25000
	s_nop 0
	global_load_lds_dwordx4 v11, s[6:7]
	s_add_u32 s6, s6, s20
	s_addc_u32 s7, s7, 0
	v_mfma_f32_16x16x32_f16 v[112:115], v[148:151], v[164:167], v[112:115]
	v_mfma_f32_16x16x32_f16 v[116:119], v[148:151], v[168:171], v[116:119]
	s_waitcnt lgkmcnt(9)
	v_mfma_f32_16x16x32_f16 v[120:123], v[152:155], v[156:159], v[120:123]
	v_mfma_f32_16x16x32_f16 v[124:127], v[152:155], v[160:163], v[124:127]
	v_mfma_f32_16x16x32_f16 v[128:131], v[152:155], v[164:167], v[128:131]
	v_mfma_f32_16x16x32_f16 v[132:135], v[152:155], v[168:171], v[132:135]
	s_waitcnt vmcnt(7) lgkmcnt(0)
	s_barrier
	s_waitcnt lgkmcnt(6)
	ds_read_b128 v[136:139], v15 offset:53248
	ds_read_b128 v[156:159], v17 offset:53248
	ds_read_b128 v[160:163], v17 offset:55296
	ds_read_b128 v[164:167], v17 offset:57344
	ds_read_b128 v[168:171], v17 offset:59392
	ds_read_b128 v[140:143], v15 offset:55296
	ds_read_b128 v[144:147], v15 offset:57344
	ds_read_b128 v[148:151], v15 offset:59392
	ds_read_b128 v[152:155], v15 offset:61440
	v_mfma_f32_16x16x32_f16 v[56:59], v[172:175], v[192:195], v[56:59]
	s_add_u32 m0, s28, 0x0
	s_nop 0
	global_load_lds_dwordx4 v10, s[4:5]
	s_waitcnt lgkmcnt(15)
	v_mfma_f32_16x16x32_f16 v[60:63], v[172:175], v[196:199], v[60:63]
	s_waitcnt lgkmcnt(14)
	v_mfma_f32_16x16x32_f16 v[64:67], v[172:175], v[200:203], v[64:67]
	s_waitcnt lgkmcnt(13)
	v_mfma_f32_16x16x32_f16 v[68:71], v[172:175], v[204:207], v[68:71]
	s_waitcnt lgkmcnt(12)
	v_mfma_f32_16x16x32_f16 v[72:75], v[176:179], v[192:195], v[72:75]
	v_mfma_f32_16x16x32_f16 v[76:79], v[176:179], v[196:199], v[76:79]
	s_add_u32 m0, s28, 0x2000
	s_nop 0
	global_load_lds_dwordx4 v11, s[4:5]
	v_mfma_f32_16x16x32_f16 v[80:83], v[176:179], v[200:203], v[80:83]
	v_mfma_f32_16x16x32_f16 v[84:87], v[176:179], v[204:207], v[84:87]
	s_waitcnt lgkmcnt(11)
	v_mfma_f32_16x16x32_f16 v[88:91], v[180:183], v[192:195], v[88:91]
	v_mfma_f32_16x16x32_f16 v[92:95], v[180:183], v[196:199], v[92:95]
	v_mfma_f32_16x16x32_f16 v[96:99], v[180:183], v[200:203], v[96:99]
	s_add_u32 m0, s28, 0x4000
	s_nop 0
	global_load_lds_dwordx4 v12, s[4:5]
	v_mfma_f32_16x16x32_f16 v[100:103], v[180:183], v[204:207], v[100:103]
	s_waitcnt lgkmcnt(10)
	v_mfma_f32_16x16x32_f16 v[104:107], v[184:187], v[192:195], v[104:107]
	v_mfma_f32_16x16x32_f16 v[108:111], v[184:187], v[196:199], v[108:111]
	v_mfma_f32_16x16x32_f16 v[112:115], v[184:187], v[200:203], v[112:115]
	v_mfma_f32_16x16x32_f16 v[116:119], v[184:187], v[204:207], v[116:119]
	s_add_u32 m0, s28, 0x6000
	s_nop 0
	global_load_lds_dwordx4 v13, s[4:5]
	s_waitcnt lgkmcnt(9)
	v_mfma_f32_16x16x32_f16 v[120:123], v[188:191], v[192:195], v[120:123]
	v_mfma_f32_16x16x32_f16 v[124:127], v[188:191], v[196:199], v[124:127]
	v_mfma_f32_16x16x32_f16 v[128:131], v[188:191], v[200:203], v[128:131]
	v_mfma_f32_16x16x32_f16 v[132:135], v[188:191], v[204:207], v[132:135]
	s_waitcnt lgkmcnt(6)
	ds_read_b128 v[172:175], v16 offset:53248
	ds_read_b128 v[192:195], v18 offset:53248
	ds_read_b128 v[196:199], v18 offset:55296
	ds_read_b128 v[200:203], v18 offset:57344
	ds_read_b128 v[204:207], v18 offset:59392
	ds_read_b128 v[176:179], v16 offset:55296
	ds_read_b128 v[180:183], v16 offset:57344
	ds_read_b128 v[184:187], v16 offset:59392
	ds_read_b128 v[188:191], v16 offset:61440
	v_mfma_f32_16x16x32_f16 v[56:59], v[136:139], v[156:159], v[56:59]
	s_add_u32 m0, s28, 0x8000
	s_nop 0
	global_load_lds_dwordx4 v14, s[4:5]
	s_add_u32 s4, s4, s20
	s_addc_u32 s5, s5, 0
	s_waitcnt lgkmcnt(15)
	v_mfma_f32_16x16x32_f16 v[60:63], v[136:139], v[160:163], v[60:63]
	s_waitcnt lgkmcnt(14)
	v_mfma_f32_16x16x32_f16 v[64:67], v[136:139], v[164:167], v[64:67]
	s_waitcnt lgkmcnt(13)
	v_mfma_f32_16x16x32_f16 v[68:71], v[136:139], v[168:171], v[68:71]
	s_waitcnt lgkmcnt(12)
	v_mfma_f32_16x16x32_f16 v[72:75], v[140:143], v[156:159], v[72:75]
	v_mfma_f32_16x16x32_f16 v[76:79], v[140:143], v[160:163], v[76:79]
	v_mfma_f32_16x16x32_f16 v[80:83], v[140:143], v[164:167], v[80:83]
	s_add_u32 m0, s28, 0x9000
	s_nop 0
	global_load_lds_dwordx4 v10, s[6:7]
	v_mfma_f32_16x16x32_f16 v[84:87], v[140:143], v[168:171], v[84:87]
	s_waitcnt lgkmcnt(11)
	v_mfma_f32_16x16x32_f16 v[88:91], v[144:147], v[156:159], v[88:91]
	v_mfma_f32_16x16x32_f16 v[92:95], v[144:147], v[160:163], v[92:95]
	v_mfma_f32_16x16x32_f16 v[96:99], v[144:147], v[164:167], v[96:99]
	v_mfma_f32_16x16x32_f16 v[100:103], v[144:147], v[168:171], v[100:103]
	s_waitcnt lgkmcnt(10)
	v_mfma_f32_16x16x32_f16 v[104:107], v[148:151], v[156:159], v[104:107]
	v_mfma_f32_16x16x32_f16 v[108:111], v[148:151], v[160:163], v[108:111]
	s_add_u32 m0, s28, 0xb000
	s_nop 0
	global_load_lds_dwordx4 v11, s[6:7]
	s_add_u32 s6, s6, s20
	s_addc_u32 s7, s7, 0
	v_mfma_f32_16x16x32_f16 v[112:115], v[148:151], v[164:167], v[112:115]
	v_mfma_f32_16x16x32_f16 v[116:119], v[148:151], v[168:171], v[116:119]
	s_waitcnt lgkmcnt(9)
	v_mfma_f32_16x16x32_f16 v[120:123], v[152:155], v[156:159], v[120:123]
	v_mfma_f32_16x16x32_f16 v[124:127], v[152:155], v[160:163], v[124:127]
	v_mfma_f32_16x16x32_f16 v[128:131], v[152:155], v[164:167], v[128:131]
	v_mfma_f32_16x16x32_f16 v[132:135], v[152:155], v[168:171], v[132:135]
	s_waitcnt vmcnt(7) lgkmcnt(0)
	s_barrier
	s_waitcnt lgkmcnt(6)
	ds_read_b128 v[136:139], v19
	ds_read_b128 v[156:159], v21
	ds_read_b128 v[160:163], v21 offset:2048
	ds_read_b128 v[164:167], v21 offset:4096
	ds_read_b128 v[168:171], v21 offset:6144
	ds_read_b128 v[140:143], v19 offset:2048
	ds_read_b128 v[144:147], v19 offset:4096
	ds_read_b128 v[148:151], v19 offset:6144
	ds_read_b128 v[152:155], v19 offset:8192
	v_mfma_f32_16x16x32_f16 v[56:59], v[172:175], v[192:195], v[56:59]
	s_waitcnt lgkmcnt(15)
	v_mfma_f32_16x16x32_f16 v[60:63], v[172:175], v[196:199], v[60:63]
	s_waitcnt lgkmcnt(14)
	v_mfma_f32_16x16x32_f16 v[64:67], v[172:175], v[200:203], v[64:67]
	s_waitcnt lgkmcnt(13)
	v_mfma_f32_16x16x32_f16 v[68:71], v[172:175], v[204:207], v[68:71]
	s_waitcnt lgkmcnt(12)
	v_mfma_f32_16x16x32_f16 v[72:75], v[176:179], v[192:195], v[72:75]
	v_mfma_f32_16x16x32_f16 v[76:79], v[176:179], v[196:199], v[76:79]
	v_mfma_f32_16x16x32_f16 v[80:83], v[176:179], v[200:203], v[80:83]
	v_mfma_f32_16x16x32_f16 v[84:87], v[176:179], v[204:207], v[84:87]
	s_waitcnt lgkmcnt(11)
	v_mfma_f32_16x16x32_f16 v[88:91], v[180:183], v[192:195], v[88:91]
	v_mfma_f32_16x16x32_f16 v[92:95], v[180:183], v[196:199], v[92:95]
	v_mfma_f32_16x16x32_f16 v[96:99], v[180:183], v[200:203], v[96:99]
	v_mfma_f32_16x16x32_f16 v[100:103], v[180:183], v[204:207], v[100:103]
	s_waitcnt lgkmcnt(10)
	v_mfma_f32_16x16x32_f16 v[104:107], v[184:187], v[192:195], v[104:107]
	v_mfma_f32_16x16x32_f16 v[108:111], v[184:187], v[196:199], v[108:111]
	v_mfma_f32_16x16x32_f16 v[112:115], v[184:187], v[200:203], v[112:115]
	v_mfma_f32_16x16x32_f16 v[116:119], v[184:187], v[204:207], v[116:119]
	s_waitcnt lgkmcnt(9)
	v_mfma_f32_16x16x32_f16 v[120:123], v[188:191], v[192:195], v[120:123]
	v_mfma_f32_16x16x32_f16 v[124:127], v[188:191], v[196:199], v[124:127]
	v_mfma_f32_16x16x32_f16 v[128:131], v[188:191], v[200:203], v[128:131]
	v_mfma_f32_16x16x32_f16 v[132:135], v[188:191], v[204:207], v[132:135]
	s_waitcnt lgkmcnt(6)
	ds_read_b128 v[172:175], v20
	ds_read_b128 v[192:195], v22
	ds_read_b128 v[196:199], v22 offset:2048
	ds_read_b128 v[200:203], v22 offset:4096
	ds_read_b128 v[204:207], v22 offset:6144
	ds_read_b128 v[176:179], v20 offset:2048
	ds_read_b128 v[180:183], v20 offset:4096
	ds_read_b128 v[184:187], v20 offset:6144
	ds_read_b128 v[188:191], v20 offset:8192
	v_mfma_f32_16x16x32_f16 v[56:59], v[136:139], v[156:159], v[56:59]
	s_waitcnt lgkmcnt(15)
	v_mfma_f32_16x16x32_f16 v[60:63], v[136:139], v[160:163], v[60:63]
	s_waitcnt lgkmcnt(14)
	v_mfma_f32_16x16x32_f16 v[64:67], v[136:139], v[164:167], v[64:67]
	s_waitcnt lgkmcnt(13)
	v_mfma_f32_16x16x32_f16 v[68:71], v[136:139], v[168:171], v[68:71]
	s_waitcnt lgkmcnt(12)
	v_mfma_f32_16x16x32_f16 v[72:75], v[140:143], v[156:159], v[72:75]
	v_mfma_f32_16x16x32_f16 v[76:79], v[140:143], v[160:163], v[76:79]
	v_mfma_f32_16x16x32_f16 v[80:83], v[140:143], v[164:167], v[80:83]
	v_mfma_f32_16x16x32_f16 v[84:87], v[140:143], v[168:171], v[84:87]
	s_waitcnt lgkmcnt(11)
	v_mfma_f32_16x16x32_f16 v[88:91], v[144:147], v[156:159], v[88:91]
	v_mfma_f32_16x16x32_f16 v[92:95], v[144:147], v[160:163], v[92:95]
	v_mfma_f32_16x16x32_f16 v[96:99], v[144:147], v[164:167], v[96:99]
	v_mfma_f32_16x16x32_f16 v[100:103], v[144:147], v[168:171], v[100:103]
	s_waitcnt lgkmcnt(10)
	v_mfma_f32_16x16x32_f16 v[104:107], v[148:151], v[156:159], v[104:107]
	v_mfma_f32_16x16x32_f16 v[108:111], v[148:151], v[160:163], v[108:111]
	v_mfma_f32_16x16x32_f16 v[112:115], v[148:151], v[164:167], v[112:115]
	v_mfma_f32_16x16x32_f16 v[116:119], v[148:151], v[168:171], v[116:119]
	s_waitcnt lgkmcnt(9)
	v_mfma_f32_16x16x32_f16 v[120:123], v[152:155], v[156:159], v[120:123]
	v_mfma_f32_16x16x32_f16 v[124:127], v[152:155], v[160:163], v[124:127]
	v_mfma_f32_16x16x32_f16 v[128:131], v[152:155], v[164:167], v[128:131]
	v_mfma_f32_16x16x32_f16 v[132:135], v[152:155], v[168:171], v[132:135]
	s_waitcnt vmcnt(0) lgkmcnt(0)
	s_barrier
	s_waitcnt lgkmcnt(6)
	ds_read_b128 v[136:139], v15
	ds_read_b128 v[156:159], v17
	ds_read_b128 v[160:163], v17 offset:2048
	ds_read_b128 v[164:167], v17 offset:4096
	ds_read_b128 v[168:171], v17 offset:6144
	ds_read_b128 v[140:143], v15 offset:2048
	ds_read_b128 v[144:147], v15 offset:4096
	ds_read_b128 v[148:151], v15 offset:6144
	ds_read_b128 v[152:155], v15 offset:8192
	v_mfma_f32_16x16x32_f16 v[56:59], v[172:175], v[192:195], v[56:59]
	s_waitcnt lgkmcnt(15)
	v_mfma_f32_16x16x32_f16 v[60:63], v[172:175], v[196:199], v[60:63]
	s_waitcnt lgkmcnt(14)
	v_mfma_f32_16x16x32_f16 v[64:67], v[172:175], v[200:203], v[64:67]
	s_waitcnt lgkmcnt(13)
	v_mfma_f32_16x16x32_f16 v[68:71], v[172:175], v[204:207], v[68:71]
	s_waitcnt lgkmcnt(12)
	v_mfma_f32_16x16x32_f16 v[72:75], v[176:179], v[192:195], v[72:75]
	v_mfma_f32_16x16x32_f16 v[76:79], v[176:179], v[196:199], v[76:79]
	v_mfma_f32_16x16x32_f16 v[80:83], v[176:179], v[200:203], v[80:83]
	v_mfma_f32_16x16x32_f16 v[84:87], v[176:179], v[204:207], v[84:87]
	s_waitcnt lgkmcnt(11)
	v_mfma_f32_16x16x32_f16 v[88:91], v[180:183], v[192:195], v[88:91]
	v_mfma_f32_16x16x32_f16 v[92:95], v[180:183], v[196:199], v[92:95]
	v_mfma_f32_16x16x32_f16 v[96:99], v[180:183], v[200:203], v[96:99]
	v_mfma_f32_16x16x32_f16 v[100:103], v[180:183], v[204:207], v[100:103]
	s_waitcnt lgkmcnt(10)
	v_mfma_f32_16x16x32_f16 v[104:107], v[184:187], v[192:195], v[104:107]
	v_mfma_f32_16x16x32_f16 v[108:111], v[184:187], v[196:199], v[108:111]
	v_mfma_f32_16x16x32_f16 v[112:115], v[184:187], v[200:203], v[112:115]
	v_mfma_f32_16x16x32_f16 v[116:119], v[184:187], v[204:207], v[116:119]
	s_waitcnt lgkmcnt(9)
	v_mfma_f32_16x16x32_f16 v[120:123], v[188:191], v[192:195], v[120:123]
	v_mfma_f32_16x16x32_f16 v[124:127], v[188:191], v[196:199], v[124:127]
	v_mfma_f32_16x16x32_f16 v[128:131], v[188:191], v[200:203], v[128:131]
	v_mfma_f32_16x16x32_f16 v[132:135], v[188:191], v[204:207], v[132:135]
	s_waitcnt lgkmcnt(6)
	ds_read_b128 v[172:175], v16
	ds_read_b128 v[192:195], v18
	ds_read_b128 v[196:199], v18 offset:2048
	ds_read_b128 v[200:203], v18 offset:4096
	ds_read_b128 v[204:207], v18 offset:6144
	ds_read_b128 v[176:179], v16 offset:2048
	ds_read_b128 v[180:183], v16 offset:4096
	ds_read_b128 v[184:187], v16 offset:6144
	ds_read_b128 v[188:191], v16 offset:8192
	v_mfma_f32_16x16x32_f16 v[56:59], v[136:139], v[156:159], v[56:59]
	s_waitcnt lgkmcnt(15)
	v_mfma_f32_16x16x32_f16 v[60:63], v[136:139], v[160:163], v[60:63]
	s_waitcnt lgkmcnt(14)
	v_mfma_f32_16x16x32_f16 v[64:67], v[136:139], v[164:167], v[64:67]
	s_waitcnt lgkmcnt(13)
	v_mfma_f32_16x16x32_f16 v[68:71], v[136:139], v[168:171], v[68:71]
	s_waitcnt lgkmcnt(12)
	v_mfma_f32_16x16x32_f16 v[72:75], v[140:143], v[156:159], v[72:75]
	v_mfma_f32_16x16x32_f16 v[76:79], v[140:143], v[160:163], v[76:79]
	v_mfma_f32_16x16x32_f16 v[80:83], v[140:143], v[164:167], v[80:83]
	v_mfma_f32_16x16x32_f16 v[84:87], v[140:143], v[168:171], v[84:87]
	s_waitcnt lgkmcnt(11)
	v_mfma_f32_16x16x32_f16 v[88:91], v[144:147], v[156:159], v[88:91]
	v_mfma_f32_16x16x32_f16 v[92:95], v[144:147], v[160:163], v[92:95]
	v_mfma_f32_16x16x32_f16 v[96:99], v[144:147], v[164:167], v[96:99]
	v_mfma_f32_16x16x32_f16 v[100:103], v[144:147], v[168:171], v[100:103]
	s_waitcnt lgkmcnt(10)
	v_mfma_f32_16x16x32_f16 v[104:107], v[148:151], v[156:159], v[104:107]
	v_mfma_f32_16x16x32_f16 v[108:111], v[148:151], v[160:163], v[108:111]
	v_mfma_f32_16x16x32_f16 v[112:115], v[148:151], v[164:167], v[112:115]
	v_mfma_f32_16x16x32_f16 v[116:119], v[148:151], v[168:171], v[116:119]
	s_waitcnt lgkmcnt(9)
	v_mfma_f32_16x16x32_f16 v[120:123], v[152:155], v[156:159], v[120:123]
	v_mfma_f32_16x16x32_f16 v[124:127], v[152:155], v[160:163], v[124:127]
	v_mfma_f32_16x16x32_f16 v[128:131], v[152:155], v[164:167], v[128:131]
	v_mfma_f32_16x16x32_f16 v[132:135], v[152:155], v[168:171], v[132:135]
	s_waitcnt lgkmcnt(7)
	v_mfma_f32_16x16x32_f16 v[56:59], v[172:175], v[192:195], v[56:59]
	s_waitcnt lgkmcnt(6)
	v_mfma_f32_16x16x32_f16 v[60:63], v[172:175], v[196:199], v[60:63]
	s_waitcnt lgkmcnt(5)
	v_mfma_f32_16x16x32_f16 v[64:67], v[172:175], v[200:203], v[64:67]
	s_waitcnt lgkmcnt(4)
	v_mfma_f32_16x16x32_f16 v[68:71], v[172:175], v[204:207], v[68:71]
	s_waitcnt lgkmcnt(3)
	v_mfma_f32_16x16x32_f16 v[72:75], v[176:179], v[192:195], v[72:75]
	v_mfma_f32_16x16x32_f16 v[76:79], v[176:179], v[196:199], v[76:79]
	v_mfma_f32_16x16x32_f16 v[80:83], v[176:179], v[200:203], v[80:83]
	v_mfma_f32_16x16x32_f16 v[84:87], v[176:179], v[204:207], v[84:87]
	s_waitcnt lgkmcnt(2)
	v_mfma_f32_16x16x32_f16 v[88:91], v[180:183], v[192:195], v[88:91]
	v_mfma_f32_16x16x32_f16 v[92:95], v[180:183], v[196:199], v[92:95]
	v_mfma_f32_16x16x32_f16 v[96:99], v[180:183], v[200:203], v[96:99]
	v_mfma_f32_16x16x32_f16 v[100:103], v[180:183], v[204:207], v[100:103]
	s_waitcnt lgkmcnt(1)
	v_mfma_f32_16x16x32_f16 v[104:107], v[184:187], v[192:195], v[104:107]
	v_mfma_f32_16x16x32_f16 v[108:111], v[184:187], v[196:199], v[108:111]
	v_mfma_f32_16x16x32_f16 v[112:115], v[184:187], v[200:203], v[112:115]
	v_mfma_f32_16x16x32_f16 v[116:119], v[184:187], v[204:207], v[116:119]
	s_waitcnt lgkmcnt(0)
	v_mfma_f32_16x16x32_f16 v[120:123], v[188:191], v[192:195], v[120:123]
	v_mfma_f32_16x16x32_f16 v[124:127], v[188:191], v[196:199], v[124:127]
	v_mfma_f32_16x16x32_f16 v[128:131], v[188:191], v[200:203], v[128:131]
	v_mfma_f32_16x16x32_f16 v[132:135], v[188:191], v[204:207], v[132:135]
	s_nop 7
	s_nop 1
	s_add_u32 s24, s29, 0
	s_lshl_b32 s8, s24, 11
	s_nop 0
	v_add_u32_e32 v212, s8, v23
	v_add_f32_e32 v56, v56, v24
	v_add_f32_e32 v57, v57, v24
	v_add_f32_e32 v58, v58, v24
	v_add_f32_e32 v59, v59, v24
	v_cvt_pk_f16_f32 v56, v56, v57
	v_cvt_pk_f16_f32 v57, v58, v59
	global_store_dwordx2 v212, v[56:57], s[22:23] offset:0
	v_add_f32_e32 v60, v60, v25
	v_add_f32_e32 v61, v61, v25
	v_add_f32_e32 v62, v62, v25
	v_add_f32_e32 v63, v63, v25
	v_cvt_pk_f16_f32 v60, v60, v61
	v_cvt_pk_f16_f32 v61, v62, v63
	global_store_dwordx2 v212, v[60:61], s[22:23] offset:256
	v_add_f32_e32 v64, v64, v26
	v_add_f32_e32 v65, v65, v26
	v_add_f32_e32 v66, v66, v26
	v_add_f32_e32 v67, v67, v26
	v_cvt_pk_f16_f32 v64, v64, v65
	v_cvt_pk_f16_f32 v65, v66, v67
	global_store_dwordx2 v212, v[64:65], s[22:23] offset:1024
	v_add_f32_e32 v68, v68, v27
	v_add_f32_e32 v69, v69, v27
	v_add_f32_e32 v70, v70, v27
	v_add_f32_e32 v71, v71, v27
	v_cvt_pk_f16_f32 v68, v68, v69
	v_cvt_pk_f16_f32 v69, v70, v71
	global_store_dwordx2 v212, v[68:69], s[22:23] offset:1280
	s_add_u32 s24, s29, 1
	s_lshl_b32 s8, s24, 11
	s_nop 0
	v_add_u32_e32 v212, s8, v23
	v_add_f32_e32 v72, v72, v24
	v_add_f32_e32 v73, v73, v24
	v_add_f32_e32 v74, v74, v24
	v_add_f32_e32 v75, v75, v24
	v_cvt_pk_f16_f32 v72, v72, v73
	v_cvt_pk_f16_f32 v73, v74, v75
	global_store_dwordx2 v212, v[72:73], s[22:23] offset:0
	v_add_f32_e32 v76, v76, v25
	v_add_f32_e32 v77, v77, v25
	v_add_f32_e32 v78, v78, v25
	v_add_f32_e32 v79, v79, v25
	v_cvt_pk_f16_f32 v76, v76, v77
	v_cvt_pk_f16_f32 v77, v78, v79
	global_store_dwordx2 v212, v[76:77], s[22:23] offset:256
	v_add_f32_e32 v80, v80, v26
	v_add_f32_e32 v81, v81, v26
	v_add_f32_e32 v82, v82, v26
	v_add_f32_e32 v83, v83, v26
	v_cvt_pk_f16_f32 v80, v80, v81
	v_cvt_pk_f16_f32 v81, v82, v83
	global_store_dwordx2 v212, v[80:81], s[22:23] offset:1024
	v_add_f32_e32 v84, v84, v27
	v_add_f32_e32 v85, v85, v27
	v_add_f32_e32 v86, v86, v27
	v_add_f32_e32 v87, v87, v27
	v_cvt_pk_f16_f32 v84, v84, v85
	v_cvt_pk_f16_f32 v85, v86, v87
	global_store_dwordx2 v212, v[84:85], s[22:23] offset:1280
	s_add_u32 s24, s29, 2
	s_lshl_b32 s8, s24, 11
	s_nop 0
	v_add_u32_e32 v212, s8, v23
	v_add_f32_e32 v88, v88, v24
	v_add_f32_e32 v89, v89, v24
	v_add_f32_e32 v90, v90, v24
	v_add_f32_e32 v91, v91, v24
	v_cvt_pk_f16_f32 v88, v88, v89
	v_cvt_pk_f16_f32 v89, v90, v91
	global_store_dwordx2 v212, v[88:89], s[22:23] offset:0
	v_add_f32_e32 v92, v92, v25
	v_add_f32_e32 v93, v93, v25
	v_add_f32_e32 v94, v94, v25
	v_add_f32_e32 v95, v95, v25
	v_cvt_pk_f16_f32 v92, v92, v93
	v_cvt_pk_f16_f32 v93, v94, v95
	global_store_dwordx2 v212, v[92:93], s[22:23] offset:256
	v_add_f32_e32 v96, v96, v26
	v_add_f32_e32 v97, v97, v26
	v_add_f32_e32 v98, v98, v26
	v_add_f32_e32 v99, v99, v26
	v_cvt_pk_f16_f32 v96, v96, v97
	v_cvt_pk_f16_f32 v97, v98, v99
	global_store_dwordx2 v212, v[96:97], s[22:23] offset:1024
	v_add_f32_e32 v100, v100, v27
	v_add_f32_e32 v101, v101, v27
	v_add_f32_e32 v102, v102, v27
	v_add_f32_e32 v103, v103, v27
	v_cvt_pk_f16_f32 v100, v100, v101
	v_cvt_pk_f16_f32 v101, v102, v103
	global_store_dwordx2 v212, v[100:101], s[22:23] offset:1280
	s_add_u32 s24, s29, 3
	s_lshl_b32 s8, s24, 11
	s_nop 0
	v_add_u32_e32 v212, s8, v23
	v_add_f32_e32 v104, v104, v24
	v_add_f32_e32 v105, v105, v24
	v_add_f32_e32 v106, v106, v24
	v_add_f32_e32 v107, v107, v24
	v_cvt_pk_f16_f32 v104, v104, v105
	v_cvt_pk_f16_f32 v105, v106, v107
	global_store_dwordx2 v212, v[104:105], s[22:23] offset:0
	v_add_f32_e32 v108, v108, v25
	v_add_f32_e32 v109, v109, v25
	v_add_f32_e32 v110, v110, v25
	v_add_f32_e32 v111, v111, v25
	v_cvt_pk_f16_f32 v108, v108, v109
	v_cvt_pk_f16_f32 v109, v110, v111
	global_store_dwordx2 v212, v[108:109], s[22:23] offset:256
	v_add_f32_e32 v112, v112, v26
	v_add_f32_e32 v113, v113, v26
	v_add_f32_e32 v114, v114, v26
	v_add_f32_e32 v115, v115, v26
	v_cvt_pk_f16_f32 v112, v112, v113
	v_cvt_pk_f16_f32 v113, v114, v115
	global_store_dwordx2 v212, v[112:113], s[22:23] offset:1024
	v_add_f32_e32 v116, v116, v27
	v_add_f32_e32 v117, v117, v27
	v_add_f32_e32 v118, v118, v27
	v_add_f32_e32 v119, v119, v27
	v_cvt_pk_f16_f32 v116, v116, v117
	v_cvt_pk_f16_f32 v117, v118, v119
	global_store_dwordx2 v212, v[116:117], s[22:23] offset:1280
	s_add_u32 s24, s29, 4
	s_lshl_b32 s8, s24, 11
	s_nop 0
	v_add_u32_e32 v212, s8, v23
	v_add_f32_e32 v120, v120, v24
	v_add_f32_e32 v121, v121, v24
	v_add_f32_e32 v122, v122, v24
	v_add_f32_e32 v123, v123, v24
	v_cvt_pk_f16_f32 v120, v120, v121
	v_cvt_pk_f16_f32 v121, v122, v123
	global_store_dwordx2 v212, v[120:121], s[22:23] offset:0
	v_add_f32_e32 v124, v124, v25
	v_add_f32_e32 v125, v125, v25
	v_add_f32_e32 v126, v126, v25
	v_add_f32_e32 v127, v127, v25
	v_cvt_pk_f16_f32 v124, v124, v125
	v_cvt_pk_f16_f32 v125, v126, v127
	global_store_dwordx2 v212, v[124:125], s[22:23] offset:256
	v_add_f32_e32 v128, v128, v26
	v_add_f32_e32 v129, v129, v26
	v_add_f32_e32 v130, v130, v26
	v_add_f32_e32 v131, v131, v26
	v_cvt_pk_f16_f32 v128, v128, v129
	v_cvt_pk_f16_f32 v129, v130, v131
	global_store_dwordx2 v212, v[128:129], s[22:23] offset:1024
	v_add_f32_e32 v132, v132, v27
	v_add_f32_e32 v133, v133, v27
	v_add_f32_e32 v134, v134, v27
	v_add_f32_e32 v135, v135, v27
	v_cvt_pk_f16_f32 v132, v132, v133
	v_cvt_pk_f16_f32 v133, v134, v135
	global_store_dwordx2 v212, v[132:133], s[22:23] offset:1280
	s_branch .Lpf_done
.Lpf_vVB:
	s_lshl_b32 s25, s25, 6
	s_add_u32 s25, s25, 32
	s_add_u32 s29, s10, s25
	s_lshr_b32 s29, s29, 4
	v_add_u32_e32 v5, s25, v3
	v_lshlrev_b32_e32 v5, 7, v5
	v_add_u32_e32 v15, v5, v6
	v_add_u32_e32 v16, v5, v7
	v_add_u32_e32 v5, 0x9000, v9
	v_add_u32_e32 v17, v5, v6
	v_add_u32_e32 v18, v5, v7
	v_add_u32_e32 v19, 0x1a000, v15
	v_add_u32_e32 v20, 0x1a000, v16
	v_add_u32_e32 v21, 0x1a000, v17
	v_add_u32_e32 v22, 0x1a000, v18
	v_lshlrev_b32_e32 v5, 2, v3
	global_load_dword v24, v5, s[14:15] offset:0
	global_load_dword v25, v5, s[14:15] offset:64
	global_load_dword v26, v5, s[14:15] offset:128
	global_load_dword v27, v5, s[14:15] offset:192
	s_add_u32 m0, s28, 0x0
	s_nop 0
	global_load_lds_dwordx4 v10, s[4:5]
	s_add_u32 m0, s28, 0x2000
	s_nop 0
	global_load_lds_dwordx4 v11, s[4:5]
	s_add_u32 m0, s28, 0x4000
	s_nop 0
	global_load_lds_dwordx4 v12, s[4:5]
	s_add_u32 m0, s28, 0x6000
	s_nop 0
	global_load_lds_dwordx4 v13, s[4:5]
	s_add_u32 s4, s4, s20
	s_addc_u32 s5, s5, 0
	s_add_u32 m0, s28, 0x9000
	s_nop 0
	global_load_lds_dwordx4 v10, s[6:7]
	s_add_u32 m0, s28, 0xb000
	s_nop 0
	global_load_lds_dwordx4 v11, s[6:7]
	s_add_u32 s6, s6, s20
	s_addc_u32 s7, s7, 0
	s_add_u32 m0, s28, 0xd000
	s_nop 0
	global_load_lds_dwordx4 v10, s[4:5]
	s_add_u32 m0, s28, 0xf000
	s_nop 0
	global_load_lds_dwordx4 v11, s[4:5]
	s_add_u32 m0, s28, 0x11000
	s_nop 0
	global_load_lds_dwordx4 v12, s[4:5]
	s_add_u32 m0, s28, 0x13000
	s_nop 0
	global_load_lds_dwordx4 v13, s[4:5]
	s_add_u32 s4, s4, s20
	s_addc_u32 s5, s5, 0
	s_add_u32 m0, s28, 0x16000
	s_nop 0
	global_load_lds_dwordx4 v10, s[6:7]
	s_add_u32 m0, s28, 0x18000
	s_nop 0
	global_load_lds_dwordx4 v11, s[6:7]
	s_add_u32 s6, s6, s20
	s_addc_u32 s7, s7, 0
	s_add_u32 m0, s28, 0x1a000
	s_nop 0
	global_load_lds_dwordx4 v10, s[4:5]
	s_add_u32 m0, s28, 0x1c000
	s_nop 0
	global_load_lds_dwordx4 v11, s[4:5]
	s_add_u32 m0, s28, 0x1e000
	s_nop 0
	global_load_lds_dwordx4 v12, s[4:5]
	s_add_u32 m0, s28, 0x20000
	s_nop 0
	global_load_lds_dwordx4 v13, s[4:5]
	s_add_u32 s4, s4, s20
	s_addc_u32 s5, s5, 0
	s_add_u32 m0, s28, 0x23000
	s_nop 0
	global_load_lds_dwordx4 v10, s[6:7]
	s_add_u32 m0, s28, 0x25000
	s_nop 0
	global_load_lds_dwordx4 v11, s[6:7]
	s_add_u32 s6, s6, s20
	s_addc_u32 s7, s7, 0
	s_waitcnt vmcnt(12) lgkmcnt(0)
	s_barrier
	s_waitcnt lgkmcnt(7)
	ds_read_b128 v[136:139], v15
	ds_read_b128 v[156:159], v17
	ds_read_b128 v[160:163], v17 offset:2048
	ds_read_b128 v[164:167], v17 offset:4096
	ds_read_b128 v[168:171], v17 offset:6144
	ds_read_b128 v[140:143], v15 offset:2048
	ds_read_b128 v[144:147], v15 offset:4096
	ds_read_b128 v[148:151], v15 offset:6144
	s_waitcnt lgkmcnt(7)
	ds_read_b128 v[172:175], v16
	ds_read_b128 v[192:195], v18
	ds_read_b128 v[196:199], v18 offset:2048
	ds_read_b128 v[200:203], v18 offset:4096
	ds_read_b128 v[204:207], v18 offset:6144
	ds_read_b128 v[176:179], v16 offset:2048
	ds_read_b128 v[180:183], v16 offset:4096
	ds_read_b128 v[184:187], v16 offset:6144
	s_waitcnt lgkmcnt(14)
	v_mfma_f32_16x16x32_f16 v[56:59], v[136:139], v[156:159], 0
	s_waitcnt lgkmcnt(13)
	v_mfma_f32_16x16x32_f16 v[60:63], v[136:139], v[160:163], 0
	s_waitcnt lgkmcnt(12)
	v_mfma_f32_16x16x32_f16 v[64:67], v[136:139], v[164:167], 0
	s_waitcnt lgkmcnt(11)
	v_mfma_f32_16x16x32_f16 v[68:71], v[136:139], v[168:171], 0
	s_waitcnt lgkmcnt(10)
	v_mfma_f32_16x16x32_f16 v[72:75], v[140:143], v[156:159], 0
	v_mfma_f32_16x16x32_f16 v[76:79], v[140:143], v[160:163], 0
	v_mfma_f32_16x16x32_f16 v[80:83], v[140:143], v[164:167], 0
	v_mfma_f32_16x16x32_f16 v[84:87], v[140:143], v[168:171], 0
	s_waitcnt lgkmcnt(9)
	v_mfma_f32_16x16x32_f16 v[88:91], v[144:147], v[156:159], 0
	v_mfma_f32_16x16x32_f16 v[92:95], v[144:147], v[160:163], 0
	v_mfma_f32_16x16x32_f16 v[96:99], v[144:147], v[164:167], 0
	v_mfma_f32_16x16x32_f16 v[100:103], v[144:147], v[168:171], 0
	s_waitcnt lgkmcnt(8)
	v_mfma_f32_16x16x32_f16 v[104:107], v[148:151], v[156:159], 0
	v_mfma_f32_16x16x32_f16 v[108:111], v[148:151], v[160:163], 0
	v_mfma_f32_16x16x32_f16 v[112:115], v[148:151], v[164:167], 0
	v_mfma_f32_16x16x32_f16 v[116:119], v[148:151], v[168:171], 0
	s_waitcnt vmcnt(6) lgkmcnt(0)
	s_barrier
	s_waitcnt lgkmcnt(7)
	ds_read_b128 v[136:139], v15 offset:53248
	ds_read_b128 v[156:159], v17 offset:53248
	ds_read_b128 v[160:163], v17 offset:55296
	ds_read_b128 v[164:167], v17 offset:57344
	ds_read_b128 v[168:171], v17 offset:59392
	ds_read_b128 v[140:143], v15 offset:55296
	ds_read_b128 v[144:147], v15 offset:57344
	ds_read_b128 v[148:151], v15 offset:59392
	s_waitcnt lgkmcnt(14)
	v_mfma_f32_16x16x32_f16 v[56:59], v[172:175], v[192:195], v[56:59]
	s_add_u32 m0, s28, 0x0
	s_nop 0
	global_load_lds_dwordx4 v10, s[4:5]
	s_waitcnt lgkmcnt(13)
	v_mfma_f32_16x16x32_f16 v[60:63], v[172:175], v[196:199], v[60:63]
	s_waitcnt lgkmcnt(12)
	v_mfma_f32_16x16x32_f16 v[64:67], v[172:175], v[200:203], v[64:67]
	s_waitcnt lgkmcnt(11)
	v_mfma_f32_16x16x32_f16 v[68:71], v[172:175], v[204:207], v[68:71]
	s_waitcnt lgkmcnt(10)
	v_mfma_f32_16x16x32_f16 v[72:75], v[176:179], v[192:195], v[72:75]
	v_mfma_f32_16x16x32_f16 v[76:79], v[176:179], v[196:199], v[76:79]
	s_add_u32 m0, s28, 0x2000
	s_nop 0
	global_load_lds_dwordx4 v11, s[4:5]
	v_mfma_f32_16x16x32_f16 v[80:83], v[176:179], v[200:203], v[80:83]
	v_mfma_f32_16x16x32_f16 v[84:87], v[176:179], v[204:207], v[84:87]
	s_waitcnt lgkmcnt(9)
	v_mfma_f32_16x16x32_f16 v[88:91], v[180:183], v[192:195], v[88:91]
	v_mfma_f32_16x16x32_f16 v[92:95], v[180:183], v[196:199], v[92:95]
	v_mfma_f32_16x16x32_f16 v[96:99], v[180:183], v[200:203], v[96:99]
	s_add_u32 m0, s28, 0x4000
	s_nop 0
	global_load_lds_dwordx4 v12, s[4:5]
	v_mfma_f32_16x16x32_f16 v[100:103], v[180:183], v[204:207], v[100:103]
	s_waitcnt lgkmcnt(8)
	v_mfma_f32_16x16x32_f16 v[104:107], v[184:187], v[192:195], v[104:107]
	v_mfma_f32_16x16x32_f16 v[108:111], v[184:187], v[196:199], v[108:111]
	v_mfma_f32_16x16x32_f16 v[112:115], v[184:187], v[200:203], v[112:115]
	v_mfma_f32_16x16x32_f16 v[116:119], v[184:187], v[204:207], v[116:119]
	s_waitcnt lgkmcnt(7)
	ds_read_b128 v[172:175], v16 offset:53248
	ds_read_b128 v[192:195], v18 offset:53248
	ds_read_b128 v[196:199], v18 offset:55296
	ds_read_b128 v[200:203], v18 offset:57344
	ds_read_b128 v[204:207], v18 offset:59392
	ds_read_b128 v[176:179], v16 offset:55296
	ds_read_b128 v[180:183], v16 offset:57344
	ds_read_b128 v[184:187], v16 offset:59392
	s_waitcnt lgkmcnt(14)
	v_mfma_f32_16x16x32_f16 v[56:59], v[136:139], v[156:159], v[56:59]
	s_add_u32 m0, s28, 0x6000
	s_nop 0
	global_load_lds_dwordx4 v13, s[4:5]
	s_add_u32 s4, s4, s20
	s_addc_u32 s5, s5, 0
	s_waitcnt lgkmcnt(13)
	v_mfma_f32_16x16x32_f16 v[60:63], v[136:139], v[160:163], v[60:63]
	s_waitcnt lgkmcnt(12)
	v_mfma_f32_16x16x32_f16 v[64:67], v[136:139], v[164:167], v[64:67]
	s_waitcnt lgkmcnt(11)
	v_mfma_f32_16x16x32_f16 v[68:71], v[136:139], v[168:171], v[68:71]
	s_waitcnt lgkmcnt(10)
	v_mfma_f32_16x16x32_f16 v[72:75], v[140:143], v[156:159], v[72:75]
	v_mfma_f32_16x16x32_f16 v[76:79], v[140:143], v[160:163], v[76:79]
	s_add_u32 m0, s28, 0x9000
	s_nop 0
	global_load_lds_dwordx4 v10, s[6:7]
	v_mfma_f32_16x16x32_f16 v[80:83], v[140:143], v[164:167], v[80:83]
	v_mfma_f32_16x16x32_f16 v[84:87], v[140:143], v[168:171], v[84:87]
	s_waitcnt lgkmcnt(9)
	v_mfma_f32_16x16x32_f16 v[88:91], v[144:147], v[156:159], v[88:91]
	v_mfma_f32_16x16x32_f16 v[92:95], v[144:147], v[160:163], v[92:95]
	v_mfma_f32_16x16x32_f16 v[96:99], v[144:147], v[164:167], v[96:99]
	s_add_u32 m0, s28, 0xb000
	s_nop 0
	global_load_lds_dwordx4 v11, s[6:7]
	s_add_u32 s6, s6, s20
	s_addc_u32 s7, s7, 0
	v_mfma_f32_16x16x32_f16 v[100:103], v[144:147], v[168:171], v[100:103]
	s_waitcnt lgkmcnt(8)
	v_mfma_f32_16x16x32_f16 v[104:107], v[148:151], v[156:159], v[104:107]
	v_mfma_f32_16x16x32_f16 v[108:111], v[148:151], v[160:163], v[108:111]
	v_mfma_f32_16x16x32_f16 v[112:115], v[148:151], v[164:167], v[112:115]
	v_mfma_f32_16x16x32_f16 v[116:119], v[148:151], v[168:171], v[116:119]
	s_waitcnt vmcnt(6) lgkmcnt(0)
	s_barrier
	s_waitcnt lgkmcnt(7)
	ds_read_b128 v[136:139], v19
	ds_read_b128 v[156:159], v21
	ds_read_b128 v[160:163], v21 offset:2048
	ds_read_b128 v[164:167], v21 offset:4096
	ds_read_b128 v[168:171], v21 offset:6144
	ds_read_b128 v[140:143], v19 offset:2048
	ds_read_b128 v[144:147], v19 offset:4096
	ds_read_b128 v[148:151], v19 offset:6144
	s_waitcnt lgkmcnt(14)
	v_mfma_f32_16x16x32_f16 v[56:59], v[172:175], v[192:195], v[56:59]
	s_add_u32 m0, s28, 0xd000
	s_nop 0
	global_load_lds_dwordx4 v10, s[4:5]
	s_waitcnt lgkmcnt(13)
	v_mfma_f32_16x16x32_f16 v[60:63], v[172:175], v[196:199], v[60:63]
	s_waitcnt lgkmcnt(12)
	v_mfma_f32_16x16x32_f16 v[64:67], v[172:175], v[200:203], v[64:67]
	s_waitcnt lgkmcnt(11)
	v_mfma_f32_16x16x32_f16 v[68:71], v[172:175], v[204:207], v[68:71]
	s_waitcnt lgkmcnt(10)
	v_mfma_f32_16x16x32_f16 v[72:75], v[176:179], v[192:195], v[72:75]
	v_mfma_f32_16x16x32_f16 v[76:79], v[176:179], v[196:199], v[76:79]
	s_add_u32 m0, s28, 0xf000
	s_nop 0
	global_load_lds_dwordx4 v11, s[4:5]
	v_mfma_f32_16x16x32_f16 v[80:83], v[176:179], v[200:203], v[80:83]
	v_mfma_f32_16x16x32_f16 v[84:87], v[176:179], v[204:207], v[84:87]
	s_waitcnt lgkmcnt(9)
	v_mfma_f32_16x16x32_f16 v[88:91], v[180:183], v[192:195], v[88:91]
	v_mfma_f32_16x16x32_f16 v[92:95], v[180:183], v[196:199], v[92:95]
	v_mfma_f32_16x16x32_f16 v[96:99], v[180:183], v[200:203], v[96:99]
	s_add_u32 m0, s28, 0x11000
	s_nop 0
	global_load_lds_dwordx4 v12, s[4:5]
	v_mfma_f32_16x16x32_f16 v[100:103], v[180:183], v[204:207], v[100:103]
	s_waitcnt lgkmcnt(8)
	v_mfma_f32_16x16x32_f16 v[104:107], v[184:187], v[192:195], v[104:107]
	v_mfma_f32_16x16x32_f16 v[108:111], v[184:187], v[196:199], v[108:111]
	v_mfma_f32_16x16x32_f16 v[112:115], v[184:187], v[200:203], v[112:115]
	v_mfma_f32_16x16x32_f16 v[116:119], v[184:187], v[204:207], v[116:119]
	s_waitcnt lgkmcnt(7)
	ds_read_b128 v[172:175], v20
	ds_read_b128 v[192:195], v22
	ds_read_b128 v[196:199], v22 offset:2048
	ds_read_b128 v[200:203], v22 offset:4096
	ds_read_b128 v[204:207], v22 offset:6144
	ds_read_b128 v[176:179], v20 offset:2048
	ds_read_b128 v[180:183], v20 offset:4096
	ds_read_b128 v[184:187], v20 offset:6144
	s_waitcnt lgkmcnt(14)
	v_mfma_f32_16x16x32_f16 v[56:59], v[136:139], v[156:159], v[56:59]
	s_add_u32 m0, s28, 0x13000
	s_nop 0
	global_load_lds_dwordx4 v13, s[4:5]
	s_add_u32 s4, s4, s20
	s_addc_u32 s5, s5, 0
	s_waitcnt lgkmcnt(13)
	v_mfma_f32_16x16x32_f16 v[60:63], v[136:139], v[160:163], v[60:63]
	s_waitcnt lgkmcnt(12)
	v_mfma_f32_16x16x32_f16 v[64:67], v[136:139], v[164:167], v[64:67]
	s_waitcnt lgkmcnt(11)
	v_mfma_f32_16x16x32_f16 v[68:71], v[136:139], v[168:171], v[68:71]
	s_waitcnt lgkmcnt(10)
	v_mfma_f32_16x16x32_f16 v[72:75], v[140:143], v[156:159], v[72:75]
	v_mfma_f32_16x16x32_f16 v[76:79], v[140:143], v[160:163], v[76:79]
	s_add_u32 m0, s28, 0x16000
	s_nop 0
	global_load_lds_dwordx4 v10, s[6:7]
	v_mfma_f32_16x16x32_f16 v[80:83], v[140:143], v[164:167], v[80:83]
	v_mfma_f32_16x16x32_f16 v[84:87], v[140:143], v[168:171], v[84:87]
	s_waitcnt lgkmcnt(9)
	v_mfma_f32_16x16x32_f16 v[88:91], v[144:147], v[156:159], v[88:91]
	v_mfma_f32_16x16x32_f16 v[92:95], v[144:147], v[160:163], v[92:95]
	v_mfma_f32_16x16x32_f16 v[96:99], v[144:147], v[164:167], v[96:99]
	s_add_u32 m0, s28, 0x18000
	s_nop 0
	global_load_lds_dwordx4 v11, s[6:7]
	s_add_u32 s6, s6, s20
	s_addc_u32 s7, s7, 0
	v_mfma_f32_16x16x32_f16 v[100:103], v[144:147], v[168:171], v[100:103]
	s_waitcnt lgkmcnt(8)
	v_mfma_f32_16x16x32_f16 v[104:107], v[148:151], v[156:159], v[104:107]
	v_mfma_f32_16x16x32_f16 v[108:111], v[148:151], v[160:163], v[108:111]
	v_mfma_f32_16x16x32_f16 v[112:115], v[148:151], v[164:167], v[112:115]
	v_mfma_f32_16x16x32_f16 v[116:119], v[148:151], v[168:171], v[116:119]
	s_waitcnt vmcnt(6) lgkmcnt(0)
	s_barrier
	s_waitcnt lgkmcnt(7)
	ds_read_b128 v[136:139], v15
	ds_read_b128 v[156:159], v17
	ds_read_b128 v[160:163], v17 offset:2048
	ds_read_b128 v[164:167], v17 offset:4096
	ds_read_b128 v[168:171], v17 offset:6144
	ds_read_b128 v[140:143], v15 offset:2048
	ds_read_b128 v[144:147], v15 offset:4096
	ds_read_b128 v[148:151], v15 offset:6144
	s_waitcnt lgkmcnt(14)
	v_mfma_f32_16x16x32_f16 v[56:59], v[172:175], v[192:195], v[56:59]
	s_add_u32 m0, s28, 0x1a000
	s_nop 0
	global_load_lds_dwordx4 v10, s[4:5]
	s_waitcnt lgkmcnt(13)
	v_mfma_f32_16x16x32_f16 v[60:63], v[172:175], v[196:199], v[60:63]
	s_waitcnt lgkmcnt(12)
	v_mfma_f32_16x16x32_f16 v[64:67], v[172:175], v[200:203], v[64:67]
	s_waitcnt lgkmcnt(11)
	v_mfma_f32_16x16x32_f16 v[68:71], v[172:175], v[204:207], v[68:71]
	s_waitcnt lgkmcnt(10)
	v_mfma_f32_16x16x32_f16 v[72:75], v[176:179], v[192:195], v[72:75]
	v_mfma_f32_16x16x32_f16 v[76:79], v[176:179], v[196:199], v[76:79]
	s_add_u32 m0, s28, 0x1c000
	s_nop 0
	global_load_lds_dwordx4 v11, s[4:5]
	v_mfma_f32_16x16x32_f16 v[80:83], v[176:179], v[200:203], v[80:83]
	v_mfma_f32_16x16x32_f16 v[84:87], v[176:179], v[204:207], v[84:87]
	s_waitcnt lgkmcnt(9)
	v_mfma_f32_16x16x32_f16 v[88:91], v[180:183], v[192:195], v[88:91]
	v_mfma_f32_16x16x32_f16 v[92:95], v[180:183], v[196:199], v[92:95]
	v_mfma_f32_16x16x32_f16 v[96:99], v[180:183], v[200:203], v[96:99]
	s_add_u32 m0, s28, 0x1e000
	s_nop 0
	global_load_lds_dwordx4 v12, s[4:5]
	v_mfma_f32_16x16x32_f16 v[100:103], v[180:183], v[204:207], v[100:103]
	s_waitcnt lgkmcnt(8)
	v_mfma_f32_16x16x32_f16 v[104:107], v[184:187], v[192:195], v[104:107]
	v_mfma_f32_16x16x32_f16 v[108:111], v[184:187], v[196:199], v[108:111]
	v_mfma_f32_16x16x32_f16 v[112:115], v[184:187], v[200:203], v[112:115]
	v_mfma_f32_16x16x32_f16 v[116:119], v[184:187], v[204:207], v[116:119]
	s_waitcnt lgkmcnt(7)
	ds_read_b128 v[172:175], v16
	ds_read_b128 v[192:195], v18
	ds_read_b128 v[196:199], v18 offset:2048
	ds_read_b128 v[200:203], v18 offset:4096
	ds_read_b128 v[204:207], v18 offset:6144
	ds_read_b128 v[176:179], v16 offset:2048
	ds_read_b128 v[180:183], v16 offset:4096
	ds_read_b128 v[184:187], v16 offset:6144
	s_waitcnt lgkmcnt(14)
	v_mfma_f32_16x16x32_f16 v[56:59], v[136:139], v[156:159], v[56:59]
	s_add_u32 m0, s28, 0x20000
	s_nop 0
	global_load_lds_dwordx4 v13, s[4:5]
	s_add_u32 s4, s4, s20
	s_addc_u32 s5, s5, 0
	s_waitcnt lgkmcnt(13)
	v_mfma_f32_16x16x32_f16 v[60:63], v[136:139], v[160:163], v[60:63]
	s_waitcnt lgkmcnt(12)
	v_mfma_f32_16x16x32_f16 v[64:67], v[136:139], v[164:167], v[64:67]
	s_waitcnt lgkmcnt(11)
	v_mfma_f32_16x16x32_f16 v[68:71], v[136:139], v[168:171], v[68:71]
	s_waitcnt lgkmcnt(10)
	v_mfma_f32_16x16x32_f16 v[72:75], v[140:143], v[156:159], v[72:75]
	v_mfma_f32_16x16x32_f16 v[76:79], v[140:143], v[160:163], v[76:79]
	s_add_u32 m0, s28, 0x23000
	s_nop 0
	global_load_lds_dwordx4 v10, s[6:7]
	v_mfma_f32_16x16x32_f16 v[80:83], v[140:143], v[164:167], v[80:83]
	v_mfma_f32_16x16x32_f16 v[84:87], v[140:143], v[168:171], v[84:87]
	s_waitcnt lgkmcnt(9)
	v_mfma_f32_16x16x32_f16 v[88:91], v[144:147], v[156:159], v[88:91]
	v_mfma_f32_16x16x32_f16 v[92:95], v[144:147], v[160:163], v[92:95]
	v_mfma_f32_16x16x32_f16 v[96:99], v[144:147], v[164:167], v[96:99]
	s_add_u32 m0, s28, 0x25000
	s_nop 0
	global_load_lds_dwordx4 v11, s[6:7]
	s_add_u32 s6, s6, s20
	s_addc_u32 s7, s7, 0
	v_mfma_f32_16x16x32_f16 v[100:103], v[144:147], v[168:171], v[100:103]
	s_waitcnt lgkmcnt(8)
	v_mfma_f32_16x16x32_f16 v[104:107], v[148:151], v[156:159], v[104:107]
	v_mfma_f32_16x16x32_f16 v[108:111], v[148:151], v[160:163], v[108:111]
	v_mfma_f32_16x16x32_f16 v[112:115], v[148:151], v[164:167], v[112:115]
	v_mfma_f32_16x16x32_f16 v[116:119], v[148:151], v[168:171], v[116:119]
	s_waitcnt vmcnt(6) lgkmcnt(0)
	s_barrier
	s_waitcnt lgkmcnt(7)
	ds_read_b128 v[136:139], v15 offset:53248
	ds_read_b128 v[156:159], v17 offset:53248
	ds_read_b128 v[160:163], v17 offset:55296
	ds_read_b128 v[164:167], v17 offset:57344
	ds_read_b128 v[168:171], v17 offset:59392
	ds_read_b128 v[140:143], v15 offset:55296
	ds_read_b128 v[144:147], v15 offset:57344
	ds_read_b128 v[148:151], v15 offset:59392
	s_waitcnt lgkmcnt(14)
	v_mfma_f32_16x16x32_f16 v[56:59], v[172:175], v[192:195], v[56:59]
	s_add_u32 m0, s28, 0x0
	s_nop 0
	global_load_lds_dwordx4 v10, s[4:5]
	s_waitcnt lgkmcnt(13)
	v_mfma_f32_16x16x32_f16 v[60:63], v[172:175], v[196:199], v[60:63]
	s_waitcnt lgkmcnt(12)
	v_mfma_f32_16x16x32_f16 v[64:67], v[172:175], v[200:203], v[64:67]
	s_waitcnt lgkmcnt(11)
	v_mfma_f32_16x16x32_f16 v[68:71], v[172:175], v[204:207], v[68:71]
	s_waitcnt lgkmcnt(10)
	v_mfma_f32_16x16x32_f16 v[72:75], v[176:179], v[192:195], v[72:75]
	v_mfma_f32_16x16x32_f16 v[76:79], v[176:179], v[196:199], v[76:79]
	s_add_u32 m0, s28, 0x2000
	s_nop 0
	global_load_lds_dwordx4 v11, s[4:5]
	v_mfma_f32_16x16x32_f16 v[80:83], v[176:179], v[200:203], v[80:83]
	v_mfma_f32_16x16x32_f16 v[84:87], v[176:179], v[204:207], v[84:87]
	s_waitcnt lgkmcnt(9)
	v_mfma_f32_16x16x32_f16 v[88:91], v[180:183], v[192:195], v[88:91]
	v_mfma_f32_16x16x32_f16 v[92:95], v[180:183], v[196:199], v[92:95]
	v_mfma_f32_16x16x32_f16 v[96:99], v[180:183], v[200:203], v[96:99]
	s_add_u32 m0, s28, 0x4000
	s_nop 0
	global_load_lds_dwordx4 v12, s[4:5]
	v_mfma_f32_16x16x32_f16 v[100:103], v[180:183], v[204:207], v[100:103]
	s_waitcnt lgkmcnt(8)
	v_mfma_f32_16x16x32_f16 v[104:107], v[184:187], v[192:195], v[104:107]
	v_mfma_f32_16x16x32_f16 v[108:111], v[184:187], v[196:199], v[108:111]
	v_mfma_f32_16x16x32_f16 v[112:115], v[184:187], v[200:203], v[112:115]
	v_mfma_f32_16x16x32_f16 v[116:119], v[184:187], v[204:207], v[116:119]
	s_waitcnt lgkmcnt(7)
	ds_read_b128 v[172:175], v16 offset:53248
	ds_read_b128 v[192:195], v18 offset:53248
	ds_read_b128 v[196:199], v18 offset:55296
	ds_read_b128 v[200:203], v18 offset:57344
	ds_read_b128 v[204:207], v18 offset:59392
	ds_read_b128 v[176:179], v16 offset:55296
	ds_read_b128 v[180:183], v16 offset:57344
	ds_read_b128 v[184:187], v16 offset:59392
	s_waitcnt lgkmcnt(14)
	v_mfma_f32_16x16x32_f16 v[56:59], v[136:139], v[156:159], v[56:59]
	s_add_u32 m0, s28, 0x6000
	s_nop 0
	global_load_lds_dwordx4 v13, s[4:5]
	s_add_u32 s4, s4, s20
	s_addc_u32 s5, s5, 0
	s_waitcnt lgkmcnt(13)
	v_mfma_f32_16x16x32_f16 v[60:63], v[136:139], v[160:163], v[60:63]
	s_waitcnt lgkmcnt(12)
	v_mfma_f32_16x16x32_f16 v[64:67], v[136:139], v[164:167], v[64:67]
	s_waitcnt lgkmcnt(11)
	v_mfma_f32_16x16x32_f16 v[68:71], v[136:139], v[168:171], v[68:71]
	s_waitcnt lgkmcnt(10)
	v_mfma_f32_16x16x32_f16 v[72:75], v[140:143], v[156:159], v[72:75]
	v_mfma_f32_16x16x32_f16 v[76:79], v[140:143], v[160:163], v[76:79]
	s_add_u32 m0, s28, 0x9000
	s_nop 0
	global_load_lds_dwordx4 v10, s[6:7]
	v_mfma_f32_16x16x32_f16 v[80:83], v[140:143], v[164:167], v[80:83]
	v_mfma_f32_16x16x32_f16 v[84:87], v[140:143], v[168:171], v[84:87]
	s_waitcnt lgkmcnt(9)
	v_mfma_f32_16x16x32_f16 v[88:91], v[144:147], v[156:159], v[88:91]
	v_mfma_f32_16x16x32_f16 v[92:95], v[144:147], v[160:163], v[92:95]
	v_mfma_f32_16x16x32_f16 v[96:99], v[144:147], v[164:167], v[96:99]
	s_add_u32 m0, s28, 0xb000
	s_nop 0
	global_load_lds_dwordx4 v11, s[6:7]
	s_add_u32 s6, s6, s20
	s_addc_u32 s7, s7, 0
	v_mfma_f32_16x16x32_f16 v[100:103], v[144:147], v[168:171], v[100:103]
	s_waitcnt lgkmcnt(8)
	v_mfma_f32_16x16x32_f16 v[104:107], v[148:151], v[156:159], v[104:107]
	v_mfma_f32_16x16x32_f16 v[108:111], v[148:151], v[160:163], v[108:111]
	v_mfma_f32_16x16x32_f16 v[112:115], v[148:151], v[164:167], v[112:115]
	v_mfma_f32_16x16x32_f16 v[116:119], v[148:151], v[168:171], v[116:119]
	s_waitcnt vmcnt(6) lgkmcnt(0)
	s_barrier
	s_waitcnt lgkmcnt(7)
	ds_read_b128 v[136:139], v19
	ds_read_b128 v[156:159], v21
	ds_read_b128 v[160:163], v21 offset:2048
	ds_read_b128 v[164:167], v21 offset:4096
	ds_read_b128 v[168:171], v21 offset:6144
	ds_read_b128 v[140:143], v19 offset:2048
	ds_read_b128 v[144:147], v19 offset:4096
	ds_read_b128 v[148:151], v19 offset:6144
	s_waitcnt lgkmcnt(14)
	v_mfma_f32_16x16x32_f16 v[56:59], v[172:175], v[192:195], v[56:59]
	s_add_u32 m0, s28, 0xd000
	s_nop 0
	global_load_lds_dwordx4 v10, s[4:5]
	s_waitcnt lgkmcnt(13)
	v_mfma_f32_16x16x32_f16 v[60:63], v[172:175], v[196:199], v[60:63]
	s_waitcnt lgkmcnt(12)
	v_mfma_f32_16x16x32_f16 v[64:67], v[172:175], v[200:203], v[64:67]
	s_waitcnt lgkmcnt(11)
	v_mfma_f32_16x16x32_f16 v[68:71], v[172:175], v[204:207], v[68:71]
	s_waitcnt lgkmcnt(10)
	v_mfma_f32_16x16x32_f16 v[72:75], v[176:179], v[192:195], v[72:75]
	v_mfma_f32_16x16x32_f16 v[76:79], v[176:179], v[196:199], v[76:79]
	s_add_u32 m0, s28, 0xf000
	s_nop 0
	global_load_lds_dwordx4 v11, s[4:5]
	v_mfma_f32_16x16x32_f16 v[80:83], v[176:179], v[200:203], v[80:83]
	v_mfma_f32_16x16x32_f16 v[84:87], v[176:179], v[204:207], v[84:87]
	s_waitcnt lgkmcnt(9)
	v_mfma_f32_16x16x32_f16 v[88:91], v[180:183], v[192:195], v[88:91]
	v_mfma_f32_16x16x32_f16 v[92:95], v[180:183], v[196:199], v[92:95]
	v_mfma_f32_16x16x32_f16 v[96:99], v[180:183], v[200:203], v[96:99]
	s_add_u32 m0, s28, 0x11000
	s_nop 0
	global_load_lds_dwordx4 v12, s[4:5]
	v_mfma_f32_16x16x32_f16 v[100:103], v[180:183], v[204:207], v[100:103]
	s_waitcnt lgkmcnt(8)
	v_mfma_f32_16x16x32_f16 v[104:107], v[184:187], v[192:195], v[104:107]
	v_mfma_f32_16x16x32_f16 v[108:111], v[184:187], v[196:199], v[108:111]
	v_mfma_f32_16x16x32_f16 v[112:115], v[184:187], v[200:203], v[112:115]
	v_mfma_f32_16x16x32_f16 v[116:119], v[184:187], v[204:207], v[116:119]
	s_waitcnt lgkmcnt(7)
	ds_read_b128 v[172:175], v20
	ds_read_b128 v[192:195], v22
	ds_read_b128 v[196:199], v22 offset:2048
	ds_read_b128 v[200:203], v22 offset:4096
	ds_read_b128 v[204:207], v22 offset:6144
	ds_read_b128 v[176:179], v20 offset:2048
	ds_read_b128 v[180:183], v20 offset:4096
	ds_read_b128 v[184:187], v20 offset:6144
	s_waitcnt lgkmcnt(14)
	v_mfma_f32_16x16x32_f16 v[56:59], v[136:139], v[156:159], v[56:59]
	s_add_u32 m0, s28, 0x13000
	s_nop 0
	global_load_lds_dwordx4 v13, s[4:5]
	s_add_u32 s4, s4, s20
	s_addc_u32 s5, s5, 0
	s_waitcnt lgkmcnt(13)
	v_mfma_f32_16x16x32_f16 v[60:63], v[136:139], v[160:163], v[60:63]
	s_waitcnt lgkmcnt(12)
	v_mfma_f32_16x16x32_f16 v[64:67], v[136:139], v[164:167], v[64:67]
	s_waitcnt lgkmcnt(11)
	v_mfma_f32_16x16x32_f16 v[68:71], v[136:139], v[168:171], v[68:71]
	s_waitcnt lgkmcnt(10)
	v_mfma_f32_16x16x32_f16 v[72:75], v[140:143], v[156:159], v[72:75]
	v_mfma_f32_16x16x32_f16 v[76:79], v[140:143], v[160:163], v[76:79]
	s_add_u32 m0, s28, 0x16000
	s_nop 0
	global_load_lds_dwordx4 v10, s[6:7]
	v_mfma_f32_16x16x32_f16 v[80:83], v[140:143], v[164:167], v[80:83]
	v_mfma_f32_16x16x32_f16 v[84:87], v[140:143], v[168:171], v[84:87]
	s_waitcnt lgkmcnt(9)
	v_mfma_f32_16x16x32_f16 v[88:91], v[144:147], v[156:159], v[88:91]
	v_mfma_f32_16x16x32_f16 v[92:95], v[144:147], v[160:163], v[92:95]
	v_mfma_f32_16x16x32_f16 v[96:99], v[144:147], v[164:167], v[96:99]
	s_add_u32 m0, s28, 0x18000
	s_nop 0
	global_load_lds_dwordx4 v11, s[6:7]
	s_add_u32 s6, s6, s20
	s_addc_u32 s7, s7, 0
	v_mfma_f32_16x16x32_f16 v[100:103], v[144:147], v[168:171], v[100:103]
	s_waitcnt lgkmcnt(8)
	v_mfma_f32_16x16x32_f16 v[104:107], v[148:151], v[156:159], v[104:107]
	v_mfma_f32_16x16x32_f16 v[108:111], v[148:151], v[160:163], v[108:111]
	v_mfma_f32_16x16x32_f16 v[112:115], v[148:151], v[164:167], v[112:115]
	v_mfma_f32_16x16x32_f16 v[116:119], v[148:151], v[168:171], v[116:119]
	s_waitcnt vmcnt(6) lgkmcnt(0)
	s_barrier
	s_waitcnt lgkmcnt(7)
	ds_read_b128 v[136:139], v15
	ds_read_b128 v[156:159], v17
	ds_read_b128 v[160:163], v17 offset:2048
	ds_read_b128 v[164:167], v17 offset:4096
	ds_read_b128 v[168:171], v17 offset:6144
	ds_read_b128 v[140:143], v15 offset:2048
	ds_read_b128 v[144:147], v15 offset:4096
	ds_read_b128 v[148:151], v15 offset:6144
	s_waitcnt lgkmcnt(14)
	v_mfma_f32_16x16x32_f16 v[56:59], v[172:175], v[192:195], v[56:59]
	s_add_u32 m0, s28, 0x1a000
	s_nop 0
	global_load_lds_dwordx4 v10, s[4:5]
	s_waitcnt lgkmcnt(13)
	v_mfma_f32_16x16x32_f16 v[60:63], v[172:175], v[196:199], v[60:63]
	s_waitcnt lgkmcnt(12)
	v_mfma_f32_16x16x32_f16 v[64:67], v[172:175], v[200:203], v[64:67]
	s_waitcnt lgkmcnt(11)
	v_mfma_f32_16x16x32_f16 v[68:71], v[172:175], v[204:207], v[68:71]
	s_waitcnt lgkmcnt(10)
	v_mfma_f32_16x16x32_f16 v[72:75], v[176:179], v[192:195], v[72:75]
	v_mfma_f32_16x16x32_f16 v[76:79], v[176:179], v[196:199], v[76:79]
	s_add_u32 m0, s28, 0x1c000
	s_nop 0
	global_load_lds_dwordx4 v11, s[4:5]
	v_mfma_f32_16x16x32_f16 v[80:83], v[176:179], v[200:203], v[80:83]
	v_mfma_f32_16x16x32_f16 v[84:87], v[176:179], v[204:207], v[84:87]
	s_waitcnt lgkmcnt(9)
	v_mfma_f32_16x16x32_f16 v[88:91], v[180:183], v[192:195], v[88:91]
	v_mfma_f32_16x16x32_f16 v[92:95], v[180:183], v[196:199], v[92:95]
	v_mfma_f32_16x16x32_f16 v[96:99], v[180:183], v[200:203], v[96:99]
	s_add_u32 m0, s28, 0x1e000
	s_nop 0
	global_load_lds_dwordx4 v12, s[4:5]
	v_mfma_f32_16x16x32_f16 v[100:103], v[180:183], v[204:207], v[100:103]
	s_waitcnt lgkmcnt(8)
	v_mfma_f32_16x16x32_f16 v[104:107], v[184:187], v[192:195], v[104:107]
	v_mfma_f32_16x16x32_f16 v[108:111], v[184:187], v[196:199], v[108:111]
	v_mfma_f32_16x16x32_f16 v[112:115], v[184:187], v[200:203], v[112:115]
	v_mfma_f32_16x16x32_f16 v[116:119], v[184:187], v[204:207], v[116:119]
	s_waitcnt lgkmcnt(7)
	ds_read_b128 v[172:175], v16
	ds_read_b128 v[192:195], v18
	ds_read_b128 v[196:199], v18 offset:2048
	ds_read_b128 v[200:203], v18 offset:4096
	ds_read_b128 v[204:207], v18 offset:6144
	ds_read_b128 v[176:179], v16 offset:2048
	ds_read_b128 v[180:183], v16 offset:4096
	ds_read_b128 v[184:187], v16 offset:6144
	s_waitcnt lgkmcnt(14)
	v_mfma_f32_16x16x32_f16 v[56:59], v[136:139], v[156:159], v[56:59]
	s_add_u32 m0, s28, 0x20000
	s_nop 0
	global_load_lds_dwordx4 v13, s[4:5]
	s_add_u32 s4, s4, s20
	s_addc_u32 s5, s5, 0
	s_waitcnt lgkmcnt(13)
	v_mfma_f32_16x16x32_f16 v[60:63], v[136:139], v[160:163], v[60:63]
	s_waitcnt lgkmcnt(12)
	v_mfma_f32_16x16x32_f16 v[64:67], v[136:139], v[164:167], v[64:67]
	s_waitcnt lgkmcnt(11)
	v_mfma_f32_16x16x32_f16 v[68:71], v[136:139], v[168:171], v[68:71]
	s_waitcnt lgkmcnt(10)
	v_mfma_f32_16x16x32_f16 v[72:75], v[140:143], v[156:159], v[72:75]
	v_mfma_f32_16x16x32_f16 v[76:79], v[140:143], v[160:163], v[76:79]
	s_add_u32 m0, s28, 0x23000
	s_nop 0
	global_load_lds_dwordx4 v10, s[6:7]
	v_mfma_f32_16x16x32_f16 v[80:83], v[140:143], v[164:167], v[80:83]
	v_mfma_f32_16x16x32_f16 v[84:87], v[140:143], v[168:171], v[84:87]
	s_waitcnt lgkmcnt(9)
	v_mfma_f32_16x16x32_f16 v[88:91], v[144:147], v[156:159], v[88:91]
	v_mfma_f32_16x16x32_f16 v[92:95], v[144:147], v[160:163], v[92:95]
	v_mfma_f32_16x16x32_f16 v[96:99], v[144:147], v[164:167], v[96:99]
	s_add_u32 m0, s28, 0x25000
	s_nop 0
	global_load_lds_dwordx4 v11, s[6:7]
	s_add_u32 s6, s6, s20
	s_addc_u32 s7, s7, 0
	v_mfma_f32_16x16x32_f16 v[100:103], v[144:147], v[168:171], v[100:103]
	s_waitcnt lgkmcnt(8)
	v_mfma_f32_16x16x32_f16 v[104:107], v[148:151], v[156:159], v[104:107]
	v_mfma_f32_16x16x32_f16 v[108:111], v[148:151], v[160:163], v[108:111]
	v_mfma_f32_16x16x32_f16 v[112:115], v[148:151], v[164:167], v[112:115]
	v_mfma_f32_16x16x32_f16 v[116:119], v[148:151], v[168:171], v[116:119]
	s_waitcnt vmcnt(6) lgkmcnt(0)
	s_barrier
	s_waitcnt lgkmcnt(7)
	ds_read_b128 v[136:139], v15 offset:53248
	ds_read_b128 v[156:159], v17 offset:53248
	ds_read_b128 v[160:163], v17 offset:55296
	ds_read_b128 v[164:167], v17 offset:57344
	ds_read_b128 v[168:171], v17 offset:59392
	ds_read_b128 v[140:143], v15 offset:55296
	ds_read_b128 v[144:147], v15 offset:57344
	ds_read_b128 v[148:151], v15 offset:59392
	s_waitcnt lgkmcnt(14)
	v_mfma_f32_16x16x32_f16 v[56:59], v[172:175], v[192:195], v[56:59]
	s_add_u32 m0, s28, 0x0
	s_nop 0
	global_load_lds_dwordx4 v10, s[4:5]
	s_waitcnt lgkmcnt(13)
	v_mfma_f32_16x16x32_f16 v[60:63], v[172:175], v[196:199], v[60:63]
	s_waitcnt lgkmcnt(12)
	v_mfma_f32_16x16x32_f16 v[64:67], v[172:175], v[200:203], v[64:67]
	s_waitcnt lgkmcnt(11)
	v_mfma_f32_16x16x32_f16 v[68:71], v[172:175], v[204:207], v[68:71]
	s_waitcnt lgkmcnt(10)
	v_mfma_f32_16x16x32_f16 v[72:75], v[176:179], v[192:195], v[72:75]
	v_mfma_f32_16x16x32_f16 v[76:79], v[176:179], v[196:199], v[76:79]
	s_add_u32 m0, s28, 0x2000
	s_nop 0
	global_load_lds_dwordx4 v11, s[4:5]
	v_mfma_f32_16x16x32_f16 v[80:83], v[176:179], v[200:203], v[80:83]
	v_mfma_f32_16x16x32_f16 v[84:87], v[176:179], v[204:207], v[84:87]
	s_waitcnt lgkmcnt(9)
	v_mfma_f32_16x16x32_f16 v[88:91], v[180:183], v[192:195], v[88:91]
	v_mfma_f32_16x16x32_f16 v[92:95], v[180:183], v[196:199], v[92:95]
	v_mfma_f32_16x16x32_f16 v[96:99], v[180:183], v[200:203], v[96:99]
	s_add_u32 m0, s28, 0x4000
	s_nop 0
	global_load_lds_dwordx4 v12, s[4:5]
	v_mfma_f32_16x16x32_f16 v[100:103], v[180:183], v[204:207], v[100:103]
	s_waitcnt lgkmcnt(8)
	v_mfma_f32_16x16x32_f16 v[104:107], v[184:187], v[192:195], v[104:107]
	v_mfma_f32_16x16x32_f16 v[108:111], v[184:187], v[196:199], v[108:111]
	v_mfma_f32_16x16x32_f16 v[112:115], v[184:187], v[200:203], v[112:115]
	v_mfma_f32_16x16x32_f16 v[116:119], v[184:187], v[204:207], v[116:119]
	s_waitcnt lgkmcnt(7)
	ds_read_b128 v[172:175], v16 offset:53248
	ds_read_b128 v[192:195], v18 offset:53248
	ds_read_b128 v[196:199], v18 offset:55296
	ds_read_b128 v[200:203], v18 offset:57344
	ds_read_b128 v[204:207], v18 offset:59392
	ds_read_b128 v[176:179], v16 offset:55296
	ds_read_b128 v[180:183], v16 offset:57344
	ds_read_b128 v[184:187], v16 offset:59392
	s_waitcnt lgkmcnt(14)
	v_mfma_f32_16x16x32_f16 v[56:59], v[136:139], v[156:159], v[56:59]
	s_add_u32 m0, s28, 0x6000
	s_nop 0
	global_load_lds_dwordx4 v13, s[4:5]
	s_add_u32 s4, s4, s20
	s_addc_u32 s5, s5, 0
	s_waitcnt lgkmcnt(13)
	v_mfma_f32_16x16x32_f16 v[60:63], v[136:139], v[160:163], v[60:63]
	s_waitcnt lgkmcnt(12)
	v_mfma_f32_16x16x32_f16 v[64:67], v[136:139], v[164:167], v[64:67]
	s_waitcnt lgkmcnt(11)
	v_mfma_f32_16x16x32_f16 v[68:71], v[136:139], v[168:171], v[68:71]
	s_waitcnt lgkmcnt(10)
	v_mfma_f32_16x16x32_f16 v[72:75], v[140:143], v[156:159], v[72:75]
	v_mfma_f32_16x16x32_f16 v[76:79], v[140:143], v[160:163], v[76:79]
	s_add_u32 m0, s28, 0x9000
	s_nop 0
	global_load_lds_dwordx4 v10, s[6:7]
	v_mfma_f32_16x16x32_f16 v[80:83], v[140:143], v[164:167], v[80:83]
	v_mfma_f32_16x16x32_f16 v[84:87], v[140:143], v[168:171], v[84:87]
	s_waitcnt lgkmcnt(9)
	v_mfma_f32_16x16x32_f16 v[88:91], v[144:147], v[156:159], v[88:91]
	v_mfma_f32_16x16x32_f16 v[92:95], v[144:147], v[160:163], v[92:95]
	v_mfma_f32_16x16x32_f16 v[96:99], v[144:147], v[164:167], v[96:99]
	s_add_u32 m0, s28, 0xb000
	s_nop 0
	global_load_lds_dwordx4 v11, s[6:7]
	s_add_u32 s6, s6, s20
	s_addc_u32 s7, s7, 0
	v_mfma_f32_16x16x32_f16 v[100:103], v[144:147], v[168:171], v[100:103]
	s_waitcnt lgkmcnt(8)
	v_mfma_f32_16x16x32_f16 v[104:107], v[148:151], v[156:159], v[104:107]
	v_mfma_f32_16x16x32_f16 v[108:111], v[148:151], v[160:163], v[108:111]
	v_mfma_f32_16x16x32_f16 v[112:115], v[148:151], v[164:167], v[112:115]
	v_mfma_f32_16x16x32_f16 v[116:119], v[148:151], v[168:171], v[116:119]
	s_waitcnt vmcnt(6) lgkmcnt(0)
	s_barrier
	s_waitcnt lgkmcnt(7)
	ds_read_b128 v[136:139], v19
	ds_read_b128 v[156:159], v21
	ds_read_b128 v[160:163], v21 offset:2048
	ds_read_b128 v[164:167], v21 offset:4096
	ds_read_b128 v[168:171], v21 offset:6144
	ds_read_b128 v[140:143], v19 offset:2048
	ds_read_b128 v[144:147], v19 offset:4096
	ds_read_b128 v[148:151], v19 offset:6144
	s_waitcnt lgkmcnt(14)
	v_mfma_f32_16x16x32_f16 v[56:59], v[172:175], v[192:195], v[56:59]
	s_add_u32 m0, s28, 0xd000
	s_nop 0
	global_load_lds_dwordx4 v10, s[4:5]
	s_waitcnt lgkmcnt(13)
	v_mfma_f32_16x16x32_f16 v[60:63], v[172:175], v[196:199], v[60:63]
	s_waitcnt lgkmcnt(12)
	v_mfma_f32_16x16x32_f16 v[64:67], v[172:175], v[200:203], v[64:67]
	s_waitcnt lgkmcnt(11)
	v_mfma_f32_16x16x32_f16 v[68:71], v[172:175], v[204:207], v[68:71]
	s_waitcnt lgkmcnt(10)
	v_mfma_f32_16x16x32_f16 v[72:75], v[176:179], v[192:195], v[72:75]
	v_mfma_f32_16x16x32_f16 v[76:79], v[176:179], v[196:199], v[76:79]
	s_add_u32 m0, s28, 0xf000
	s_nop 0
	global_load_lds_dwordx4 v11, s[4:5]
	v_mfma_f32_16x16x32_f16 v[80:83], v[176:179], v[200:203], v[80:83]
	v_mfma_f32_16x16x32_f16 v[84:87], v[176:179], v[204:207], v[84:87]
	s_waitcnt lgkmcnt(9)
	v_mfma_f32_16x16x32_f16 v[88:91], v[180:183], v[192:195], v[88:91]
	v_mfma_f32_16x16x32_f16 v[92:95], v[180:183], v[196:199], v[92:95]
	v_mfma_f32_16x16x32_f16 v[96:99], v[180:183], v[200:203], v[96:99]
	s_add_u32 m0, s28, 0x11000
	s_nop 0
	global_load_lds_dwordx4 v12, s[4:5]
	v_mfma_f32_16x16x32_f16 v[100:103], v[180:183], v[204:207], v[100:103]
	s_waitcnt lgkmcnt(8)
	v_mfma_f32_16x16x32_f16 v[104:107], v[184:187], v[192:195], v[104:107]
	v_mfma_f32_16x16x32_f16 v[108:111], v[184:187], v[196:199], v[108:111]
	v_mfma_f32_16x16x32_f16 v[112:115], v[184:187], v[200:203], v[112:115]
	v_mfma_f32_16x16x32_f16 v[116:119], v[184:187], v[204:207], v[116:119]
	s_waitcnt lgkmcnt(7)
	ds_read_b128 v[172:175], v20
	ds_read_b128 v[192:195], v22
	ds_read_b128 v[196:199], v22 offset:2048
	ds_read_b128 v[200:203], v22 offset:4096
	ds_read_b128 v[204:207], v22 offset:6144
	ds_read_b128 v[176:179], v20 offset:2048
	ds_read_b128 v[180:183], v20 offset:4096
	ds_read_b128 v[184:187], v20 offset:6144
	s_waitcnt lgkmcnt(14)
	v_mfma_f32_16x16x32_f16 v[56:59], v[136:139], v[156:159], v[56:59]
	s_add_u32 m0, s28, 0x13000
	s_nop 0
	global_load_lds_dwordx4 v13, s[4:5]
	s_add_u32 s4, s4, s20
	s_addc_u32 s5, s5, 0
	s_waitcnt lgkmcnt(13)
	v_mfma_f32_16x16x32_f16 v[60:63], v[136:139], v[160:163], v[60:63]
	s_waitcnt lgkmcnt(12)
	v_mfma_f32_16x16x32_f16 v[64:67], v[136:139], v[164:167], v[64:67]
	s_waitcnt lgkmcnt(11)
	v_mfma_f32_16x16x32_f16 v[68:71], v[136:139], v[168:171], v[68:71]
	s_waitcnt lgkmcnt(10)
	v_mfma_f32_16x16x32_f16 v[72:75], v[140:143], v[156:159], v[72:75]
	v_mfma_f32_16x16x32_f16 v[76:79], v[140:143], v[160:163], v[76:79]
	s_add_u32 m0, s28, 0x16000
	s_nop 0
	global_load_lds_dwordx4 v10, s[6:7]
	v_mfma_f32_16x16x32_f16 v[80:83], v[140:143], v[164:167], v[80:83]
	v_mfma_f32_16x16x32_f16 v[84:87], v[140:143], v[168:171], v[84:87]
	s_waitcnt lgkmcnt(9)
	v_mfma_f32_16x16x32_f16 v[88:91], v[144:147], v[156:159], v[88:91]
	v_mfma_f32_16x16x32_f16 v[92:95], v[144:147], v[160:163], v[92:95]
	v_mfma_f32_16x16x32_f16 v[96:99], v[144:147], v[164:167], v[96:99]
	s_add_u32 m0, s28, 0x18000
	s_nop 0
	global_load_lds_dwordx4 v11, s[6:7]
	s_add_u32 s6, s6, s20
	s_addc_u32 s7, s7, 0
	v_mfma_f32_16x16x32_f16 v[100:103], v[144:147], v[168:171], v[100:103]
	s_waitcnt lgkmcnt(8)
	v_mfma_f32_16x16x32_f16 v[104:107], v[148:151], v[156:159], v[104:107]
	v_mfma_f32_16x16x32_f16 v[108:111], v[148:151], v[160:163], v[108:111]
	v_mfma_f32_16x16x32_f16 v[112:115], v[148:151], v[164:167], v[112:115]
	v_mfma_f32_16x16x32_f16 v[116:119], v[148:151], v[168:171], v[116:119]
	s_waitcnt vmcnt(6) lgkmcnt(0)
	s_barrier
	s_waitcnt lgkmcnt(7)
	ds_read_b128 v[136:139], v15
	ds_read_b128 v[156:159], v17
	ds_read_b128 v[160:163], v17 offset:2048
	ds_read_b128 v[164:167], v17 offset:4096
	ds_read_b128 v[168:171], v17 offset:6144
	ds_read_b128 v[140:143], v15 offset:2048
	ds_read_b128 v[144:147], v15 offset:4096
	ds_read_b128 v[148:151], v15 offset:6144
	s_waitcnt lgkmcnt(14)
	v_mfma_f32_16x16x32_f16 v[56:59], v[172:175], v[192:195], v[56:59]
	s_add_u32 m0, s28, 0x1a000
	s_nop 0
	global_load_lds_dwordx4 v10, s[4:5]
	s_waitcnt lgkmcnt(13)
	v_mfma_f32_16x16x32_f16 v[60:63], v[172:175], v[196:199], v[60:63]
	s_waitcnt lgkmcnt(12)
	v_mfma_f32_16x16x32_f16 v[64:67], v[172:175], v[200:203], v[64:67]
	s_waitcnt lgkmcnt(11)
	v_mfma_f32_16x16x32_f16 v[68:71], v[172:175], v[204:207], v[68:71]
	s_waitcnt lgkmcnt(10)
	v_mfma_f32_16x16x32_f16 v[72:75], v[176:179], v[192:195], v[72:75]
	v_mfma_f32_16x16x32_f16 v[76:79], v[176:179], v[196:199], v[76:79]
	s_add_u32 m0, s28, 0x1c000
	s_nop 0
	global_load_lds_dwordx4 v11, s[4:5]
	v_mfma_f32_16x16x32_f16 v[80:83], v[176:179], v[200:203], v[80:83]
	v_mfma_f32_16x16x32_f16 v[84:87], v[176:179], v[204:207], v[84:87]
	s_waitcnt lgkmcnt(9)
	v_mfma_f32_16x16x32_f16 v[88:91], v[180:183], v[192:195], v[88:91]
	v_mfma_f32_16x16x32_f16 v[92:95], v[180:183], v[196:199], v[92:95]
	v_mfma_f32_16x16x32_f16 v[96:99], v[180:183], v[200:203], v[96:99]
	s_add_u32 m0, s28, 0x1e000
	s_nop 0
	global_load_lds_dwordx4 v12, s[4:5]
	v_mfma_f32_16x16x32_f16 v[100:103], v[180:183], v[204:207], v[100:103]
	s_waitcnt lgkmcnt(8)
	v_mfma_f32_16x16x32_f16 v[104:107], v[184:187], v[192:195], v[104:107]
	v_mfma_f32_16x16x32_f16 v[108:111], v[184:187], v[196:199], v[108:111]
	v_mfma_f32_16x16x32_f16 v[112:115], v[184:187], v[200:203], v[112:115]
	v_mfma_f32_16x16x32_f16 v[116:119], v[184:187], v[204:207], v[116:119]
	s_waitcnt lgkmcnt(7)
	ds_read_b128 v[172:175], v16
	ds_read_b128 v[192:195], v18
	ds_read_b128 v[196:199], v18 offset:2048
	ds_read_b128 v[200:203], v18 offset:4096
	ds_read_b128 v[204:207], v18 offset:6144
	ds_read_b128 v[176:179], v16 offset:2048
	ds_read_b128 v[180:183], v16 offset:4096
	ds_read_b128 v[184:187], v16 offset:6144
	s_waitcnt lgkmcnt(14)
	v_mfma_f32_16x16x32_f16 v[56:59], v[136:139], v[156:159], v[56:59]
	s_add_u32 m0, s28, 0x20000
	s_nop 0
	global_load_lds_dwordx4 v13, s[4:5]
	s_add_u32 s4, s4, s20
	s_addc_u32 s5, s5, 0
	s_waitcnt lgkmcnt(13)
	v_mfma_f32_16x16x32_f16 v[60:63], v[136:139], v[160:163], v[60:63]
	s_waitcnt lgkmcnt(12)
	v_mfma_f32_16x16x32_f16 v[64:67], v[136:139], v[164:167], v[64:67]
	s_waitcnt lgkmcnt(11)
	v_mfma_f32_16x16x32_f16 v[68:71], v[136:139], v[168:171], v[68:71]
	s_waitcnt lgkmcnt(10)
	v_mfma_f32_16x16x32_f16 v[72:75], v[140:143], v[156:159], v[72:75]
	v_mfma_f32_16x16x32_f16 v[76:79], v[140:143], v[160:163], v[76:79]
	s_add_u32 m0, s28, 0x23000
	s_nop 0
	global_load_lds_dwordx4 v10, s[6:7]
	v_mfma_f32_16x16x32_f16 v[80:83], v[140:143], v[164:167], v[80:83]
	v_mfma_f32_16x16x32_f16 v[84:87], v[140:143], v[168:171], v[84:87]
	s_waitcnt lgkmcnt(9)
	v_mfma_f32_16x16x32_f16 v[88:91], v[144:147], v[156:159], v[88:91]
	v_mfma_f32_16x16x32_f16 v[92:95], v[144:147], v[160:163], v[92:95]
	v_mfma_f32_16x16x32_f16 v[96:99], v[144:147], v[164:167], v[96:99]
	s_add_u32 m0, s28, 0x25000
	s_nop 0
	global_load_lds_dwordx4 v11, s[6:7]
	s_add_u32 s6, s6, s20
	s_addc_u32 s7, s7, 0
	v_mfma_f32_16x16x32_f16 v[100:103], v[144:147], v[168:171], v[100:103]
	s_waitcnt lgkmcnt(8)
	v_mfma_f32_16x16x32_f16 v[104:107], v[148:151], v[156:159], v[104:107]
	v_mfma_f32_16x16x32_f16 v[108:111], v[148:151], v[160:163], v[108:111]
	v_mfma_f32_16x16x32_f16 v[112:115], v[148:151], v[164:167], v[112:115]
	v_mfma_f32_16x16x32_f16 v[116:119], v[148:151], v[168:171], v[116:119]
	s_waitcnt vmcnt(6) lgkmcnt(0)
	s_barrier
	s_waitcnt lgkmcnt(7)
	ds_read_b128 v[136:139], v15 offset:53248
	ds_read_b128 v[156:159], v17 offset:53248
	ds_read_b128 v[160:163], v17 offset:55296
	ds_read_b128 v[164:167], v17 offset:57344
	ds_read_b128 v[168:171], v17 offset:59392
	ds_read_b128 v[140:143], v15 offset:55296
	ds_read_b128 v[144:147], v15 offset:57344
	ds_read_b128 v[148:151], v15 offset:59392
	s_waitcnt lgkmcnt(14)
	v_mfma_f32_16x16x32_f16 v[56:59], v[172:175], v[192:195], v[56:59]
	s_add_u32 m0, s28, 0x0
	s_nop 0
	global_load_lds_dwordx4 v10, s[4:5]
	s_waitcnt lgkmcnt(13)
	v_mfma_f32_16x16x32_f16 v[60:63], v[172:175], v[196:199], v[60:63]
	s_waitcnt lgkmcnt(12)
	v_mfma_f32_16x16x32_f16 v[64:67], v[172:175], v[200:203], v[64:67]
	s_waitcnt lgkmcnt(11)
	v_mfma_f32_16x16x32_f16 v[68:71], v[172:175], v[204:207], v[68:71]
	s_waitcnt lgkmcnt(10)
	v_mfma_f32_16x16x32_f16 v[72:75], v[176:179], v[192:195], v[72:75]
	v_mfma_f32_16x16x32_f16 v[76:79], v[176:179], v[196:199], v[76:79]
	s_add_u32 m0, s28, 0x2000
	s_nop 0
	global_load_lds_dwordx4 v11, s[4:5]
	v_mfma_f32_16x16x32_f16 v[80:83], v[176:179], v[200:203], v[80:83]
	v_mfma_f32_16x16x32_f16 v[84:87], v[176:179], v[204:207], v[84:87]
	s_waitcnt lgkmcnt(9)
	v_mfma_f32_16x16x32_f16 v[88:91], v[180:183], v[192:195], v[88:91]
	v_mfma_f32_16x16x32_f16 v[92:95], v[180:183], v[196:199], v[92:95]
	v_mfma_f32_16x16x32_f16 v[96:99], v[180:183], v[200:203], v[96:99]
	s_add_u32 m0, s28, 0x4000
	s_nop 0
	global_load_lds_dwordx4 v12, s[4:5]
	v_mfma_f32_16x16x32_f16 v[100:103], v[180:183], v[204:207], v[100:103]
	s_waitcnt lgkmcnt(8)
	v_mfma_f32_16x16x32_f16 v[104:107], v[184:187], v[192:195], v[104:107]
	v_mfma_f32_16x16x32_f16 v[108:111], v[184:187], v[196:199], v[108:111]
	v_mfma_f32_16x16x32_f16 v[112:115], v[184:187], v[200:203], v[112:115]
	v_mfma_f32_16x16x32_f16 v[116:119], v[184:187], v[204:207], v[116:119]
	s_waitcnt lgkmcnt(7)
	ds_read_b128 v[172:175], v16 offset:53248
	ds_read_b128 v[192:195], v18 offset:53248
	ds_read_b128 v[196:199], v18 offset:55296
	ds_read_b128 v[200:203], v18 offset:57344
	ds_read_b128 v[204:207], v18 offset:59392
	ds_read_b128 v[176:179], v16 offset:55296
	ds_read_b128 v[180:183], v16 offset:57344
	ds_read_b128 v[184:187], v16 offset:59392
	s_waitcnt lgkmcnt(14)
	v_mfma_f32_16x16x32_f16 v[56:59], v[136:139], v[156:159], v[56:59]
	s_add_u32 m0, s28, 0x6000
	s_nop 0
	global_load_lds_dwordx4 v13, s[4:5]
	s_add_u32 s4, s4, s20
	s_addc_u32 s5, s5, 0
	s_waitcnt lgkmcnt(13)
	v_mfma_f32_16x16x32_f16 v[60:63], v[136:139], v[160:163], v[60:63]
	s_waitcnt lgkmcnt(12)
	v_mfma_f32_16x16x32_f16 v[64:67], v[136:139], v[164:167], v[64:67]
	s_waitcnt lgkmcnt(11)
	v_mfma_f32_16x16x32_f16 v[68:71], v[136:139], v[168:171], v[68:71]
	s_waitcnt lgkmcnt(10)
	v_mfma_f32_16x16x32_f16 v[72:75], v[140:143], v[156:159], v[72:75]
	v_mfma_f32_16x16x32_f16 v[76:79], v[140:143], v[160:163], v[76:79]
	s_add_u32 m0, s28, 0x9000
	s_nop 0
	global_load_lds_dwordx4 v10, s[6:7]
	v_mfma_f32_16x16x32_f16 v[80:83], v[140:143], v[164:167], v[80:83]
	v_mfma_f32_16x16x32_f16 v[84:87], v[140:143], v[168:171], v[84:87]
	s_waitcnt lgkmcnt(9)
	v_mfma_f32_16x16x32_f16 v[88:91], v[144:147], v[156:159], v[88:91]
	v_mfma_f32_16x16x32_f16 v[92:95], v[144:147], v[160:163], v[92:95]
	v_mfma_f32_16x16x32_f16 v[96:99], v[144:147], v[164:167], v[96:99]
	s_add_u32 m0, s28, 0xb000
	s_nop 0
	global_load_lds_dwordx4 v11, s[6:7]
	s_add_u32 s6, s6, s20
	s_addc_u32 s7, s7, 0
	v_mfma_f32_16x16x32_f16 v[100:103], v[144:147], v[168:171], v[100:103]
	s_waitcnt lgkmcnt(8)
	v_mfma_f32_16x16x32_f16 v[104:107], v[148:151], v[156:159], v[104:107]
	v_mfma_f32_16x16x32_f16 v[108:111], v[148:151], v[160:163], v[108:111]
	v_mfma_f32_16x16x32_f16 v[112:115], v[148:151], v[164:167], v[112:115]
	v_mfma_f32_16x16x32_f16 v[116:119], v[148:151], v[168:171], v[116:119]
	s_waitcnt vmcnt(6) lgkmcnt(0)
	s_barrier
	s_waitcnt lgkmcnt(7)
	ds_read_b128 v[136:139], v19
	ds_read_b128 v[156:159], v21
	ds_read_b128 v[160:163], v21 offset:2048
	ds_read_b128 v[164:167], v21 offset:4096
	ds_read_b128 v[168:171], v21 offset:6144
	ds_read_b128 v[140:143], v19 offset:2048
	ds_read_b128 v[144:147], v19 offset:4096
	ds_read_b128 v[148:151], v19 offset:6144
	s_waitcnt lgkmcnt(14)
	v_mfma_f32_16x16x32_f16 v[56:59], v[172:175], v[192:195], v[56:59]
	s_add_u32 m0, s28, 0xd000
	s_nop 0
	global_load_lds_dwordx4 v10, s[4:5]
	s_waitcnt lgkmcnt(13)
	v_mfma_f32_16x16x32_f16 v[60:63], v[172:175], v[196:199], v[60:63]
	s_waitcnt lgkmcnt(12)
	v_mfma_f32_16x16x32_f16 v[64:67], v[172:175], v[200:203], v[64:67]
	s_waitcnt lgkmcnt(11)
	v_mfma_f32_16x16x32_f16 v[68:71], v[172:175], v[204:207], v[68:71]
	s_waitcnt lgkmcnt(10)
	v_mfma_f32_16x16x32_f16 v[72:75], v[176:179], v[192:195], v[72:75]
	v_mfma_f32_16x16x32_f16 v[76:79], v[176:179], v[196:199], v[76:79]
	s_add_u32 m0, s28, 0xf000
	s_nop 0
	global_load_lds_dwordx4 v11, s[4:5]
	v_mfma_f32_16x16x32_f16 v[80:83], v[176:179], v[200:203], v[80:83]
	v_mfma_f32_16x16x32_f16 v[84:87], v[176:179], v[204:207], v[84:87]
	s_waitcnt lgkmcnt(9)
	v_mfma_f32_16x16x32_f16 v[88:91], v[180:183], v[192:195], v[88:91]
	v_mfma_f32_16x16x32_f16 v[92:95], v[180:183], v[196:199], v[92:95]
	v_mfma_f32_16x16x32_f16 v[96:99], v[180:183], v[200:203], v[96:99]
	s_add_u32 m0, s28, 0x11000
	s_nop 0
	global_load_lds_dwordx4 v12, s[4:5]
	v_mfma_f32_16x16x32_f16 v[100:103], v[180:183], v[204:207], v[100:103]
	s_waitcnt lgkmcnt(8)
	v_mfma_f32_16x16x32_f16 v[104:107], v[184:187], v[192:195], v[104:107]
	v_mfma_f32_16x16x32_f16 v[108:111], v[184:187], v[196:199], v[108:111]
	v_mfma_f32_16x16x32_f16 v[112:115], v[184:187], v[200:203], v[112:115]
	v_mfma_f32_16x16x32_f16 v[116:119], v[184:187], v[204:207], v[116:119]
	s_waitcnt lgkmcnt(7)
	ds_read_b128 v[172:175], v20
	ds_read_b128 v[192:195], v22
	ds_read_b128 v[196:199], v22 offset:2048
	ds_read_b128 v[200:203], v22 offset:4096
	ds_read_b128 v[204:207], v22 offset:6144
	ds_read_b128 v[176:179], v20 offset:2048
	ds_read_b128 v[180:183], v20 offset:4096
	ds_read_b128 v[184:187], v20 offset:6144
	s_waitcnt lgkmcnt(14)
	v_mfma_f32_16x16x32_f16 v[56:59], v[136:139], v[156:159], v[56:59]
	s_add_u32 m0, s28, 0x13000
	s_nop 0
	global_load_lds_dwordx4 v13, s[4:5]
	s_add_u32 s4, s4, s20
	s_addc_u32 s5, s5, 0
	s_waitcnt lgkmcnt(13)
	v_mfma_f32_16x16x32_f16 v[60:63], v[136:139], v[160:163], v[60:63]
	s_waitcnt lgkmcnt(12)
	v_mfma_f32_16x16x32_f16 v[64:67], v[136:139], v[164:167], v[64:67]
	s_waitcnt lgkmcnt(11)
	v_mfma_f32_16x16x32_f16 v[68:71], v[136:139], v[168:171], v[68:71]
	s_waitcnt lgkmcnt(10)
	v_mfma_f32_16x16x32_f16 v[72:75], v[140:143], v[156:159], v[72:75]
	v_mfma_f32_16x16x32_f16 v[76:79], v[140:143], v[160:163], v[76:79]
	s_add_u32 m0, s28, 0x16000
	s_nop 0
	global_load_lds_dwordx4 v10, s[6:7]
	v_mfma_f32_16x16x32_f16 v[80:83], v[140:143], v[164:167], v[80:83]
	v_mfma_f32_16x16x32_f16 v[84:87], v[140:143], v[168:171], v[84:87]
	s_waitcnt lgkmcnt(9)
	v_mfma_f32_16x16x32_f16 v[88:91], v[144:147], v[156:159], v[88:91]
	v_mfma_f32_16x16x32_f16 v[92:95], v[144:147], v[160:163], v[92:95]
	v_mfma_f32_16x16x32_f16 v[96:99], v[144:147], v[164:167], v[96:99]
	s_add_u32 m0, s28, 0x18000
	s_nop 0
	global_load_lds_dwordx4 v11, s[6:7]
	s_add_u32 s6, s6, s20
	s_addc_u32 s7, s7, 0
	v_mfma_f32_16x16x32_f16 v[100:103], v[144:147], v[168:171], v[100:103]
	s_waitcnt lgkmcnt(8)
	v_mfma_f32_16x16x32_f16 v[104:107], v[148:151], v[156:159], v[104:107]
	v_mfma_f32_16x16x32_f16 v[108:111], v[148:151], v[160:163], v[108:111]
	v_mfma_f32_16x16x32_f16 v[112:115], v[148:151], v[164:167], v[112:115]
	v_mfma_f32_16x16x32_f16 v[116:119], v[148:151], v[168:171], v[116:119]
	s_waitcnt vmcnt(6) lgkmcnt(0)
	s_barrier
	s_waitcnt lgkmcnt(7)
	ds_read_b128 v[136:139], v15
	ds_read_b128 v[156:159], v17
	ds_read_b128 v[160:163], v17 offset:2048
	ds_read_b128 v[164:167], v17 offset:4096
	ds_read_b128 v[168:171], v17 offset:6144
	ds_read_b128 v[140:143], v15 offset:2048
	ds_read_b128 v[144:147], v15 offset:4096
	ds_read_b128 v[148:151], v15 offset:6144
	s_waitcnt lgkmcnt(14)
	v_mfma_f32_16x16x32_f16 v[56:59], v[172:175], v[192:195], v[56:59]
	s_add_u32 m0, s28, 0x1a000
	s_nop 0
	global_load_lds_dwordx4 v10, s[4:5]
	s_waitcnt lgkmcnt(13)
	v_mfma_f32_16x16x32_f16 v[60:63], v[172:175], v[196:199], v[60:63]
	s_waitcnt lgkmcnt(12)
	v_mfma_f32_16x16x32_f16 v[64:67], v[172:175], v[200:203], v[64:67]
	s_waitcnt lgkmcnt(11)
	v_mfma_f32_16x16x32_f16 v[68:71], v[172:175], v[204:207], v[68:71]
	s_waitcnt lgkmcnt(10)
	v_mfma_f32_16x16x32_f16 v[72:75], v[176:179], v[192:195], v[72:75]
	v_mfma_f32_16x16x32_f16 v[76:79], v[176:179], v[196:199], v[76:79]
	s_add_u32 m0, s28, 0x1c000
	s_nop 0
	global_load_lds_dwordx4 v11, s[4:5]
	v_mfma_f32_16x16x32_f16 v[80:83], v[176:179], v[200:203], v[80:83]
	v_mfma_f32_16x16x32_f16 v[84:87], v[176:179], v[204:207], v[84:87]
	s_waitcnt lgkmcnt(9)
	v_mfma_f32_16x16x32_f16 v[88:91], v[180:183], v[192:195], v[88:91]
	v_mfma_f32_16x16x32_f16 v[92:95], v[180:183], v[196:199], v[92:95]
	v_mfma_f32_16x16x32_f16 v[96:99], v[180:183], v[200:203], v[96:99]
	s_add_u32 m0, s28, 0x1e000
	s_nop 0
	global_load_lds_dwordx4 v12, s[4:5]
	v_mfma_f32_16x16x32_f16 v[100:103], v[180:183], v[204:207], v[100:103]
	s_waitcnt lgkmcnt(8)
	v_mfma_f32_16x16x32_f16 v[104:107], v[184:187], v[192:195], v[104:107]
	v_mfma_f32_16x16x32_f16 v[108:111], v[184:187], v[196:199], v[108:111]
	v_mfma_f32_16x16x32_f16 v[112:115], v[184:187], v[200:203], v[112:115]
	v_mfma_f32_16x16x32_f16 v[116:119], v[184:187], v[204:207], v[116:119]
	s_waitcnt lgkmcnt(7)
	ds_read_b128 v[172:175], v16
	ds_read_b128 v[192:195], v18
	ds_read_b128 v[196:199], v18 offset:2048
	ds_read_b128 v[200:203], v18 offset:4096
	ds_read_b128 v[204:207], v18 offset:6144
	ds_read_b128 v[176:179], v16 offset:2048
	ds_read_b128 v[180:183], v16 offset:4096
	ds_read_b128 v[184:187], v16 offset:6144
	s_waitcnt lgkmcnt(14)
	v_mfma_f32_16x16x32_f16 v[56:59], v[136:139], v[156:159], v[56:59]
	s_add_u32 m0, s28, 0x20000
	s_nop 0
	global_load_lds_dwordx4 v13, s[4:5]
	s_add_u32 s4, s4, s20
	s_addc_u32 s5, s5, 0
	s_waitcnt lgkmcnt(13)
	v_mfma_f32_16x16x32_f16 v[60:63], v[136:139], v[160:163], v[60:63]
	s_waitcnt lgkmcnt(12)
	v_mfma_f32_16x16x32_f16 v[64:67], v[136:139], v[164:167], v[64:67]
	s_waitcnt lgkmcnt(11)
	v_mfma_f32_16x16x32_f16 v[68:71], v[136:139], v[168:171], v[68:71]
	s_waitcnt lgkmcnt(10)
	v_mfma_f32_16x16x32_f16 v[72:75], v[140:143], v[156:159], v[72:75]
	v_mfma_f32_16x16x32_f16 v[76:79], v[140:143], v[160:163], v[76:79]
	s_add_u32 m0, s28, 0x23000
	s_nop 0
	global_load_lds_dwordx4 v10, s[6:7]
	v_mfma_f32_16x16x32_f16 v[80:83], v[140:143], v[164:167], v[80:83]
	v_mfma_f32_16x16x32_f16 v[84:87], v[140:143], v[168:171], v[84:87]
	s_waitcnt lgkmcnt(9)
	v_mfma_f32_16x16x32_f16 v[88:91], v[144:147], v[156:159], v[88:91]
	v_mfma_f32_16x16x32_f16 v[92:95], v[144:147], v[160:163], v[92:95]
	v_mfma_f32_16x16x32_f16 v[96:99], v[144:147], v[164:167], v[96:99]
	s_add_u32 m0, s28, 0x25000
	s_nop 0
	global_load_lds_dwordx4 v11, s[6:7]
	s_add_u32 s6, s6, s20
	s_addc_u32 s7, s7, 0
	v_mfma_f32_16x16x32_f16 v[100:103], v[144:147], v[168:171], v[100:103]
	s_waitcnt lgkmcnt(8)
	v_mfma_f32_16x16x32_f16 v[104:107], v[148:151], v[156:159], v[104:107]
	v_mfma_f32_16x16x32_f16 v[108:111], v[148:151], v[160:163], v[108:111]
	v_mfma_f32_16x16x32_f16 v[112:115], v[148:151], v[164:167], v[112:115]
	v_mfma_f32_16x16x32_f16 v[116:119], v[148:151], v[168:171], v[116:119]
	s_waitcnt vmcnt(6) lgkmcnt(0)
	s_barrier
	s_waitcnt lgkmcnt(7)
	ds_read_b128 v[136:139], v15 offset:53248
	ds_read_b128 v[156:159], v17 offset:53248
	ds_read_b128 v[160:163], v17 offset:55296
	ds_read_b128 v[164:167], v17 offset:57344
	ds_read_b128 v[168:171], v17 offset:59392
	ds_read_b128 v[140:143], v15 offset:55296
	ds_read_b128 v[144:147], v15 offset:57344
	ds_read_b128 v[148:151], v15 offset:59392
	s_waitcnt lgkmcnt(14)
	v_mfma_f32_16x16x32_f16 v[56:59], v[172:175], v[192:195], v[56:59]
	s_add_u32 m0, s28, 0x0
	s_nop 0
	global_load_lds_dwordx4 v10, s[4:5]
	s_waitcnt lgkmcnt(13)
	v_mfma_f32_16x16x32_f16 v[60:63], v[172:175], v[196:199], v[60:63]
	s_waitcnt lgkmcnt(12)
	v_mfma_f32_16x16x32_f16 v[64:67], v[172:175], v[200:203], v[64:67]
	s_waitcnt lgkmcnt(11)
	v_mfma_f32_16x16x32_f16 v[68:71], v[172:175], v[204:207], v[68:71]
	s_waitcnt lgkmcnt(10)
	v_mfma_f32_16x16x32_f16 v[72:75], v[176:179], v[192:195], v[72:75]
	v_mfma_f32_16x16x32_f16 v[76:79], v[176:179], v[196:199], v[76:79]
	s_add_u32 m0, s28, 0x2000
	s_nop 0
	global_load_lds_dwordx4 v11, s[4:5]
	v_mfma_f32_16x16x32_f16 v[80:83], v[176:179], v[200:203], v[80:83]
	v_mfma_f32_16x16x32_f16 v[84:87], v[176:179], v[204:207], v[84:87]
	s_waitcnt lgkmcnt(9)
	v_mfma_f32_16x16x32_f16 v[88:91], v[180:183], v[192:195], v[88:91]
	v_mfma_f32_16x16x32_f16 v[92:95], v[180:183], v[196:199], v[92:95]
	v_mfma_f32_16x16x32_f16 v[96:99], v[180:183], v[200:203], v[96:99]
	s_add_u32 m0, s28, 0x4000
	s_nop 0
	global_load_lds_dwordx4 v12, s[4:5]
	v_mfma_f32_16x16x32_f16 v[100:103], v[180:183], v[204:207], v[100:103]
	s_waitcnt lgkmcnt(8)
	v_mfma_f32_16x16x32_f16 v[104:107], v[184:187], v[192:195], v[104:107]
	v_mfma_f32_16x16x32_f16 v[108:111], v[184:187], v[196:199], v[108:111]
	v_mfma_f32_16x16x32_f16 v[112:115], v[184:187], v[200:203], v[112:115]
	v_mfma_f32_16x16x32_f16 v[116:119], v[184:187], v[204:207], v[116:119]
	s_waitcnt lgkmcnt(7)
	ds_read_b128 v[172:175], v16 offset:53248
	ds_read_b128 v[192:195], v18 offset:53248
	ds_read_b128 v[196:199], v18 offset:55296
	ds_read_b128 v[200:203], v18 offset:57344
	ds_read_b128 v[204:207], v18 offset:59392
	ds_read_b128 v[176:179], v16 offset:55296
	ds_read_b128 v[180:183], v16 offset:57344
	ds_read_b128 v[184:187], v16 offset:59392
	s_waitcnt lgkmcnt(14)
	v_mfma_f32_16x16x32_f16 v[56:59], v[136:139], v[156:159], v[56:59]
	s_add_u32 m0, s28, 0x6000
	s_nop 0
	global_load_lds_dwordx4 v13, s[4:5]
	s_add_u32 s4, s4, s20
	s_addc_u32 s5, s5, 0
	s_waitcnt lgkmcnt(13)
	v_mfma_f32_16x16x32_f16 v[60:63], v[136:139], v[160:163], v[60:63]
	s_waitcnt lgkmcnt(12)
	v_mfma_f32_16x16x32_f16 v[64:67], v[136:139], v[164:167], v[64:67]
	s_waitcnt lgkmcnt(11)
	v_mfma_f32_16x16x32_f16 v[68:71], v[136:139], v[168:171], v[68:71]
	s_waitcnt lgkmcnt(10)
	v_mfma_f32_16x16x32_f16 v[72:75], v[140:143], v[156:159], v[72:75]
	v_mfma_f32_16x16x32_f16 v[76:79], v[140:143], v[160:163], v[76:79]
	s_add_u32 m0, s28, 0x9000
	s_nop 0
	global_load_lds_dwordx4 v10, s[6:7]
	v_mfma_f32_16x16x32_f16 v[80:83], v[140:143], v[164:167], v[80:83]
	v_mfma_f32_16x16x32_f16 v[84:87], v[140:143], v[168:171], v[84:87]
	s_waitcnt lgkmcnt(9)
	v_mfma_f32_16x16x32_f16 v[88:91], v[144:147], v[156:159], v[88:91]
	v_mfma_f32_16x16x32_f16 v[92:95], v[144:147], v[160:163], v[92:95]
	v_mfma_f32_16x16x32_f16 v[96:99], v[144:147], v[164:167], v[96:99]
	s_add_u32 m0, s28, 0xb000
	s_nop 0
	global_load_lds_dwordx4 v11, s[6:7]
	s_add_u32 s6, s6, s20
	s_addc_u32 s7, s7, 0
	v_mfma_f32_16x16x32_f16 v[100:103], v[144:147], v[168:171], v[100:103]
	s_waitcnt lgkmcnt(8)
	v_mfma_f32_16x16x32_f16 v[104:107], v[148:151], v[156:159], v[104:107]
	v_mfma_f32_16x16x32_f16 v[108:111], v[148:151], v[160:163], v[108:111]
	v_mfma_f32_16x16x32_f16 v[112:115], v[148:151], v[164:167], v[112:115]
	v_mfma_f32_16x16x32_f16 v[116:119], v[148:151], v[168:171], v[116:119]
	s_waitcnt vmcnt(6) lgkmcnt(0)
	s_barrier
	s_waitcnt lgkmcnt(7)
	ds_read_b128 v[136:139], v19
	ds_read_b128 v[156:159], v21
	ds_read_b128 v[160:163], v21 offset:2048
	ds_read_b128 v[164:167], v21 offset:4096
	ds_read_b128 v[168:171], v21 offset:6144
	ds_read_b128 v[140:143], v19 offset:2048
	ds_read_b128 v[144:147], v19 offset:4096
	ds_read_b128 v[148:151], v19 offset:6144
	s_waitcnt lgkmcnt(14)
	v_mfma_f32_16x16x32_f16 v[56:59], v[172:175], v[192:195], v[56:59]
	s_waitcnt lgkmcnt(13)
	v_mfma_f32_16x16x32_f16 v[60:63], v[172:175], v[196:199], v[60:63]
	s_waitcnt lgkmcnt(12)
	v_mfma_f32_16x16x32_f16 v[64:67], v[172:175], v[200:203], v[64:67]
	s_waitcnt lgkmcnt(11)
	v_mfma_f32_16x16x32_f16 v[68:71], v[172:175], v[204:207], v[68:71]
	s_waitcnt lgkmcnt(10)
	v_mfma_f32_16x16x32_f16 v[72:75], v[176:179], v[192:195], v[72:75]
	v_mfma_f32_16x16x32_f16 v[76:79], v[176:179], v[196:199], v[76:79]
	v_mfma_f32_16x16x32_f16 v[80:83], v[176:179], v[200:203], v[80:83]
	v_mfma_f32_16x16x32_f16 v[84:87], v[176:179], v[204:207], v[84:87]
	s_waitcnt lgkmcnt(9)
	v_mfma_f32_16x16x32_f16 v[88:91], v[180:183], v[192:195], v[88:91]
	v_mfma_f32_16x16x32_f16 v[92:95], v[180:183], v[196:199], v[92:95]
	v_mfma_f32_16x16x32_f16 v[96:99], v[180:183], v[200:203], v[96:99]
	v_mfma_f32_16x16x32_f16 v[100:103], v[180:183], v[204:207], v[100:103]
	s_waitcnt lgkmcnt(8)
	v_mfma_f32_16x16x32_f16 v[104:107], v[184:187], v[192:195], v[104:107]
	v_mfma_f32_16x16x32_f16 v[108:111], v[184:187], v[196:199], v[108:111]
	v_mfma_f32_16x16x32_f16 v[112:115], v[184:187], v[200:203], v[112:115]
	v_mfma_f32_16x16x32_f16 v[116:119], v[184:187], v[204:207], v[116:119]
	s_waitcnt lgkmcnt(7)
	ds_read_b128 v[172:175], v20
	ds_read_b128 v[192:195], v22
	ds_read_b128 v[196:199], v22 offset:2048
	ds_read_b128 v[200:203], v22 offset:4096
	ds_read_b128 v[204:207], v22 offset:6144
	ds_read_b128 v[176:179], v20 offset:2048
	ds_read_b128 v[180:183], v20 offset:4096
	ds_read_b128 v[184:187], v20 offset:6144
	s_waitcnt lgkmcnt(14)
	v_mfma_f32_16x16x32_f16 v[56:59], v[136:139], v[156:159], v[56:59]
	s_waitcnt lgkmcnt(13)
	v_mfma_f32_16x16x32_f16 v[60:63], v[136:139], v[160:163], v[60:63]
	s_waitcnt lgkmcnt(12)
	v_mfma_f32_16x16x32_f16 v[64:67], v[136:139], v[164:167], v[64:67]
	s_waitcnt lgkmcnt(11)
	v_mfma_f32_16x16x32_f16 v[68:71], v[136:139], v[168:171], v[68:71]
	s_waitcnt lgkmcnt(10)
	v_mfma_f32_16x16x32_f16 v[72:75], v[140:143], v[156:159], v[72:75]
	v_mfma_f32_16x16x32_f16 v[76:79], v[140:143], v[160:163], v[76:79]
	v_mfma_f32_16x16x32_f16 v[80:83], v[140:143], v[164:167], v[80:83]
	v_mfma_f32_16x16x32_f16 v[84:87], v[140:143], v[168:171], v[84:87]
	s_waitcnt lgkmcnt(9)
	v_mfma_f32_16x16x32_f16 v[88:91], v[144:147], v[156:159], v[88:91]
	v_mfma_f32_16x16x32_f16 v[92:95], v[144:147], v[160:163], v[92:95]
	v_mfma_f32_16x16x32_f16 v[96:99], v[144:147], v[164:167], v[96:99]
	v_mfma_f32_16x16x32_f16 v[100:103], v[144:147], v[168:171], v[100:103]
	s_waitcnt lgkmcnt(8)
	v_mfma_f32_16x16x32_f16 v[104:107], v[148:151], v[156:159], v[104:107]
	v_mfma_f32_16x16x32_f16 v[108:111], v[148:151], v[160:163], v[108:111]
	v_mfma_f32_16x16x32_f16 v[112:115], v[148:151], v[164:167], v[112:115]
	v_mfma_f32_16x16x32_f16 v[116:119], v[148:151], v[168:171], v[116:119]
	s_waitcnt vmcnt(0) lgkmcnt(0)
	s_barrier
	s_waitcnt lgkmcnt(7)
	ds_read_b128 v[136:139], v15
	ds_read_b128 v[156:159], v17
	ds_read_b128 v[160:163], v17 offset:2048
	ds_read_b128 v[164:167], v17 offset:4096
	ds_read_b128 v[168:171], v17 offset:6144
	ds_read_b128 v[140:143], v15 offset:2048
	ds_read_b128 v[144:147], v15 offset:4096
	ds_read_b128 v[148:151], v15 offset:6144
	s_waitcnt lgkmcnt(14)
	v_mfma_f32_16x16x32_f16 v[56:59], v[172:175], v[192:195], v[56:59]
	s_waitcnt lgkmcnt(13)
	v_mfma_f32_16x16x32_f16 v[60:63], v[172:175], v[196:199], v[60:63]
	s_waitcnt lgkmcnt(12)
	v_mfma_f32_16x16x32_f16 v[64:67], v[172:175], v[200:203], v[64:67]
	s_waitcnt lgkmcnt(11)
	v_mfma_f32_16x16x32_f16 v[68:71], v[172:175], v[204:207], v[68:71]
	s_waitcnt lgkmcnt(10)
	v_mfma_f32_16x16x32_f16 v[72:75], v[176:179], v[192:195], v[72:75]
	v_mfma_f32_16x16x32_f16 v[76:79], v[176:179], v[196:199], v[76:79]
	v_mfma_f32_16x16x32_f16 v[80:83], v[176:179], v[200:203], v[80:83]
	v_mfma_f32_16x16x32_f16 v[84:87], v[176:179], v[204:207], v[84:87]
	s_waitcnt lgkmcnt(9)
	v_mfma_f32_16x16x32_f16 v[88:91], v[180:183], v[192:195], v[88:91]
	v_mfma_f32_16x16x32_f16 v[92:95], v[180:183], v[196:199], v[92:95]
	v_mfma_f32_16x16x32_f16 v[96:99], v[180:183], v[200:203], v[96:99]
	v_mfma_f32_16x16x32_f16 v[100:103], v[180:183], v[204:207], v[100:103]
	s_waitcnt lgkmcnt(8)
	v_mfma_f32_16x16x32_f16 v[104:107], v[184:187], v[192:195], v[104:107]
	v_mfma_f32_16x16x32_f16 v[108:111], v[184:187], v[196:199], v[108:111]
	v_mfma_f32_16x16x32_f16 v[112:115], v[184:187], v[200:203], v[112:115]
	v_mfma_f32_16x16x32_f16 v[116:119], v[184:187], v[204:207], v[116:119]
	s_waitcnt lgkmcnt(7)
	ds_read_b128 v[172:175], v16
	ds_read_b128 v[192:195], v18
	ds_read_b128 v[196:199], v18 offset:2048
	ds_read_b128 v[200:203], v18 offset:4096
	ds_read_b128 v[204:207], v18 offset:6144
	ds_read_b128 v[176:179], v16 offset:2048
	ds_read_b128 v[180:183], v16 offset:4096
	ds_read_b128 v[184:187], v16 offset:6144
	s_waitcnt lgkmcnt(14)
	v_mfma_f32_16x16x32_f16 v[56:59], v[136:139], v[156:159], v[56:59]
	s_waitcnt lgkmcnt(13)
	v_mfma_f32_16x16x32_f16 v[60:63], v[136:139], v[160:163], v[60:63]
	s_waitcnt lgkmcnt(12)
	v_mfma_f32_16x16x32_f16 v[64:67], v[136:139], v[164:167], v[64:67]
	s_waitcnt lgkmcnt(11)
	v_mfma_f32_16x16x32_f16 v[68:71], v[136:139], v[168:171], v[68:71]
	s_waitcnt lgkmcnt(10)
	v_mfma_f32_16x16x32_f16 v[72:75], v[140:143], v[156:159], v[72:75]
	v_mfma_f32_16x16x32_f16 v[76:79], v[140:143], v[160:163], v[76:79]
	v_mfma_f32_16x16x32_f16 v[80:83], v[140:143], v[164:167], v[80:83]
	v_mfma_f32_16x16x32_f16 v[84:87], v[140:143], v[168:171], v[84:87]
	s_waitcnt lgkmcnt(9)
	v_mfma_f32_16x16x32_f16 v[88:91], v[144:147], v[156:159], v[88:91]
	v_mfma_f32_16x16x32_f16 v[92:95], v[144:147], v[160:163], v[92:95]
	v_mfma_f32_16x16x32_f16 v[96:99], v[144:147], v[164:167], v[96:99]
	v_mfma_f32_16x16x32_f16 v[100:103], v[144:147], v[168:171], v[100:103]
	s_waitcnt lgkmcnt(8)
	v_mfma_f32_16x16x32_f16 v[104:107], v[148:151], v[156:159], v[104:107]
	v_mfma_f32_16x16x32_f16 v[108:111], v[148:151], v[160:163], v[108:111]
	v_mfma_f32_16x16x32_f16 v[112:115], v[148:151], v[164:167], v[112:115]
	v_mfma_f32_16x16x32_f16 v[116:119], v[148:151], v[168:171], v[116:119]
	s_waitcnt lgkmcnt(6)
	v_mfma_f32_16x16x32_f16 v[56:59], v[172:175], v[192:195], v[56:59]
	s_waitcnt lgkmcnt(5)
	v_mfma_f32_16x16x32_f16 v[60:63], v[172:175], v[196:199], v[60:63]
	s_waitcnt lgkmcnt(4)
	v_mfma_f32_16x16x32_f16 v[64:67], v[172:175], v[200:203], v[64:67]
	s_waitcnt lgkmcnt(3)
	v_mfma_f32_16x16x32_f16 v[68:71], v[172:175], v[204:207], v[68:71]
	s_waitcnt lgkmcnt(2)
	v_mfma_f32_16x16x32_f16 v[72:75], v[176:179], v[192:195], v[72:75]
	v_mfma_f32_16x16x32_f16 v[76:79], v[176:179], v[196:199], v[76:79]
	v_mfma_f32_16x16x32_f16 v[80:83], v[176:179], v[200:203], v[80:83]
	v_mfma_f32_16x16x32_f16 v[84:87], v[176:179], v[204:207], v[84:87]
	s_waitcnt lgkmcnt(1)
	v_mfma_f32_16x16x32_f16 v[88:91], v[180:183], v[192:195], v[88:91]
	v_mfma_f32_16x16x32_f16 v[92:95], v[180:183], v[196:199], v[92:95]
	v_mfma_f32_16x16x32_f16 v[96:99], v[180:183], v[200:203], v[96:99]
	v_mfma_f32_16x16x32_f16 v[100:103], v[180:183], v[204:207], v[100:103]
	s_waitcnt lgkmcnt(0)
	v_mfma_f32_16x16x32_f16 v[104:107], v[184:187], v[192:195], v[104:107]
	v_mfma_f32_16x16x32_f16 v[108:111], v[184:187], v[196:199], v[108:111]
	v_mfma_f32_16x16x32_f16 v[112:115], v[184:187], v[200:203], v[112:115]
	v_mfma_f32_16x16x32_f16 v[116:119], v[184:187], v[204:207], v[116:119]
	s_nop 7
	s_nop 1
	s_add_u32 s24, s29, 0
	s_lshl_b32 s8, s24, 11
	s_nop 0
	v_add_u32_e32 v212, s8, v23
	v_add_f32_e32 v56, v56, v24
	v_add_f32_e32 v57, v57, v24
	v_add_f32_e32 v58, v58, v24
	v_add_f32_e32 v59, v59, v24
	v_cvt_pk_f16_f32 v56, v56, v57
	v_cvt_pk_f16_f32 v57, v58, v59
	global_store_dwordx2 v212, v[56:57], s[22:23] offset:0
	v_add_f32_e32 v60, v60, v25
	v_add_f32_e32 v61, v61, v25
	v_add_f32_e32 v62, v62, v25
	v_add_f32_e32 v63, v63, v25
	v_cvt_pk_f16_f32 v60, v60, v61
	v_cvt_pk_f16_f32 v61, v62, v63
	global_store_dwordx2 v212, v[60:61], s[22:23] offset:256
	v_add_f32_e32 v64, v64, v26
	v_add_f32_e32 v65, v65, v26
	v_add_f32_e32 v66, v66, v26
	v_add_f32_e32 v67, v67, v26
	v_cvt_pk_f16_f32 v64, v64, v65
	v_cvt_pk_f16_f32 v65, v66, v67
	global_store_dwordx2 v212, v[64:65], s[22:23] offset:1024
	v_add_f32_e32 v68, v68, v27
	v_add_f32_e32 v69, v69, v27
	v_add_f32_e32 v70, v70, v27
	v_add_f32_e32 v71, v71, v27
	v_cvt_pk_f16_f32 v68, v68, v69
	v_cvt_pk_f16_f32 v69, v70, v71
	global_store_dwordx2 v212, v[68:69], s[22:23] offset:1280
	s_add_u32 s24, s29, 1
	s_lshl_b32 s8, s24, 11
	s_nop 0
	v_add_u32_e32 v212, s8, v23
	v_add_f32_e32 v72, v72, v24
	v_add_f32_e32 v73, v73, v24
	v_add_f32_e32 v74, v74, v24
	v_add_f32_e32 v75, v75, v24
	v_cvt_pk_f16_f32 v72, v72, v73
	v_cvt_pk_f16_f32 v73, v74, v75
	global_store_dwordx2 v212, v[72:73], s[22:23] offset:0
	v_add_f32_e32 v76, v76, v25
	v_add_f32_e32 v77, v77, v25
	v_add_f32_e32 v78, v78, v25
	v_add_f32_e32 v79, v79, v25
	v_cvt_pk_f16_f32 v76, v76, v77
	v_cvt_pk_f16_f32 v77, v78, v79
	global_store_dwordx2 v212, v[76:77], s[22:23] offset:256
	v_add_f32_e32 v80, v80, v26
	v_add_f32_e32 v81, v81, v26
	v_add_f32_e32 v82, v82, v26
	v_add_f32_e32 v83, v83, v26
	v_cvt_pk_f16_f32 v80, v80, v81
	v_cvt_pk_f16_f32 v81, v82, v83
	global_store_dwordx2 v212, v[80:81], s[22:23] offset:1024
	v_add_f32_e32 v84, v84, v27
	v_add_f32_e32 v85, v85, v27
	v_add_f32_e32 v86, v86, v27
	v_add_f32_e32 v87, v87, v27
	v_cvt_pk_f16_f32 v84, v84, v85
	v_cvt_pk_f16_f32 v85, v86, v87
	global_store_dwordx2 v212, v[84:85], s[22:23] offset:1280
	s_add_u32 s24, s29, 2
	s_lshl_b32 s8, s24, 11
	s_nop 0
	v_add_u32_e32 v212, s8, v23
	v_add_f32_e32 v88, v88, v24
	v_add_f32_e32 v89, v89, v24
	v_add_f32_e32 v90, v90, v24
	v_add_f32_e32 v91, v91, v24
	v_cvt_pk_f16_f32 v88, v88, v89
	v_cvt_pk_f16_f32 v89, v90, v91
	global_store_dwordx2 v212, v[88:89], s[22:23] offset:0
	v_add_f32_e32 v92, v92, v25
	v_add_f32_e32 v93, v93, v25
	v_add_f32_e32 v94, v94, v25
	v_add_f32_e32 v95, v95, v25
	v_cvt_pk_f16_f32 v92, v92, v93
	v_cvt_pk_f16_f32 v93, v94, v95
	global_store_dwordx2 v212, v[92:93], s[22:23] offset:256
	v_add_f32_e32 v96, v96, v26
	v_add_f32_e32 v97, v97, v26
	v_add_f32_e32 v98, v98, v26
	v_add_f32_e32 v99, v99, v26
	v_cvt_pk_f16_f32 v96, v96, v97
	v_cvt_pk_f16_f32 v97, v98, v99
	global_store_dwordx2 v212, v[96:97], s[22:23] offset:1024
	v_add_f32_e32 v100, v100, v27
	v_add_f32_e32 v101, v101, v27
	v_add_f32_e32 v102, v102, v27
	v_add_f32_e32 v103, v103, v27
	v_cvt_pk_f16_f32 v100, v100, v101
	v_cvt_pk_f16_f32 v101, v102, v103
	global_store_dwordx2 v212, v[100:101], s[22:23] offset:1280
	s_add_u32 s24, s29, 3
	s_lshl_b32 s8, s24, 11
	s_nop 0
	v_add_u32_e32 v212, s8, v23
	v_add_f32_e32 v104, v104, v24
	v_add_f32_e32 v105, v105, v24
	v_add_f32_e32 v106, v106, v24
	v_add_f32_e32 v107, v107, v24
	v_cvt_pk_f16_f32 v104, v104, v105
	v_cvt_pk_f16_f32 v105, v106, v107
	global_store_dwordx2 v212, v[104:105], s[22:23] offset:0
	v_add_f32_e32 v108, v108, v25
	v_add_f32_e32 v109, v109, v25
	v_add_f32_e32 v110, v110, v25
	v_add_f32_e32 v111, v111, v25
	v_cvt_pk_f16_f32 v108, v108, v109
	v_cvt_pk_f16_f32 v109, v110, v111
	global_store_dwordx2 v212, v[108:109], s[22:23] offset:256
	v_add_f32_e32 v112, v112, v26
	v_add_f32_e32 v113, v113, v26
	v_add_f32_e32 v114, v114, v26
	v_add_f32_e32 v115, v115, v26
	v_cvt_pk_f16_f32 v112, v112, v113
	v_cvt_pk_f16_f32 v113, v114, v115
	global_store_dwordx2 v212, v[112:113], s[22:23] offset:1024
	v_add_f32_e32 v116, v116, v27
	v_add_f32_e32 v117, v117, v27
	v_add_f32_e32 v118, v118, v27
	v_add_f32_e32 v119, v119, v27
	v_cvt_pk_f16_f32 v116, v116, v117
	v_cvt_pk_f16_f32 v117, v118, v119
	global_store_dwordx2 v212, v[116:117], s[22:23] offset:1280
	s_branch .Lpf_done
.Lpf_done:
	s_waitcnt lgkmcnt(0)
	s_max_i32 s54, s52, s53
	s_cmpk_gt_i32 s54, 0x480
	s_cbranch_scc1 .Lpf_rare
	s_endpgm
.Lpf_rare:
	s_mov_b32 s59, 0
.Lpf_rare_next:
	s_waitcnt vmcnt(0) lgkmcnt(0)
	s_barrier
	s_mov_b64 exec, -1
	s_cmp_eq_u32 s59, 0
	s_cbranch_scc0 .Lpf_rare_p1
	s_mov_b32 s59, 1
	s_add_u32 s2, s58, 0x200
	s_lshr_b32 s3, s2, 3
	s_and_b32 s3, s3, 24
	s_and_b32 s4, s2, 2
	s_or_b32 s3, s3, s4
	s_cmp_eq_u32 s3, 0
	s_cbranch_scc0 .Lpf_rare_go
.Lpf_rare_p1:
	s_cmp_eq_u32 s59, 1
	s_cbranch_scc0 .Lpf_rare_end
	s_mov_b32 s59, 2
	s_add_u32 s2, s58, 0x300
.Lpf_rare_go:
	s_mov_b32 s0, s56
	s_mov_b32 s1, s57
	v_mov_b32_e32 v0, v216
	s_branch .Lpf_old
.Lpf_rare_end:
	s_endpgm
.Lpf_old:
	s_load_dwordx4 s[16:19], s[0:1], 0x58
	s_load_dwordx8 s[8:15], s[0:1], 0x8
	s_load_dwordx2 s[6:7], s[0:1], 0x48
	s_load_dwordx4 s[20:23], s[0:1], 0x30
	v_and_b32_e32 v1, 63, v0
	v_lshrrev_b32_e32 v152, 6, v0
	s_cmpk_lt_i32 s2, 0x300
	s_mov_b64 s[4:5], -1
	s_cbranch_scc0 .LBB1_13
	s_ashr_i32 s3, s2, 3
	s_cmp_lt_i32 s3, 32
	s_cselect_b64 s[4:5], -1, 0
	s_cmp_gt_i32 s3, 31
	s_cbranch_scc0 .LBB1_5
	s_lshr_b32 s25, s3, 1
	s_and_b32 s24, s2, 2
	s_and_b32 s25, s25, 12
	s_cmp_gt_u32 s3, 63
	s_cselect_b32 s26, 16, 0
	s_and_b32 s29, s2, 1
	s_lshl_b32 s27, s29, 2
	s_waitcnt lgkmcnt(0)
	s_load_dword s30, s[14:15], s27 offset:0x0
	s_or_b32 s24, s26, s24
	s_or_b32 s33, s24, s25
	s_lshl_b32 s31, s33, 6
	s_mov_b64 s[26:27], 0
	s_waitcnt lgkmcnt(0)
	s_cmp_lt_i32 s31, s30
	s_mov_b64 s[24:25], 0
	s_cbranch_scc1 .LBB1_6
	s_bfe_u32 s30, s2, 0x10002
	s_and_b64 vcc, exec, s[26:27]
	s_cbranch_vccnz .LBB1_7

.LBB1_13:
	s_andn2_b64 vcc, exec, s[4:5]
	s_cbranch_vccnz .LBB1_69
	s_bfe_u32 s24, s2, 0x10006
	s_lshl_b32 s0, s24, 2
	s_waitcnt lgkmcnt(0)
	s_load_dword s5, s[14:15], s0 offset:0x0
	s_waitcnt lgkmcnt(0)
	s_ashr_i32 s14, s5, 7
	s_cmp_lt_i32 s14, 9
	s_cbranch_scc1 .LBB1_69
	s_and_b32 s3, s5, 0x7f
	s_and_b32 s15, s2, 3
	s_add_i32 s0, s3, 63
	s_lshl_b32 s4, s15, 5
	s_and_b32 s0, s0, 0xc0
	s_cmp_ge_u32 s4, s0
	s_cbranch_scc1 .LBB1_69
	s_add_i32 s26, s2, 0xfffffd00
	s_bfe_u32 s25, s2, 0x40002
	s_mov_b64 s[0:1], -1
	s_cmp_lt_u32 s4, s3
	v_cmp_gt_u32_e32 vcc, 64, v0
	s_cbranch_scc1 .LBB1_23
	s_and_saveexec_b64 s[0:1], vcc
	s_cbranch_execz .LBB1_22
	s_lshl_b32 s2, s24, 4
	s_or_b32 s27, s2, s25
	s_cmpk_lt_u32 s26, 0x80
	s_mov_b64 s[2:3], -1
	s_cbranch_scc1 .LBB1_20
	s_lshl_b32 s2, s27, 7
	s_lshl_b32 s3, s14, 3
	s_add_i32 s2, s3, s2
	s_lshl_b32 s2, s2, 1
	s_lshl_b32 s28, s15, 2
	v_lshlrev_b32_e32 v2, 4, v0
	s_mov_b32 s3, 0
	v_mov_b32_e32 v3, 0
	s_or_b32 s2, s28, s2
	v_lshl_add_u64 v[2:3], s[18:19], 0, v[2:3]
	s_lshl_b64 s[28:29], s[2:3], 10
	v_lshl_add_u64 v[4:5], v[2:3], 0, s[28:29]
	s_mov_b32 s28, s3
	s_mov_b32 s29, s3
	s_mov_b32 s30, s3
	s_mov_b32 s31, s3
	v_mov_b64_e32 v[6:7], s[28:29]
	v_mov_b64_e32 v[8:9], s[30:31]
	s_or_b32 s28, s2, 1
	s_lshl_b64 s[28:29], s[28:29], 10
	global_store_dwordx4 v[4:5], v[6:9], off
	v_lshl_add_u64 v[4:5], v[2:3], 0, s[28:29]
	s_or_b32 s28, s2, 2
	s_mov_b32 s29, s3
	s_or_b32 s2, s2, 3
	s_lshl_b64 s[28:29], s[28:29], 10
	s_lshl_b64 s[2:3], s[2:3], 10
	global_store_dwordx4 v[4:5], v[6:9], off
	v_lshl_add_u64 v[4:5], v[2:3], 0, s[28:29]
	v_lshl_add_u64 v[2:3], v[2:3], 0, s[2:3]
	s_mov_b64 s[2:3], 0
	global_store_dwordx4 v[4:5], v[6:9], off
	global_store_dwordx4 v[2:3], v[6:9], off

.LBB1_67:
	s_andn2_b64 vcc, exec, s[4:5]
	s_cbranch_vccnz .LBB1_69
	s_lshl_b32 s0, s8, 2
	s_add_u32 s0, s20, s0
	s_addc_u32 s1, s21, 0
	global_load_dwordx4 v[36:39], v150, s[0:1] offset:224
	global_load_dwordx4 v[40:43], v150, s[0:1] offset:96
	global_load_dwordx4 v[44:47], v150, s[0:1] offset:192
	global_load_dwordx4 v[48:51], v150, s[0:1] offset:64
	global_load_dwordx4 v[52:55], v150, s[0:1] offset:160
	global_load_dwordx4 v[56:59], v150, s[0:1] offset:32
	global_load_dwordx4 v[60:63], v150, s[0:1] offset:128
	global_load_dwordx4 v[64:67], v150, s[0:1]
	global_load_dwordx4 v[68:71], v150, s[6:7]
	global_load_dwordx4 v[72:75], v150, s[6:7] offset:128
	global_load_dwordx4 v[76:79], v150, s[6:7] offset:32
	global_load_dwordx4 v[80:83], v150, s[6:7] offset:160
	global_load_dwordx4 v[84:87], v150, s[6:7] offset:96
	global_load_dwordx4 v[88:91], v150, s[6:7] offset:64
	global_load_dwordx4 v[92:95], v150, s[6:7] offset:224
	global_load_dwordx4 v[96:99], v150, s[6:7] offset:192
	v_mbcnt_lo_u32_b32 v0, -1, 0
	v_mbcnt_hi_u32_b32 v0, -1, v0
	v_and_b32_e32 v100, 64, v0
	v_xor_b32_e32 v1, 32, v0
	v_add_u32_e32 v100, 64, v100
	v_cmp_lt_i32_e32 vcc, v1, v100
	v_mov_b32_e32 v19, 0x358637bd
	s_lshl_b32 s0, s9, 6
	v_cndmask_b32_e32 v0, v0, v1, vcc
	v_lshlrev_b32_e32 v100, 2, v0
	s_lshl_b32 s2, s14, 2
	s_add_i32 s2, s2, s0
	s_mov_b32 s1, 0
	s_or_b32 s0, s2, s15
	s_lshl_b64 s[0:1], s[0:1], 12
	s_add_u32 s0, s16, s0
	s_addc_u32 s1, s17, s1
	s_waitcnt vmcnt(15)
	v_pk_add_f32 v[0:1], v[38:39], v[34:35]
	s_waitcnt vmcnt(14)
	v_pk_add_f32 v[28:29], v[28:29], v[40:41]
	s_waitcnt vmcnt(13)
	v_pk_add_f32 v[22:23], v[22:23], v[44:45]
	s_waitcnt vmcnt(12)
	v_pk_add_f32 v[20:21], v[20:21], v[48:49]
	s_waitcnt vmcnt(11)
	v_pk_add_f32 v[12:13], v[12:13], v[52:53]
	s_waitcnt vmcnt(10)
	v_pk_add_f32 v[10:11], v[10:11], v[56:57]
	s_waitcnt vmcnt(9)
	v_pk_add_f32 v[4:5], v[4:5], v[60:61]
	s_waitcnt vmcnt(8)
	v_pk_add_f32 v[2:3], v[2:3], v[64:65]
	v_pk_add_f32 v[6:7], v[66:67], v[6:7]
	v_fma_f32 v34, v2, v2, 0
	v_fmac_f32_e32 v34, v4, v4
	v_fmac_f32_e32 v34, v3, v3
	v_fmac_f32_e32 v34, v5, v5
	v_pk_add_f32 v[8:9], v[62:63], v[8:9]
	v_fmac_f32_e32 v34, v6, v6
	v_fmac_f32_e32 v34, v8, v8
	v_fmac_f32_e32 v34, v7, v7
	v_fmac_f32_e32 v34, v9, v9
	v_fmac_f32_e32 v34, v10, v10
	v_fmac_f32_e32 v34, v12, v12
	v_fmac_f32_e32 v34, v11, v11
	v_pk_add_f32 v[14:15], v[58:59], v[14:15]
	v_fmac_f32_e32 v34, v13, v13
	v_pk_add_f32 v[16:17], v[54:55], v[16:17]
	v_fmac_f32_e32 v34, v14, v14
	v_fmac_f32_e32 v34, v16, v16
	v_fmac_f32_e32 v34, v15, v15
	v_fmac_f32_e32 v34, v17, v17
	v_fmac_f32_e32 v34, v20, v20
	v_fmac_f32_e32 v34, v22, v22
	v_fmac_f32_e32 v34, v21, v21
	v_pk_add_f32 v[24:25], v[50:51], v[24:25]
	v_fmac_f32_e32 v34, v23, v23
	v_pk_add_f32 v[26:27], v[46:47], v[26:27]
	v_fmac_f32_e32 v34, v24, v24
	v_fmac_f32_e32 v34, v26, v26
	v_fmac_f32_e32 v34, v25, v25
	v_fmac_f32_e32 v34, v27, v27
	v_pk_add_f32 v[30:31], v[30:31], v[36:37]
	v_fmac_f32_e32 v34, v28, v28
	v_fmac_f32_e32 v34, v30, v30
	v_fmac_f32_e32 v34, v29, v29
	v_pk_add_f32 v[32:33], v[42:43], v[32:33]
	v_fmac_f32_e32 v34, v31, v31
	v_fmac_f32_e32 v34, v32, v32
	v_fmac_f32_e32 v34, v0, v0
	v_fmac_f32_e32 v34, v33, v33
	v_fmac_f32_e32 v34, v1, v1
	ds_bpermute_b32 v35, v100, v34
	s_waitcnt lgkmcnt(0)
	v_add_f32_e32 v34, v34, v35
	v_fmac_f32_e32 v19, 0x3c800000, v34
	v_rsq_f32_e32 v34, v19
	s_waitcnt vmcnt(7)
	v_pk_mul_f32 v[36:37], v[34:35], v[68:69] op_sel_hi:[0,1]
	v_pk_mul_f32 v[38:39], v[34:35], v[70:71] op_sel_hi:[0,1]
	s_waitcnt vmcnt(6)
	v_pk_mul_f32 v[40:41], v[34:35], v[72:73] op_sel_hi:[0,1]
	v_pk_mul_f32 v[42:43], v[34:35], v[74:75] op_sel_hi:[0,1]
	s_waitcnt vmcnt(5)
	v_pk_mul_f32 v[44:45], v[34:35], v[76:77] op_sel_hi:[0,1]
	v_pk_mul_f32 v[46:47], v[34:35], v[78:79] op_sel_hi:[0,1]
	s_waitcnt vmcnt(4)
	v_pk_mul_f32 v[48:49], v[34:35], v[80:81] op_sel_hi:[0,1]
	v_pk_mul_f32 v[50:51], v[34:35], v[82:83] op_sel_hi:[0,1]
	s_waitcnt vmcnt(2)
	v_pk_mul_f32 v[52:53], v[34:35], v[88:89] op_sel_hi:[0,1]
	v_pk_mul_f32 v[54:55], v[34:35], v[90:91] op_sel_hi:[0,1]
	s_waitcnt vmcnt(0)
	v_pk_mul_f32 v[56:57], v[34:35], v[96:97] op_sel_hi:[0,1]
	v_pk_mul_f32 v[58:59], v[34:35], v[98:99] op_sel_hi:[0,1]
	v_pk_mul_f32 v[60:61], v[34:35], v[84:85] op_sel_hi:[0,1]
	v_pk_mul_f32 v[62:63], v[34:35], v[86:87] op_sel_hi:[0,1]
	v_pk_mul_f32 v[64:65], v[34:35], v[92:93] op_sel_hi:[0,1]
	v_pk_mul_f32 v[34:35], v[34:35], v[94:95] op_sel_hi:[0,1]
	v_pk_mul_f32 v[2:3], v[2:3], v[36:37]
	v_pk_mul_f32 v[6:7], v[38:39], v[6:7]
	v_pk_mul_f32 v[36:37], v[4:5], v[40:41]
	v_pk_mul_f32 v[38:39], v[42:43], v[8:9]
	v_pk_mul_f32 v[4:5], v[10:11], v[44:45]
	v_pk_mul_f32 v[8:9], v[46:47], v[14:15]
	v_pk_mul_f32 v[10:11], v[12:13], v[48:49]
	v_pk_mul_f32 v[12:13], v[50:51], v[16:17]
	v_pk_mul_f32 v[14:15], v[20:21], v[52:53]
	v_pk_mul_f32 v[16:17], v[54:55], v[24:25]
	v_pk_mul_f32 v[20:21], v[22:23], v[56:57]
	v_pk_mul_f32 v[22:23], v[58:59], v[26:27]
	v_pk_mul_f32 v[24:25], v[28:29], v[60:61]
	v_pk_mul_f32 v[26:27], v[62:63], v[32:33]
	v_pk_mul_f32 v[28:29], v[30:31], v[64:65]
	v_pk_mul_f32 v[30:31], v[34:35], v[0:1]
	v_cvt_pk_f16_f32 v0, v2, v3
	v_cvt_pk_f16_f32 v1, v6, v7
	v_cvt_pk_f16_f32 v2, v4, v5
	v_cvt_pk_f16_f32 v3, v8, v9
	v_cvt_pk_f16_f32 v4, v14, v15
	v_cvt_pk_f16_f32 v5, v16, v17
	v_cvt_pk_f16_f32 v6, v24, v25
	v_cvt_pk_f16_f32 v7, v26, v27
	v_cvt_pk_f16_f32 v8, v36, v37
	global_store_dwordx4 v18, v[0:3], s[0:1]
	global_store_dwordx4 v18, v[4:7], s[0:1] offset:1024
	v_cvt_pk_f16_f32 v9, v38, v39
	v_cvt_pk_f16_f32 v10, v10, v11
	v_cvt_pk_f16_f32 v11, v12, v13
	v_cvt_pk_f16_f32 v0, v20, v21
	v_cvt_pk_f16_f32 v1, v22, v23
	v_cvt_pk_f16_f32 v2, v28, v29
	v_cvt_pk_f16_f32 v3, v30, v31
	global_store_dwordx4 v18, v[8:11], s[0:1] offset:2048
	global_store_dwordx4 v18, v[0:3], s[0:1] offset:3072
.LBB1_69:
	s_branch .Lpf_rare_next
	.section	.rodata,"a",@progbits
	.p2align	6, 0x0
	.amdhsa_kernel _Z11proj_kernelPKDF16_S0_S0_S0_PKiPKfS4_S4_S4_S4_PDF16_S5_S5_
		.amdhsa_group_segment_fixed_size 28672
		.amdhsa_private_segment_fixed_size 0
		.amdhsa_kernarg_size 104
		.amdhsa_user_sgpr_count 2
		.amdhsa_user_sgpr_dispatch_ptr 0
		.amdhsa_user_sgpr_queue_ptr 0
		.amdhsa_user_sgpr_kernarg_segment_ptr 1
		.amdhsa_user_sgpr_dispatch_id 0
		.amdhsa_user_sgpr_kernarg_preload_length 0
		.amdhsa_user_sgpr_kernarg_preload_offset 0
		.amdhsa_user_sgpr_private_segment_size 0
		.amdhsa_uses_dynamic_stack 0
		.amdhsa_enable_private_segment 0
		.amdhsa_system_sgpr_workgroup_id_x 1
		.amdhsa_system_sgpr_workgroup_id_y 0
		.amdhsa_system_sgpr_workgroup_id_z 0
		.amdhsa_system_sgpr_workgroup_info 0
		.amdhsa_system_vgpr_workitem_id 0
		.amdhsa_next_free_vgpr 217
		.amdhsa_next_free_sgpr 60
		.amdhsa_accum_offset 220
		.amdhsa_reserve_vcc 1
		.amdhsa_float_round_mode_32 0
		.amdhsa_float_round_mode_16_64 0
		.amdhsa_float_denorm_mode_32 3
		.amdhsa_float_denorm_mode_16_64 3
		.amdhsa_dx10_clamp 1
		.amdhsa_ieee_mode 1
		.amdhsa_fp16_overflow 0
		.amdhsa_tg_split 0
		.amdhsa_exception_fp_ieee_invalid_op 0
		.amdhsa_exception_fp_denorm_src 0
		.amdhsa_exception_fp_ieee_div_zero 0
		.amdhsa_exception_fp_ieee_overflow 0
		.amdhsa_exception_fp_ieee_underflow 0
		.amdhsa_exception_fp_ieee_inexact 0
		.amdhsa_exception_int_div_zero 0
	.end_amdhsa_kernel

amdhsa.kernels:
  - .agpr_count:     0
    .args:
      - .actual_access:  read_only
        .address_space:  global
        .offset:         0
        .size:           8
        .value_kind:     global_buffer
      - .actual_access:  read_only
        .address_space:  global
        .offset:         8
        .size:           8
        .value_kind:     global_buffer
      - .actual_access:  read_only
        .address_space:  global
        .offset:         16
        .size:           8
        .value_kind:     global_buffer
      - .actual_access:  read_only
        .address_space:  global
        .offset:         24
        .size:           8
        .value_kind:     global_buffer
      - .actual_access:  read_only
        .address_space:  global
        .offset:         32
        .size:           8
        .value_kind:     global_buffer
      - .actual_access:  read_only
        .address_space:  global
        .offset:         40
        .size:           8
        .value_kind:     global_buffer
      - .actual_access:  read_only
        .address_space:  global
        .offset:         48
        .size:           8
        .value_kind:     global_buffer
      - .actual_access:  read_only
        .address_space:  global
        .offset:         56
        .size:           8
        .value_kind:     global_buffer
      - .actual_access:  write_only
        .address_space:  global
        .offset:         64
        .size:           8
        .value_kind:     global_buffer
      - .actual_access:  write_only
        .address_space:  global
        .offset:         72
        .size:           8
        .value_kind:     global_buffer
      - .actual_access:  write_only
        .address_space:  global
        .offset:         80
        .size:           8
        .value_kind:     global_buffer
      - .actual_access:  write_only
        .address_space:  global
        .offset:         88
        .size:           8
        .value_kind:     global_buffer
      - .actual_access:  write_only
        .address_space:  global
        .offset:         96
        .size:           8
        .value_kind:     global_buffer
    .group_segment_fixed_size: 80
    .kernarg_segment_align: 8
    .kernarg_segment_size: 104
    .language:       OpenCL C
    .language_version:
      - 2
      - 0
    .max_flat_workgroup_size: 256
    .name:           _Z11prep_kernelPKfS0_S0_PKiS0_S0_S0_S0_PDF16_S3_S3_S3_Pi
    .private_segment_fixed_size: 0
    .sgpr_count:     43
    .sgpr_spill_count: 0
    .symbol:         _Z11prep_kernelPKfS0_S0_PKiS0_S0_S0_S0_PDF16_S3_S3_S3_Pi.kd
    .uniform_work_group_size: 1
    .uses_dynamic_stack: false
    .vgpr_count:     64
    .vgpr_spill_count: 0
    .wavefront_size: 64
  - .agpr_count:     0
    .args:
      - .address_space:  global
        .offset:         0
        .size:           8
        .value_kind:     global_buffer
      - .address_space:  global
        .offset:         8
        .size:           8
        .value_kind:     global_buffer
      - .address_space:  global
        .offset:         16
        .size:           8
        .value_kind:     global_buffer
      - .address_space:  global
        .offset:         24
        .size:           8
        .value_kind:     global_buffer
      - .actual_access:  read_only
        .address_space:  global
        .offset:         32
        .size:           8
        .value_kind:     global_buffer
      - .actual_access:  read_only
        .address_space:  global
        .offset:         40
        .size:           8
        .value_kind:     global_buffer
      - .actual_access:  read_only
        .address_space:  global
        .offset:         48
        .size:           8
        .value_kind:     global_buffer
      - .actual_access:  read_only
        .address_space:  global
        .offset:         56
        .size:           8
        .value_kind:     global_buffer
      - .actual_access:  read_only
        .address_space:  global
        .offset:         64
        .size:           8
        .value_kind:     global_buffer
      - .actual_access:  read_only
        .address_space:  global
        .offset:         72
        .size:           8
        .value_kind:     global_buffer
      - .actual_access:  write_only
        .address_space:  global
        .offset:         80
        .size:           8
        .value_kind:     global_buffer
      - .actual_access:  write_only
        .address_space:  global
        .offset:         88
        .size:           8
        .value_kind:     global_buffer
      - .actual_access:  write_only
        .address_space:  global
        .offset:         96
        .size:           8
        .value_kind:     global_buffer
    .group_segment_fixed_size: 28672
    .kernarg_segment_align: 8
    .kernarg_segment_size: 104
    .language:       OpenCL C
    .language_version:
      - 2
      - 0
    .max_flat_workgroup_size: 512
    .name:           _Z11proj_kernelPKDF16_S0_S0_S0_PKiPKfS4_S4_S4_S4_PDF16_S5_S5_
    .private_segment_fixed_size: 0
    .sgpr_count:     66
    .sgpr_spill_count: 0
    .symbol:         _Z11proj_kernelPKDF16_S0_S0_S0_PKiPKfS4_S4_S4_S4_PDF16_S5_S5_.kd
    .uniform_work_group_size: 1
    .uses_dynamic_stack: false
    .vgpr_count:     217
    .vgpr_spill_count: 0
    .wavefront_size: 64
  - .agpr_count:     0
    .args:
      - .actual_access:  read_only
        .address_space:  global
        .offset:         0
        .size:           8
        .value_kind:     global_buffer
      - .address_space:  global
        .offset:         8
        .size:           8
        .value_kind:     global_buffer
      - .address_space:  global
        .offset:         16
        .size:           8
        .value_kind:     global_buffer
      - .actual_access:  read_only
        .address_space:  global
        .offset:         24
        .size:           8
        .value_kind:     global_buffer
      - .actual_access:  write_only
        .address_space:  global
        .offset:         32
        .size:           8
        .value_kind:     global_buffer
      - .actual_access:  read_only
        .address_space:  global
        .offset:         40
        .size:           8
        .value_kind:     global_buffer
      - .actual_access:  write_only
        .address_space:  global
        .offset:         48
        .size:           8
        .value_kind:     global_buffer
    .group_segment_fixed_size: 0
    .kernarg_segment_align: 8
    .kernarg_segment_size: 56
    .language:       OpenCL C
    .language_version:
      - 2
      - 0
    .max_flat_workgroup_size: 512
    .name:           _Z11attn_kernelPKDF16_S0_S0_PKiPDF16_PKfS3_
    .private_segment_fixed_size: 0
    .sgpr_count:     100
    .sgpr_spill_count: 0
    .symbol:         _Z11attn_kernelPKDF16_S0_S0_PKiPDF16_PKfS3_.kd
    .uniform_work_group_size: 1
    .uses_dynamic_stack: false
    .vgpr_count:     204
    .vgpr_spill_count: 0
    .wavefront_size: 64
  - .agpr_count:     0
    .args:
      - .address_space:  global
        .offset:         0
        .size:           8
        .value_kind:     global_buffer
      - .address_space:  global
        .offset:         8
        .size:           8
        .value_kind:     global_buffer
      - .actual_access:  read_only
        .address_space:  global
        .offset:         16
        .size:           8
        .value_kind:     global_buffer
      - .actual_access:  write_only
        .address_space:  global
        .offset:         24
        .size:           8
        .value_kind:     global_buffer
    .group_segment_fixed_size: 0
    .kernarg_segment_align: 8
    .kernarg_segment_size: 32
    .language:       OpenCL C
    .language_version:
      - 2
      - 0
    .max_flat_workgroup_size: 512
    .name:           _Z12oproj_kernelPKDF16_S0_PKfPf
    .private_segment_fixed_size: 0
    .sgpr_count:     33
    .sgpr_spill_count: 0
    .symbol:         _Z12oproj_kernelPKDF16_S0_PKfPf.kd
    .uniform_work_group_size: 1
    .uses_dynamic_stack: false
    .vgpr_count:     108
    .vgpr_spill_count: 0
    .wavefront_size: 64
